# v74 plus nt policy on the converted expert-weight stores of the P9/P10 conversion loops (116 stores)
# speedup vs baseline: 1.0088x; 1.0088x over previous
; #define LAS __attribute__((address_space(3)))
; __device__ __forceinline__ void tr_item8(const float* W, int ld, int K, int nblk, int item, unsigned char* WT, bool gu, float scale, LAS float* scr, int lane) {
;     const int kb = item / nblk, nb = item % nblk, k0 = 64 * kb, n0 = 32 * nb;
;     int drow0 = n0;
;     if (gu) { const int bj = n0 / FF, j = n0 - bj * FF; drow0 = 256 * (j / 128) + 128 * bj + (j % 128); }
;     { float t_[32];
; #pragma unroll
;       for (int i = 0; i < 32; ++i) t_[i] = W[(size_t)(k0 + 2 * i + (lane >> 5)) * ld + n0 + (lane & 31)];
; __device__ __forceinline__ void convert_items(Frame& F, const Args& a, int lo, int hi, int w, int nw) {
;     ...
;         if (r < NE * I_GU) { const int e = r / I_GU, rr = r % I_GU; tr_item8(a.in[18] + (size_t)e * D * 2 * FF, 2 * FF, D, 224, rr, F.ws + WS_WMGU + (size_t)e * 2 * FF * D, true, WSC_GU, scr, lane); continue; } r -= NE * I_GU;
.LBB0_1132:
	s_cmpk_gt_i32 s37, 0x5ff
	s_mov_b64 s[24:25], -1
	s_cbranch_scc0 .LBB0_1154
	s_cmpk_gt_u32 s37, 0x7ff
	s_cbranch_scc0 .LBB0_1151
	s_cmpk_gt_u32 s37, 0xaff
	s_cbranch_scc0 .LBB0_1148
	s_cmpk_gt_u32 s37, 0xcff
	s_cbranch_scc0 .LBB0_1145
	s_cmpk_gt_u32 s37, 0x1aff
	s_cbranch_scc0 .LBB0_1142
	s_cmpk_gt_u32 s37, 0x21ff
	s_cbranch_scc0 .LBB0_1139
	s_add_i32 s16, s37, 0xde00
	s_bfe_u32 s24, s16, 0x70009
	s_mulk_i32 s24, 0x2493
	s_lshr_b32 s24, s24, 16
	s_mul_i32 s25, s24, 0xe00
	s_sub_i32 s16, s16, s25
	s_mul_i32 s25, s24, 0x1c00000
	s_add_u32 s27, s72, s25
	s_addc_u32 s51, s73, 0
	s_mul_i32 s24, s24, 0x700000
	s_add_u32 s24, s3, s24
	s_addc_u32 s25, s30, 0
	s_bfe_u32 s26, s16, 0xb0005
	s_mulk_i32 s26, 0x2493
	s_lshr_b32 s26, s26, 16
	s_mul_i32 s50, s26, 0xe0
	s_sub_i32 s50, s16, s50
	s_lshl_b32 s16, s50, 5
	s_and_b32 s52, s50, 0xffff
	s_cmpk_gt_u32 s52, 0x6f
	s_cselect_b32 s52, 0xfffff200, 0
	s_cselect_b32 s53, 0x80, 0
	s_add_i32 s16, s52, s16
	s_sext_i32_i16 s52, s16
	s_bfe_u32 s52, s52, 0x70018
	s_add_i32 s52, s16, s52
	s_sext_i32_i16 s54, s52
	s_and_b32 s52, s52, 0xff80
	s_sub_i32 s16, s16, s52
	s_lshl_b32 s54, s54, 1
	s_sext_i32_i16 s16, s16
	s_and_b32 s54, s54, 0xffffff00
	s_add_i32 s16, s53, s16
	s_lshl_b32 s50, s50, 7
	s_add_i32 s16, s16, s54
	s_lshl_b32 s26, s26, 6
	s_and_b32 s50, s50, 0x3ff80
	s_add_u32 s50, s27, s50
	s_addc_u32 s51, s51, 0
	v_add_u32_e32 v50, s26, v30
	v_lshl_add_u64 v[28:29], s[50:51], 0, v[0:1]
	v_mad_i64_i32 v[48:49], s[50:51], v50, s45, v[28:29]
	global_load_dword v51, v[48:49], off nt
	v_add_u32_e32 v48, 2, v50
	v_mad_i64_i32 v[48:49], s[50:51], v48, s45, v[28:29]
	global_load_dword v52, v[48:49], off nt
	v_add_u32_e32 v48, 4, v50
	v_mad_i64_i32 v[48:49], s[50:51], v48, s45, v[28:29]
	global_load_dword v53, v[48:49], off nt
	v_add_u32_e32 v48, 6, v50
	v_mad_i64_i32 v[48:49], s[50:51], v48, s45, v[28:29]
	global_load_dword v54, v[48:49], off nt
	v_add_u32_e32 v48, 8, v50
	v_mad_i64_i32 v[48:49], s[50:51], v48, s45, v[28:29]
	global_load_dword v55, v[48:49], off nt
	v_add_u32_e32 v48, 10, v50
	v_mad_i64_i32 v[48:49], s[50:51], v48, s45, v[28:29]
	global_load_dword v56, v[48:49], off nt
	v_add_u32_e32 v48, 12, v50
	v_mad_i64_i32 v[48:49], s[50:51], v48, s45, v[28:29]
	global_load_dword v57, v[48:49], off nt
	v_add_u32_e32 v48, 14, v50
	v_mad_i64_i32 v[48:49], s[50:51], v48, s45, v[28:29]
	global_load_dword v58, v[48:49], off nt
	v_add_u32_e32 v48, 16, v50
	v_mad_i64_i32 v[48:49], s[50:51], v48, s45, v[28:29]
	global_load_dword v59, v[48:49], off nt
	v_add_u32_e32 v48, 18, v50
	v_mad_i64_i32 v[48:49], s[50:51], v48, s45, v[28:29]
	global_load_dword v60, v[48:49], off nt
	v_add_u32_e32 v48, 20, v50
	v_mad_i64_i32 v[48:49], s[50:51], v48, s45, v[28:29]
	global_load_dword v61, v[48:49], off nt
	v_add_u32_e32 v48, 22, v50
	v_mad_i64_i32 v[48:49], s[50:51], v48, s45, v[28:29]
	global_load_dword v62, v[48:49], off nt
	v_add_u32_e32 v48, 24, v50
	v_mad_i64_i32 v[48:49], s[50:51], v48, s45, v[28:29]
	global_load_dword v63, v[48:49], off nt
	v_add_u32_e32 v48, 26, v50
	v_mad_i64_i32 v[48:49], s[50:51], v48, s45, v[28:29]
	global_load_dword v64, v[48:49], off nt
	v_add_u32_e32 v48, 28, v50
	v_mad_i64_i32 v[48:49], s[50:51], v48, s45, v[28:29]
	global_load_dword v65, v[48:49], off nt
	v_add_u32_e32 v48, 30, v50
	v_mad_i64_i32 v[48:49], s[50:51], v48, s45, v[28:29]
	global_load_dword v66, v[48:49], off nt
	v_add_u32_e32 v48, 32, v50
	v_mad_i64_i32 v[48:49], s[50:51], v48, s45, v[28:29]
	global_load_dword v67, v[48:49], off nt
	v_add_u32_e32 v48, 34, v50
	v_mad_i64_i32 v[48:49], s[50:51], v48, s45, v[28:29]
	global_load_dword v68, v[48:49], off nt
	v_add_u32_e32 v48, 36, v50
	v_mad_i64_i32 v[48:49], s[50:51], v48, s45, v[28:29]
	global_load_dword v69, v[48:49], off nt
	v_add_u32_e32 v48, 38, v50
	v_mad_i64_i32 v[48:49], s[50:51], v48, s45, v[28:29]
	global_load_dword v70, v[48:49], off nt
	v_add_u32_e32 v48, 40, v50
	v_mad_i64_i32 v[48:49], s[50:51], v48, s45, v[28:29]
	global_load_dword v71, v[48:49], off nt
	v_add_u32_e32 v48, 42, v50
	v_mad_i64_i32 v[48:49], s[50:51], v48, s45, v[28:29]
	global_load_dword v72, v[48:49], off nt
	v_add_u32_e32 v48, 44, v50
	v_mad_i64_i32 v[48:49], s[50:51], v48, s45, v[28:29]
	global_load_dword v73, v[48:49], off nt
	v_add_u32_e32 v48, 46, v50
	v_mad_i64_i32 v[48:49], s[50:51], v48, s45, v[28:29]
	global_load_dword v74, v[48:49], off nt
	v_add_u32_e32 v48, 48, v50
	v_mad_i64_i32 v[48:49], s[50:51], v48, s45, v[28:29]
	global_load_dword v75, v[48:49], off nt
	v_add_u32_e32 v48, 50, v50
	v_mad_i64_i32 v[48:49], s[50:51], v48, s45, v[28:29]
	global_load_dword v76, v[48:49], off nt
	v_add_u32_e32 v48, 52, v50
	v_mad_i64_i32 v[48:49], s[50:51], v48, s45, v[28:29]
	global_load_dword v77, v[48:49], off nt
	v_add_u32_e32 v48, 54, v50
	v_mad_i64_i32 v[48:49], s[50:51], v48, s45, v[28:29]
	global_load_dword v78, v[48:49], off nt
	v_add_u32_e32 v48, 56, v50
	v_mad_i64_i32 v[48:49], s[50:51], v48, s45, v[28:29]
	global_load_dword v79, v[48:49], off nt
	v_add_u32_e32 v48, 58, v50
	v_mad_i64_i32 v[48:49], s[50:51], v48, s45, v[28:29]
	global_load_dword v80, v[48:49], off nt
	v_add_u32_e32 v48, 60, v50
	v_mad_i64_i32 v[48:49], s[50:51], v48, s45, v[28:29]
	global_load_dword v48, v[48:49], off nt
	v_add_u32_e32 v49, 62, v50
	v_mad_i64_i32 v[28:29], s[50:51], v49, s45, v[28:29]
	global_load_dword v28, v[28:29], off nt
	s_waitcnt vmcnt(0)
; __device__ __forceinline__ unsigned cvt_pk4_fp8(float a, float b, float c, float d) { int w = 0; w = __builtin_amdgcn_cvt_pk_fp8_f32(a, b, w, false); w = __builtin_amdgcn_cvt_pk_fp8_f32(c, d, w, true); return (unsigned)w; }
; #define GAS __attribute__((address_space(1)))
; #define LAS __attribute__((address_space(3)))
; #define LDS_WAIT() asm volatile("s_waitcnt lgkmcnt(0)" ::: "memory")
; __device__ __forceinline__ void tr_item8(const float* W, int ld, int K, int nblk, int item, unsigned char* WT, bool gu, float scale, LAS float* scr, int lane) {
;     ...
; #pragma unroll
;       for (int i = 0; i < 32; ++i) scr[(2 * i + (lane >> 5)) * 33 + (lane & 31)] = t_[i] * scale; }
;     LDS_WAIT(); asm volatile("" ::: "memory");
;     const int c = lane & 3;
; #pragma unroll
;     for (int j = 0; j < 2; ++j) { const int n = (lane >> 2) + 16 * j; const LAS float* sp = scr + (16 * c) * 33 + n;
;         v4u o; o.x = pg8::cvt_pk4_fp8(sp[0 * 33], sp[1 * 33], sp[2 * 33], sp[3 * 33]); o.y = pg8::cvt_pk4_fp8(sp[4 * 33], sp[5 * 33], sp[6 * 33], sp[7 * 33]);
;         o.z = pg8::cvt_pk4_fp8(sp[8 * 33], sp[9 * 33], sp[10 * 33], sp[11 * 33]); o.w = pg8::cvt_pk4_fp8(sp[12 * 33], sp[13 * 33], sp[14 * 33], sp[15 * 33]);
;         *(GAS v4u*)(WT + (size_t)(drow0 + n) * K + k0 + 16 * c) = o; }
;     LDS_WAIT(); asm volatile("" ::: "memory");
	v_mul_f32_e32 v29, 0x42800000, v51
	v_mul_f32_e32 v49, 0x42800000, v52
	ds_write2_b32 v31, v29, v49 offset1:66
	v_mul_f32_e32 v29, 0x42800000, v53
	v_mul_f32_e32 v49, 0x42800000, v54
	ds_write2_b32 v31, v29, v49 offset0:132 offset1:198
	v_mul_f32_e32 v29, 0x42800000, v55
	v_mul_f32_e32 v49, 0x42800000, v56
	ds_write2_b32 v40, v29, v49 offset0:8 offset1:74
	v_mul_f32_e32 v29, 0x42800000, v57
	v_mul_f32_e32 v49, 0x42800000, v58
	ds_write2_b32 v40, v29, v49 offset0:140 offset1:206
	v_mul_f32_e32 v29, 0x42800000, v59
	v_mul_f32_e32 v49, 0x42800000, v60
	ds_write2_b32 v41, v29, v49 offset0:16 offset1:82
	v_mul_f32_e32 v29, 0x42800000, v61
	v_mul_f32_e32 v49, 0x42800000, v62
	ds_write2_b32 v41, v29, v49 offset0:148 offset1:214
	v_mul_f32_e32 v29, 0x42800000, v63
	v_mul_f32_e32 v49, 0x42800000, v64
	ds_write2_b32 v42, v29, v49 offset0:24 offset1:90
	v_mul_f32_e32 v29, 0x42800000, v65
	v_mul_f32_e32 v49, 0x42800000, v66
	ds_write2_b32 v42, v29, v49 offset0:156 offset1:222
	v_mul_f32_e32 v29, 0x42800000, v67
	v_mul_f32_e32 v49, 0x42800000, v68
	ds_write2_b32 v43, v29, v49 offset0:32 offset1:98
	v_mul_f32_e32 v29, 0x42800000, v69
	v_mov_b32_e32 v50, v1
	v_mov_b32_e32 v51, v1
	s_add_u32 s24, s24, s26
	v_mul_f32_e32 v49, 0x42800000, v70
	ds_write2_b32 v43, v29, v49 offset0:164 offset1:230
	v_add_u32_e32 v84, s16, v32
	s_addc_u32 s25, s25, 0
	v_mul_f32_e32 v29, 0x42800000, v71
	v_ashrrev_i32_e32 v85, 31, v84
	v_lshlrev_b64 v[84:85], 10, v[84:85]
	v_readlane_b32 s52, v254, 36
	v_mul_f32_e32 v49, 0x42800000, v72
	ds_write2_b32 v44, v29, v49 offset0:40 offset1:106
	v_readlane_b32 s58, v254, 42
	v_readlane_b32 s59, v254, 43
	v_mul_f32_e32 v29, 0x42800000, v73
	v_readlane_b32 s60, v254, 44
	v_readlane_b32 s61, v254, 45
	v_readlane_b32 s62, v254, 46
	v_mul_f32_e32 v49, 0x42800000, v74
	ds_write2_b32 v44, v29, v49 offset0:172 offset1:238
	v_readlane_b32 s63, v254, 47
	v_readlane_b32 s64, v254, 48
	v_mul_f32_e32 v29, 0x42800000, v75
	v_readlane_b32 s65, v254, 49
	v_readlane_b32 s66, v254, 50
	v_readlane_b32 s67, v254, 51
	v_mul_f32_e32 v49, 0x42800000, v76
	ds_write2_b32 v45, v29, v49 offset0:48 offset1:114
	s_mov_b64 s[58:59], s[62:63]
	s_mov_b64 s[60:61], s[64:65]
	v_mul_f32_e32 v29, 0x42800000, v77
	v_readlane_b32 s53, v254, 37
	v_readlane_b32 s54, v254, 38
	v_readlane_b32 s55, v254, 39
	v_mul_f32_e32 v49, 0x42800000, v78
	ds_write2_b32 v45, v29, v49 offset0:180 offset1:246
	v_readlane_b32 s56, v254, 40
	v_readlane_b32 s57, v254, 41
	v_mul_f32_e32 v29, 0x42800000, v79
	s_mov_b64 s[62:63], s[66:67]
	v_mul_f32_e32 v49, 0x42800000, v80
	ds_write2_b32 v46, v29, v49 offset0:56 offset1:122
	v_mov_b32_e32 v49, v1
	v_mul_f32_e32 v29, 0x42800000, v48
	v_mov_b32_e32 v48, v1
	v_mul_f32_e32 v28, 0x42800000, v28
	ds_write2_b32 v46, v29, v28 offset0:188 offset1:254
	s_waitcnt lgkmcnt(0)
	ds_read2_b32 v[52:53], v33 offset1:16
	ds_read2_b32 v[54:55], v33 offset0:33 offset1:49
	ds_read2_b32 v[56:57], v33 offset0:66 offset1:82
	ds_read2_b32 v[58:59], v33 offset0:99 offset1:115
	ds_read2_b32 v[60:61], v33 offset0:132 offset1:148
	ds_read2_b32 v[62:63], v33 offset0:165 offset1:181
	ds_read2_b32 v[64:65], v33 offset0:198 offset1:214
	ds_read2_b32 v[66:67], v33 offset0:231 offset1:247
	ds_read2_b32 v[68:69], v47 offset0:8 offset1:24
	ds_read2_b32 v[70:71], v47 offset0:41 offset1:57
	ds_read2_b32 v[72:73], v47 offset0:74 offset1:90
	ds_read2_b32 v[74:75], v47 offset0:107 offset1:123
	ds_read2_b32 v[76:77], v47 offset0:140 offset1:156
	ds_read2_b32 v[78:79], v47 offset0:173 offset1:189
	ds_read2_b32 v[80:81], v47 offset0:206 offset1:222
	ds_read2_b32 v[82:83], v47 offset0:239 offset1:255
	s_waitcnt lgkmcnt(14)
	v_cvt_pk_fp8_f32 v48, v52, v54
	s_waitcnt lgkmcnt(10)
	v_cvt_pk_fp8_f32 v49, v60, v62
	s_waitcnt lgkmcnt(6)
	v_cvt_pk_fp8_f32 v50, v68, v70
	s_waitcnt lgkmcnt(2)
	v_cvt_pk_fp8_f32 v51, v76, v78
	v_cvt_pk_fp8_f32 v48, v56, v58 op_sel:[0,0,1]
	v_cvt_pk_fp8_f32 v49, v64, v66 op_sel:[0,0,1]
	v_cvt_pk_fp8_f32 v50, v72, v74 op_sel:[0,0,1]
	s_waitcnt lgkmcnt(0)
	v_cvt_pk_fp8_f32 v51, v80, v82 op_sel:[0,0,1]
	v_lshl_add_u64 v[28:29], s[24:25], 0, v[2:3]
	v_lshl_add_u64 v[84:85], v[28:29], 0, v[84:85]
	v_add_u32_e32 v52, s16, v34
	global_store_dwordx4 v[84:85], v[48:51], off nt
	s_mov_b64 s[24:25], 0
	s_nop 0
	v_mov_b32_e32 v48, v1
	v_mov_b32_e32 v49, v1
	v_mov_b32_e32 v50, v1
	v_mov_b32_e32 v51, v1
	v_cvt_pk_fp8_f32 v48, v53, v55
	v_cvt_pk_fp8_f32 v49, v61, v63
	v_cvt_pk_fp8_f32 v50, v69, v71
	v_cvt_pk_fp8_f32 v51, v77, v79
	v_cvt_pk_fp8_f32 v48, v57, v59 op_sel:[0,0,1]
	v_cvt_pk_fp8_f32 v49, v65, v67 op_sel:[0,0,1]
	v_cvt_pk_fp8_f32 v50, v73, v75 op_sel:[0,0,1]
	v_cvt_pk_fp8_f32 v51, v81, v83 op_sel:[0,0,1]
	v_ashrrev_i32_e32 v53, 31, v52
	v_lshlrev_b64 v[52:53], 10, v[52:53]
	v_lshl_add_u64 v[28:29], v[28:29], 0, v[52:53]
	global_store_dwordx4 v[28:29], v[48:51], off nt
	s_waitcnt lgkmcnt(0)
; #define LAS __attribute__((address_space(3)))
; __device__ __forceinline__ void tr_item8(const float* W, int ld, int K, int nblk, int item, unsigned char* WT, bool gu, float scale, LAS float* scr, int lane) {
;     const int kb = item / nblk, nb = item % nblk, k0 = 64 * kb, n0 = 32 * nb;
;     int drow0 = n0;
;     if (gu) { const int bj = n0 / FF, j = n0 - bj * FF; drow0 = 256 * (j / 128) + 128 * bj + (j % 128); }
;     { float t_[32];
; #pragma unroll
;       for (int i = 0; i < 32; ++i) t_[i] = W[(size_t)(k0 + 2 * i + (lane >> 5)) * ld + n0 + (lane & 31)];
; __device__ __forceinline__ void convert_items(Frame& F, const Args& a, int lo, int hi, int w, int nw) {
;     ...
;         { const int e = r / I_DN, rr = r % I_DN; tr_item8(a.in[19] + (size_t)e * FF * D, D, FF, 32, rr, F.ws + WS_WMDN + (size_t)e * D * FF, false, WSC_DN, scr, lane); }
.LBB0_1139:
	s_andn2_b64 vcc, exec, s[24:25]
	s_cbranch_vccnz .LBB0_1141
	s_lshl_b32 s16, s37, 5
	s_and_b32 s24, s42, 0x1ffc0
	s_and_b32 s26, s16, 0x3e0
	v_add_u32_e32 v28, s24, v30
	s_lshl_b32 s16, s26, 2
	v_ashrrev_i32_e32 v29, 31, v28
	v_lshl_add_u64 v[48:49], v[4:5], 0, s[16:17]
	v_lshlrev_b64 v[28:29], 12, v[28:29]
	v_lshl_add_u64 v[28:29], v[48:49], 0, v[28:29]
	v_add_co_u32_e32 v48, vcc, 0x2000, v28
	global_load_dword v50, v[28:29], off nt
	s_nop 0
	v_addc_co_u32_e32 v49, vcc, 0, v29, vcc
	global_load_dword v51, v[48:49], off nt
	v_add_co_u32_e32 v48, vcc, 0x4000, v28
	s_mov_b32 s25, s17
	s_nop 0
	v_addc_co_u32_e32 v49, vcc, 0, v29, vcc
	global_load_dword v52, v[48:49], off nt
	v_add_co_u32_e32 v48, vcc, 0x6000, v28
	s_nop 1
	v_addc_co_u32_e32 v49, vcc, 0, v29, vcc
	global_load_dword v53, v[48:49], off nt
	v_add_co_u32_e32 v48, vcc, 0x8000, v28
	s_nop 1
	v_addc_co_u32_e32 v49, vcc, 0, v29, vcc
	global_load_dword v54, v[48:49], off nt
	v_add_co_u32_e32 v48, vcc, 0xa000, v28
	s_nop 1
	v_addc_co_u32_e32 v49, vcc, 0, v29, vcc
	global_load_dword v55, v[48:49], off nt
	v_add_co_u32_e32 v48, vcc, 0xc000, v28
	s_nop 1
	v_addc_co_u32_e32 v49, vcc, 0, v29, vcc
	global_load_dword v56, v[48:49], off nt
	v_add_co_u32_e32 v48, vcc, 0xe000, v28
	s_nop 1
	v_addc_co_u32_e32 v49, vcc, 0, v29, vcc
	global_load_dword v57, v[48:49], off nt
	v_add_co_u32_e32 v48, vcc, 0x10000, v28
	s_nop 1
	v_addc_co_u32_e32 v49, vcc, 0, v29, vcc
	global_load_dword v58, v[48:49], off nt
	v_add_co_u32_e32 v48, vcc, 0x12000, v28
	s_nop 1
	v_addc_co_u32_e32 v49, vcc, 0, v29, vcc
	global_load_dword v59, v[48:49], off nt
	v_add_co_u32_e32 v48, vcc, 0x14000, v28
	s_nop 1
	v_addc_co_u32_e32 v49, vcc, 0, v29, vcc
	global_load_dword v60, v[48:49], off nt
	v_add_co_u32_e32 v48, vcc, 0x16000, v28
	s_nop 1
	v_addc_co_u32_e32 v49, vcc, 0, v29, vcc
	global_load_dword v61, v[48:49], off nt
	v_add_co_u32_e32 v48, vcc, 0x18000, v28
	s_nop 1
	v_addc_co_u32_e32 v49, vcc, 0, v29, vcc
	global_load_dword v62, v[48:49], off nt
	v_add_co_u32_e32 v48, vcc, 0x1a000, v28
	s_nop 1
	v_addc_co_u32_e32 v49, vcc, 0, v29, vcc
	global_load_dword v63, v[48:49], off nt
	v_add_co_u32_e32 v48, vcc, 0x1c000, v28
	s_nop 1
	v_addc_co_u32_e32 v49, vcc, 0, v29, vcc
	global_load_dword v64, v[48:49], off nt
	v_add_co_u32_e32 v48, vcc, 0x1e000, v28
	s_nop 1
	v_addc_co_u32_e32 v49, vcc, 0, v29, vcc
	global_load_dword v65, v[48:49], off nt
	v_add_co_u32_e32 v48, vcc, 0x20000, v28
	s_nop 1
	v_addc_co_u32_e32 v49, vcc, 0, v29, vcc
	global_load_dword v66, v[48:49], off nt
	v_add_co_u32_e32 v48, vcc, 0x22000, v28
	s_nop 1
	v_addc_co_u32_e32 v49, vcc, 0, v29, vcc
	global_load_dword v67, v[48:49], off nt
	v_add_co_u32_e32 v48, vcc, 0x24000, v28
	s_nop 1
	v_addc_co_u32_e32 v49, vcc, 0, v29, vcc
	global_load_dword v68, v[48:49], off nt
	v_add_co_u32_e32 v48, vcc, 0x26000, v28
	s_nop 1
	v_addc_co_u32_e32 v49, vcc, 0, v29, vcc
	global_load_dword v69, v[48:49], off nt
	v_add_co_u32_e32 v48, vcc, 0x28000, v28
	s_nop 1
	v_addc_co_u32_e32 v49, vcc, 0, v29, vcc
	global_load_dword v70, v[48:49], off nt
	v_add_co_u32_e32 v48, vcc, 0x2a000, v28
	s_nop 1
	v_addc_co_u32_e32 v49, vcc, 0, v29, vcc
	global_load_dword v71, v[48:49], off nt
	v_add_co_u32_e32 v48, vcc, 0x2c000, v28
	s_nop 1
	v_addc_co_u32_e32 v49, vcc, 0, v29, vcc
	global_load_dword v72, v[48:49], off nt
	v_add_co_u32_e32 v48, vcc, 0x2e000, v28
	s_nop 1
	v_addc_co_u32_e32 v49, vcc, 0, v29, vcc
	global_load_dword v73, v[48:49], off nt
	v_add_co_u32_e32 v48, vcc, 0x30000, v28
	s_nop 1
	v_addc_co_u32_e32 v49, vcc, 0, v29, vcc
	global_load_dword v74, v[48:49], off nt
	v_add_co_u32_e32 v48, vcc, 0x32000, v28
	s_nop 1
	v_addc_co_u32_e32 v49, vcc, 0, v29, vcc
	global_load_dword v75, v[48:49], off nt
	v_add_co_u32_e32 v48, vcc, 0x34000, v28
	s_nop 1
	v_addc_co_u32_e32 v49, vcc, 0, v29, vcc
	global_load_dword v76, v[48:49], off nt
	v_add_co_u32_e32 v48, vcc, 0x36000, v28
	s_nop 1
	v_addc_co_u32_e32 v49, vcc, 0, v29, vcc
	global_load_dword v77, v[48:49], off nt
	v_add_co_u32_e32 v48, vcc, 0x38000, v28
	s_nop 1
	v_addc_co_u32_e32 v49, vcc, 0, v29, vcc
	global_load_dword v78, v[48:49], off nt
	v_add_co_u32_e32 v48, vcc, 0x3a000, v28
	s_nop 1
	v_addc_co_u32_e32 v49, vcc, 0, v29, vcc
	global_load_dword v79, v[48:49], off nt
	v_add_co_u32_e32 v48, vcc, 0x3c000, v28
	s_nop 1
	v_addc_co_u32_e32 v49, vcc, 0, v29, vcc
	v_add_co_u32_e32 v28, vcc, 0x3e000, v28
	global_load_dword v48, v[48:49], off nt
	s_nop 0
	v_addc_co_u32_e32 v29, vcc, 0, v29, vcc
	global_load_dword v28, v[28:29], off nt
	s_waitcnt vmcnt(0)
; __device__ __forceinline__ unsigned cvt_pk4_fp8(float a, float b, float c, float d) { int w = 0; w = __builtin_amdgcn_cvt_pk_fp8_f32(a, b, w, false); w = __builtin_amdgcn_cvt_pk_fp8_f32(c, d, w, true); return (unsigned)w; }
; #define GAS __attribute__((address_space(1)))
; #define LAS __attribute__((address_space(3)))
; #define LDS_WAIT() asm volatile("s_waitcnt lgkmcnt(0)" ::: "memory")
; __device__ __forceinline__ void tr_item8(const float* W, int ld, int K, int nblk, int item, unsigned char* WT, bool gu, float scale, LAS float* scr, int lane) {
;     ...
; #pragma unroll
;       for (int i = 0; i < 32; ++i) scr[(2 * i + (lane >> 5)) * 33 + (lane & 31)] = t_[i] * scale; }
;     LDS_WAIT(); asm volatile("" ::: "memory");
;     const int c = lane & 3;
; #pragma unroll
;     for (int j = 0; j < 2; ++j) { const int n = (lane >> 2) + 16 * j; const LAS float* sp = scr + (16 * c) * 33 + n;
;         v4u o; o.x = pg8::cvt_pk4_fp8(sp[0 * 33], sp[1 * 33], sp[2 * 33], sp[3 * 33]); o.y = pg8::cvt_pk4_fp8(sp[4 * 33], sp[5 * 33], sp[6 * 33], sp[7 * 33]);
;         o.z = pg8::cvt_pk4_fp8(sp[8 * 33], sp[9 * 33], sp[10 * 33], sp[11 * 33]); o.w = pg8::cvt_pk4_fp8(sp[12 * 33], sp[13 * 33], sp[14 * 33], sp[15 * 33]);
;         *(GAS v4u*)(WT + (size_t)(drow0 + n) * K + k0 + 16 * c) = o; }
;     LDS_WAIT(); asm volatile("" ::: "memory");
	v_mul_f32_e32 v29, 0x43000000, v50
	v_mul_f32_e32 v49, 0x43000000, v51
	ds_write2_b32 v31, v29, v49 offset1:66
	v_mul_f32_e32 v29, 0x43000000, v52
	v_mul_f32_e32 v49, 0x43000000, v53
	ds_write2_b32 v31, v29, v49 offset0:132 offset1:198
	v_mul_f32_e32 v29, 0x43000000, v54
	v_mul_f32_e32 v49, 0x43000000, v55
	ds_write2_b32 v40, v29, v49 offset0:8 offset1:74
	v_mul_f32_e32 v29, 0x43000000, v56
	v_mul_f32_e32 v49, 0x43000000, v57
	ds_write2_b32 v40, v29, v49 offset0:140 offset1:206
	v_mul_f32_e32 v29, 0x43000000, v58
	v_mul_f32_e32 v49, 0x43000000, v59
	ds_write2_b32 v41, v29, v49 offset0:16 offset1:82
	v_mul_f32_e32 v29, 0x43000000, v60
	v_mul_f32_e32 v49, 0x43000000, v61
	ds_write2_b32 v41, v29, v49 offset0:148 offset1:214
	v_mul_f32_e32 v29, 0x43000000, v62
	v_mul_f32_e32 v49, 0x43000000, v63
	ds_write2_b32 v42, v29, v49 offset0:24 offset1:90
	v_mul_f32_e32 v29, 0x43000000, v64
	v_mul_f32_e32 v49, 0x43000000, v65
	ds_write2_b32 v42, v29, v49 offset0:156 offset1:222
	v_mul_f32_e32 v29, 0x43000000, v66
	v_mul_f32_e32 v49, 0x43000000, v67
	ds_write2_b32 v43, v29, v49 offset0:32 offset1:98
	v_mul_f32_e32 v29, 0x43000000, v68
	v_mul_f32_e32 v49, 0x43000000, v69
	ds_write2_b32 v43, v29, v49 offset0:164 offset1:230
	v_mul_f32_e32 v29, 0x43000000, v70
	v_mul_f32_e32 v49, 0x43000000, v71
	ds_write2_b32 v44, v29, v49 offset0:40 offset1:106
	v_mul_f32_e32 v29, 0x43000000, v72
	v_mul_f32_e32 v49, 0x43000000, v73
	ds_write2_b32 v44, v29, v49 offset0:172 offset1:238
	v_mov_b32_e32 v50, 0
	v_mov_b32_e32 v51, 0
	v_mul_f32_e32 v29, 0x43000000, v74
	v_mul_f32_e32 v49, 0x43000000, v75
	ds_write2_b32 v45, v29, v49 offset0:48 offset1:114
	v_mul_f32_e32 v29, 0x43000000, v76
	v_mul_f32_e32 v49, 0x43000000, v77
	ds_write2_b32 v45, v29, v49 offset0:180 offset1:246
	v_mul_f32_e32 v29, 0x43000000, v78
	v_mul_f32_e32 v49, 0x43000000, v79
	ds_write2_b32 v46, v29, v49 offset0:56 offset1:122
	v_mov_b32_e32 v49, 0
	v_mul_f32_e32 v29, 0x43000000, v48
	v_mov_b32_e32 v48, 0
	v_mul_f32_e32 v28, 0x43000000, v28
	ds_write2_b32 v46, v29, v28 offset0:188 offset1:254
	s_waitcnt lgkmcnt(0)
	ds_read2_b32 v[52:53], v33 offset1:16
	ds_read2_b32 v[54:55], v33 offset0:33 offset1:49
	ds_read2_b32 v[56:57], v33 offset0:66 offset1:82
	ds_read2_b32 v[58:59], v33 offset0:99 offset1:115
	ds_read2_b32 v[60:61], v33 offset0:132 offset1:148
	ds_read2_b32 v[62:63], v33 offset0:165 offset1:181
	ds_read2_b32 v[64:65], v33 offset0:198 offset1:214
	ds_read2_b32 v[66:67], v33 offset0:231 offset1:247
	ds_read2_b32 v[68:69], v47 offset0:8 offset1:24
	ds_read2_b32 v[70:71], v47 offset0:41 offset1:57
	ds_read2_b32 v[72:73], v47 offset0:74 offset1:90
	ds_read2_b32 v[74:75], v47 offset0:107 offset1:123
	ds_read2_b32 v[76:77], v47 offset0:140 offset1:156
	ds_read2_b32 v[78:79], v47 offset0:173 offset1:189
	ds_read2_b32 v[80:81], v47 offset0:206 offset1:222
	ds_read2_b32 v[82:83], v47 offset0:239 offset1:255
	s_waitcnt lgkmcnt(14)
	v_cvt_pk_fp8_f32 v48, v52, v54
	s_waitcnt lgkmcnt(10)
	v_cvt_pk_fp8_f32 v49, v60, v62
	s_waitcnt lgkmcnt(6)
	v_cvt_pk_fp8_f32 v50, v68, v70
	s_waitcnt lgkmcnt(2)
	v_cvt_pk_fp8_f32 v51, v76, v78
	v_cvt_pk_fp8_f32 v48, v56, v58 op_sel:[0,0,1]
	v_cvt_pk_fp8_f32 v49, v64, v66 op_sel:[0,0,1]
	v_cvt_pk_fp8_f32 v50, v72, v74 op_sel:[0,0,1]
	s_waitcnt lgkmcnt(0)
	v_cvt_pk_fp8_f32 v51, v80, v82 op_sel:[0,0,1]
	v_lshl_add_u64 v[28:29], v[18:19], 0, s[24:25]
	v_add_u32_e32 v52, s26, v32
	v_mad_i64_i32 v[84:85], s[24:25], v52, s44, v[28:29]
	global_store_dwordx4 v[84:85], v[48:51], off nt
	v_add_u32_e32 v52, s26, v34
	v_mad_i64_i32 v[28:29], s[24:25], v52, s44, v[28:29]
	v_mov_b32_e32 v48, 0
	v_mov_b32_e32 v49, 0
	v_mov_b32_e32 v50, 0
	v_mov_b32_e32 v51, 0
	v_cvt_pk_fp8_f32 v48, v53, v55
	v_cvt_pk_fp8_f32 v49, v61, v63
	v_cvt_pk_fp8_f32 v50, v69, v71
	v_cvt_pk_fp8_f32 v51, v77, v79
	v_cvt_pk_fp8_f32 v48, v57, v59 op_sel:[0,0,1]
	v_cvt_pk_fp8_f32 v49, v65, v67 op_sel:[0,0,1]
	v_cvt_pk_fp8_f32 v50, v73, v75 op_sel:[0,0,1]
	v_cvt_pk_fp8_f32 v51, v81, v83 op_sel:[0,0,1]
	global_store_dwordx4 v[28:29], v[48:51], off nt
	s_waitcnt lgkmcnt(0)

; __device__ __forceinline__ void tr_item8(const float* W, int ld, int K, int nblk, int item, unsigned char* WT, bool gu, float scale, LAS float* scr, int lane) {
;     const int kb = item / nblk, nb = item % nblk, k0 = 64 * kb, n0 = 32 * nb;
;     int drow0 = n0;
;     if (gu) { const int bj = n0 / FF, j = n0 - bj * FF; drow0 = 256 * (j / 128) + 128 * bj + (j % 128); }
;     { float t_[32];
; #pragma unroll
;       for (int i = 0; i < 32; ++i) t_[i] = W[(size_t)(k0 + 2 * i + (lane >> 5)) * ld + n0 + (lane & 31)];
; __device__ __forceinline__ void convert_items(Frame& F, const Args& a, int lo, int hi, int w, int nw) {
;     ...
;         if (r < I_GU) { tr_item8(a.in[14], 2 * FF, D, 224, r, F.ws + WS_WGU, true, WSC_GU, scr, lane); continue; } r -= I_GU;
.LBB0_1142:
	s_andn2_b64 vcc, exec, s[24:25]
	s_cbranch_vccnz .LBB0_1144
	s_add_i32 s16, s37, 0xf300
	s_bfe_u32 s24, s16, 0xb0005
	s_mulk_i32 s24, 0x2493
	s_lshr_b32 s24, s24, 16
	s_mul_i32 s25, s24, 0xe0
	s_sub_i32 s16, s16, s25
	s_lshl_b32 s25, s16, 5
	s_and_b32 s26, s16, 0xffff
	s_cmpk_gt_u32 s26, 0x6f
	s_cselect_b32 s50, 0xfffff200, 0
	s_cselect_b32 s51, 0x80, 0
	s_lshl_b32 s16, s16, 7
	s_lshl_b32 s24, s24, 6
	s_and_b32 s16, s16, 0x3ff80
	v_add_u32_e32 v64, s24, v30
	v_lshl_add_u64 v[28:29], v[6:7], 0, s[16:17]
	v_mad_i64_i32 v[48:49], s[26:27], v64, s45, v[28:29]
	v_add_u32_e32 v50, 2, v64
	v_add_u32_e32 v52, 4, v64
	v_add_u32_e32 v54, 6, v64
	v_add_u32_e32 v56, 8, v64
	v_add_u32_e32 v58, 10, v64
	v_add_u32_e32 v60, 12, v64
	v_add_u32_e32 v62, 14, v64
	v_mad_i64_i32 v[50:51], s[26:27], v50, s45, v[28:29]
	v_mad_i64_i32 v[52:53], s[26:27], v52, s45, v[28:29]
	v_mad_i64_i32 v[54:55], s[26:27], v54, s45, v[28:29]
	v_mad_i64_i32 v[56:57], s[26:27], v56, s45, v[28:29]
	v_mad_i64_i32 v[58:59], s[26:27], v58, s45, v[28:29]
	v_mad_i64_i32 v[60:61], s[26:27], v60, s45, v[28:29]
	v_mad_i64_i32 v[62:63], s[26:27], v62, s45, v[28:29]
	global_load_dword v65, v[48:49], off nt
	global_load_dword v66, v[50:51], off nt
	global_load_dword v67, v[52:53], off nt
	global_load_dword v68, v[54:55], off nt
	global_load_dword v69, v[56:57], off nt
	global_load_dword v70, v[58:59], off nt
	global_load_dword v71, v[60:61], off nt
	global_load_dword v72, v[62:63], off nt
	v_add_u32_e32 v48, 16, v64
	v_mad_i64_i32 v[48:49], s[26:27], v48, s45, v[28:29]
	v_add_u32_e32 v50, 18, v64
	v_add_u32_e32 v52, 20, v64
	v_add_u32_e32 v54, 22, v64
	v_add_u32_e32 v56, 24, v64
	v_add_u32_e32 v58, 26, v64
	v_add_u32_e32 v60, 28, v64
	v_add_u32_e32 v62, 30, v64
	v_mad_i64_i32 v[50:51], s[26:27], v50, s45, v[28:29]
	v_mad_i64_i32 v[52:53], s[26:27], v52, s45, v[28:29]
	v_mad_i64_i32 v[54:55], s[26:27], v54, s45, v[28:29]
	v_mad_i64_i32 v[56:57], s[26:27], v56, s45, v[28:29]
	v_mad_i64_i32 v[58:59], s[26:27], v58, s45, v[28:29]
	v_mad_i64_i32 v[60:61], s[26:27], v60, s45, v[28:29]
	v_mad_i64_i32 v[62:63], s[26:27], v62, s45, v[28:29]
	global_load_dword v73, v[48:49], off nt
	global_load_dword v74, v[50:51], off nt
	global_load_dword v75, v[52:53], off nt
	global_load_dword v76, v[54:55], off nt
	global_load_dword v77, v[56:57], off nt
	global_load_dword v78, v[58:59], off nt
	global_load_dword v79, v[60:61], off nt
	global_load_dword v80, v[62:63], off nt
	v_add_u32_e32 v48, 32, v64
	v_add_u32_e32 v50, 34, v64
	v_add_u32_e32 v52, 36, v64
	v_add_u32_e32 v54, 38, v64
	v_add_u32_e32 v60, 44, v64
	v_mad_i64_i32 v[48:49], s[26:27], v48, s45, v[28:29]
	v_mad_i64_i32 v[50:51], s[26:27], v50, s45, v[28:29]
	v_mad_i64_i32 v[52:53], s[26:27], v52, s45, v[28:29]
	v_mad_i64_i32 v[54:55], s[26:27], v54, s45, v[28:29]
	v_add_u32_e32 v56, 40, v64
	v_add_u32_e32 v58, 42, v64
	v_mad_i64_i32 v[60:61], s[26:27], v60, s45, v[28:29]
	v_add_u32_e32 v62, 46, v64
	v_mad_i64_i32 v[56:57], s[26:27], v56, s45, v[28:29]
	v_mad_i64_i32 v[58:59], s[26:27], v58, s45, v[28:29]
	v_mad_i64_i32 v[62:63], s[26:27], v62, s45, v[28:29]
	global_load_dword v81, v[48:49], off nt
	global_load_dword v82, v[50:51], off nt
	global_load_dword v83, v[52:53], off nt
	global_load_dword v84, v[54:55], off nt
	global_load_dword v85, v[56:57], off nt
	global_load_dword v86, v[58:59], off nt
	s_nop 0
	global_load_dword v60, v[60:61], off nt
	s_nop 0
	global_load_dword v61, v[62:63], off nt
	v_add_u32_e32 v48, 48, v64
	v_add_u32_e32 v50, 50, v64
	v_add_u32_e32 v52, 52, v64
	v_add_u32_e32 v54, 54, v64
	v_mad_i64_i32 v[48:49], s[26:27], v48, s45, v[28:29]
	v_mad_i64_i32 v[50:51], s[26:27], v50, s45, v[28:29]
	v_mad_i64_i32 v[52:53], s[26:27], v52, s45, v[28:29]
	v_mad_i64_i32 v[54:55], s[26:27], v54, s45, v[28:29]
	v_add_u32_e32 v56, 56, v64
	v_add_u32_e32 v58, 58, v64
	v_mad_i64_i32 v[56:57], s[26:27], v56, s45, v[28:29]
	v_mad_i64_i32 v[58:59], s[26:27], v58, s45, v[28:29]
	global_load_dword v62, v[48:49], off nt
	s_nop 0
	global_load_dword v50, v[50:51], off nt
	s_nop 0
	global_load_dword v51, v[52:53], off nt
	s_nop 0
	global_load_dword v52, v[54:55], off nt
	global_load_dword v53, v[56:57], off nt
	s_nop 0
	global_load_dword v54, v[58:59], off nt
	v_add_u32_e32 v48, 60, v64
	v_add_u32_e32 v55, 62, v64
	v_mad_i64_i32 v[48:49], s[26:27], v48, s45, v[28:29]
	v_mad_i64_i32 v[28:29], s[26:27], v55, s45, v[28:29]
	global_load_dword v48, v[48:49], off nt
	s_nop 0
	global_load_dword v28, v[28:29], off nt
	s_waitcnt vmcnt(0)
; __device__ __forceinline__ unsigned cvt_pk4_fp8(float a, float b, float c, float d) { int w = 0; w = __builtin_amdgcn_cvt_pk_fp8_f32(a, b, w, false); w = __builtin_amdgcn_cvt_pk_fp8_f32(c, d, w, true); return (unsigned)w; }
; #define GAS __attribute__((address_space(1)))
; #define LAS __attribute__((address_space(3)))
; #define LDS_WAIT() asm volatile("s_waitcnt lgkmcnt(0)" ::: "memory")
; __device__ __forceinline__ void tr_item8(const float* W, int ld, int K, int nblk, int item, unsigned char* WT, bool gu, float scale, LAS float* scr, int lane) {
;     ...
; #pragma unroll
;       for (int i = 0; i < 32; ++i) scr[(2 * i + (lane >> 5)) * 33 + (lane & 31)] = t_[i] * scale; }
;     LDS_WAIT(); asm volatile("" ::: "memory");
;     const int c = lane & 3;
; #pragma unroll
;     for (int j = 0; j < 2; ++j) { const int n = (lane >> 2) + 16 * j; const LAS float* sp = scr + (16 * c) * 33 + n;
;         v4u o; o.x = pg8::cvt_pk4_fp8(sp[0 * 33], sp[1 * 33], sp[2 * 33], sp[3 * 33]); o.y = pg8::cvt_pk4_fp8(sp[4 * 33], sp[5 * 33], sp[6 * 33], sp[7 * 33]);
;         o.z = pg8::cvt_pk4_fp8(sp[8 * 33], sp[9 * 33], sp[10 * 33], sp[11 * 33]); o.w = pg8::cvt_pk4_fp8(sp[12 * 33], sp[13 * 33], sp[14 * 33], sp[15 * 33]);
;         *(GAS v4u*)(WT + (size_t)(drow0 + n) * K + k0 + 16 * c) = o; }
;     LDS_WAIT(); asm volatile("" ::: "memory");
	v_mul_f32_e32 v29, 0x42800000, v65
	v_mul_f32_e32 v49, 0x42800000, v66
	ds_write2_b32 v31, v29, v49 offset1:66
	v_mul_f32_e32 v29, 0x42800000, v67
	v_mul_f32_e32 v49, 0x42800000, v68
	ds_write2_b32 v31, v29, v49 offset0:132 offset1:198
	v_mul_f32_e32 v29, 0x42800000, v69
	v_mul_f32_e32 v49, 0x42800000, v70
	ds_write2_b32 v40, v29, v49 offset0:8 offset1:74
	v_mul_f32_e32 v29, 0x42800000, v71
	v_mul_f32_e32 v49, 0x42800000, v72
	ds_write2_b32 v40, v29, v49 offset0:140 offset1:206
	s_add_i32 s16, s50, s25
	s_sext_i32_i16 s25, s16
	s_bfe_u32 s25, s25, 0x70018
	s_add_i32 s25, s16, s25
	s_sext_i32_i16 s26, s25
	s_and_b32 s25, s25, 0xff80
	s_sub_i32 s16, s16, s25
	s_lshl_b32 s26, s26, 1
	s_sext_i32_i16 s16, s16
	v_mul_f32_e32 v29, 0x42800000, v73
	v_mul_f32_e32 v49, 0x42800000, v74
	ds_write2_b32 v41, v29, v49 offset0:16 offset1:82
	v_mul_f32_e32 v29, 0x42800000, v75
	v_mul_f32_e32 v49, 0x42800000, v76
	ds_write2_b32 v41, v29, v49 offset0:148 offset1:214
	v_mul_f32_e32 v29, 0x42800000, v77
	v_mul_f32_e32 v49, 0x42800000, v78
	ds_write2_b32 v42, v29, v49 offset0:24 offset1:90
	v_mul_f32_e32 v29, 0x42800000, v79
	v_mul_f32_e32 v49, 0x42800000, v80
	ds_write2_b32 v42, v29, v49 offset0:156 offset1:222
	s_and_b32 s26, s26, 0xffffff00
	s_add_i32 s16, s51, s16
	s_add_i32 s16, s16, s26
	s_mov_b32 s25, s17
	v_mul_f32_e32 v29, 0x42800000, v81
	v_mul_f32_e32 v49, 0x42800000, v82
	ds_write2_b32 v43, v29, v49 offset0:32 offset1:98
	v_mul_f32_e32 v29, 0x42800000, v83
	v_mul_f32_e32 v49, 0x42800000, v84
	ds_write2_b32 v43, v29, v49 offset0:164 offset1:230
	v_mul_f32_e32 v29, 0x42800000, v85
	v_mul_f32_e32 v49, 0x42800000, v86
	ds_write2_b32 v44, v29, v49 offset0:40 offset1:106
	v_mul_f32_e32 v29, 0x42800000, v60
	v_mul_f32_e32 v49, 0x42800000, v61
	ds_write2_b32 v44, v29, v49 offset0:172 offset1:238
	v_add_u32_e32 v84, s16, v32
	v_ashrrev_i32_e32 v85, 31, v84
	v_lshlrev_b64 v[84:85], 10, v[84:85]
	v_mul_f32_e32 v29, 0x42800000, v62
	v_mul_f32_e32 v49, 0x42800000, v50
	ds_write2_b32 v45, v29, v49 offset0:48 offset1:114
	v_mul_f32_e32 v29, 0x42800000, v51
	v_mul_f32_e32 v49, 0x42800000, v52
	ds_write2_b32 v45, v29, v49 offset0:180 offset1:246
	v_mul_f32_e32 v29, 0x42800000, v53
	v_mul_f32_e32 v49, 0x42800000, v54
	ds_write2_b32 v46, v29, v49 offset0:56 offset1:122
	v_mov_b32_e32 v49, 0
	v_mov_b32_e32 v50, 0
	v_mul_f32_e32 v29, 0x42800000, v48
	v_mul_f32_e32 v28, 0x42800000, v28
	ds_write2_b32 v46, v29, v28 offset0:188 offset1:254
	s_waitcnt lgkmcnt(0)
	ds_read2_b32 v[52:53], v33 offset1:16
	ds_read2_b32 v[54:55], v33 offset0:33 offset1:49
	ds_read2_b32 v[56:57], v33 offset0:66 offset1:82
	ds_read2_b32 v[58:59], v33 offset0:99 offset1:115
	ds_read2_b32 v[60:61], v33 offset0:132 offset1:148
	ds_read2_b32 v[62:63], v33 offset0:165 offset1:181
	ds_read2_b32 v[64:65], v33 offset0:198 offset1:214
	ds_read2_b32 v[66:67], v33 offset0:231 offset1:247
	ds_read2_b32 v[68:69], v47 offset0:8 offset1:24
	ds_read2_b32 v[70:71], v47 offset0:41 offset1:57
	ds_read2_b32 v[72:73], v47 offset0:74 offset1:90
	ds_read2_b32 v[74:75], v47 offset0:107 offset1:123
	ds_read2_b32 v[76:77], v47 offset0:140 offset1:156
	ds_read2_b32 v[78:79], v47 offset0:173 offset1:189
	v_mov_b32_e32 v48, 0
	ds_read2_b32 v[80:81], v47 offset0:206 offset1:222
	ds_read2_b32 v[82:83], v47 offset0:239 offset1:255
	v_mov_b32_e32 v51, 0
	s_waitcnt lgkmcnt(14)
	v_cvt_pk_fp8_f32 v48, v52, v54
	s_waitcnt lgkmcnt(10)
	v_cvt_pk_fp8_f32 v49, v60, v62
	s_waitcnt lgkmcnt(6)
	v_cvt_pk_fp8_f32 v50, v68, v70
	s_waitcnt lgkmcnt(2)
	v_cvt_pk_fp8_f32 v51, v76, v78
	v_cvt_pk_fp8_f32 v48, v56, v58 op_sel:[0,0,1]
	v_cvt_pk_fp8_f32 v49, v64, v66 op_sel:[0,0,1]
	v_cvt_pk_fp8_f32 v50, v72, v74 op_sel:[0,0,1]
	s_waitcnt lgkmcnt(0)
	v_cvt_pk_fp8_f32 v51, v80, v82 op_sel:[0,0,1]
	v_lshl_add_u64 v[28:29], v[20:21], 0, s[24:25]
	v_lshl_add_u64 v[84:85], v[28:29], 0, v[84:85]
	v_add_u32_e32 v52, s16, v34
	global_store_dwordx4 v[84:85], v[48:51], off nt
	s_nop 1
	v_mov_b32_e32 v48, 0
	v_mov_b32_e32 v49, 0
	v_mov_b32_e32 v50, 0
	v_mov_b32_e32 v51, 0
	v_cvt_pk_fp8_f32 v48, v53, v55
	v_cvt_pk_fp8_f32 v49, v61, v63
	v_cvt_pk_fp8_f32 v50, v69, v71
	v_cvt_pk_fp8_f32 v51, v77, v79
	v_cvt_pk_fp8_f32 v48, v57, v59 op_sel:[0,0,1]
	v_cvt_pk_fp8_f32 v49, v65, v67 op_sel:[0,0,1]
	v_cvt_pk_fp8_f32 v50, v73, v75 op_sel:[0,0,1]
	v_cvt_pk_fp8_f32 v51, v81, v83 op_sel:[0,0,1]
	v_ashrrev_i32_e32 v53, 31, v52
	v_lshlrev_b64 v[52:53], 10, v[52:53]
	v_lshl_add_u64 v[28:29], v[28:29], 0, v[52:53]
	global_store_dwordx4 v[28:29], v[48:51], off nt
	s_waitcnt lgkmcnt(0)

; __device__ __forceinline__ void tr_item(const float* W, int ld, int K, int nblk, int item, bf16* WT, bool gu, LAS float* scr, int lane) {
;     const int kb = item / nblk, nb = item % nblk, k0 = 64 * kb, n0 = 32 * nb;
;     int drow0 = n0;
;     if (gu) { const int bj = n0 / FF, j = n0 - bj * FF; drow0 = 256 * (j / 128) + 128 * bj + (j % 128); }
;     { float t_[32];
; #pragma unroll
;       for (int i = 0; i < 32; ++i) t_[i] = W[(size_t)(k0 + 2 * i + (lane >> 5)) * ld + n0 + (lane & 31)];
; __device__ __forceinline__ void convert_items(Frame& F, const Args& a, int lo, int hi, int w, int nw) {
;     ...
;         if (r < I_SO) { tr_item(a.in[12], D, D, 32, r, (bf16*)(F.ws + WS_WSWAOUT), false, scr, lane); continue; } r -= I_SO;
.LBB0_1145:
	s_andn2_b64 vcc, exec, s[24:25]
	s_cbranch_vccnz .LBB0_1147
	s_add_i32 s16, s42, 0x2000
	s_and_b32 s25, s16, 0x1ffc0
	s_and_b32 s24, s40, 0x3e0
	v_add_u32_e32 v28, s25, v30
	s_lshl_b32 s16, s24, 2
	v_ashrrev_i32_e32 v29, 31, v28
	v_lshl_add_u64 v[48:49], v[8:9], 0, s[16:17]
	v_lshlrev_b64 v[28:29], 12, v[28:29]
	v_lshl_add_u64 v[28:29], v[48:49], 0, v[28:29]
	v_add_co_u32_e32 v48, vcc, 0x2000, v28
	global_load_dword v50, v[28:29], off nt
	s_nop 0
	v_addc_co_u32_e32 v49, vcc, 0, v29, vcc
	global_load_dword v51, v[48:49], off nt
	v_add_co_u32_e32 v48, vcc, 0x4000, v28
	s_lshl_b32 s16, s25, 1
	s_nop 0
	v_addc_co_u32_e32 v49, vcc, 0, v29, vcc
	global_load_dword v52, v[48:49], off nt
	v_add_co_u32_e32 v48, vcc, 0x6000, v28
	s_nop 1
	v_addc_co_u32_e32 v49, vcc, 0, v29, vcc
	global_load_dword v53, v[48:49], off nt
	v_add_co_u32_e32 v48, vcc, 0x8000, v28
	s_nop 1
	v_addc_co_u32_e32 v49, vcc, 0, v29, vcc
	global_load_dword v54, v[48:49], off nt
	v_add_co_u32_e32 v48, vcc, 0xa000, v28
	s_nop 1
	v_addc_co_u32_e32 v49, vcc, 0, v29, vcc
	global_load_dword v55, v[48:49], off nt
	v_add_co_u32_e32 v48, vcc, 0xc000, v28
	s_nop 1
	v_addc_co_u32_e32 v49, vcc, 0, v29, vcc
	global_load_dword v56, v[48:49], off nt
	v_add_co_u32_e32 v48, vcc, 0xe000, v28
	s_nop 1
	v_addc_co_u32_e32 v49, vcc, 0, v29, vcc
	global_load_dword v57, v[48:49], off nt
	v_add_co_u32_e32 v48, vcc, 0x10000, v28
	s_nop 1
	v_addc_co_u32_e32 v49, vcc, 0, v29, vcc
	global_load_dword v58, v[48:49], off nt
	v_add_co_u32_e32 v48, vcc, 0x12000, v28
	s_nop 1
	v_addc_co_u32_e32 v49, vcc, 0, v29, vcc
	global_load_dword v59, v[48:49], off nt
	v_add_co_u32_e32 v48, vcc, 0x14000, v28
	s_nop 1
	v_addc_co_u32_e32 v49, vcc, 0, v29, vcc
	global_load_dword v60, v[48:49], off nt
	v_add_co_u32_e32 v48, vcc, 0x16000, v28
	s_nop 1
	v_addc_co_u32_e32 v49, vcc, 0, v29, vcc
	global_load_dword v61, v[48:49], off nt
	v_add_co_u32_e32 v48, vcc, 0x18000, v28
	s_nop 1
	v_addc_co_u32_e32 v49, vcc, 0, v29, vcc
	global_load_dword v62, v[48:49], off nt
	v_add_co_u32_e32 v48, vcc, 0x1a000, v28
	s_nop 1
	v_addc_co_u32_e32 v49, vcc, 0, v29, vcc
	global_load_dword v63, v[48:49], off nt
	v_add_co_u32_e32 v48, vcc, 0x1c000, v28
	s_nop 1
	v_addc_co_u32_e32 v49, vcc, 0, v29, vcc
	global_load_dword v64, v[48:49], off nt
	v_add_co_u32_e32 v48, vcc, 0x1e000, v28
	s_nop 1
	v_addc_co_u32_e32 v49, vcc, 0, v29, vcc
	global_load_dword v65, v[48:49], off nt
	v_add_co_u32_e32 v48, vcc, 0x20000, v28
	s_nop 1
	v_addc_co_u32_e32 v49, vcc, 0, v29, vcc
	global_load_dword v66, v[48:49], off nt
	v_add_co_u32_e32 v48, vcc, 0x22000, v28
	s_nop 1
	v_addc_co_u32_e32 v49, vcc, 0, v29, vcc
	global_load_dword v67, v[48:49], off nt
	v_add_co_u32_e32 v48, vcc, 0x24000, v28
	s_nop 1
	v_addc_co_u32_e32 v49, vcc, 0, v29, vcc
	global_load_dword v68, v[48:49], off nt
	v_add_co_u32_e32 v48, vcc, 0x26000, v28
	s_nop 1
	v_addc_co_u32_e32 v49, vcc, 0, v29, vcc
	global_load_dword v69, v[48:49], off nt
	v_add_co_u32_e32 v48, vcc, 0x28000, v28
	s_nop 1
	v_addc_co_u32_e32 v49, vcc, 0, v29, vcc
	global_load_dword v70, v[48:49], off nt
	v_add_co_u32_e32 v48, vcc, 0x2a000, v28
	s_nop 1
	v_addc_co_u32_e32 v49, vcc, 0, v29, vcc
	global_load_dword v71, v[48:49], off nt
	v_add_co_u32_e32 v48, vcc, 0x2c000, v28
	s_nop 1
	v_addc_co_u32_e32 v49, vcc, 0, v29, vcc
	global_load_dword v72, v[48:49], off nt
	v_add_co_u32_e32 v48, vcc, 0x2e000, v28
	s_nop 1
	v_addc_co_u32_e32 v49, vcc, 0, v29, vcc
	global_load_dword v73, v[48:49], off nt
	v_add_co_u32_e32 v48, vcc, 0x30000, v28
	s_nop 1
	v_addc_co_u32_e32 v49, vcc, 0, v29, vcc
	global_load_dword v74, v[48:49], off nt
	v_add_co_u32_e32 v48, vcc, 0x32000, v28
	s_nop 1
	v_addc_co_u32_e32 v49, vcc, 0, v29, vcc
	global_load_dword v75, v[48:49], off nt
	v_add_co_u32_e32 v48, vcc, 0x34000, v28
	s_nop 1
	v_addc_co_u32_e32 v49, vcc, 0, v29, vcc
	global_load_dword v76, v[48:49], off nt
	v_add_co_u32_e32 v48, vcc, 0x36000, v28
	s_nop 1
	v_addc_co_u32_e32 v49, vcc, 0, v29, vcc
	global_load_dword v77, v[48:49], off nt
	v_add_co_u32_e32 v48, vcc, 0x38000, v28
	s_nop 1
	v_addc_co_u32_e32 v49, vcc, 0, v29, vcc
	global_load_dword v78, v[48:49], off nt
	v_add_co_u32_e32 v48, vcc, 0x3a000, v28
	s_nop 1
	v_addc_co_u32_e32 v49, vcc, 0, v29, vcc
	global_load_dword v79, v[48:49], off nt
	v_add_co_u32_e32 v48, vcc, 0x3c000, v28
	s_nop 1
	v_addc_co_u32_e32 v49, vcc, 0, v29, vcc
	v_add_co_u32_e32 v28, vcc, 0x3e000, v28
	global_load_dword v48, v[48:49], off nt
	s_nop 0
	v_addc_co_u32_e32 v29, vcc, 0, v29, vcc
	global_load_dword v28, v[28:29], off nt
	s_waitcnt vmcnt(0)
	ds_write2_b32 v31, v50, v51 offset1:66
	ds_write2_b32 v31, v52, v53 offset0:132 offset1:198
	ds_write2_b32 v40, v54, v55 offset0:8 offset1:74
	ds_write2_b32 v40, v56, v57 offset0:140 offset1:206
	ds_write2_b32 v41, v58, v59 offset0:16 offset1:82
	ds_write2_b32 v41, v60, v61 offset0:148 offset1:214
	ds_write2_b32 v42, v62, v63 offset0:24 offset1:90
	ds_write2_b32 v42, v64, v65 offset0:156 offset1:222
	ds_write2_b32 v43, v66, v67 offset0:32 offset1:98
	ds_write2_b32 v43, v68, v69 offset0:164 offset1:230
	ds_write2_b32 v44, v70, v71 offset0:40 offset1:106
	ds_write2_b32 v44, v72, v73 offset0:172 offset1:238
	ds_write2_b32 v45, v74, v75 offset0:48 offset1:114
	ds_write2_b32 v45, v76, v77 offset0:180 offset1:246
	ds_write2_b32 v46, v78, v79 offset0:56 offset1:122
	ds_write2_b32 v46, v48, v28 offset0:188 offset1:254
	s_waitcnt lgkmcnt(0)
; #define GAS __attribute__((address_space(1)))
; #define LAS __attribute__((address_space(3)))
; #define LDS_WAIT() asm volatile("s_waitcnt lgkmcnt(0)" ::: "memory")
; __device__ __forceinline__ unsigned pk2(float lo, float hi) { return f2bf(lo) | (f2bf(hi) << 16); }
; __device__ __forceinline__ void tr_item(const float* W, int ld, int K, int nblk, int item, bf16* WT, bool gu, LAS float* scr, int lane) {
;     ...
;     LDS_WAIT(); asm volatile("" ::: "memory");
;     const int c = lane & 7;
; #pragma unroll
;     for (int j = 0; j < 4; ++j) { const int n = (lane >> 3) + 8 * j; const LAS float* s = scr + (8 * c) * 33 + n;
;         v4u o; o.x = pk2(s[0 * 33], s[1 * 33]); o.y = pk2(s[2 * 33], s[3 * 33]); o.z = pk2(s[4 * 33], s[5 * 33]); o.w = pk2(s[6 * 33], s[7 * 33]);
;         *(GAS v4u*)(WT + (size_t)(drow0 + n) * K + k0 + 8 * c) = o; }
;     LDS_WAIT(); asm volatile("" ::: "memory");
	ds_read2_b32 v[52:53], v36 offset0:33 offset1:41
	ds_read2_b32 v[54:55], v36 offset1:8
	ds_read2_b32 v[56:57], v36 offset0:66 offset1:74
	ds_read2_b32 v[58:59], v36 offset0:99 offset1:107
	ds_read2_b32 v[60:61], v36 offset0:132 offset1:140
	ds_read2_b32 v[62:63], v36 offset0:165 offset1:173
	ds_read2_b32 v[64:65], v36 offset0:198 offset1:206
	ds_read2_b32 v[66:67], v36 offset0:231 offset1:239
	s_waitcnt lgkmcnt(7)
	v_bfe_u32 v49, v52, 16, 1
	s_waitcnt lgkmcnt(6)
	v_bfe_u32 v48, v54, 16, 1
	v_add3_u32 v48, v54, v48, s46
	v_lshrrev_b32_e32 v48, 16, v48
	v_add3_u32 v49, v52, v49, s46
	v_and_or_b32 v48, v49, s47, v48
	s_waitcnt lgkmcnt(5)
	v_bfe_u32 v49, v56, 16, 1
	v_add3_u32 v49, v56, v49, s46
	s_waitcnt lgkmcnt(4)
	v_bfe_u32 v50, v58, 16, 1
	v_lshrrev_b32_e32 v49, 16, v49
	v_add3_u32 v50, v58, v50, s46
	v_and_or_b32 v49, v50, s47, v49
	s_waitcnt lgkmcnt(3)
	v_bfe_u32 v50, v60, 16, 1
	v_add3_u32 v50, v60, v50, s46
	s_waitcnt lgkmcnt(2)
	v_bfe_u32 v51, v62, 16, 1
	v_lshrrev_b32_e32 v50, 16, v50
	v_add3_u32 v51, v62, v51, s46
	v_and_or_b32 v50, v51, s47, v50
	s_waitcnt lgkmcnt(1)
	v_bfe_u32 v51, v64, 16, 1
	v_add_u32_e32 v68, s24, v35
	v_add3_u32 v51, v64, v51, s46
	s_waitcnt lgkmcnt(0)
	v_bfe_u32 v52, v66, 16, 1
	v_ashrrev_i32_e32 v69, 31, v68
	v_lshl_add_u64 v[28:29], v[22:23], 0, s[16:17]
	v_lshrrev_b32_e32 v51, 16, v51
	v_add3_u32 v52, v66, v52, s46
	v_lshlrev_b64 v[68:69], 11, v[68:69]
	v_and_or_b32 v51, v52, s47, v51
	v_lshl_add_u64 v[68:69], v[28:29], 0, v[68:69]
	global_store_dwordx4 v[68:69], v[48:51], off nt
	v_bfe_u32 v52, v67, 16, 1
	v_add3_u32 v52, v67, v52, s46
	v_bfe_u32 v48, v55, 16, 1
	v_add3_u32 v48, v55, v48, s46
	v_bfe_u32 v49, v53, 16, 1
	v_lshrrev_b32_e32 v48, 16, v48
	v_add3_u32 v49, v53, v49, s46
	v_and_or_b32 v48, v49, s47, v48
	v_bfe_u32 v49, v57, 16, 1
	v_add3_u32 v49, v57, v49, s46
	v_bfe_u32 v50, v59, 16, 1
	v_lshrrev_b32_e32 v49, 16, v49
	v_add3_u32 v50, v59, v50, s46
	v_and_or_b32 v49, v50, s47, v49
	v_bfe_u32 v50, v61, 16, 1
	v_add3_u32 v50, v61, v50, s46
	v_bfe_u32 v51, v63, 16, 1
	v_lshrrev_b32_e32 v50, 16, v50
	v_add3_u32 v51, v63, v51, s46
	v_and_or_b32 v50, v51, s47, v50
	v_bfe_u32 v51, v65, 16, 1
	v_add3_u32 v51, v65, v51, s46
	v_lshrrev_b32_e32 v51, 16, v51
	v_and_or_b32 v51, v52, s47, v51
	v_add_u32_e32 v52, s24, v37
	v_ashrrev_i32_e32 v53, 31, v52
	v_lshlrev_b64 v[52:53], 11, v[52:53]
	v_lshl_add_u64 v[52:53], v[28:29], 0, v[52:53]
	global_store_dwordx4 v[52:53], v[48:51], off nt
	ds_read2_b32 v[52:53], v36 offset0:49 offset1:57
	ds_read2_b32 v[54:55], v36 offset0:16 offset1:24
	ds_read2_b32 v[56:57], v36 offset0:82 offset1:90
	ds_read2_b32 v[58:59], v36 offset0:115 offset1:123
	ds_read2_b32 v[60:61], v36 offset0:148 offset1:156
	ds_read2_b32 v[62:63], v36 offset0:181 offset1:189
	ds_read2_b32 v[64:65], v36 offset0:214 offset1:222
	ds_read2_b32 v[66:67], v36 offset0:247 offset1:255
	s_waitcnt lgkmcnt(7)
	v_bfe_u32 v49, v52, 16, 1
	s_waitcnt lgkmcnt(6)
	v_bfe_u32 v48, v54, 16, 1
	v_add3_u32 v48, v54, v48, s46
	v_lshrrev_b32_e32 v48, 16, v48
	v_add3_u32 v49, v52, v49, s46
	v_and_or_b32 v48, v49, s47, v48
	s_waitcnt lgkmcnt(5)
	v_bfe_u32 v49, v56, 16, 1
	v_add3_u32 v49, v56, v49, s46
	s_waitcnt lgkmcnt(4)
	v_bfe_u32 v50, v58, 16, 1
	v_lshrrev_b32_e32 v49, 16, v49
	v_add3_u32 v50, v58, v50, s46
	v_and_or_b32 v49, v50, s47, v49
	s_waitcnt lgkmcnt(3)
	v_bfe_u32 v50, v60, 16, 1
	v_add3_u32 v50, v60, v50, s46
	s_waitcnt lgkmcnt(2)
	v_bfe_u32 v51, v62, 16, 1
	v_lshrrev_b32_e32 v50, 16, v50
	v_add3_u32 v51, v62, v51, s46
	v_and_or_b32 v50, v51, s47, v50
	s_waitcnt lgkmcnt(1)
	v_bfe_u32 v51, v64, 16, 1
	v_add_u32_e32 v68, s24, v38
	v_add3_u32 v51, v64, v51, s46
	s_waitcnt lgkmcnt(0)
	v_bfe_u32 v52, v66, 16, 1
	v_ashrrev_i32_e32 v69, 31, v68
	v_lshrrev_b32_e32 v51, 16, v51
	v_add3_u32 v52, v66, v52, s46
	v_lshlrev_b64 v[68:69], 11, v[68:69]
	v_and_or_b32 v51, v52, s47, v51
	v_lshl_add_u64 v[68:69], v[28:29], 0, v[68:69]
	global_store_dwordx4 v[68:69], v[48:51], off nt
	v_bfe_u32 v52, v67, 16, 1
	v_add3_u32 v52, v67, v52, s46
	v_bfe_u32 v48, v55, 16, 1
	v_add3_u32 v48, v55, v48, s46
	v_bfe_u32 v49, v53, 16, 1
	v_lshrrev_b32_e32 v48, 16, v48
	v_add3_u32 v49, v53, v49, s46
	v_and_or_b32 v48, v49, s47, v48
	v_bfe_u32 v49, v57, 16, 1
	v_add3_u32 v49, v57, v49, s46
	v_bfe_u32 v50, v59, 16, 1
	v_lshrrev_b32_e32 v49, 16, v49
	v_add3_u32 v50, v59, v50, s46
	v_and_or_b32 v49, v50, s47, v49
	v_bfe_u32 v50, v61, 16, 1
	v_add3_u32 v50, v61, v50, s46
	v_bfe_u32 v51, v63, 16, 1
	v_lshrrev_b32_e32 v50, 16, v50
	v_add3_u32 v51, v63, v51, s46
	v_and_or_b32 v50, v51, s47, v50
	v_bfe_u32 v51, v65, 16, 1
	v_add3_u32 v51, v65, v51, s46
	v_lshrrev_b32_e32 v51, 16, v51
	v_and_or_b32 v51, v52, s47, v51
	v_add_u32_e32 v52, s24, v39
	v_ashrrev_i32_e32 v53, 31, v52
	v_lshlrev_b64 v[52:53], 11, v[52:53]
	v_lshl_add_u64 v[28:29], v[28:29], 0, v[52:53]
	global_store_dwordx4 v[28:29], v[48:51], off nt
	s_waitcnt lgkmcnt(0)

; __device__ __forceinline__ void tr_item(const float* W, int ld, int K, int nblk, int item, bf16* WT, bool gu, LAS float* scr, int lane) {
;     const int kb = item / nblk, nb = item % nblk, k0 = 64 * kb, n0 = 32 * nb;
;     int drow0 = n0;
;     if (gu) { const int bj = n0 / FF, j = n0 - bj * FF; drow0 = 256 * (j / 128) + 128 * bj + (j % 128); }
;     { float t_[32];
; #pragma unroll
;       for (int i = 0; i < 32; ++i) t_[i] = W[(size_t)(k0 + 2 * i + (lane >> 5)) * ld + n0 + (lane & 31)];
; __device__ __forceinline__ void convert_items(Frame& F, const Args& a, int lo, int hi, int w, int nw) {
;     ...
;         if (r < I_SI) { tr_item(a.in[10], D + 512, D, 48, r, (bf16*)(F.ws + WS_WSWAIN), false, scr, lane); continue; } r -= I_SI;
.LBB0_1148:
	s_andn2_b64 vcc, exec, s[24:25]
	s_cbranch_vccnz .LBB0_1150
	s_add_i32 s16, s37, 0xf800
	s_and_b32 s24, s16, 0xffff
	s_mul_i32 s24, s24, 0xaaab
	s_lshr_b32 s25, s24, 21
	s_mul_i32 s24, s25, 48
	s_sub_i32 s16, s16, s24
	s_lshl_b32 s16, s16, 5
	s_and_b32 s24, s16, 0xffe0
	v_lshl_add_u32 v64, s25, 6, v30
	s_lshl_b32 s16, s24, 2
	v_lshl_add_u64 v[28:29], v[10:11], 0, s[16:17]
	v_add_u32_e32 v50, 2, v64
	v_add_u32_e32 v52, 4, v64
	v_add_u32_e32 v54, 6, v64
	v_add_u32_e32 v56, 8, v64
	v_add_u32_e32 v58, 10, v64
	v_add_u32_e32 v60, 12, v64
	v_add_u32_e32 v62, 14, v64
	v_mad_i64_i32 v[48:49], s[26:27], v64, s48, v[28:29]
	v_mad_i64_i32 v[50:51], s[26:27], v50, s48, v[28:29]
	v_mad_i64_i32 v[52:53], s[26:27], v52, s48, v[28:29]
	v_mad_i64_i32 v[54:55], s[26:27], v54, s48, v[28:29]
	v_mad_i64_i32 v[56:57], s[26:27], v56, s48, v[28:29]
	v_mad_i64_i32 v[58:59], s[26:27], v58, s48, v[28:29]
	v_mad_i64_i32 v[60:61], s[26:27], v60, s48, v[28:29]
	v_mad_i64_i32 v[62:63], s[26:27], v62, s48, v[28:29]
	global_load_dword v65, v[48:49], off nt
	global_load_dword v66, v[50:51], off nt
	global_load_dword v67, v[52:53], off nt
	global_load_dword v68, v[54:55], off nt
	global_load_dword v69, v[56:57], off nt
	global_load_dword v70, v[58:59], off nt
	global_load_dword v71, v[60:61], off nt
	global_load_dword v72, v[62:63], off nt
	v_add_u32_e32 v48, 16, v64
	v_add_u32_e32 v50, 18, v64
	v_add_u32_e32 v52, 20, v64
	v_add_u32_e32 v54, 22, v64
	v_add_u32_e32 v56, 24, v64
	v_add_u32_e32 v58, 26, v64
	v_add_u32_e32 v60, 28, v64
	v_add_u32_e32 v62, 30, v64
	v_mad_i64_i32 v[48:49], s[26:27], v48, s48, v[28:29]
	v_mad_i64_i32 v[50:51], s[26:27], v50, s48, v[28:29]
	v_mad_i64_i32 v[52:53], s[26:27], v52, s48, v[28:29]
	v_mad_i64_i32 v[54:55], s[26:27], v54, s48, v[28:29]
	v_mad_i64_i32 v[56:57], s[26:27], v56, s48, v[28:29]
	v_mad_i64_i32 v[58:59], s[26:27], v58, s48, v[28:29]
	v_mad_i64_i32 v[60:61], s[26:27], v60, s48, v[28:29]
	v_mad_i64_i32 v[62:63], s[26:27], v62, s48, v[28:29]
	global_load_dword v73, v[48:49], off nt
	global_load_dword v74, v[50:51], off nt
	global_load_dword v75, v[52:53], off nt
	global_load_dword v76, v[54:55], off nt
	global_load_dword v77, v[56:57], off nt
	global_load_dword v78, v[58:59], off nt
	global_load_dword v79, v[60:61], off nt
	global_load_dword v80, v[62:63], off nt
	v_add_u32_e32 v48, 32, v64
	v_add_u32_e32 v50, 34, v64
	v_add_u32_e32 v52, 36, v64
	v_add_u32_e32 v54, 38, v64
	v_add_u32_e32 v56, 40, v64
	v_add_u32_e32 v58, 42, v64
	v_add_u32_e32 v60, 44, v64
	v_add_u32_e32 v62, 46, v64
	v_mad_i64_i32 v[48:49], s[26:27], v48, s48, v[28:29]
	v_mad_i64_i32 v[50:51], s[26:27], v50, s48, v[28:29]
	v_mad_i64_i32 v[52:53], s[26:27], v52, s48, v[28:29]
	v_mad_i64_i32 v[54:55], s[26:27], v54, s48, v[28:29]
	v_mad_i64_i32 v[56:57], s[26:27], v56, s48, v[28:29]
	v_mad_i64_i32 v[58:59], s[26:27], v58, s48, v[28:29]
	v_mad_i64_i32 v[60:61], s[26:27], v60, s48, v[28:29]
	v_mad_i64_i32 v[62:63], s[26:27], v62, s48, v[28:29]
	global_load_dword v81, v[48:49], off nt
	global_load_dword v82, v[50:51], off nt
	global_load_dword v83, v[52:53], off nt
	global_load_dword v84, v[54:55], off nt
	global_load_dword v85, v[56:57], off nt
	global_load_dword v86, v[58:59], off nt
	global_load_dword v87, v[60:61], off nt
	s_nop 0
	global_load_dword v62, v[62:63], off nt
	v_add_u32_e32 v48, 48, v64
	v_add_u32_e32 v50, 50, v64
	v_add_u32_e32 v52, 52, v64
	v_add_u32_e32 v54, 54, v64
	v_add_u32_e32 v56, 56, v64
	v_add_u32_e32 v58, 58, v64
	v_add_u32_e32 v60, 60, v64
	v_add_u32_e32 v63, 62, v64
	v_mad_i64_i32 v[48:49], s[26:27], v48, s48, v[28:29]
	v_mad_i64_i32 v[50:51], s[26:27], v50, s48, v[28:29]
	v_mad_i64_i32 v[52:53], s[26:27], v52, s48, v[28:29]
	v_mad_i64_i32 v[54:55], s[26:27], v54, s48, v[28:29]
	v_mad_i64_i32 v[56:57], s[26:27], v56, s48, v[28:29]
	v_mad_i64_i32 v[58:59], s[26:27], v58, s48, v[28:29]
	v_mad_i64_i32 v[60:61], s[26:27], v60, s48, v[28:29]
	v_mad_i64_i32 v[28:29], s[26:27], v63, s48, v[28:29]
	global_load_dword v48, v[48:49], off nt
	s_nop 0
	global_load_dword v49, v[50:51], off nt
	s_nop 0
	global_load_dword v50, v[52:53], off nt
	global_load_dword v51, v[54:55], off nt
	s_nop 0
	global_load_dword v52, v[56:57], off nt
	global_load_dword v53, v[58:59], off nt
	global_load_dword v54, v[60:61], off nt
	s_nop 0
	global_load_dword v28, v[28:29], off nt
	s_waitcnt vmcnt(0)
	ds_write2_b32 v31, v65, v66 offset1:66
	ds_write2_b32 v31, v67, v68 offset0:132 offset1:198
	ds_write2_b32 v40, v69, v70 offset0:8 offset1:74
	ds_write2_b32 v40, v71, v72 offset0:140 offset1:206
	ds_write2_b32 v41, v73, v74 offset0:16 offset1:82
	ds_write2_b32 v41, v75, v76 offset0:148 offset1:214
	ds_write2_b32 v42, v77, v78 offset0:24 offset1:90
	ds_write2_b32 v42, v79, v80 offset0:156 offset1:222
	ds_write2_b32 v43, v81, v82 offset0:32 offset1:98
	ds_write2_b32 v43, v83, v84 offset0:164 offset1:230
	ds_write2_b32 v44, v85, v86 offset0:40 offset1:106
	ds_write2_b32 v44, v87, v62 offset0:172 offset1:238
	ds_write2_b32 v45, v48, v49 offset0:48 offset1:114
	ds_write2_b32 v45, v50, v51 offset0:180 offset1:246
	ds_write2_b32 v46, v52, v53 offset0:56 offset1:122
	ds_write2_b32 v46, v54, v28 offset0:188 offset1:254
	s_waitcnt lgkmcnt(0)
; #define GAS __attribute__((address_space(1)))
; #define LAS __attribute__((address_space(3)))
; #define LDS_WAIT() asm volatile("s_waitcnt lgkmcnt(0)" ::: "memory")
; __device__ __forceinline__ unsigned pk2(float lo, float hi) { return f2bf(lo) | (f2bf(hi) << 16); }
; __device__ __forceinline__ void tr_item(const float* W, int ld, int K, int nblk, int item, bf16* WT, bool gu, LAS float* scr, int lane) {
;     ...
;     LDS_WAIT(); asm volatile("" ::: "memory");
;     const int c = lane & 7;
; #pragma unroll
;     for (int j = 0; j < 4; ++j) { const int n = (lane >> 3) + 8 * j; const LAS float* s = scr + (8 * c) * 33 + n;
;         v4u o; o.x = pk2(s[0 * 33], s[1 * 33]); o.y = pk2(s[2 * 33], s[3 * 33]); o.z = pk2(s[4 * 33], s[5 * 33]); o.w = pk2(s[6 * 33], s[7 * 33]);
;         *(GAS v4u*)(WT + (size_t)(drow0 + n) * K + k0 + 8 * c) = o; }
;     LDS_WAIT(); asm volatile("" ::: "memory");
	ds_read2_b32 v[28:29], v36 offset1:8
	ds_read2_b32 v[54:55], v36 offset0:33 offset1:41
	ds_read2_b32 v[56:57], v36 offset0:66 offset1:74
	ds_read2_b32 v[58:59], v36 offset0:99 offset1:107
	ds_read2_b32 v[60:61], v36 offset0:132 offset1:140
	s_waitcnt lgkmcnt(4)
	v_bfe_u32 v48, v28, 16, 1
	v_add3_u32 v28, v28, v48, s46
	s_waitcnt lgkmcnt(3)
	v_bfe_u32 v48, v54, 16, 1
	v_lshrrev_b32_e32 v28, 16, v28
	v_add3_u32 v48, v54, v48, s46
	ds_read2_b32 v[62:63], v36 offset0:165 offset1:173
	v_and_or_b32 v48, v48, s47, v28
	s_waitcnt lgkmcnt(3)
	v_bfe_u32 v28, v56, 16, 1
	v_add3_u32 v28, v56, v28, s46
	s_waitcnt lgkmcnt(2)
	v_bfe_u32 v49, v58, 16, 1
	ds_read2_b32 v[64:65], v36 offset0:198 offset1:206
	v_lshrrev_b32_e32 v28, 16, v28
	v_add3_u32 v49, v58, v49, s46
	ds_read2_b32 v[66:67], v36 offset0:231 offset1:239
	v_and_or_b32 v49, v49, s47, v28
	s_waitcnt lgkmcnt(3)
	v_bfe_u32 v28, v60, 16, 1
	v_add3_u32 v28, v60, v28, s46
	s_waitcnt lgkmcnt(2)
	v_bfe_u32 v50, v62, 16, 1
	v_lshrrev_b32_e32 v28, 16, v28
	v_add3_u32 v50, v62, v50, s46
	v_and_or_b32 v50, v50, s47, v28
	s_waitcnt lgkmcnt(1)
	v_bfe_u32 v28, v64, 16, 1
	v_add3_u32 v28, v64, v28, s46
	s_waitcnt lgkmcnt(0)
	v_bfe_u32 v51, v66, 16, 1
	v_lshrrev_b32_e32 v28, 16, v28
	v_add3_u32 v51, v66, v51, s46
	v_add_u32_e32 v68, s24, v35
	s_lshl_b32 s16, s25, 7
	v_and_or_b32 v51, v51, s47, v28
	v_ashrrev_i32_e32 v69, 31, v68
	v_bfe_u32 v28, v29, 16, 1
	v_lshl_add_u64 v[52:53], v[12:13], 0, s[16:17]
	v_lshlrev_b64 v[68:69], 11, v[68:69]
	v_add3_u32 v28, v29, v28, s46
	v_bfe_u32 v29, v55, 16, 1
	v_lshl_add_u64 v[68:69], v[52:53], 0, v[68:69]
	v_lshrrev_b32_e32 v28, 16, v28
	v_add3_u32 v29, v55, v29, s46
	global_store_dwordx4 v[68:69], v[48:51], off nt
	ds_read2_b32 v[54:55], v36 offset0:16 offset1:24
	v_add_u32_e32 v68, s24, v38
	v_and_or_b32 v48, v29, s47, v28
	v_bfe_u32 v28, v57, 16, 1
	v_add3_u32 v28, v57, v28, s46
	v_bfe_u32 v29, v59, 16, 1
	v_lshrrev_b32_e32 v28, 16, v28
	v_add3_u32 v29, v59, v29, s46
	v_and_or_b32 v49, v29, s47, v28
	v_bfe_u32 v28, v61, 16, 1
	v_add3_u32 v28, v61, v28, s46
	v_bfe_u32 v29, v63, 16, 1
	v_lshrrev_b32_e32 v28, 16, v28
	v_add3_u32 v29, v63, v29, s46
	v_and_or_b32 v50, v29, s47, v28
	v_bfe_u32 v28, v65, 16, 1
	v_add3_u32 v28, v65, v28, s46
	v_bfe_u32 v29, v67, 16, 1
	v_lshrrev_b32_e32 v28, 16, v28
	v_add3_u32 v29, v67, v29, s46
	v_and_or_b32 v51, v29, s47, v28
	v_add_u32_e32 v28, s24, v37
	v_ashrrev_i32_e32 v29, 31, v28
	v_lshlrev_b64 v[28:29], 11, v[28:29]
	v_lshl_add_u64 v[28:29], v[52:53], 0, v[28:29]
	global_store_dwordx4 v[28:29], v[48:51], off nt
	ds_read2_b32 v[28:29], v36 offset0:49 offset1:57
	ds_read2_b32 v[56:57], v36 offset0:82 offset1:90
	ds_read2_b32 v[58:59], v36 offset0:115 offset1:123
	s_waitcnt lgkmcnt(3)
	v_bfe_u32 v48, v54, 16, 1
	v_add3_u32 v48, v54, v48, s46
	s_waitcnt lgkmcnt(2)
	v_bfe_u32 v49, v28, 16, 1
	ds_read2_b32 v[60:61], v36 offset0:148 offset1:156
	v_lshrrev_b32_e32 v48, 16, v48
	v_add3_u32 v28, v28, v49, s46
	ds_read2_b32 v[62:63], v36 offset0:181 offset1:189
	v_and_or_b32 v48, v28, s47, v48
	s_waitcnt lgkmcnt(3)
	v_bfe_u32 v28, v56, 16, 1
	v_add3_u32 v28, v56, v28, s46
	s_waitcnt lgkmcnt(2)
	v_bfe_u32 v49, v58, 16, 1
	ds_read2_b32 v[64:65], v36 offset0:214 offset1:222
	v_lshrrev_b32_e32 v28, 16, v28
	v_add3_u32 v49, v58, v49, s46
	ds_read2_b32 v[66:67], v36 offset0:247 offset1:255
	v_and_or_b32 v49, v49, s47, v28
	s_waitcnt lgkmcnt(3)
	v_bfe_u32 v28, v60, 16, 1
	v_add3_u32 v28, v60, v28, s46
	s_waitcnt lgkmcnt(2)
	v_bfe_u32 v50, v62, 16, 1
	v_lshrrev_b32_e32 v28, 16, v28
	v_add3_u32 v50, v62, v50, s46
	v_and_or_b32 v50, v50, s47, v28
	s_waitcnt lgkmcnt(1)
	v_bfe_u32 v28, v64, 16, 1
	v_add3_u32 v28, v64, v28, s46
	s_waitcnt lgkmcnt(0)
	v_bfe_u32 v51, v66, 16, 1
	v_ashrrev_i32_e32 v69, 31, v68
	v_lshrrev_b32_e32 v28, 16, v28
	v_add3_u32 v51, v66, v51, s46
	v_lshlrev_b64 v[68:69], 11, v[68:69]
	v_and_or_b32 v51, v51, s47, v28
	v_lshl_add_u64 v[68:69], v[52:53], 0, v[68:69]
	v_bfe_u32 v28, v55, 16, 1
	global_store_dwordx4 v[68:69], v[48:51], off nt
	v_add3_u32 v28, v55, v28, s46
	v_lshrrev_b32_e32 v28, 16, v28
	v_bfe_u32 v48, v29, 16, 1
	v_add3_u32 v29, v29, v48, s46
	v_and_or_b32 v48, v29, s47, v28
	v_bfe_u32 v28, v57, 16, 1
	v_add3_u32 v28, v57, v28, s46
	v_bfe_u32 v29, v59, 16, 1
	v_lshrrev_b32_e32 v28, 16, v28
	v_add3_u32 v29, v59, v29, s46
	v_and_or_b32 v49, v29, s47, v28
	v_bfe_u32 v28, v61, 16, 1
	v_add3_u32 v28, v61, v28, s46
	v_bfe_u32 v29, v63, 16, 1
	v_lshrrev_b32_e32 v28, 16, v28
	v_add3_u32 v29, v63, v29, s46
	v_and_or_b32 v50, v29, s47, v28
	v_bfe_u32 v28, v65, 16, 1
	v_add3_u32 v28, v65, v28, s46
	v_bfe_u32 v29, v67, 16, 1
	v_lshrrev_b32_e32 v28, 16, v28
	v_add3_u32 v29, v67, v29, s46
	v_and_or_b32 v51, v29, s47, v28
	v_add_u32_e32 v28, s24, v39
	v_ashrrev_i32_e32 v29, 31, v28
	v_lshlrev_b64 v[28:29], 11, v[28:29]
	v_lshl_add_u64 v[28:29], v[52:53], 0, v[28:29]
	global_store_dwordx4 v[28:29], v[48:51], off nt
	s_waitcnt lgkmcnt(0)

; __device__ __forceinline__ void tr_item(const float* W, int ld, int K, int nblk, int item, bf16* WT, bool gu, LAS float* scr, int lane) {
;     const int kb = item / nblk, nb = item % nblk, k0 = 64 * kb, n0 = 32 * nb;
;     int drow0 = n0;
;     if (gu) { const int bj = n0 / FF, j = n0 - bj * FF; drow0 = 256 * (j / 128) + 128 * bj + (j % 128); }
;     { float t_[32];
; #pragma unroll
;       for (int i = 0; i < 32; ++i) t_[i] = W[(size_t)(k0 + 2 * i + (lane >> 5)) * ld + n0 + (lane & 31)];
; __device__ __forceinline__ void convert_items(Frame& F, const Args& a, int lo, int hi, int w, int nw) {
;     ...
;         if (r < I_FO) { tr_item(a.in[9], D, D, 32, r, (bf16*)(F.ws + WS_WFOXOUT), false, scr, lane); continue; } r -= I_FO;
.LBB0_1151:
	s_andn2_b64 vcc, exec, s[24:25]
	s_cbranch_vccnz .LBB0_1153
	s_add_i32 s16, s42, 0x2a00
	s_and_b32 s25, s16, 0x1ffc0
	s_and_b32 s24, s40, 0x3e0
	v_add_u32_e32 v28, s25, v30
	s_lshl_b32 s16, s24, 2
	v_ashrrev_i32_e32 v29, 31, v28
	v_lshl_add_u64 v[48:49], v[14:15], 0, s[16:17]
	v_lshlrev_b64 v[28:29], 12, v[28:29]
	v_lshl_add_u64 v[28:29], v[48:49], 0, v[28:29]
	v_add_co_u32_e32 v48, vcc, 0x2000, v28
	global_load_dword v50, v[28:29], off nt
	s_nop 0
	v_addc_co_u32_e32 v49, vcc, 0, v29, vcc
	global_load_dword v51, v[48:49], off nt
	v_add_co_u32_e32 v48, vcc, 0x4000, v28
	s_lshl_b32 s16, s25, 1
	s_nop 0
	v_addc_co_u32_e32 v49, vcc, 0, v29, vcc
	global_load_dword v52, v[48:49], off nt
	v_add_co_u32_e32 v48, vcc, 0x6000, v28
	s_nop 1
	v_addc_co_u32_e32 v49, vcc, 0, v29, vcc
	global_load_dword v53, v[48:49], off nt
	v_add_co_u32_e32 v48, vcc, 0x8000, v28
	s_nop 1
	v_addc_co_u32_e32 v49, vcc, 0, v29, vcc
	global_load_dword v54, v[48:49], off nt
	v_add_co_u32_e32 v48, vcc, 0xa000, v28
	s_nop 1
	v_addc_co_u32_e32 v49, vcc, 0, v29, vcc
	global_load_dword v55, v[48:49], off nt
	v_add_co_u32_e32 v48, vcc, 0xc000, v28
	s_nop 1
	v_addc_co_u32_e32 v49, vcc, 0, v29, vcc
	global_load_dword v56, v[48:49], off nt
	v_add_co_u32_e32 v48, vcc, 0xe000, v28
	s_nop 1
	v_addc_co_u32_e32 v49, vcc, 0, v29, vcc
	global_load_dword v57, v[48:49], off nt
	v_add_co_u32_e32 v48, vcc, 0x10000, v28
	s_nop 1
	v_addc_co_u32_e32 v49, vcc, 0, v29, vcc
	global_load_dword v58, v[48:49], off nt
	v_add_co_u32_e32 v48, vcc, 0x12000, v28
	s_nop 1
	v_addc_co_u32_e32 v49, vcc, 0, v29, vcc
	global_load_dword v59, v[48:49], off nt
	v_add_co_u32_e32 v48, vcc, 0x14000, v28
	s_nop 1
	v_addc_co_u32_e32 v49, vcc, 0, v29, vcc
	global_load_dword v60, v[48:49], off nt
	v_add_co_u32_e32 v48, vcc, 0x16000, v28
	s_nop 1
	v_addc_co_u32_e32 v49, vcc, 0, v29, vcc
	global_load_dword v61, v[48:49], off nt
	v_add_co_u32_e32 v48, vcc, 0x18000, v28
	s_nop 1
	v_addc_co_u32_e32 v49, vcc, 0, v29, vcc
	global_load_dword v62, v[48:49], off nt
	v_add_co_u32_e32 v48, vcc, 0x1a000, v28
	s_nop 1
	v_addc_co_u32_e32 v49, vcc, 0, v29, vcc
	global_load_dword v63, v[48:49], off nt
	v_add_co_u32_e32 v48, vcc, 0x1c000, v28
	s_nop 1
	v_addc_co_u32_e32 v49, vcc, 0, v29, vcc
	global_load_dword v64, v[48:49], off nt
	v_add_co_u32_e32 v48, vcc, 0x1e000, v28
	s_nop 1
	v_addc_co_u32_e32 v49, vcc, 0, v29, vcc
	global_load_dword v65, v[48:49], off nt
	v_add_co_u32_e32 v48, vcc, 0x20000, v28
	s_nop 1
	v_addc_co_u32_e32 v49, vcc, 0, v29, vcc
	global_load_dword v66, v[48:49], off nt
	v_add_co_u32_e32 v48, vcc, 0x22000, v28
	s_nop 1
	v_addc_co_u32_e32 v49, vcc, 0, v29, vcc
	global_load_dword v67, v[48:49], off nt
	v_add_co_u32_e32 v48, vcc, 0x24000, v28
	s_nop 1
	v_addc_co_u32_e32 v49, vcc, 0, v29, vcc
	global_load_dword v68, v[48:49], off nt
	v_add_co_u32_e32 v48, vcc, 0x26000, v28
	s_nop 1
	v_addc_co_u32_e32 v49, vcc, 0, v29, vcc
	global_load_dword v69, v[48:49], off nt
	v_add_co_u32_e32 v48, vcc, 0x28000, v28
	s_nop 1
	v_addc_co_u32_e32 v49, vcc, 0, v29, vcc
	global_load_dword v70, v[48:49], off nt
	v_add_co_u32_e32 v48, vcc, 0x2a000, v28
	s_nop 1
	v_addc_co_u32_e32 v49, vcc, 0, v29, vcc
	global_load_dword v71, v[48:49], off nt
	v_add_co_u32_e32 v48, vcc, 0x2c000, v28
	s_nop 1
	v_addc_co_u32_e32 v49, vcc, 0, v29, vcc
	global_load_dword v72, v[48:49], off nt
	v_add_co_u32_e32 v48, vcc, 0x2e000, v28
	s_nop 1
	v_addc_co_u32_e32 v49, vcc, 0, v29, vcc
	global_load_dword v73, v[48:49], off nt
	v_add_co_u32_e32 v48, vcc, 0x30000, v28
	s_nop 1
	v_addc_co_u32_e32 v49, vcc, 0, v29, vcc
	global_load_dword v74, v[48:49], off nt
	v_add_co_u32_e32 v48, vcc, 0x32000, v28
	s_nop 1
	v_addc_co_u32_e32 v49, vcc, 0, v29, vcc
	global_load_dword v75, v[48:49], off nt
	v_add_co_u32_e32 v48, vcc, 0x34000, v28
	s_nop 1
	v_addc_co_u32_e32 v49, vcc, 0, v29, vcc
	global_load_dword v76, v[48:49], off nt
	v_add_co_u32_e32 v48, vcc, 0x36000, v28
	s_nop 1
	v_addc_co_u32_e32 v49, vcc, 0, v29, vcc
	global_load_dword v77, v[48:49], off nt
	v_add_co_u32_e32 v48, vcc, 0x38000, v28
	s_nop 1
	v_addc_co_u32_e32 v49, vcc, 0, v29, vcc
	global_load_dword v78, v[48:49], off nt
	v_add_co_u32_e32 v48, vcc, 0x3a000, v28
	s_nop 1
	v_addc_co_u32_e32 v49, vcc, 0, v29, vcc
	global_load_dword v79, v[48:49], off nt
	v_add_co_u32_e32 v48, vcc, 0x3c000, v28
	s_nop 1
	v_addc_co_u32_e32 v49, vcc, 0, v29, vcc
	v_add_co_u32_e32 v28, vcc, 0x3e000, v28
	global_load_dword v48, v[48:49], off nt
	s_nop 0
	v_addc_co_u32_e32 v29, vcc, 0, v29, vcc
	global_load_dword v28, v[28:29], off nt
	s_waitcnt vmcnt(0)
	ds_write2_b32 v31, v50, v51 offset1:66
	ds_write2_b32 v31, v52, v53 offset0:132 offset1:198
	ds_write2_b32 v40, v54, v55 offset0:8 offset1:74
	ds_write2_b32 v40, v56, v57 offset0:140 offset1:206
	ds_write2_b32 v41, v58, v59 offset0:16 offset1:82
	ds_write2_b32 v41, v60, v61 offset0:148 offset1:214
	ds_write2_b32 v42, v62, v63 offset0:24 offset1:90
	ds_write2_b32 v42, v64, v65 offset0:156 offset1:222
	ds_write2_b32 v43, v66, v67 offset0:32 offset1:98
	ds_write2_b32 v43, v68, v69 offset0:164 offset1:230
	ds_write2_b32 v44, v70, v71 offset0:40 offset1:106
	ds_write2_b32 v44, v72, v73 offset0:172 offset1:238
	ds_write2_b32 v45, v74, v75 offset0:48 offset1:114
	ds_write2_b32 v45, v76, v77 offset0:180 offset1:246
	ds_write2_b32 v46, v78, v79 offset0:56 offset1:122
	ds_write2_b32 v46, v48, v28 offset0:188 offset1:254
	s_waitcnt lgkmcnt(0)
; #define GAS __attribute__((address_space(1)))
; #define LAS __attribute__((address_space(3)))
; #define LDS_WAIT() asm volatile("s_waitcnt lgkmcnt(0)" ::: "memory")
; __device__ __forceinline__ unsigned pk2(float lo, float hi) { return f2bf(lo) | (f2bf(hi) << 16); }
; __device__ __forceinline__ void tr_item(const float* W, int ld, int K, int nblk, int item, bf16* WT, bool gu, LAS float* scr, int lane) {
;     ...
;     LDS_WAIT(); asm volatile("" ::: "memory");
;     const int c = lane & 7;
; #pragma unroll
;     for (int j = 0; j < 4; ++j) { const int n = (lane >> 3) + 8 * j; const LAS float* s = scr + (8 * c) * 33 + n;
;         v4u o; o.x = pk2(s[0 * 33], s[1 * 33]); o.y = pk2(s[2 * 33], s[3 * 33]); o.z = pk2(s[4 * 33], s[5 * 33]); o.w = pk2(s[6 * 33], s[7 * 33]);
;         *(GAS v4u*)(WT + (size_t)(drow0 + n) * K + k0 + 8 * c) = o; }
;     LDS_WAIT(); asm volatile("" ::: "memory");
	ds_read2_b32 v[52:53], v36 offset0:33 offset1:41
	ds_read2_b32 v[54:55], v36 offset1:8
	ds_read2_b32 v[56:57], v36 offset0:66 offset1:74
	ds_read2_b32 v[58:59], v36 offset0:99 offset1:107
	ds_read2_b32 v[60:61], v36 offset0:132 offset1:140
	ds_read2_b32 v[62:63], v36 offset0:165 offset1:173
	ds_read2_b32 v[64:65], v36 offset0:198 offset1:206
	ds_read2_b32 v[66:67], v36 offset0:231 offset1:239
	s_waitcnt lgkmcnt(7)
	v_bfe_u32 v49, v52, 16, 1
	s_waitcnt lgkmcnt(6)
	v_bfe_u32 v48, v54, 16, 1
	v_add3_u32 v48, v54, v48, s46
	v_lshrrev_b32_e32 v48, 16, v48
	v_add3_u32 v49, v52, v49, s46
	v_and_or_b32 v48, v49, s47, v48
	s_waitcnt lgkmcnt(5)
	v_bfe_u32 v49, v56, 16, 1
	v_add3_u32 v49, v56, v49, s46
	s_waitcnt lgkmcnt(4)
	v_bfe_u32 v50, v58, 16, 1
	v_lshrrev_b32_e32 v49, 16, v49
	v_add3_u32 v50, v58, v50, s46
	v_and_or_b32 v49, v50, s47, v49
	s_waitcnt lgkmcnt(3)
	v_bfe_u32 v50, v60, 16, 1
	v_add3_u32 v50, v60, v50, s46
	s_waitcnt lgkmcnt(2)
	v_bfe_u32 v51, v62, 16, 1
	v_lshrrev_b32_e32 v50, 16, v50
	v_add3_u32 v51, v62, v51, s46
	v_and_or_b32 v50, v51, s47, v50
	s_waitcnt lgkmcnt(1)
	v_bfe_u32 v51, v64, 16, 1
	v_add_u32_e32 v68, s24, v35
	v_add3_u32 v51, v64, v51, s46
	s_waitcnt lgkmcnt(0)
	v_bfe_u32 v52, v66, 16, 1
	v_ashrrev_i32_e32 v69, 31, v68
	v_lshl_add_u64 v[28:29], v[24:25], 0, s[16:17]
	v_lshrrev_b32_e32 v51, 16, v51
	v_add3_u32 v52, v66, v52, s46
	v_lshlrev_b64 v[68:69], 11, v[68:69]
	v_and_or_b32 v51, v52, s47, v51
	v_lshl_add_u64 v[68:69], v[28:29], 0, v[68:69]
	global_store_dwordx4 v[68:69], v[48:51], off nt
	v_bfe_u32 v52, v67, 16, 1
	v_add3_u32 v52, v67, v52, s46
	v_bfe_u32 v48, v55, 16, 1
	v_add3_u32 v48, v55, v48, s46
	v_bfe_u32 v49, v53, 16, 1
	v_lshrrev_b32_e32 v48, 16, v48
	v_add3_u32 v49, v53, v49, s46
	v_and_or_b32 v48, v49, s47, v48
	v_bfe_u32 v49, v57, 16, 1
	v_add3_u32 v49, v57, v49, s46
	v_bfe_u32 v50, v59, 16, 1
	v_lshrrev_b32_e32 v49, 16, v49
	v_add3_u32 v50, v59, v50, s46
	v_and_or_b32 v49, v50, s47, v49
	v_bfe_u32 v50, v61, 16, 1
	v_add3_u32 v50, v61, v50, s46
	v_bfe_u32 v51, v63, 16, 1
	v_lshrrev_b32_e32 v50, 16, v50
	v_add3_u32 v51, v63, v51, s46
	v_and_or_b32 v50, v51, s47, v50
	v_bfe_u32 v51, v65, 16, 1
	v_add3_u32 v51, v65, v51, s46
	v_lshrrev_b32_e32 v51, 16, v51
	v_and_or_b32 v51, v52, s47, v51
	v_add_u32_e32 v52, s24, v37
	v_ashrrev_i32_e32 v53, 31, v52
	v_lshlrev_b64 v[52:53], 11, v[52:53]
	v_lshl_add_u64 v[52:53], v[28:29], 0, v[52:53]
	global_store_dwordx4 v[52:53], v[48:51], off nt
	ds_read2_b32 v[52:53], v36 offset0:49 offset1:57
	ds_read2_b32 v[54:55], v36 offset0:16 offset1:24
	ds_read2_b32 v[56:57], v36 offset0:82 offset1:90
	ds_read2_b32 v[58:59], v36 offset0:115 offset1:123
	ds_read2_b32 v[60:61], v36 offset0:148 offset1:156
	ds_read2_b32 v[62:63], v36 offset0:181 offset1:189
	ds_read2_b32 v[64:65], v36 offset0:214 offset1:222
	ds_read2_b32 v[66:67], v36 offset0:247 offset1:255
	s_waitcnt lgkmcnt(7)
	v_bfe_u32 v49, v52, 16, 1
	s_waitcnt lgkmcnt(6)
	v_bfe_u32 v48, v54, 16, 1
	v_add3_u32 v48, v54, v48, s46
	v_lshrrev_b32_e32 v48, 16, v48
	v_add3_u32 v49, v52, v49, s46
	v_and_or_b32 v48, v49, s47, v48
	s_waitcnt lgkmcnt(5)
	v_bfe_u32 v49, v56, 16, 1
	v_add3_u32 v49, v56, v49, s46
	s_waitcnt lgkmcnt(4)
	v_bfe_u32 v50, v58, 16, 1
	v_lshrrev_b32_e32 v49, 16, v49
	v_add3_u32 v50, v58, v50, s46
	v_and_or_b32 v49, v50, s47, v49
	s_waitcnt lgkmcnt(3)
	v_bfe_u32 v50, v60, 16, 1
	v_add3_u32 v50, v60, v50, s46
	s_waitcnt lgkmcnt(2)
	v_bfe_u32 v51, v62, 16, 1
	v_lshrrev_b32_e32 v50, 16, v50
	v_add3_u32 v51, v62, v51, s46
	v_and_or_b32 v50, v51, s47, v50
	s_waitcnt lgkmcnt(1)
	v_bfe_u32 v51, v64, 16, 1
	v_add_u32_e32 v68, s24, v38
	v_add3_u32 v51, v64, v51, s46
	s_waitcnt lgkmcnt(0)
	v_bfe_u32 v52, v66, 16, 1
	v_ashrrev_i32_e32 v69, 31, v68
	v_lshrrev_b32_e32 v51, 16, v51
	v_add3_u32 v52, v66, v52, s46
	v_lshlrev_b64 v[68:69], 11, v[68:69]
	v_and_or_b32 v51, v52, s47, v51
	v_lshl_add_u64 v[68:69], v[28:29], 0, v[68:69]
	global_store_dwordx4 v[68:69], v[48:51], off nt
	v_bfe_u32 v52, v67, 16, 1
	v_add3_u32 v52, v67, v52, s46
	v_bfe_u32 v48, v55, 16, 1
	v_add3_u32 v48, v55, v48, s46
	v_bfe_u32 v49, v53, 16, 1
	v_lshrrev_b32_e32 v48, 16, v48
	v_add3_u32 v49, v53, v49, s46
	v_and_or_b32 v48, v49, s47, v48
	v_bfe_u32 v49, v57, 16, 1
	v_add3_u32 v49, v57, v49, s46
	v_bfe_u32 v50, v59, 16, 1
	v_lshrrev_b32_e32 v49, 16, v49
	v_add3_u32 v50, v59, v50, s46
	v_and_or_b32 v49, v50, s47, v49
	v_bfe_u32 v50, v61, 16, 1
	v_add3_u32 v50, v61, v50, s46
	v_bfe_u32 v51, v63, 16, 1
	v_lshrrev_b32_e32 v50, 16, v50
	v_add3_u32 v51, v63, v51, s46
	v_and_or_b32 v50, v51, s47, v50
	v_bfe_u32 v51, v65, 16, 1
	v_add3_u32 v51, v65, v51, s46
	v_lshrrev_b32_e32 v51, 16, v51
	v_and_or_b32 v51, v52, s47, v51
	v_add_u32_e32 v52, s24, v39
	v_ashrrev_i32_e32 v53, 31, v52
	v_lshlrev_b64 v[52:53], 11, v[52:53]
	v_lshl_add_u64 v[28:29], v[28:29], 0, v[52:53]
	global_store_dwordx4 v[28:29], v[48:51], off nt
	s_waitcnt lgkmcnt(0)

; __device__ __forceinline__ void tr_item(const float* W, int ld, int K, int nblk, int item, bf16* WT, bool gu, LAS float* scr, int lane) {
;     const int kb = item / nblk, nb = item % nblk, k0 = 64 * kb, n0 = 32 * nb;
;     int drow0 = n0;
;     if (gu) { const int bj = n0 / FF, j = n0 - bj * FF; drow0 = 256 * (j / 128) + 128 * bj + (j % 128); }
;     { float t_[32];
; #pragma unroll
;       for (int i = 0; i < 32; ++i) t_[i] = W[(size_t)(k0 + 2 * i + (lane >> 5)) * ld + n0 + (lane & 31)];
; __device__ __forceinline__ void convert_items(Frame& F, const Args& a, int lo, int hi, int w, int nw) {
;     ...
;         if (r < I_FI) { tr_item(a.in[7], 3 * D + 16, D, 96, r, (bf16*)(F.ws + WS_WFOXIN), false, scr, lane); continue; } r -= I_FI;
.LBB0_1154:
	s_andn2_b64 vcc, exec, s[24:25]
	s_cbranch_vccnz .LBB0_1131
	s_mul_hi_i32 s16, s37, 0x2aaaaaab
	s_lshr_b32 s24, s16, 31
	s_ashr_i32 s16, s16, 4
	s_add_i32 s16, s16, s24
	s_lshl_b32 s26, s16, 6
	s_mulk_i32 s16, 0xf400
	s_add_i32 s24, s40, s16
	v_add_u32_e32 v64, s26, v30
	s_ashr_i32 s25, s24, 31
	v_lshl_add_u64 v[28:29], s[24:25], 2, v[16:17]
	v_add_u32_e32 v50, 2, v64
	v_add_u32_e32 v52, 4, v64
	v_add_u32_e32 v54, 6, v64
	v_add_u32_e32 v56, 8, v64
	v_add_u32_e32 v58, 10, v64
	v_add_u32_e32 v60, 12, v64
	v_add_u32_e32 v62, 14, v64
	v_mad_i64_i32 v[48:49], s[50:51], v64, s49, v[28:29]
	v_mad_i64_i32 v[50:51], s[50:51], v50, s49, v[28:29]
	v_mad_i64_i32 v[52:53], s[50:51], v52, s49, v[28:29]
	v_mad_i64_i32 v[54:55], s[50:51], v54, s49, v[28:29]
	v_mad_i64_i32 v[56:57], s[50:51], v56, s49, v[28:29]
	v_mad_i64_i32 v[58:59], s[50:51], v58, s49, v[28:29]
	v_mad_i64_i32 v[60:61], s[50:51], v60, s49, v[28:29]
	v_mad_i64_i32 v[62:63], s[50:51], v62, s49, v[28:29]
	global_load_dword v65, v[48:49], off nt
	global_load_dword v66, v[50:51], off nt
	global_load_dword v67, v[52:53], off nt
	global_load_dword v68, v[54:55], off nt
	global_load_dword v69, v[56:57], off nt
	global_load_dword v70, v[58:59], off nt
	global_load_dword v71, v[60:61], off nt
	global_load_dword v72, v[62:63], off nt
	v_add_u32_e32 v48, 16, v64
	v_add_u32_e32 v50, 18, v64
	v_add_u32_e32 v52, 20, v64
	v_add_u32_e32 v54, 22, v64
	v_add_u32_e32 v56, 24, v64
	v_add_u32_e32 v58, 26, v64
	v_add_u32_e32 v60, 28, v64
	v_add_u32_e32 v62, 30, v64
	v_mad_i64_i32 v[48:49], s[50:51], v48, s49, v[28:29]
	v_mad_i64_i32 v[50:51], s[50:51], v50, s49, v[28:29]
	v_mad_i64_i32 v[52:53], s[50:51], v52, s49, v[28:29]
	v_mad_i64_i32 v[54:55], s[50:51], v54, s49, v[28:29]
	v_mad_i64_i32 v[56:57], s[50:51], v56, s49, v[28:29]
	v_mad_i64_i32 v[58:59], s[50:51], v58, s49, v[28:29]
	v_mad_i64_i32 v[60:61], s[50:51], v60, s49, v[28:29]
	v_mad_i64_i32 v[62:63], s[50:51], v62, s49, v[28:29]
	global_load_dword v73, v[48:49], off nt
	global_load_dword v74, v[50:51], off nt
	global_load_dword v75, v[52:53], off nt
	global_load_dword v76, v[54:55], off nt
	global_load_dword v77, v[56:57], off nt
	global_load_dword v78, v[58:59], off nt
	global_load_dword v79, v[60:61], off nt
	global_load_dword v80, v[62:63], off nt
	v_add_u32_e32 v48, 32, v64
	v_add_u32_e32 v50, 34, v64
	v_add_u32_e32 v52, 36, v64
	v_add_u32_e32 v54, 38, v64
	v_add_u32_e32 v56, 40, v64
	v_add_u32_e32 v58, 42, v64
	v_add_u32_e32 v60, 44, v64
	v_add_u32_e32 v62, 46, v64
	v_mad_i64_i32 v[48:49], s[50:51], v48, s49, v[28:29]
	v_mad_i64_i32 v[50:51], s[50:51], v50, s49, v[28:29]
	v_mad_i64_i32 v[52:53], s[50:51], v52, s49, v[28:29]
	v_mad_i64_i32 v[54:55], s[50:51], v54, s49, v[28:29]
	v_mad_i64_i32 v[56:57], s[50:51], v56, s49, v[28:29]
	v_mad_i64_i32 v[58:59], s[50:51], v58, s49, v[28:29]
	v_mad_i64_i32 v[60:61], s[50:51], v60, s49, v[28:29]
	v_mad_i64_i32 v[62:63], s[50:51], v62, s49, v[28:29]
	global_load_dword v81, v[48:49], off nt
	global_load_dword v82, v[50:51], off nt
	global_load_dword v83, v[52:53], off nt
	global_load_dword v84, v[54:55], off nt
	global_load_dword v85, v[56:57], off nt
	global_load_dword v86, v[58:59], off nt
	global_load_dword v87, v[60:61], off nt
	s_nop 0
	global_load_dword v62, v[62:63], off nt
	v_add_u32_e32 v48, 48, v64
	v_add_u32_e32 v50, 50, v64
	v_add_u32_e32 v52, 52, v64
	v_add_u32_e32 v54, 54, v64
	v_add_u32_e32 v56, 56, v64
	v_add_u32_e32 v58, 58, v64
	v_add_u32_e32 v60, 60, v64
	v_add_u32_e32 v63, 62, v64
	v_mad_i64_i32 v[48:49], s[50:51], v48, s49, v[28:29]
	v_mad_i64_i32 v[50:51], s[50:51], v50, s49, v[28:29]
	v_mad_i64_i32 v[52:53], s[50:51], v52, s49, v[28:29]
	v_mad_i64_i32 v[54:55], s[50:51], v54, s49, v[28:29]
	v_mad_i64_i32 v[56:57], s[50:51], v56, s49, v[28:29]
	v_mad_i64_i32 v[58:59], s[50:51], v58, s49, v[28:29]
	v_mad_i64_i32 v[60:61], s[50:51], v60, s49, v[28:29]
	v_mad_i64_i32 v[28:29], s[50:51], v63, s49, v[28:29]
	global_load_dword v48, v[48:49], off nt
	s_nop 0
	global_load_dword v49, v[50:51], off nt
	s_nop 0
	global_load_dword v50, v[52:53], off nt
	global_load_dword v51, v[54:55], off nt
	s_nop 0
	global_load_dword v52, v[56:57], off nt
	global_load_dword v53, v[58:59], off nt
	global_load_dword v54, v[60:61], off nt
	s_nop 0
	global_load_dword v28, v[28:29], off nt
	s_waitcnt vmcnt(0)
	ds_write2_b32 v31, v65, v66 offset1:66
	ds_write2_b32 v31, v67, v68 offset0:132 offset1:198
	ds_write2_b32 v40, v69, v70 offset0:8 offset1:74
	ds_write2_b32 v40, v71, v72 offset0:140 offset1:206
	ds_write2_b32 v41, v73, v74 offset0:16 offset1:82
	ds_write2_b32 v41, v75, v76 offset0:148 offset1:214
	ds_write2_b32 v42, v77, v78 offset0:24 offset1:90
	ds_write2_b32 v42, v79, v80 offset0:156 offset1:222
	ds_write2_b32 v43, v81, v82 offset0:32 offset1:98
	ds_write2_b32 v43, v83, v84 offset0:164 offset1:230
	ds_write2_b32 v44, v85, v86 offset0:40 offset1:106
	ds_write2_b32 v44, v87, v62 offset0:172 offset1:238
	ds_write2_b32 v45, v48, v49 offset0:48 offset1:114
	ds_write2_b32 v45, v50, v51 offset0:180 offset1:246
	ds_write2_b32 v46, v52, v53 offset0:56 offset1:122
	ds_write2_b32 v46, v54, v28 offset0:188 offset1:254
	s_waitcnt lgkmcnt(0)
; #define GAS __attribute__((address_space(1)))
; #define LAS __attribute__((address_space(3)))
; #define LDS_WAIT() asm volatile("s_waitcnt lgkmcnt(0)" ::: "memory")
; __device__ __forceinline__ unsigned pk2(float lo, float hi) { return f2bf(lo) | (f2bf(hi) << 16); }
; __device__ __forceinline__ void tr_item(const float* W, int ld, int K, int nblk, int item, bf16* WT, bool gu, LAS float* scr, int lane) {
;     ...
;     LDS_WAIT(); asm volatile("" ::: "memory");
;     const int c = lane & 7;
; #pragma unroll
;     for (int j = 0; j < 4; ++j) { const int n = (lane >> 3) + 8 * j; const LAS float* s = scr + (8 * c) * 33 + n;
;         v4u o; o.x = pk2(s[0 * 33], s[1 * 33]); o.y = pk2(s[2 * 33], s[3 * 33]); o.z = pk2(s[4 * 33], s[5 * 33]); o.w = pk2(s[6 * 33], s[7 * 33]);
;         *(GAS v4u*)(WT + (size_t)(drow0 + n) * K + k0 + 8 * c) = o; }
;     LDS_WAIT(); asm volatile("" ::: "memory");
	ds_read2_b32 v[28:29], v36 offset1:8
	ds_read2_b32 v[54:55], v36 offset0:33 offset1:41
	ds_read2_b32 v[56:57], v36 offset0:66 offset1:74
	ds_read2_b32 v[58:59], v36 offset0:99 offset1:107
	ds_read2_b32 v[60:61], v36 offset0:132 offset1:140
	s_waitcnt lgkmcnt(4)
	v_bfe_u32 v48, v28, 16, 1
	v_add3_u32 v28, v28, v48, s46
	s_waitcnt lgkmcnt(3)
	v_bfe_u32 v48, v54, 16, 1
	v_lshrrev_b32_e32 v28, 16, v28
	v_add3_u32 v48, v54, v48, s46
	ds_read2_b32 v[62:63], v36 offset0:165 offset1:173
	v_and_or_b32 v48, v48, s47, v28
	s_waitcnt lgkmcnt(3)
	v_bfe_u32 v28, v56, 16, 1
	v_add3_u32 v28, v56, v28, s46
	s_waitcnt lgkmcnt(2)
	v_bfe_u32 v49, v58, 16, 1
	ds_read2_b32 v[64:65], v36 offset0:198 offset1:206
	v_lshrrev_b32_e32 v28, 16, v28
	v_add3_u32 v49, v58, v49, s46
	ds_read2_b32 v[66:67], v36 offset0:231 offset1:239
	v_and_or_b32 v49, v49, s47, v28
	s_waitcnt lgkmcnt(3)
	v_bfe_u32 v28, v60, 16, 1
	v_add3_u32 v28, v60, v28, s46
	s_waitcnt lgkmcnt(2)
	v_bfe_u32 v50, v62, 16, 1
	v_lshrrev_b32_e32 v28, 16, v28
	v_add3_u32 v50, v62, v50, s46
	v_and_or_b32 v50, v50, s47, v28
	s_waitcnt lgkmcnt(1)
	v_bfe_u32 v28, v64, 16, 1
	v_add3_u32 v28, v64, v28, s46
	s_waitcnt lgkmcnt(0)
	v_bfe_u32 v51, v66, 16, 1
	v_lshrrev_b32_e32 v28, 16, v28
	v_add3_u32 v51, v66, v51, s46
	v_add_u32_e32 v68, s24, v35
	s_ashr_i32 s27, s26, 31
	v_and_or_b32 v51, v51, s47, v28
	v_ashrrev_i32_e32 v69, 31, v68
	v_bfe_u32 v28, v29, 16, 1
	v_lshl_add_u64 v[52:53], s[26:27], 1, v[26:27]
	v_lshlrev_b64 v[70:71], 11, v[68:69]
	v_add3_u32 v28, v29, v28, s46
	v_bfe_u32 v29, v55, 16, 1
	v_lshl_add_u64 v[70:71], v[52:53], 0, v[70:71]
	v_lshrrev_b32_e32 v28, 16, v28
	v_add3_u32 v29, v55, v29, s46
	global_store_dwordx4 v[70:71], v[48:51], off nt
	ds_read2_b32 v[54:55], v36 offset0:16 offset1:24
	v_add_u32_e32 v70, 16, v68
	v_and_or_b32 v48, v29, s47, v28
	v_bfe_u32 v28, v57, 16, 1
	v_add3_u32 v28, v57, v28, s46
	v_bfe_u32 v29, v59, 16, 1
	v_lshrrev_b32_e32 v28, 16, v28
	v_add3_u32 v29, v59, v29, s46
	v_and_or_b32 v49, v29, s47, v28
	v_bfe_u32 v28, v61, 16, 1
	v_add3_u32 v28, v61, v28, s46
	v_bfe_u32 v29, v63, 16, 1
	v_lshrrev_b32_e32 v28, 16, v28
	v_add3_u32 v29, v63, v29, s46
	v_and_or_b32 v50, v29, s47, v28
	v_bfe_u32 v28, v65, 16, 1
	v_add3_u32 v28, v65, v28, s46
	v_bfe_u32 v29, v67, 16, 1
	v_lshrrev_b32_e32 v28, 16, v28
	v_add3_u32 v29, v67, v29, s46
	v_and_or_b32 v51, v29, s47, v28
	v_add_u32_e32 v28, 8, v68
	v_ashrrev_i32_e32 v29, 31, v28
	v_lshlrev_b64 v[28:29], 11, v[28:29]
	v_lshl_add_u64 v[28:29], v[52:53], 0, v[28:29]
	global_store_dwordx4 v[28:29], v[48:51], off nt
	ds_read2_b32 v[28:29], v36 offset0:49 offset1:57
	ds_read2_b32 v[56:57], v36 offset0:82 offset1:90
	ds_read2_b32 v[58:59], v36 offset0:115 offset1:123
	s_waitcnt lgkmcnt(3)
	v_bfe_u32 v48, v54, 16, 1
	v_add3_u32 v48, v54, v48, s46
	s_waitcnt lgkmcnt(2)
	v_bfe_u32 v49, v28, 16, 1
	ds_read2_b32 v[60:61], v36 offset0:148 offset1:156
	v_lshrrev_b32_e32 v48, 16, v48
	v_add3_u32 v28, v28, v49, s46
	ds_read2_b32 v[62:63], v36 offset0:181 offset1:189
	v_and_or_b32 v48, v28, s47, v48
	s_waitcnt lgkmcnt(3)
	v_bfe_u32 v28, v56, 16, 1
	v_add3_u32 v28, v56, v28, s46
	s_waitcnt lgkmcnt(2)
	v_bfe_u32 v49, v58, 16, 1
	ds_read2_b32 v[64:65], v36 offset0:214 offset1:222
	v_lshrrev_b32_e32 v28, 16, v28
	v_add3_u32 v49, v58, v49, s46
	ds_read2_b32 v[66:67], v36 offset0:247 offset1:255
	v_and_or_b32 v49, v49, s47, v28
	s_waitcnt lgkmcnt(3)
	v_bfe_u32 v28, v60, 16, 1
	v_add3_u32 v28, v60, v28, s46
	s_waitcnt lgkmcnt(2)
	v_bfe_u32 v50, v62, 16, 1
	v_lshrrev_b32_e32 v28, 16, v28
	v_add3_u32 v50, v62, v50, s46
	v_and_or_b32 v50, v50, s47, v28
	s_waitcnt lgkmcnt(1)
	v_bfe_u32 v28, v64, 16, 1
	v_add3_u32 v28, v64, v28, s46
	s_waitcnt lgkmcnt(0)
	v_bfe_u32 v51, v66, 16, 1
	v_ashrrev_i32_e32 v71, 31, v70
	v_lshrrev_b32_e32 v28, 16, v28
	v_add3_u32 v51, v66, v51, s46
	v_lshlrev_b64 v[70:71], 11, v[70:71]
	v_and_or_b32 v51, v51, s47, v28
	v_lshl_add_u64 v[70:71], v[52:53], 0, v[70:71]
	v_bfe_u32 v28, v55, 16, 1
	global_store_dwordx4 v[70:71], v[48:51], off nt
	v_add3_u32 v28, v55, v28, s46
	v_lshrrev_b32_e32 v28, 16, v28
	v_bfe_u32 v48, v29, 16, 1
	v_add3_u32 v29, v29, v48, s46
	v_and_or_b32 v48, v29, s47, v28
	v_bfe_u32 v28, v57, 16, 1
	v_add3_u32 v28, v57, v28, s46
	v_bfe_u32 v29, v59, 16, 1
	v_lshrrev_b32_e32 v28, 16, v28
	v_add3_u32 v29, v59, v29, s46
	v_and_or_b32 v49, v29, s47, v28
	v_bfe_u32 v28, v61, 16, 1
	v_add3_u32 v28, v61, v28, s46
	v_bfe_u32 v29, v63, 16, 1
	v_lshrrev_b32_e32 v28, 16, v28
	v_add3_u32 v29, v63, v29, s46
	v_and_or_b32 v50, v29, s47, v28
	v_bfe_u32 v28, v65, 16, 1
	v_add3_u32 v28, v65, v28, s46
	v_bfe_u32 v29, v67, 16, 1
	v_lshrrev_b32_e32 v28, 16, v28
	v_add3_u32 v29, v67, v29, s46
	v_and_or_b32 v51, v29, s47, v28
	v_add_u32_e32 v28, 24, v68
	v_ashrrev_i32_e32 v29, 31, v28
	v_lshlrev_b64 v[28:29], 11, v[28:29]
	v_lshl_add_u64 v[28:29], v[52:53], 0, v[28:29]
	global_store_dwordx4 v[28:29], v[48:51], off nt
	s_waitcnt lgkmcnt(0)
	s_branch .LBB0_1131

; __device__ __forceinline__ void tr_item8(const float* W, int ld, int K, int nblk, int item, unsigned char* WT, bool gu, float scale, LAS float* scr, int lane) {
;     const int kb = item / nblk, nb = item % nblk, k0 = 64 * kb, n0 = 32 * nb;
;     int drow0 = n0;
;     if (gu) { const int bj = n0 / FF, j = n0 - bj * FF; drow0 = 256 * (j / 128) + 128 * bj + (j % 128); }
;     { float t_[32];
; #pragma unroll
;       for (int i = 0; i < 32; ++i) t_[i] = W[(size_t)(k0 + 2 * i + (lane >> 5)) * ld + n0 + (lane & 31)];
; __device__ __forceinline__ void convert_items(Frame& F, const Args& a, int lo, int hi, int w, int nw) {
;     ...
;         int r = it;
;         if (r < I_FI) { tr_item(a.in[7], 3 * D + 16, D, 96, r, (bf16*)(F.ws + WS_WFOXIN), false, scr, lane); continue; } r -= I_FI;
;         if (r < I_FO) { tr_item(a.in[9], D, D, 32, r, (bf16*)(F.ws + WS_WFOXOUT), false, scr, lane); continue; } r -= I_FO;
;         if (r < I_SI) { tr_item(a.in[10], D + 512, D, 48, r, (bf16*)(F.ws + WS_WSWAIN), false, scr, lane); continue; } r -= I_SI;
;         if (r < I_SO) { tr_item(a.in[12], D, D, 32, r, (bf16*)(F.ws + WS_WSWAOUT), false, scr, lane); continue; } r -= I_SO;
;         if (r < I_GU) { tr_item8(a.in[14], 2 * FF, D, 224, r, F.ws + WS_WGU, true, WSC_GU, scr, lane); continue; } r -= I_GU;
;         if (r < I_DN) { tr_item8(a.in[15], D, FF, 32, r, F.ws + WS_WDN, false, WSC_DN, scr, lane); continue; } r -= I_DN;
;         if (r < NE * I_GU) { const int e = r / I_GU, rr = r % I_GU; tr_item8(a.in[18] + (size_t)e * D * 2 * FF, 2 * FF, D, 224, rr, F.ws + WS_WMGU + (size_t)e * 2 * FF * D, true, WSC_GU, scr, lane); continue; } r -= NE * I_GU;
.LBB0_1161:
	s_cmpk_gt_i32 s16, 0x5ff
	s_mov_b64 s[6:7], -1
	s_cbranch_scc0 .LBB0_1183
	s_cmpk_gt_u32 s16, 0x7ff
	s_cbranch_scc0 .LBB0_1180
	s_cmpk_gt_u32 s16, 0xaff
	s_cbranch_scc0 .LBB0_1177
	s_cmpk_gt_u32 s16, 0xcff
	s_cbranch_scc0 .LBB0_1174
	s_cmpk_gt_u32 s16, 0x1aff
	s_cbranch_scc0 .LBB0_1171
	s_cmpk_gt_u32 s16, 0x21ff
	s_cbranch_scc0 .LBB0_1168
	s_add_i32 s4, s16, 0xde00
	s_bfe_u32 s6, s4, 0x70009
	s_mulk_i32 s6, 0x2493
	s_lshr_b32 s6, s6, 16
	s_mul_i32 s7, s6, 0xe00
	s_sub_i32 s4, s4, s7
	s_mul_i32 s7, s6, 0x1c00000
	s_add_u32 s8, s72, s7
	s_addc_u32 s9, s73, 0
	s_mul_i32 s6, s6, 0x700000
	s_add_u32 s6, s3, s6
	s_addc_u32 s7, s30, 0
	s_bfe_u32 s25, s4, 0xb0005
	s_mulk_i32 s25, 0x2493
	s_lshr_b32 s25, s25, 16
	s_mul_i32 s26, s25, 0xe0
	s_sub_i32 s26, s4, s26
	s_lshl_b32 s4, s26, 5
	s_and_b32 s27, s26, 0xffff
	s_cmpk_gt_u32 s27, 0x6f
	s_cselect_b32 s27, 0xfffff200, 0
	s_cselect_b32 s31, 0x80, 0
	s_add_i32 s4, s27, s4
	s_sext_i32_i16 s27, s4
	s_bfe_u32 s27, s27, 0x70018
	s_add_i32 s27, s4, s27
	s_sext_i32_i16 s36, s27
	s_and_b32 s27, s27, 0xff80
	s_sub_i32 s4, s4, s27
	s_lshl_b32 s36, s36, 1
	s_sext_i32_i16 s4, s4
	s_and_b32 s36, s36, 0xffffff00
	s_add_i32 s4, s31, s4
	s_lshl_b32 s26, s26, 7
	s_add_i32 s4, s4, s36
	s_lshl_b32 s25, s25, 6
	s_and_b32 s26, s26, 0x3ff80
	s_add_u32 s8, s8, s26
	s_addc_u32 s9, s9, 0
	v_add_u32_e32 v64, s25, v28
	v_lshl_add_u64 v[46:47], s[8:9], 0, v[0:1]
	v_mad_i64_i32 v[48:49], s[8:9], v64, s13, v[46:47]
	v_add_u32_e32 v50, 2, v64
	v_add_u32_e32 v52, 4, v64
	v_add_u32_e32 v54, 6, v64
	v_add_u32_e32 v56, 8, v64
	v_add_u32_e32 v58, 10, v64
	v_add_u32_e32 v60, 12, v64
	v_add_u32_e32 v62, 14, v64
	v_mad_i64_i32 v[50:51], s[8:9], v50, s13, v[46:47]
	v_mad_i64_i32 v[52:53], s[8:9], v52, s13, v[46:47]
	v_mad_i64_i32 v[54:55], s[8:9], v54, s13, v[46:47]
	v_mad_i64_i32 v[56:57], s[8:9], v56, s13, v[46:47]
	v_mad_i64_i32 v[58:59], s[8:9], v58, s13, v[46:47]
	v_mad_i64_i32 v[60:61], s[8:9], v60, s13, v[46:47]
	v_mad_i64_i32 v[62:63], s[8:9], v62, s13, v[46:47]
	global_load_dword v65, v[48:49], off nt
	global_load_dword v66, v[50:51], off nt
	global_load_dword v67, v[52:53], off nt
	global_load_dword v68, v[54:55], off nt
	global_load_dword v69, v[56:57], off nt
	global_load_dword v70, v[58:59], off nt
	global_load_dword v71, v[60:61], off nt
	global_load_dword v72, v[62:63], off nt
	v_add_u32_e32 v48, 16, v64
	v_mad_i64_i32 v[48:49], s[8:9], v48, s13, v[46:47]
	v_add_u32_e32 v50, 18, v64
	v_add_u32_e32 v52, 20, v64
	v_add_u32_e32 v54, 22, v64
	v_add_u32_e32 v56, 24, v64
	v_add_u32_e32 v58, 26, v64
	v_add_u32_e32 v60, 28, v64
	v_add_u32_e32 v62, 30, v64
	v_mad_i64_i32 v[50:51], s[8:9], v50, s13, v[46:47]
	v_mad_i64_i32 v[52:53], s[8:9], v52, s13, v[46:47]
	v_mad_i64_i32 v[54:55], s[8:9], v54, s13, v[46:47]
	v_mad_i64_i32 v[56:57], s[8:9], v56, s13, v[46:47]
	v_mad_i64_i32 v[58:59], s[8:9], v58, s13, v[46:47]
	v_mad_i64_i32 v[60:61], s[8:9], v60, s13, v[46:47]
	v_mad_i64_i32 v[62:63], s[8:9], v62, s13, v[46:47]
	global_load_dword v73, v[48:49], off nt
	global_load_dword v74, v[50:51], off nt
	global_load_dword v75, v[52:53], off nt
	global_load_dword v76, v[54:55], off nt
	global_load_dword v77, v[56:57], off nt
	global_load_dword v78, v[58:59], off nt
	global_load_dword v79, v[60:61], off nt
	global_load_dword v80, v[62:63], off nt
	v_add_u32_e32 v48, 32, v64
	v_add_u32_e32 v50, 34, v64
	v_add_u32_e32 v52, 36, v64
	v_add_u32_e32 v54, 38, v64
	v_add_u32_e32 v60, 44, v64
	v_mad_i64_i32 v[48:49], s[8:9], v48, s13, v[46:47]
	v_mad_i64_i32 v[50:51], s[8:9], v50, s13, v[46:47]
	v_mad_i64_i32 v[52:53], s[8:9], v52, s13, v[46:47]
	v_mad_i64_i32 v[54:55], s[8:9], v54, s13, v[46:47]
	v_add_u32_e32 v56, 40, v64
	v_add_u32_e32 v58, 42, v64
	v_mad_i64_i32 v[60:61], s[8:9], v60, s13, v[46:47]
	v_add_u32_e32 v62, 46, v64
	v_mad_i64_i32 v[56:57], s[8:9], v56, s13, v[46:47]
	v_mad_i64_i32 v[58:59], s[8:9], v58, s13, v[46:47]
	v_mad_i64_i32 v[62:63], s[8:9], v62, s13, v[46:47]
	global_load_dword v81, v[48:49], off nt
	global_load_dword v82, v[50:51], off nt
	global_load_dword v83, v[52:53], off nt
	global_load_dword v84, v[54:55], off nt
	global_load_dword v85, v[56:57], off nt
	global_load_dword v86, v[58:59], off nt
	s_nop 0
	global_load_dword v60, v[60:61], off nt
	s_nop 0
	global_load_dword v61, v[62:63], off nt
	v_add_u32_e32 v48, 48, v64
	v_add_u32_e32 v50, 50, v64
	v_add_u32_e32 v52, 52, v64
	v_add_u32_e32 v54, 54, v64
	v_mad_i64_i32 v[48:49], s[8:9], v48, s13, v[46:47]
	v_mad_i64_i32 v[50:51], s[8:9], v50, s13, v[46:47]
	v_mad_i64_i32 v[52:53], s[8:9], v52, s13, v[46:47]
	v_mad_i64_i32 v[54:55], s[8:9], v54, s13, v[46:47]
	v_add_u32_e32 v56, 56, v64
	v_add_u32_e32 v58, 58, v64
	v_mad_i64_i32 v[56:57], s[8:9], v56, s13, v[46:47]
	v_mad_i64_i32 v[58:59], s[8:9], v58, s13, v[46:47]
	global_load_dword v62, v[48:49], off nt
	s_nop 0
	global_load_dword v50, v[50:51], off nt
	s_nop 0
	global_load_dword v51, v[52:53], off nt
	s_nop 0
	global_load_dword v52, v[54:55], off nt
	global_load_dword v53, v[56:57], off nt
	s_nop 0
	global_load_dword v54, v[58:59], off nt
	v_add_u32_e32 v48, 60, v64
	v_add_u32_e32 v55, 62, v64
	v_mad_i64_i32 v[48:49], s[8:9], v48, s13, v[46:47]
	v_mad_i64_i32 v[46:47], s[8:9], v55, s13, v[46:47]
	global_load_dword v48, v[48:49], off nt
	s_nop 0
	global_load_dword v46, v[46:47], off nt
	s_waitcnt vmcnt(0)
; __device__ __forceinline__ unsigned cvt_pk4_fp8(float a, float b, float c, float d) { int w = 0; w = __builtin_amdgcn_cvt_pk_fp8_f32(a, b, w, false); w = __builtin_amdgcn_cvt_pk_fp8_f32(c, d, w, true); return (unsigned)w; }
; #define GAS __attribute__((address_space(1)))
; #define LAS __attribute__((address_space(3)))
; #define LDS_WAIT() asm volatile("s_waitcnt lgkmcnt(0)" ::: "memory")
; __device__ __forceinline__ void tr_item8(const float* W, int ld, int K, int nblk, int item, unsigned char* WT, bool gu, float scale, LAS float* scr, int lane) {
;     ...
; #pragma unroll
;       for (int i = 0; i < 32; ++i) scr[(2 * i + (lane >> 5)) * 33 + (lane & 31)] = t_[i] * scale; }
;     LDS_WAIT(); asm volatile("" ::: "memory");
;     const int c = lane & 3;
; #pragma unroll
;     for (int j = 0; j < 2; ++j) { const int n = (lane >> 2) + 16 * j; const LAS float* sp = scr + (16 * c) * 33 + n;
;         v4u o; o.x = pg8::cvt_pk4_fp8(sp[0 * 33], sp[1 * 33], sp[2 * 33], sp[3 * 33]); o.y = pg8::cvt_pk4_fp8(sp[4 * 33], sp[5 * 33], sp[6 * 33], sp[7 * 33]);
;         o.z = pg8::cvt_pk4_fp8(sp[8 * 33], sp[9 * 33], sp[10 * 33], sp[11 * 33]); o.w = pg8::cvt_pk4_fp8(sp[12 * 33], sp[13 * 33], sp[14 * 33], sp[15 * 33]);
;         *(GAS v4u*)(WT + (size_t)(drow0 + n) * K + k0 + 16 * c) = o; }
;     LDS_WAIT(); asm volatile("" ::: "memory");
	v_mul_f32_e32 v47, 0x42800000, v65
	v_mul_f32_e32 v49, 0x42800000, v66
	ds_write2_b32 v29, v47, v49 offset1:66
	v_mul_f32_e32 v47, 0x42800000, v67
	v_mul_f32_e32 v49, 0x42800000, v68
	ds_write2_b32 v29, v47, v49 offset0:132 offset1:198
	v_mul_f32_e32 v47, 0x42800000, v69
	v_mul_f32_e32 v49, 0x42800000, v70
	ds_write2_b32 v38, v47, v49 offset0:8 offset1:74
	v_mul_f32_e32 v47, 0x42800000, v71
	v_mul_f32_e32 v49, 0x42800000, v72
	ds_write2_b32 v38, v47, v49 offset0:140 offset1:206
	s_add_u32 s6, s6, s25
	s_addc_u32 s7, s7, 0
	v_mul_f32_e32 v47, 0x42800000, v73
	v_mul_f32_e32 v49, 0x42800000, v74
	ds_write2_b32 v39, v47, v49 offset0:16 offset1:82
	v_mul_f32_e32 v47, 0x42800000, v75
	v_mul_f32_e32 v49, 0x42800000, v76
	ds_write2_b32 v39, v47, v49 offset0:148 offset1:214
	v_mul_f32_e32 v47, 0x42800000, v77
	v_mul_f32_e32 v49, 0x42800000, v78
	ds_write2_b32 v40, v47, v49 offset0:24 offset1:90
	v_mul_f32_e32 v47, 0x42800000, v79
	v_mul_f32_e32 v49, 0x42800000, v80
	ds_write2_b32 v40, v47, v49 offset0:156 offset1:222
	v_mul_f32_e32 v47, 0x42800000, v81
	v_mul_f32_e32 v49, 0x42800000, v82
	ds_write2_b32 v41, v47, v49 offset0:32 offset1:98
	v_mul_f32_e32 v47, 0x42800000, v83
	v_mul_f32_e32 v49, 0x42800000, v84
	ds_write2_b32 v41, v47, v49 offset0:164 offset1:230
	v_mul_f32_e32 v47, 0x42800000, v85
	v_mul_f32_e32 v49, 0x42800000, v86
	ds_write2_b32 v42, v47, v49 offset0:40 offset1:106
	v_mul_f32_e32 v47, 0x42800000, v60
	v_mul_f32_e32 v49, 0x42800000, v61
	ds_write2_b32 v42, v47, v49 offset0:172 offset1:238
	v_add_u32_e32 v84, s4, v30
	v_ashrrev_i32_e32 v85, 31, v84
	v_lshlrev_b64 v[84:85], 10, v[84:85]
	v_mul_f32_e32 v47, 0x42800000, v62
	v_mul_f32_e32 v49, 0x42800000, v50
	ds_write2_b32 v43, v47, v49 offset0:48 offset1:114
	v_mul_f32_e32 v47, 0x42800000, v51
	v_mul_f32_e32 v49, 0x42800000, v52
	ds_write2_b32 v43, v47, v49 offset0:180 offset1:246
	v_mul_f32_e32 v47, 0x42800000, v53
	v_mul_f32_e32 v49, 0x42800000, v54
	ds_write2_b32 v44, v47, v49 offset0:56 offset1:122
	v_mov_b32_e32 v49, v1
	v_lshl_add_u64 v[50:51], s[6:7], 0, v[2:3]
	v_mul_f32_e32 v47, 0x42800000, v48
	v_mul_f32_e32 v46, 0x42800000, v46
	ds_write2_b32 v44, v47, v46 offset0:188 offset1:254
	s_waitcnt lgkmcnt(0)
	ds_read2_b32 v[52:53], v31 offset1:16
	ds_read2_b32 v[54:55], v31 offset0:33 offset1:49
	ds_read2_b32 v[56:57], v31 offset0:66 offset1:82
	ds_read2_b32 v[58:59], v31 offset0:99 offset1:115
	ds_read2_b32 v[60:61], v31 offset0:132 offset1:148
	ds_read2_b32 v[62:63], v31 offset0:165 offset1:181
	ds_read2_b32 v[64:65], v31 offset0:198 offset1:214
	ds_read2_b32 v[66:67], v31 offset0:231 offset1:247
	ds_read2_b32 v[68:69], v45 offset0:8 offset1:24
	ds_read2_b32 v[70:71], v45 offset0:41 offset1:57
	ds_read2_b32 v[72:73], v45 offset0:74 offset1:90
	ds_read2_b32 v[74:75], v45 offset0:107 offset1:123
	ds_read2_b32 v[76:77], v45 offset0:140 offset1:156
	ds_read2_b32 v[78:79], v45 offset0:173 offset1:189
	v_mov_b32_e32 v46, v1
	v_mov_b32_e32 v47, v1
	v_mov_b32_e32 v48, v1
	ds_read2_b32 v[80:81], v45 offset0:206 offset1:222
	ds_read2_b32 v[82:83], v45 offset0:239 offset1:255
	s_waitcnt lgkmcnt(14)
	v_cvt_pk_fp8_f32 v46, v52, v54
	s_waitcnt lgkmcnt(10)
	v_cvt_pk_fp8_f32 v47, v60, v62
	s_waitcnt lgkmcnt(6)
	v_cvt_pk_fp8_f32 v48, v68, v70
	s_waitcnt lgkmcnt(2)
	v_cvt_pk_fp8_f32 v49, v76, v78
	v_cvt_pk_fp8_f32 v46, v56, v58 op_sel:[0,0,1]
	v_cvt_pk_fp8_f32 v47, v64, v66 op_sel:[0,0,1]
	v_cvt_pk_fp8_f32 v48, v72, v74 op_sel:[0,0,1]
	s_waitcnt lgkmcnt(0)
	v_cvt_pk_fp8_f32 v49, v80, v82 op_sel:[0,0,1]
	v_lshl_add_u64 v[84:85], v[50:51], 0, v[84:85]
	v_add_u32_e32 v52, s4, v32
	s_mov_b64 s[6:7], 0
	global_store_dwordx4 v[84:85], v[46:49], off nt
	s_nop 1
	v_mov_b32_e32 v46, v1
	v_mov_b32_e32 v47, v1
	v_mov_b32_e32 v48, v1
	v_mov_b32_e32 v49, v1
	v_cvt_pk_fp8_f32 v46, v53, v55
	v_cvt_pk_fp8_f32 v47, v61, v63
	v_cvt_pk_fp8_f32 v48, v69, v71
	v_cvt_pk_fp8_f32 v49, v77, v79
	v_cvt_pk_fp8_f32 v46, v57, v59 op_sel:[0,0,1]
	v_cvt_pk_fp8_f32 v47, v65, v67 op_sel:[0,0,1]
	v_cvt_pk_fp8_f32 v48, v73, v75 op_sel:[0,0,1]
	v_cvt_pk_fp8_f32 v49, v81, v83 op_sel:[0,0,1]
	v_ashrrev_i32_e32 v53, 31, v52
	v_lshlrev_b64 v[52:53], 10, v[52:53]
	v_lshl_add_u64 v[50:51], v[50:51], 0, v[52:53]
	global_store_dwordx4 v[50:51], v[46:49], off nt
	s_waitcnt lgkmcnt(0)
; __device__ __forceinline__ void tr_item8(const float* W, int ld, int K, int nblk, int item, unsigned char* WT, bool gu, float scale, LAS float* scr, int lane) {
;     const int kb = item / nblk, nb = item % nblk, k0 = 64 * kb, n0 = 32 * nb;
;     int drow0 = n0;
;     if (gu) { const int bj = n0 / FF, j = n0 - bj * FF; drow0 = 256 * (j / 128) + 128 * bj + (j % 128); }
;     { float t_[32];
; #pragma unroll
;       for (int i = 0; i < 32; ++i) t_[i] = W[(size_t)(k0 + 2 * i + (lane >> 5)) * ld + n0 + (lane & 31)];
; __device__ __forceinline__ void convert_items(Frame& F, const Args& a, int lo, int hi, int w, int nw) {
;     ...
;         if (r < I_DN) { tr_item8(a.in[15], D, FF, 32, r, F.ws + WS_WDN, false, WSC_DN, scr, lane); continue; } r -= I_DN;
.LBB0_1168:
	s_andn2_b64 vcc, exec, s[6:7]
	s_cbranch_vccnz .LBB0_1170
	s_lshl_b32 s4, s16, 5
	s_and_b32 s6, s11, 0x1ffc0
	s_and_b32 s8, s4, 0x3e0
	v_add_u32_e32 v46, s6, v28
	s_lshl_b32 s4, s8, 2
	v_ashrrev_i32_e32 v47, 31, v46
	v_lshl_add_u64 v[48:49], v[4:5], 0, s[4:5]
	v_lshlrev_b64 v[46:47], 12, v[46:47]
	v_lshl_add_u64 v[46:47], v[48:49], 0, v[46:47]
	v_add_co_u32_e32 v48, vcc, 0x2000, v46
	s_mov_b32 s7, s5
	s_nop 0
	v_addc_co_u32_e32 v49, vcc, 0, v47, vcc
	v_add_co_u32_e32 v50, vcc, 0x4000, v46
	s_nop 1
	v_addc_co_u32_e32 v51, vcc, 0, v47, vcc
	v_add_co_u32_e32 v52, vcc, 0x6000, v46
	s_nop 1
	v_addc_co_u32_e32 v53, vcc, 0, v47, vcc
	v_add_co_u32_e32 v54, vcc, 0x8000, v46
	s_nop 1
	v_addc_co_u32_e32 v55, vcc, 0, v47, vcc
	v_add_co_u32_e32 v56, vcc, 0xa000, v46
	s_nop 1
	v_addc_co_u32_e32 v57, vcc, 0, v47, vcc
	v_add_co_u32_e32 v58, vcc, 0xc000, v46
	s_nop 1
	v_addc_co_u32_e32 v59, vcc, 0, v47, vcc
	v_add_co_u32_e32 v60, vcc, 0xe000, v46
	s_nop 1
	v_addc_co_u32_e32 v61, vcc, 0, v47, vcc
	global_load_dword v64, v[46:47], off nt
	global_load_dword v65, v[48:49], off nt
	global_load_dword v66, v[50:51], off nt
	global_load_dword v67, v[52:53], off nt
	global_load_dword v68, v[54:55], off nt
	global_load_dword v69, v[56:57], off nt
	global_load_dword v70, v[58:59], off nt
	global_load_dword v71, v[60:61], off nt
	v_add_co_u32_e32 v48, vcc, 0x10000, v46
	s_nop 1
	v_addc_co_u32_e32 v49, vcc, 0, v47, vcc
	v_add_co_u32_e32 v50, vcc, 0x12000, v46
	s_nop 1
	v_addc_co_u32_e32 v51, vcc, 0, v47, vcc
	v_add_co_u32_e32 v52, vcc, 0x14000, v46
	s_nop 1
	v_addc_co_u32_e32 v53, vcc, 0, v47, vcc
	v_add_co_u32_e32 v54, vcc, 0x16000, v46
	s_nop 1
	v_addc_co_u32_e32 v55, vcc, 0, v47, vcc
	v_add_co_u32_e32 v56, vcc, 0x18000, v46
	s_nop 1
	v_addc_co_u32_e32 v57, vcc, 0, v47, vcc
	v_add_co_u32_e32 v58, vcc, 0x1a000, v46
	s_nop 1
	v_addc_co_u32_e32 v59, vcc, 0, v47, vcc
	v_add_co_u32_e32 v60, vcc, 0x1c000, v46
	s_nop 1
	v_addc_co_u32_e32 v61, vcc, 0, v47, vcc
	v_add_co_u32_e32 v62, vcc, 0x1e000, v46
	s_nop 1
	v_addc_co_u32_e32 v63, vcc, 0, v47, vcc
	global_load_dword v72, v[48:49], off nt
	global_load_dword v73, v[50:51], off nt
	global_load_dword v74, v[52:53], off nt
	global_load_dword v75, v[54:55], off nt
	global_load_dword v76, v[56:57], off nt
	global_load_dword v77, v[58:59], off nt
	global_load_dword v78, v[60:61], off nt
	global_load_dword v79, v[62:63], off nt
	v_add_co_u32_e32 v48, vcc, 0x20000, v46
	s_nop 1
	v_addc_co_u32_e32 v49, vcc, 0, v47, vcc
	v_add_co_u32_e32 v50, vcc, 0x22000, v46
	s_nop 1
	v_addc_co_u32_e32 v51, vcc, 0, v47, vcc
	v_add_co_u32_e32 v52, vcc, 0x24000, v46
	s_nop 1
	v_addc_co_u32_e32 v53, vcc, 0, v47, vcc
	v_add_co_u32_e32 v54, vcc, 0x26000, v46
	s_nop 1
	v_addc_co_u32_e32 v55, vcc, 0, v47, vcc
	v_add_co_u32_e32 v56, vcc, 0x28000, v46
	s_nop 1
	v_addc_co_u32_e32 v57, vcc, 0, v47, vcc
	v_add_co_u32_e32 v58, vcc, 0x2a000, v46
	s_nop 1
	v_addc_co_u32_e32 v59, vcc, 0, v47, vcc
	v_add_co_u32_e32 v60, vcc, 0x2c000, v46
	s_nop 1
	v_addc_co_u32_e32 v61, vcc, 0, v47, vcc
	v_add_co_u32_e32 v62, vcc, 0x2e000, v46
	s_nop 1
	v_addc_co_u32_e32 v63, vcc, 0, v47, vcc
	global_load_dword v80, v[48:49], off nt
	global_load_dword v81, v[50:51], off nt
	global_load_dword v82, v[52:53], off nt
	global_load_dword v83, v[54:55], off nt
	global_load_dword v84, v[56:57], off nt
	global_load_dword v85, v[58:59], off nt
	s_nop 0
	global_load_dword v60, v[60:61], off nt
	s_nop 0
	global_load_dword v61, v[62:63], off nt
	v_add_co_u32_e32 v48, vcc, 0x30000, v46
	s_nop 1
	v_addc_co_u32_e32 v49, vcc, 0, v47, vcc
	v_add_co_u32_e32 v50, vcc, 0x32000, v46
	s_nop 1
	v_addc_co_u32_e32 v51, vcc, 0, v47, vcc
	v_add_co_u32_e32 v52, vcc, 0x34000, v46
	s_nop 1
	v_addc_co_u32_e32 v53, vcc, 0, v47, vcc
	v_add_co_u32_e32 v54, vcc, 0x36000, v46
	s_nop 1
	v_addc_co_u32_e32 v55, vcc, 0, v47, vcc
	v_add_co_u32_e32 v56, vcc, 0x38000, v46
	s_nop 1
	v_addc_co_u32_e32 v57, vcc, 0, v47, vcc
	v_add_co_u32_e32 v58, vcc, 0x3a000, v46
	s_nop 1
	v_addc_co_u32_e32 v59, vcc, 0, v47, vcc
	global_load_dword v62, v[48:49], off nt
	s_nop 0
	global_load_dword v50, v[50:51], off nt
	s_nop 0
	global_load_dword v51, v[52:53], off nt
	s_nop 0
	global_load_dword v52, v[54:55], off nt
	global_load_dword v53, v[56:57], off nt
	s_nop 0
	global_load_dword v54, v[58:59], off nt
	v_add_co_u32_e32 v48, vcc, 0x3c000, v46
	s_nop 1
	v_addc_co_u32_e32 v49, vcc, 0, v47, vcc
	v_add_co_u32_e32 v46, vcc, 0x3e000, v46
	s_nop 1
	v_addc_co_u32_e32 v47, vcc, 0, v47, vcc
	global_load_dword v48, v[48:49], off nt
	s_nop 0
	global_load_dword v46, v[46:47], off nt
	s_waitcnt vmcnt(0)
; __device__ __forceinline__ unsigned cvt_pk4_fp8(float a, float b, float c, float d) { int w = 0; w = __builtin_amdgcn_cvt_pk_fp8_f32(a, b, w, false); w = __builtin_amdgcn_cvt_pk_fp8_f32(c, d, w, true); return (unsigned)w; }
; #define GAS __attribute__((address_space(1)))
; #define LAS __attribute__((address_space(3)))
; #define LDS_WAIT() asm volatile("s_waitcnt lgkmcnt(0)" ::: "memory")
; __device__ __forceinline__ void tr_item8(const float* W, int ld, int K, int nblk, int item, unsigned char* WT, bool gu, float scale, LAS float* scr, int lane) {
;     ...
; #pragma unroll
;       for (int i = 0; i < 32; ++i) scr[(2 * i + (lane >> 5)) * 33 + (lane & 31)] = t_[i] * scale; }
;     LDS_WAIT(); asm volatile("" ::: "memory");
;     const int c = lane & 3;
; #pragma unroll
;     for (int j = 0; j < 2; ++j) { const int n = (lane >> 2) + 16 * j; const LAS float* sp = scr + (16 * c) * 33 + n;
;         v4u o; o.x = pg8::cvt_pk4_fp8(sp[0 * 33], sp[1 * 33], sp[2 * 33], sp[3 * 33]); o.y = pg8::cvt_pk4_fp8(sp[4 * 33], sp[5 * 33], sp[6 * 33], sp[7 * 33]);
;         o.z = pg8::cvt_pk4_fp8(sp[8 * 33], sp[9 * 33], sp[10 * 33], sp[11 * 33]); o.w = pg8::cvt_pk4_fp8(sp[12 * 33], sp[13 * 33], sp[14 * 33], sp[15 * 33]);
;         *(GAS v4u*)(WT + (size_t)(drow0 + n) * K + k0 + 16 * c) = o; }
;     LDS_WAIT(); asm volatile("" ::: "memory");
	v_mul_f32_e32 v47, 0x43000000, v64
	v_mul_f32_e32 v49, 0x43000000, v65
	ds_write2_b32 v29, v47, v49 offset1:66
	v_mul_f32_e32 v47, 0x43000000, v66
	v_mul_f32_e32 v49, 0x43000000, v67
	ds_write2_b32 v29, v47, v49 offset0:132 offset1:198
	v_mul_f32_e32 v47, 0x43000000, v68
	v_mul_f32_e32 v49, 0x43000000, v69
	ds_write2_b32 v38, v47, v49 offset0:8 offset1:74
	v_mul_f32_e32 v47, 0x43000000, v70
	v_mul_f32_e32 v49, 0x43000000, v71
	ds_write2_b32 v38, v47, v49 offset0:140 offset1:206
	v_mul_f32_e32 v47, 0x43000000, v72
	v_mul_f32_e32 v49, 0x43000000, v73
	ds_write2_b32 v39, v47, v49 offset0:16 offset1:82
	v_mul_f32_e32 v47, 0x43000000, v74
	v_mul_f32_e32 v49, 0x43000000, v75
	ds_write2_b32 v39, v47, v49 offset0:148 offset1:214
	v_mul_f32_e32 v47, 0x43000000, v76
	v_mul_f32_e32 v49, 0x43000000, v77
	ds_write2_b32 v40, v47, v49 offset0:24 offset1:90
	v_mul_f32_e32 v47, 0x43000000, v78
	v_mul_f32_e32 v49, 0x43000000, v79
	ds_write2_b32 v40, v47, v49 offset0:156 offset1:222
	v_mul_f32_e32 v47, 0x43000000, v80
	v_mul_f32_e32 v49, 0x43000000, v81
	ds_write2_b32 v41, v47, v49 offset0:32 offset1:98
	v_mul_f32_e32 v47, 0x43000000, v82
	v_mul_f32_e32 v49, 0x43000000, v83
	ds_write2_b32 v41, v47, v49 offset0:164 offset1:230
	v_mul_f32_e32 v47, 0x43000000, v84
	v_mul_f32_e32 v49, 0x43000000, v85
	ds_write2_b32 v42, v47, v49 offset0:40 offset1:106
	v_mul_f32_e32 v47, 0x43000000, v60
	v_mul_f32_e32 v49, 0x43000000, v61
	ds_write2_b32 v42, v47, v49 offset0:172 offset1:238
	v_mul_f32_e32 v47, 0x43000000, v62
	v_mul_f32_e32 v49, 0x43000000, v50
	ds_write2_b32 v43, v47, v49 offset0:48 offset1:114
	v_mul_f32_e32 v47, 0x43000000, v51
	v_mul_f32_e32 v49, 0x43000000, v52
	ds_write2_b32 v43, v47, v49 offset0:180 offset1:246
	v_mul_f32_e32 v47, 0x43000000, v53
	v_mul_f32_e32 v49, 0x43000000, v54
	ds_write2_b32 v44, v47, v49 offset0:56 offset1:122
	v_mov_b32_e32 v49, 0
	v_lshl_add_u64 v[50:51], v[18:19], 0, s[6:7]
	v_mul_f32_e32 v47, 0x43000000, v48
	v_mul_f32_e32 v46, 0x43000000, v46
	ds_write2_b32 v44, v47, v46 offset0:188 offset1:254
	s_waitcnt lgkmcnt(0)
	ds_read2_b32 v[52:53], v31 offset1:16
	ds_read2_b32 v[54:55], v31 offset0:33 offset1:49
	ds_read2_b32 v[56:57], v31 offset0:66 offset1:82
	ds_read2_b32 v[58:59], v31 offset0:99 offset1:115
	ds_read2_b32 v[60:61], v31 offset0:132 offset1:148
	ds_read2_b32 v[62:63], v31 offset0:165 offset1:181
	ds_read2_b32 v[64:65], v31 offset0:198 offset1:214
	ds_read2_b32 v[66:67], v31 offset0:231 offset1:247
	ds_read2_b32 v[68:69], v45 offset0:8 offset1:24
	ds_read2_b32 v[70:71], v45 offset0:41 offset1:57
	ds_read2_b32 v[72:73], v45 offset0:74 offset1:90
	ds_read2_b32 v[74:75], v45 offset0:107 offset1:123
	ds_read2_b32 v[76:77], v45 offset0:140 offset1:156
	ds_read2_b32 v[78:79], v45 offset0:173 offset1:189
	v_mov_b32_e32 v46, 0
	v_mov_b32_e32 v47, 0
	v_mov_b32_e32 v48, 0
	ds_read2_b32 v[80:81], v45 offset0:206 offset1:222
	ds_read2_b32 v[82:83], v45 offset0:239 offset1:255
	s_waitcnt lgkmcnt(14)
	v_cvt_pk_fp8_f32 v46, v52, v54
	s_waitcnt lgkmcnt(10)
	v_cvt_pk_fp8_f32 v47, v60, v62
	s_waitcnt lgkmcnt(6)
	v_cvt_pk_fp8_f32 v48, v68, v70
	s_waitcnt lgkmcnt(2)
	v_cvt_pk_fp8_f32 v49, v76, v78
	v_cvt_pk_fp8_f32 v46, v56, v58 op_sel:[0,0,1]
	v_cvt_pk_fp8_f32 v47, v64, v66 op_sel:[0,0,1]
	v_cvt_pk_fp8_f32 v48, v72, v74 op_sel:[0,0,1]
	s_waitcnt lgkmcnt(0)
	v_cvt_pk_fp8_f32 v49, v80, v82 op_sel:[0,0,1]
	v_add_u32_e32 v52, s8, v30
	v_mad_i64_i32 v[84:85], s[6:7], v52, s12, v[50:51]
	global_store_dwordx4 v[84:85], v[46:49], off nt
	v_add_u32_e32 v52, s8, v32
	v_mad_i64_i32 v[50:51], s[6:7], v52, s12, v[50:51]
	v_mov_b32_e32 v46, 0
	v_mov_b32_e32 v47, 0
	v_mov_b32_e32 v48, 0
	v_mov_b32_e32 v49, 0
	v_cvt_pk_fp8_f32 v46, v53, v55
	v_cvt_pk_fp8_f32 v47, v61, v63
	v_cvt_pk_fp8_f32 v48, v69, v71
	v_cvt_pk_fp8_f32 v49, v77, v79
	v_cvt_pk_fp8_f32 v46, v57, v59 op_sel:[0,0,1]
	v_cvt_pk_fp8_f32 v47, v65, v67 op_sel:[0,0,1]
	v_cvt_pk_fp8_f32 v48, v73, v75 op_sel:[0,0,1]
	v_cvt_pk_fp8_f32 v49, v81, v83 op_sel:[0,0,1]
	global_store_dwordx4 v[50:51], v[46:49], off nt
	s_waitcnt lgkmcnt(0)

; __device__ __forceinline__ void tr_item8(const float* W, int ld, int K, int nblk, int item, unsigned char* WT, bool gu, float scale, LAS float* scr, int lane) {
;     const int kb = item / nblk, nb = item % nblk, k0 = 64 * kb, n0 = 32 * nb;
;     int drow0 = n0;
;     if (gu) { const int bj = n0 / FF, j = n0 - bj * FF; drow0 = 256 * (j / 128) + 128 * bj + (j % 128); }
;     { float t_[32];
; #pragma unroll
;       for (int i = 0; i < 32; ++i) t_[i] = W[(size_t)(k0 + 2 * i + (lane >> 5)) * ld + n0 + (lane & 31)];
; __device__ __forceinline__ void convert_items(Frame& F, const Args& a, int lo, int hi, int w, int nw) {
;     ...
;         if (r < I_GU) { tr_item8(a.in[14], 2 * FF, D, 224, r, F.ws + WS_WGU, true, WSC_GU, scr, lane); continue; } r -= I_GU;
.LBB0_1171:
	s_andn2_b64 vcc, exec, s[6:7]
	s_cbranch_vccnz .LBB0_1173
	s_add_i32 s4, s16, 0xf300
	s_bfe_u32 s6, s4, 0xb0005
	s_mulk_i32 s6, 0x2493
	s_lshr_b32 s6, s6, 16
	s_mul_i32 s7, s6, 0xe0
	s_sub_i32 s4, s4, s7
	s_lshl_b32 s7, s4, 5
	s_and_b32 s8, s4, 0xffff
	s_cmpk_gt_u32 s8, 0x6f
	s_cselect_b32 s25, 0xfffff200, 0
	s_cselect_b32 s26, 0x80, 0
	s_lshl_b32 s4, s4, 7
	s_lshl_b32 s6, s6, 6
	s_and_b32 s4, s4, 0x3ff80
	v_add_u32_e32 v64, s6, v28
	v_lshl_add_u64 v[46:47], v[6:7], 0, s[4:5]
	v_mad_i64_i32 v[48:49], s[8:9], v64, s13, v[46:47]
	v_add_u32_e32 v50, 2, v64
	v_add_u32_e32 v52, 4, v64
	v_add_u32_e32 v54, 6, v64
	v_add_u32_e32 v56, 8, v64
	v_add_u32_e32 v58, 10, v64
	v_add_u32_e32 v60, 12, v64
	v_add_u32_e32 v62, 14, v64
	v_mad_i64_i32 v[50:51], s[8:9], v50, s13, v[46:47]
	v_mad_i64_i32 v[52:53], s[8:9], v52, s13, v[46:47]
	v_mad_i64_i32 v[54:55], s[8:9], v54, s13, v[46:47]
	v_mad_i64_i32 v[56:57], s[8:9], v56, s13, v[46:47]
	v_mad_i64_i32 v[58:59], s[8:9], v58, s13, v[46:47]
	v_mad_i64_i32 v[60:61], s[8:9], v60, s13, v[46:47]
	v_mad_i64_i32 v[62:63], s[8:9], v62, s13, v[46:47]
	global_load_dword v65, v[48:49], off nt
	global_load_dword v66, v[50:51], off nt
	global_load_dword v67, v[52:53], off nt
	global_load_dword v68, v[54:55], off nt
	global_load_dword v69, v[56:57], off nt
	global_load_dword v70, v[58:59], off nt
	global_load_dword v71, v[60:61], off nt
	global_load_dword v72, v[62:63], off nt
	v_add_u32_e32 v48, 16, v64
	v_mad_i64_i32 v[48:49], s[8:9], v48, s13, v[46:47]
	v_add_u32_e32 v50, 18, v64
	v_add_u32_e32 v52, 20, v64
	v_add_u32_e32 v54, 22, v64
	v_add_u32_e32 v56, 24, v64
	v_add_u32_e32 v58, 26, v64
	v_add_u32_e32 v60, 28, v64
	v_add_u32_e32 v62, 30, v64
	v_mad_i64_i32 v[50:51], s[8:9], v50, s13, v[46:47]
	v_mad_i64_i32 v[52:53], s[8:9], v52, s13, v[46:47]
	v_mad_i64_i32 v[54:55], s[8:9], v54, s13, v[46:47]
	v_mad_i64_i32 v[56:57], s[8:9], v56, s13, v[46:47]
	v_mad_i64_i32 v[58:59], s[8:9], v58, s13, v[46:47]
	v_mad_i64_i32 v[60:61], s[8:9], v60, s13, v[46:47]
	v_mad_i64_i32 v[62:63], s[8:9], v62, s13, v[46:47]
	global_load_dword v73, v[48:49], off nt
	global_load_dword v74, v[50:51], off nt
	global_load_dword v75, v[52:53], off nt
	global_load_dword v76, v[54:55], off nt
	global_load_dword v77, v[56:57], off nt
	global_load_dword v78, v[58:59], off nt
	global_load_dword v79, v[60:61], off nt
	global_load_dword v80, v[62:63], off nt
	v_add_u32_e32 v48, 32, v64
	v_add_u32_e32 v50, 34, v64
	v_add_u32_e32 v52, 36, v64
	v_add_u32_e32 v54, 38, v64
	v_add_u32_e32 v60, 44, v64
	v_mad_i64_i32 v[48:49], s[8:9], v48, s13, v[46:47]
	v_mad_i64_i32 v[50:51], s[8:9], v50, s13, v[46:47]
	v_mad_i64_i32 v[52:53], s[8:9], v52, s13, v[46:47]
	v_mad_i64_i32 v[54:55], s[8:9], v54, s13, v[46:47]
	v_add_u32_e32 v56, 40, v64
	v_add_u32_e32 v58, 42, v64
	v_mad_i64_i32 v[60:61], s[8:9], v60, s13, v[46:47]
	v_add_u32_e32 v62, 46, v64
	v_mad_i64_i32 v[56:57], s[8:9], v56, s13, v[46:47]
	v_mad_i64_i32 v[58:59], s[8:9], v58, s13, v[46:47]
	v_mad_i64_i32 v[62:63], s[8:9], v62, s13, v[46:47]
	global_load_dword v81, v[48:49], off nt
	global_load_dword v82, v[50:51], off nt
	global_load_dword v83, v[52:53], off nt
	global_load_dword v84, v[54:55], off nt
	global_load_dword v85, v[56:57], off nt
	global_load_dword v86, v[58:59], off nt
	s_nop 0
	global_load_dword v60, v[60:61], off nt
	s_nop 0
	global_load_dword v61, v[62:63], off nt
	v_add_u32_e32 v48, 48, v64
	v_add_u32_e32 v50, 50, v64
	v_add_u32_e32 v52, 52, v64
	v_add_u32_e32 v54, 54, v64
	v_mad_i64_i32 v[48:49], s[8:9], v48, s13, v[46:47]
	v_mad_i64_i32 v[50:51], s[8:9], v50, s13, v[46:47]
	v_mad_i64_i32 v[52:53], s[8:9], v52, s13, v[46:47]
	v_mad_i64_i32 v[54:55], s[8:9], v54, s13, v[46:47]
	v_add_u32_e32 v56, 56, v64
	v_add_u32_e32 v58, 58, v64
	v_mad_i64_i32 v[56:57], s[8:9], v56, s13, v[46:47]
	v_mad_i64_i32 v[58:59], s[8:9], v58, s13, v[46:47]
	global_load_dword v62, v[48:49], off nt
	s_nop 0
	global_load_dword v50, v[50:51], off nt
	s_nop 0
	global_load_dword v51, v[52:53], off nt
	s_nop 0
	global_load_dword v52, v[54:55], off nt
	global_load_dword v53, v[56:57], off nt
	s_nop 0
	global_load_dword v54, v[58:59], off nt
	v_add_u32_e32 v48, 60, v64
	v_add_u32_e32 v55, 62, v64
	v_mad_i64_i32 v[48:49], s[8:9], v48, s13, v[46:47]
	v_mad_i64_i32 v[46:47], s[8:9], v55, s13, v[46:47]
	global_load_dword v48, v[48:49], off nt
	s_nop 0
	global_load_dword v46, v[46:47], off nt
	s_waitcnt vmcnt(0)
; __device__ __forceinline__ unsigned cvt_pk4_fp8(float a, float b, float c, float d) { int w = 0; w = __builtin_amdgcn_cvt_pk_fp8_f32(a, b, w, false); w = __builtin_amdgcn_cvt_pk_fp8_f32(c, d, w, true); return (unsigned)w; }
; #define GAS __attribute__((address_space(1)))
; #define LAS __attribute__((address_space(3)))
; #define LDS_WAIT() asm volatile("s_waitcnt lgkmcnt(0)" ::: "memory")
; __device__ __forceinline__ void tr_item8(const float* W, int ld, int K, int nblk, int item, unsigned char* WT, bool gu, float scale, LAS float* scr, int lane) {
;     ...
; #pragma unroll
;       for (int i = 0; i < 32; ++i) scr[(2 * i + (lane >> 5)) * 33 + (lane & 31)] = t_[i] * scale; }
;     LDS_WAIT(); asm volatile("" ::: "memory");
;     const int c = lane & 3;
; #pragma unroll
;     for (int j = 0; j < 2; ++j) { const int n = (lane >> 2) + 16 * j; const LAS float* sp = scr + (16 * c) * 33 + n;
;         v4u o; o.x = pg8::cvt_pk4_fp8(sp[0 * 33], sp[1 * 33], sp[2 * 33], sp[3 * 33]); o.y = pg8::cvt_pk4_fp8(sp[4 * 33], sp[5 * 33], sp[6 * 33], sp[7 * 33]);
;         o.z = pg8::cvt_pk4_fp8(sp[8 * 33], sp[9 * 33], sp[10 * 33], sp[11 * 33]); o.w = pg8::cvt_pk4_fp8(sp[12 * 33], sp[13 * 33], sp[14 * 33], sp[15 * 33]);
;         *(GAS v4u*)(WT + (size_t)(drow0 + n) * K + k0 + 16 * c) = o; }
;     LDS_WAIT(); asm volatile("" ::: "memory");
	v_mul_f32_e32 v47, 0x42800000, v65
	v_mul_f32_e32 v49, 0x42800000, v66
	ds_write2_b32 v29, v47, v49 offset1:66
	v_mul_f32_e32 v47, 0x42800000, v67
	v_mul_f32_e32 v49, 0x42800000, v68
	ds_write2_b32 v29, v47, v49 offset0:132 offset1:198
	v_mul_f32_e32 v47, 0x42800000, v69
	v_mul_f32_e32 v49, 0x42800000, v70
	ds_write2_b32 v38, v47, v49 offset0:8 offset1:74
	v_mul_f32_e32 v47, 0x42800000, v71
	v_mul_f32_e32 v49, 0x42800000, v72
	ds_write2_b32 v38, v47, v49 offset0:140 offset1:206
	s_add_i32 s4, s25, s7
	s_sext_i32_i16 s7, s4
	s_bfe_u32 s7, s7, 0x70018
	s_add_i32 s7, s4, s7
	s_sext_i32_i16 s8, s7
	s_and_b32 s7, s7, 0xff80
	s_sub_i32 s4, s4, s7
	s_lshl_b32 s8, s8, 1
	s_sext_i32_i16 s4, s4
	v_mul_f32_e32 v47, 0x42800000, v73
	v_mul_f32_e32 v49, 0x42800000, v74
	ds_write2_b32 v39, v47, v49 offset0:16 offset1:82
	v_mul_f32_e32 v47, 0x42800000, v75
	v_mul_f32_e32 v49, 0x42800000, v76
	ds_write2_b32 v39, v47, v49 offset0:148 offset1:214
	v_mul_f32_e32 v47, 0x42800000, v77
	v_mul_f32_e32 v49, 0x42800000, v78
	ds_write2_b32 v40, v47, v49 offset0:24 offset1:90
	v_mul_f32_e32 v47, 0x42800000, v79
	v_mul_f32_e32 v49, 0x42800000, v80
	ds_write2_b32 v40, v47, v49 offset0:156 offset1:222
	s_and_b32 s8, s8, 0xffffff00
	s_add_i32 s4, s26, s4
	s_add_i32 s4, s4, s8
	s_mov_b32 s7, s5
	v_mul_f32_e32 v47, 0x42800000, v81
	v_mul_f32_e32 v49, 0x42800000, v82
	ds_write2_b32 v41, v47, v49 offset0:32 offset1:98
	v_mul_f32_e32 v47, 0x42800000, v83
	v_mul_f32_e32 v49, 0x42800000, v84
	ds_write2_b32 v41, v47, v49 offset0:164 offset1:230
	v_mul_f32_e32 v47, 0x42800000, v85
	v_mul_f32_e32 v49, 0x42800000, v86
	ds_write2_b32 v42, v47, v49 offset0:40 offset1:106
	v_mul_f32_e32 v47, 0x42800000, v60
	v_mul_f32_e32 v49, 0x42800000, v61
	ds_write2_b32 v42, v47, v49 offset0:172 offset1:238
	v_add_u32_e32 v84, s4, v30
	v_ashrrev_i32_e32 v85, 31, v84
	v_lshlrev_b64 v[84:85], 10, v[84:85]
	v_mul_f32_e32 v47, 0x42800000, v62
	v_mul_f32_e32 v49, 0x42800000, v50
	ds_write2_b32 v43, v47, v49 offset0:48 offset1:114
	v_mul_f32_e32 v47, 0x42800000, v51
	v_mul_f32_e32 v49, 0x42800000, v52
	ds_write2_b32 v43, v47, v49 offset0:180 offset1:246
	v_mul_f32_e32 v47, 0x42800000, v53
	v_mul_f32_e32 v49, 0x42800000, v54
	ds_write2_b32 v44, v47, v49 offset0:56 offset1:122
	v_mov_b32_e32 v49, 0
	v_lshl_add_u64 v[50:51], v[20:21], 0, s[6:7]
	v_mul_f32_e32 v47, 0x42800000, v48
	v_mul_f32_e32 v46, 0x42800000, v46
	ds_write2_b32 v44, v47, v46 offset0:188 offset1:254
	s_waitcnt lgkmcnt(0)
	ds_read2_b32 v[52:53], v31 offset1:16
	ds_read2_b32 v[54:55], v31 offset0:33 offset1:49
	ds_read2_b32 v[56:57], v31 offset0:66 offset1:82
	ds_read2_b32 v[58:59], v31 offset0:99 offset1:115
	ds_read2_b32 v[60:61], v31 offset0:132 offset1:148
	ds_read2_b32 v[62:63], v31 offset0:165 offset1:181
	ds_read2_b32 v[64:65], v31 offset0:198 offset1:214
	ds_read2_b32 v[66:67], v31 offset0:231 offset1:247
	ds_read2_b32 v[68:69], v45 offset0:8 offset1:24
	ds_read2_b32 v[70:71], v45 offset0:41 offset1:57
	ds_read2_b32 v[72:73], v45 offset0:74 offset1:90
	ds_read2_b32 v[74:75], v45 offset0:107 offset1:123
	ds_read2_b32 v[76:77], v45 offset0:140 offset1:156
	ds_read2_b32 v[78:79], v45 offset0:173 offset1:189
	v_mov_b32_e32 v46, 0
	v_mov_b32_e32 v47, 0
	v_mov_b32_e32 v48, 0
	ds_read2_b32 v[80:81], v45 offset0:206 offset1:222
	ds_read2_b32 v[82:83], v45 offset0:239 offset1:255
	s_waitcnt lgkmcnt(14)
	v_cvt_pk_fp8_f32 v46, v52, v54
	s_waitcnt lgkmcnt(10)
	v_cvt_pk_fp8_f32 v47, v60, v62
	s_waitcnt lgkmcnt(6)
	v_cvt_pk_fp8_f32 v48, v68, v70
	s_waitcnt lgkmcnt(2)
	v_cvt_pk_fp8_f32 v49, v76, v78
	v_cvt_pk_fp8_f32 v46, v56, v58 op_sel:[0,0,1]
	v_cvt_pk_fp8_f32 v47, v64, v66 op_sel:[0,0,1]
	v_cvt_pk_fp8_f32 v48, v72, v74 op_sel:[0,0,1]
	s_waitcnt lgkmcnt(0)
	v_cvt_pk_fp8_f32 v49, v80, v82 op_sel:[0,0,1]
	v_lshl_add_u64 v[84:85], v[50:51], 0, v[84:85]
	v_add_u32_e32 v52, s4, v32
	global_store_dwordx4 v[84:85], v[46:49], off nt
	s_nop 1
	v_mov_b32_e32 v46, 0
	v_mov_b32_e32 v47, 0
	v_mov_b32_e32 v48, 0
	v_mov_b32_e32 v49, 0
	v_cvt_pk_fp8_f32 v46, v53, v55
	v_cvt_pk_fp8_f32 v47, v61, v63
	v_cvt_pk_fp8_f32 v48, v69, v71
	v_cvt_pk_fp8_f32 v49, v77, v79
	v_cvt_pk_fp8_f32 v46, v57, v59 op_sel:[0,0,1]
	v_cvt_pk_fp8_f32 v47, v65, v67 op_sel:[0,0,1]
	v_cvt_pk_fp8_f32 v48, v73, v75 op_sel:[0,0,1]
	v_cvt_pk_fp8_f32 v49, v81, v83 op_sel:[0,0,1]
	v_ashrrev_i32_e32 v53, 31, v52
	v_lshlrev_b64 v[52:53], 10, v[52:53]
	v_lshl_add_u64 v[50:51], v[50:51], 0, v[52:53]
	global_store_dwordx4 v[50:51], v[46:49], off nt
	s_waitcnt lgkmcnt(0)

; __device__ __forceinline__ void tr_item(const float* W, int ld, int K, int nblk, int item, bf16* WT, bool gu, LAS float* scr, int lane) {
;     const int kb = item / nblk, nb = item % nblk, k0 = 64 * kb, n0 = 32 * nb;
;     int drow0 = n0;
;     if (gu) { const int bj = n0 / FF, j = n0 - bj * FF; drow0 = 256 * (j / 128) + 128 * bj + (j % 128); }
;     { float t_[32];
; #pragma unroll
;       for (int i = 0; i < 32; ++i) t_[i] = W[(size_t)(k0 + 2 * i + (lane >> 5)) * ld + n0 + (lane & 31)];
; __device__ __forceinline__ void convert_items(Frame& F, const Args& a, int lo, int hi, int w, int nw) {
;     ...
;         if (r < I_SO) { tr_item(a.in[12], D, D, 32, r, (bf16*)(F.ws + WS_WSWAOUT), false, scr, lane); continue; } r -= I_SO;
.LBB0_1174:
	s_andn2_b64 vcc, exec, s[6:7]
	s_cbranch_vccnz .LBB0_1176
	s_add_i32 s4, s11, 0x2000
	s_and_b32 s7, s4, 0x1ffc0
	s_and_b32 s6, s10, 0x3e0
	v_add_u32_e32 v46, s7, v28
	s_lshl_b32 s4, s6, 2
	v_ashrrev_i32_e32 v47, 31, v46
	v_lshl_add_u64 v[48:49], v[8:9], 0, s[4:5]
	v_lshlrev_b64 v[46:47], 12, v[46:47]
	v_lshl_add_u64 v[46:47], v[48:49], 0, v[46:47]
	v_add_co_u32_e32 v48, vcc, 0x2000, v46
	s_lshl_b32 s4, s7, 1
	s_nop 0
	v_addc_co_u32_e32 v49, vcc, 0, v47, vcc
	v_add_co_u32_e32 v50, vcc, 0x4000, v46
	s_nop 1
	v_addc_co_u32_e32 v51, vcc, 0, v47, vcc
	v_add_co_u32_e32 v52, vcc, 0x6000, v46
	s_nop 1
	v_addc_co_u32_e32 v53, vcc, 0, v47, vcc
	v_add_co_u32_e32 v54, vcc, 0x8000, v46
	s_nop 1
	v_addc_co_u32_e32 v55, vcc, 0, v47, vcc
	v_add_co_u32_e32 v56, vcc, 0xa000, v46
	s_nop 1
	v_addc_co_u32_e32 v57, vcc, 0, v47, vcc
	v_add_co_u32_e32 v58, vcc, 0xc000, v46
	s_nop 1
	v_addc_co_u32_e32 v59, vcc, 0, v47, vcc
	v_add_co_u32_e32 v60, vcc, 0xe000, v46
	s_nop 1
	v_addc_co_u32_e32 v61, vcc, 0, v47, vcc
	global_load_dword v64, v[46:47], off nt
	global_load_dword v65, v[48:49], off nt
	global_load_dword v66, v[50:51], off nt
	global_load_dword v67, v[52:53], off nt
	global_load_dword v68, v[54:55], off nt
	global_load_dword v69, v[56:57], off nt
	global_load_dword v70, v[58:59], off nt
	global_load_dword v71, v[60:61], off nt
	v_add_co_u32_e32 v48, vcc, 0x10000, v46
	s_nop 1
	v_addc_co_u32_e32 v49, vcc, 0, v47, vcc
	v_add_co_u32_e32 v50, vcc, 0x12000, v46
	s_nop 1
	v_addc_co_u32_e32 v51, vcc, 0, v47, vcc
	v_add_co_u32_e32 v52, vcc, 0x14000, v46
	s_nop 1
	v_addc_co_u32_e32 v53, vcc, 0, v47, vcc
	v_add_co_u32_e32 v54, vcc, 0x16000, v46
	s_nop 1
	v_addc_co_u32_e32 v55, vcc, 0, v47, vcc
	v_add_co_u32_e32 v56, vcc, 0x18000, v46
	s_nop 1
	v_addc_co_u32_e32 v57, vcc, 0, v47, vcc
	v_add_co_u32_e32 v58, vcc, 0x1a000, v46
	s_nop 1
	v_addc_co_u32_e32 v59, vcc, 0, v47, vcc
	v_add_co_u32_e32 v60, vcc, 0x1c000, v46
	s_nop 1
	v_addc_co_u32_e32 v61, vcc, 0, v47, vcc
	v_add_co_u32_e32 v62, vcc, 0x1e000, v46
	s_nop 1
	v_addc_co_u32_e32 v63, vcc, 0, v47, vcc
	global_load_dword v72, v[48:49], off nt
	global_load_dword v73, v[50:51], off nt
	global_load_dword v74, v[52:53], off nt
	global_load_dword v75, v[54:55], off nt
	global_load_dword v76, v[56:57], off nt
	global_load_dword v77, v[58:59], off nt
	global_load_dword v78, v[60:61], off nt
	global_load_dword v79, v[62:63], off nt
	v_add_co_u32_e32 v48, vcc, 0x20000, v46
	s_nop 1
	v_addc_co_u32_e32 v49, vcc, 0, v47, vcc
	v_add_co_u32_e32 v50, vcc, 0x22000, v46
	s_nop 1
	v_addc_co_u32_e32 v51, vcc, 0, v47, vcc
	v_add_co_u32_e32 v52, vcc, 0x24000, v46
	s_nop 1
	v_addc_co_u32_e32 v53, vcc, 0, v47, vcc
	v_add_co_u32_e32 v54, vcc, 0x26000, v46
	s_nop 1
	v_addc_co_u32_e32 v55, vcc, 0, v47, vcc
	v_add_co_u32_e32 v56, vcc, 0x28000, v46
	s_nop 1
	v_addc_co_u32_e32 v57, vcc, 0, v47, vcc
	v_add_co_u32_e32 v58, vcc, 0x2a000, v46
	s_nop 1
	v_addc_co_u32_e32 v59, vcc, 0, v47, vcc
	v_add_co_u32_e32 v60, vcc, 0x2c000, v46
	s_nop 1
	v_addc_co_u32_e32 v61, vcc, 0, v47, vcc
	v_add_co_u32_e32 v62, vcc, 0x2e000, v46
	s_nop 1
	v_addc_co_u32_e32 v63, vcc, 0, v47, vcc
	global_load_dword v80, v[48:49], off nt
	global_load_dword v81, v[50:51], off nt
	global_load_dword v82, v[52:53], off nt
	global_load_dword v83, v[54:55], off nt
	global_load_dword v84, v[56:57], off nt
	global_load_dword v85, v[58:59], off nt
	global_load_dword v86, v[60:61], off nt
	s_nop 0
	global_load_dword v62, v[62:63], off nt
	v_add_co_u32_e32 v48, vcc, 0x30000, v46
	s_nop 1
	v_addc_co_u32_e32 v49, vcc, 0, v47, vcc
	v_add_co_u32_e32 v50, vcc, 0x32000, v46
	s_nop 1
	v_addc_co_u32_e32 v51, vcc, 0, v47, vcc
	v_add_co_u32_e32 v52, vcc, 0x34000, v46
	s_nop 1
	v_addc_co_u32_e32 v53, vcc, 0, v47, vcc
	v_add_co_u32_e32 v54, vcc, 0x36000, v46
	s_nop 1
	v_addc_co_u32_e32 v55, vcc, 0, v47, vcc
	v_add_co_u32_e32 v56, vcc, 0x38000, v46
	s_nop 1
	v_addc_co_u32_e32 v57, vcc, 0, v47, vcc
	v_add_co_u32_e32 v58, vcc, 0x3a000, v46
	s_nop 1
	v_addc_co_u32_e32 v59, vcc, 0, v47, vcc
	v_add_co_u32_e32 v60, vcc, 0x3c000, v46
	s_nop 1
	v_addc_co_u32_e32 v61, vcc, 0, v47, vcc
	v_add_co_u32_e32 v46, vcc, 0x3e000, v46
	s_nop 1
	v_addc_co_u32_e32 v47, vcc, 0, v47, vcc
	global_load_dword v48, v[48:49], off nt
	s_nop 0
	global_load_dword v49, v[50:51], off nt
	s_nop 0
	global_load_dword v50, v[52:53], off nt
	global_load_dword v51, v[54:55], off nt
	s_nop 0
	global_load_dword v52, v[56:57], off nt
	global_load_dword v53, v[58:59], off nt
	global_load_dword v54, v[60:61], off nt
	s_nop 0
	global_load_dword v46, v[46:47], off nt
	s_waitcnt vmcnt(0)
	ds_write2_b32 v29, v64, v65 offset1:66
	ds_write2_b32 v29, v66, v67 offset0:132 offset1:198
	ds_write2_b32 v38, v68, v69 offset0:8 offset1:74
	ds_write2_b32 v38, v70, v71 offset0:140 offset1:206
	ds_write2_b32 v39, v72, v73 offset0:16 offset1:82
	ds_write2_b32 v39, v74, v75 offset0:148 offset1:214
	ds_write2_b32 v40, v76, v77 offset0:24 offset1:90
	ds_write2_b32 v40, v78, v79 offset0:156 offset1:222
	ds_write2_b32 v41, v80, v81 offset0:32 offset1:98
	ds_write2_b32 v41, v82, v83 offset0:164 offset1:230
	ds_write2_b32 v42, v84, v85 offset0:40 offset1:106
	ds_write2_b32 v42, v86, v62 offset0:172 offset1:238
	ds_write2_b32 v43, v48, v49 offset0:48 offset1:114
	ds_write2_b32 v43, v50, v51 offset0:180 offset1:246
	ds_write2_b32 v44, v52, v53 offset0:56 offset1:122
	ds_write2_b32 v44, v54, v46 offset0:188 offset1:254
	s_waitcnt lgkmcnt(0)
; #define GAS __attribute__((address_space(1)))
; #define LAS __attribute__((address_space(3)))
; #define LDS_WAIT() asm volatile("s_waitcnt lgkmcnt(0)" ::: "memory")
; __device__ __forceinline__ unsigned pk2(float lo, float hi) { return f2bf(lo) | (f2bf(hi) << 16); }
; __device__ __forceinline__ void tr_item(const float* W, int ld, int K, int nblk, int item, bf16* WT, bool gu, LAS float* scr, int lane) {
;     ...
;     LDS_WAIT(); asm volatile("" ::: "memory");
;     const int c = lane & 7;
; #pragma unroll
;     for (int j = 0; j < 4; ++j) { const int n = (lane >> 3) + 8 * j; const LAS float* s = scr + (8 * c) * 33 + n;
;         v4u o; o.x = pk2(s[0 * 33], s[1 * 33]); o.y = pk2(s[2 * 33], s[3 * 33]); o.z = pk2(s[4 * 33], s[5 * 33]); o.w = pk2(s[6 * 33], s[7 * 33]);
;         *(GAS v4u*)(WT + (size_t)(drow0 + n) * K + k0 + 8 * c) = o; }
;     LDS_WAIT(); asm volatile("" ::: "memory");
	ds_read2_b32 v[50:51], v34 offset1:8
	ds_read2_b32 v[54:55], v34 offset0:33 offset1:41
	ds_read2_b32 v[56:57], v34 offset0:66 offset1:74
	ds_read2_b32 v[58:59], v34 offset0:99 offset1:107
	ds_read2_b32 v[60:61], v34 offset0:132 offset1:140
	s_waitcnt lgkmcnt(4)
	v_bfe_u32 v46, v50, 16, 1
	v_add3_u32 v46, v50, v46, s14
	s_waitcnt lgkmcnt(3)
	v_bfe_u32 v47, v54, 16, 1
	v_lshrrev_b32_e32 v46, 16, v46
	v_add3_u32 v47, v54, v47, s14
	ds_read2_b32 v[62:63], v34 offset0:165 offset1:173
	v_and_or_b32 v46, v47, s15, v46
	s_waitcnt lgkmcnt(3)
	v_bfe_u32 v47, v56, 16, 1
	v_add3_u32 v47, v56, v47, s14
	s_waitcnt lgkmcnt(2)
	v_bfe_u32 v48, v58, 16, 1
	ds_read2_b32 v[64:65], v34 offset0:198 offset1:206
	v_lshrrev_b32_e32 v47, 16, v47
	v_add3_u32 v48, v58, v48, s14
	ds_read2_b32 v[66:67], v34 offset0:231 offset1:239
	v_and_or_b32 v47, v48, s15, v47
	s_waitcnt lgkmcnt(3)
	v_bfe_u32 v48, v60, 16, 1
	v_add3_u32 v48, v60, v48, s14
	s_waitcnt lgkmcnt(2)
	v_bfe_u32 v49, v62, 16, 1
	v_lshrrev_b32_e32 v48, 16, v48
	v_add3_u32 v49, v62, v49, s14
	v_and_or_b32 v48, v49, s15, v48
	s_waitcnt lgkmcnt(1)
	v_bfe_u32 v49, v64, 16, 1
	v_add_u32_e32 v68, s6, v33
	v_add3_u32 v49, v64, v49, s14
	s_waitcnt lgkmcnt(0)
	v_bfe_u32 v50, v66, 16, 1
	v_ashrrev_i32_e32 v69, 31, v68
	v_lshl_add_u64 v[52:53], v[22:23], 0, s[4:5]
	v_lshrrev_b32_e32 v49, 16, v49
	v_add3_u32 v50, v66, v50, s14
	v_lshlrev_b64 v[68:69], 11, v[68:69]
	v_and_or_b32 v49, v50, s15, v49
	v_lshl_add_u64 v[68:69], v[52:53], 0, v[68:69]
	global_store_dwordx4 v[68:69], v[46:49], off nt
	v_bfe_u32 v50, v67, 16, 1
	v_add3_u32 v50, v67, v50, s14
	v_bfe_u32 v46, v51, 16, 1
	v_add3_u32 v46, v51, v46, s14
	v_bfe_u32 v47, v55, 16, 1
	v_lshrrev_b32_e32 v46, 16, v46
	v_add3_u32 v47, v55, v47, s14
	v_and_or_b32 v46, v47, s15, v46
	v_bfe_u32 v47, v57, 16, 1
	v_add3_u32 v47, v57, v47, s14
	v_bfe_u32 v48, v59, 16, 1
	v_lshrrev_b32_e32 v47, 16, v47
	v_add3_u32 v48, v59, v48, s14
	v_and_or_b32 v47, v48, s15, v47
	v_bfe_u32 v48, v61, 16, 1
	v_add3_u32 v48, v61, v48, s14
	v_bfe_u32 v49, v63, 16, 1
	v_lshrrev_b32_e32 v48, 16, v48
	v_add3_u32 v49, v63, v49, s14
	v_and_or_b32 v48, v49, s15, v48
	v_bfe_u32 v49, v65, 16, 1
	v_add3_u32 v49, v65, v49, s14
	v_lshrrev_b32_e32 v49, 16, v49
	v_and_or_b32 v49, v50, s15, v49
	v_add_u32_e32 v50, s6, v35
	v_ashrrev_i32_e32 v51, 31, v50
	v_lshlrev_b64 v[50:51], 11, v[50:51]
	ds_read2_b32 v[54:55], v34 offset0:16 offset1:24
	v_lshl_add_u64 v[50:51], v[52:53], 0, v[50:51]
	global_store_dwordx4 v[50:51], v[46:49], off nt
	ds_read2_b32 v[50:51], v34 offset0:49 offset1:57
	ds_read2_b32 v[56:57], v34 offset0:82 offset1:90
	ds_read2_b32 v[58:59], v34 offset0:115 offset1:123
	s_waitcnt lgkmcnt(3)
	v_bfe_u32 v46, v54, 16, 1
	v_add3_u32 v46, v54, v46, s14
	s_waitcnt lgkmcnt(2)
	v_bfe_u32 v47, v50, 16, 1
	ds_read2_b32 v[60:61], v34 offset0:148 offset1:156
	v_lshrrev_b32_e32 v46, 16, v46
	v_add3_u32 v47, v50, v47, s14
	ds_read2_b32 v[62:63], v34 offset0:181 offset1:189
	v_and_or_b32 v46, v47, s15, v46
	s_waitcnt lgkmcnt(3)
	v_bfe_u32 v47, v56, 16, 1
	v_add3_u32 v47, v56, v47, s14
	s_waitcnt lgkmcnt(2)
	v_bfe_u32 v48, v58, 16, 1
	ds_read2_b32 v[64:65], v34 offset0:214 offset1:222
	v_lshrrev_b32_e32 v47, 16, v47
	v_add3_u32 v48, v58, v48, s14
	ds_read2_b32 v[66:67], v34 offset0:247 offset1:255
	v_and_or_b32 v47, v48, s15, v47
	s_waitcnt lgkmcnt(3)
	v_bfe_u32 v48, v60, 16, 1
	v_add3_u32 v48, v60, v48, s14
	s_waitcnt lgkmcnt(2)
	v_bfe_u32 v49, v62, 16, 1
	v_lshrrev_b32_e32 v48, 16, v48
	v_add3_u32 v49, v62, v49, s14
	v_and_or_b32 v48, v49, s15, v48
	s_waitcnt lgkmcnt(1)
	v_bfe_u32 v49, v64, 16, 1
	v_add_u32_e32 v68, s6, v36
	v_add3_u32 v49, v64, v49, s14
	s_waitcnt lgkmcnt(0)
	v_bfe_u32 v50, v66, 16, 1
	v_ashrrev_i32_e32 v69, 31, v68
	v_lshrrev_b32_e32 v49, 16, v49
	v_add3_u32 v50, v66, v50, s14
	v_lshlrev_b64 v[68:69], 11, v[68:69]
	v_and_or_b32 v49, v50, s15, v49
	v_lshl_add_u64 v[68:69], v[52:53], 0, v[68:69]
	global_store_dwordx4 v[68:69], v[46:49], off nt
	v_bfe_u32 v50, v67, 16, 1
	v_add3_u32 v50, v67, v50, s14
	v_bfe_u32 v46, v55, 16, 1
	v_add3_u32 v46, v55, v46, s14
	v_bfe_u32 v47, v51, 16, 1
	v_lshrrev_b32_e32 v46, 16, v46
	v_add3_u32 v47, v51, v47, s14
	v_and_or_b32 v46, v47, s15, v46
	v_bfe_u32 v47, v57, 16, 1
	v_add3_u32 v47, v57, v47, s14
	v_bfe_u32 v48, v59, 16, 1
	v_lshrrev_b32_e32 v47, 16, v47
	v_add3_u32 v48, v59, v48, s14
	v_and_or_b32 v47, v48, s15, v47
	v_bfe_u32 v48, v61, 16, 1
	v_add3_u32 v48, v61, v48, s14
	v_bfe_u32 v49, v63, 16, 1
	v_lshrrev_b32_e32 v48, 16, v48
	v_add3_u32 v49, v63, v49, s14
	v_and_or_b32 v48, v49, s15, v48
	v_bfe_u32 v49, v65, 16, 1
	v_add3_u32 v49, v65, v49, s14
	v_lshrrev_b32_e32 v49, 16, v49
	v_and_or_b32 v49, v50, s15, v49
	v_add_u32_e32 v50, s6, v37
	v_ashrrev_i32_e32 v51, 31, v50
	v_lshlrev_b64 v[50:51], 11, v[50:51]
	v_lshl_add_u64 v[50:51], v[52:53], 0, v[50:51]
	global_store_dwordx4 v[50:51], v[46:49], off nt
	s_waitcnt lgkmcnt(0)

; __device__ __forceinline__ void tr_item(const float* W, int ld, int K, int nblk, int item, bf16* WT, bool gu, LAS float* scr, int lane) {
;     const int kb = item / nblk, nb = item % nblk, k0 = 64 * kb, n0 = 32 * nb;
;     int drow0 = n0;
;     if (gu) { const int bj = n0 / FF, j = n0 - bj * FF; drow0 = 256 * (j / 128) + 128 * bj + (j % 128); }
;     { float t_[32];
; #pragma unroll
;       for (int i = 0; i < 32; ++i) t_[i] = W[(size_t)(k0 + 2 * i + (lane >> 5)) * ld + n0 + (lane & 31)];
; __device__ __forceinline__ void convert_items(Frame& F, const Args& a, int lo, int hi, int w, int nw) {
;     ...
;         if (r < I_SI) { tr_item(a.in[10], D + 512, D, 48, r, (bf16*)(F.ws + WS_WSWAIN), false, scr, lane); continue; } r -= I_SI;
.LBB0_1177:
	s_andn2_b64 vcc, exec, s[6:7]
	s_cbranch_vccnz .LBB0_1179
	s_add_i32 s4, s16, 0xf800
	s_and_b32 s6, s4, 0xffff
	s_mul_i32 s6, s6, 0xaaab
	s_lshr_b32 s7, s6, 21
	s_mul_i32 s6, s7, 48
	s_sub_i32 s4, s4, s6
	s_lshl_b32 s4, s4, 5
	s_and_b32 s6, s4, 0xffe0
	v_lshl_add_u32 v64, s7, 6, v28
	s_lshl_b32 s4, s6, 2
	v_lshl_add_u64 v[46:47], v[10:11], 0, s[4:5]
	v_add_u32_e32 v50, 2, v64
	v_add_u32_e32 v52, 4, v64
	v_add_u32_e32 v54, 6, v64
	v_add_u32_e32 v56, 8, v64
	v_add_u32_e32 v58, 10, v64
	v_add_u32_e32 v60, 12, v64
	v_add_u32_e32 v62, 14, v64
	v_mad_i64_i32 v[48:49], s[8:9], v64, s17, v[46:47]
	v_mad_i64_i32 v[50:51], s[8:9], v50, s17, v[46:47]
	v_mad_i64_i32 v[52:53], s[8:9], v52, s17, v[46:47]
	v_mad_i64_i32 v[54:55], s[8:9], v54, s17, v[46:47]
	v_mad_i64_i32 v[56:57], s[8:9], v56, s17, v[46:47]
	v_mad_i64_i32 v[58:59], s[8:9], v58, s17, v[46:47]
	v_mad_i64_i32 v[60:61], s[8:9], v60, s17, v[46:47]
	v_mad_i64_i32 v[62:63], s[8:9], v62, s17, v[46:47]
	global_load_dword v65, v[48:49], off nt
	global_load_dword v66, v[50:51], off nt
	global_load_dword v67, v[52:53], off nt
	global_load_dword v68, v[54:55], off nt
	global_load_dword v69, v[56:57], off nt
	global_load_dword v70, v[58:59], off nt
	global_load_dword v71, v[60:61], off nt
	global_load_dword v72, v[62:63], off nt
	v_add_u32_e32 v48, 16, v64
	v_add_u32_e32 v50, 18, v64
	v_add_u32_e32 v52, 20, v64
	v_add_u32_e32 v54, 22, v64
	v_add_u32_e32 v56, 24, v64
	v_add_u32_e32 v58, 26, v64
	v_add_u32_e32 v60, 28, v64
	v_add_u32_e32 v62, 30, v64
	v_mad_i64_i32 v[48:49], s[8:9], v48, s17, v[46:47]
	v_mad_i64_i32 v[50:51], s[8:9], v50, s17, v[46:47]
	v_mad_i64_i32 v[52:53], s[8:9], v52, s17, v[46:47]
	v_mad_i64_i32 v[54:55], s[8:9], v54, s17, v[46:47]
	v_mad_i64_i32 v[56:57], s[8:9], v56, s17, v[46:47]
	v_mad_i64_i32 v[58:59], s[8:9], v58, s17, v[46:47]
	v_mad_i64_i32 v[60:61], s[8:9], v60, s17, v[46:47]
	v_mad_i64_i32 v[62:63], s[8:9], v62, s17, v[46:47]
	global_load_dword v73, v[48:49], off nt
	global_load_dword v74, v[50:51], off nt
	global_load_dword v75, v[52:53], off nt
	global_load_dword v76, v[54:55], off nt
	global_load_dword v77, v[56:57], off nt
	global_load_dword v78, v[58:59], off nt
	global_load_dword v79, v[60:61], off nt
	global_load_dword v80, v[62:63], off nt
	v_add_u32_e32 v48, 32, v64
	v_add_u32_e32 v50, 34, v64
	v_add_u32_e32 v52, 36, v64
	v_add_u32_e32 v54, 38, v64
	v_add_u32_e32 v56, 40, v64
	v_add_u32_e32 v58, 42, v64
	v_add_u32_e32 v60, 44, v64
	v_add_u32_e32 v62, 46, v64
	v_mad_i64_i32 v[48:49], s[8:9], v48, s17, v[46:47]
	v_mad_i64_i32 v[50:51], s[8:9], v50, s17, v[46:47]
	v_mad_i64_i32 v[52:53], s[8:9], v52, s17, v[46:47]
	v_mad_i64_i32 v[54:55], s[8:9], v54, s17, v[46:47]
	v_mad_i64_i32 v[56:57], s[8:9], v56, s17, v[46:47]
	v_mad_i64_i32 v[58:59], s[8:9], v58, s17, v[46:47]
	v_mad_i64_i32 v[60:61], s[8:9], v60, s17, v[46:47]
	v_mad_i64_i32 v[62:63], s[8:9], v62, s17, v[46:47]
	global_load_dword v81, v[48:49], off nt
	global_load_dword v82, v[50:51], off nt
	global_load_dword v83, v[52:53], off nt
	global_load_dword v84, v[54:55], off nt
	global_load_dword v85, v[56:57], off nt
	global_load_dword v86, v[58:59], off nt
	global_load_dword v87, v[60:61], off nt
	s_nop 0
	global_load_dword v62, v[62:63], off nt
	v_add_u32_e32 v48, 48, v64
	v_add_u32_e32 v50, 50, v64
	v_add_u32_e32 v52, 52, v64
	v_add_u32_e32 v54, 54, v64
	v_add_u32_e32 v56, 56, v64
	v_add_u32_e32 v58, 58, v64
	v_add_u32_e32 v60, 60, v64
	v_add_u32_e32 v63, 62, v64
	v_mad_i64_i32 v[48:49], s[8:9], v48, s17, v[46:47]
	v_mad_i64_i32 v[50:51], s[8:9], v50, s17, v[46:47]
	v_mad_i64_i32 v[52:53], s[8:9], v52, s17, v[46:47]
	v_mad_i64_i32 v[54:55], s[8:9], v54, s17, v[46:47]
	v_mad_i64_i32 v[56:57], s[8:9], v56, s17, v[46:47]
	v_mad_i64_i32 v[58:59], s[8:9], v58, s17, v[46:47]
	v_mad_i64_i32 v[60:61], s[8:9], v60, s17, v[46:47]
	v_mad_i64_i32 v[46:47], s[8:9], v63, s17, v[46:47]
	global_load_dword v48, v[48:49], off nt
	s_nop 0
	global_load_dword v49, v[50:51], off nt
	s_nop 0
	global_load_dword v50, v[52:53], off nt
	global_load_dword v51, v[54:55], off nt
	s_nop 0
	global_load_dword v52, v[56:57], off nt
	global_load_dword v53, v[58:59], off nt
	global_load_dword v54, v[60:61], off nt
	s_nop 0
	global_load_dword v46, v[46:47], off nt
	s_waitcnt vmcnt(0)
	ds_write2_b32 v29, v65, v66 offset1:66
	ds_write2_b32 v29, v67, v68 offset0:132 offset1:198
	ds_write2_b32 v38, v69, v70 offset0:8 offset1:74
	ds_write2_b32 v38, v71, v72 offset0:140 offset1:206
	ds_write2_b32 v39, v73, v74 offset0:16 offset1:82
	ds_write2_b32 v39, v75, v76 offset0:148 offset1:214
	ds_write2_b32 v40, v77, v78 offset0:24 offset1:90
	ds_write2_b32 v40, v79, v80 offset0:156 offset1:222
	ds_write2_b32 v41, v81, v82 offset0:32 offset1:98
	ds_write2_b32 v41, v83, v84 offset0:164 offset1:230
	ds_write2_b32 v42, v85, v86 offset0:40 offset1:106
	ds_write2_b32 v42, v87, v62 offset0:172 offset1:238
	ds_write2_b32 v43, v48, v49 offset0:48 offset1:114
	ds_write2_b32 v43, v50, v51 offset0:180 offset1:246
	ds_write2_b32 v44, v52, v53 offset0:56 offset1:122
	ds_write2_b32 v44, v54, v46 offset0:188 offset1:254
	s_waitcnt lgkmcnt(0)
; #define GAS __attribute__((address_space(1)))
; #define LAS __attribute__((address_space(3)))
; #define LDS_WAIT() asm volatile("s_waitcnt lgkmcnt(0)" ::: "memory")
; __device__ __forceinline__ unsigned pk2(float lo, float hi) { return f2bf(lo) | (f2bf(hi) << 16); }
; __device__ __forceinline__ void tr_item(const float* W, int ld, int K, int nblk, int item, bf16* WT, bool gu, LAS float* scr, int lane) {
;     ...
;     LDS_WAIT(); asm volatile("" ::: "memory");
;     const int c = lane & 7;
; #pragma unroll
;     for (int j = 0; j < 4; ++j) { const int n = (lane >> 3) + 8 * j; const LAS float* s = scr + (8 * c) * 33 + n;
;         v4u o; o.x = pk2(s[0 * 33], s[1 * 33]); o.y = pk2(s[2 * 33], s[3 * 33]); o.z = pk2(s[4 * 33], s[5 * 33]); o.w = pk2(s[6 * 33], s[7 * 33]);
;         *(GAS v4u*)(WT + (size_t)(drow0 + n) * K + k0 + 8 * c) = o; }
;     LDS_WAIT(); asm volatile("" ::: "memory");
	ds_read2_b32 v[50:51], v34 offset1:8
	ds_read2_b32 v[54:55], v34 offset0:33 offset1:41
	ds_read2_b32 v[56:57], v34 offset0:66 offset1:74
	ds_read2_b32 v[58:59], v34 offset0:99 offset1:107
	ds_read2_b32 v[60:61], v34 offset0:132 offset1:140
	s_waitcnt lgkmcnt(4)
	v_bfe_u32 v46, v50, 16, 1
	v_add3_u32 v46, v50, v46, s14
	s_waitcnt lgkmcnt(3)
	v_bfe_u32 v47, v54, 16, 1
	v_lshrrev_b32_e32 v46, 16, v46
	v_add3_u32 v47, v54, v47, s14
	ds_read2_b32 v[62:63], v34 offset0:165 offset1:173
	v_and_or_b32 v46, v47, s15, v46
	s_waitcnt lgkmcnt(3)
	v_bfe_u32 v47, v56, 16, 1
	v_add3_u32 v47, v56, v47, s14
	s_waitcnt lgkmcnt(2)
	v_bfe_u32 v48, v58, 16, 1
	ds_read2_b32 v[64:65], v34 offset0:198 offset1:206
	v_lshrrev_b32_e32 v47, 16, v47
	v_add3_u32 v48, v58, v48, s14
	ds_read2_b32 v[66:67], v34 offset0:231 offset1:239
	v_and_or_b32 v47, v48, s15, v47
	s_waitcnt lgkmcnt(3)
	v_bfe_u32 v48, v60, 16, 1
	v_add3_u32 v48, v60, v48, s14
	s_waitcnt lgkmcnt(2)
	v_bfe_u32 v49, v62, 16, 1
	v_lshrrev_b32_e32 v48, 16, v48
	v_add3_u32 v49, v62, v49, s14
	v_and_or_b32 v48, v49, s15, v48
	s_waitcnt lgkmcnt(1)
	v_bfe_u32 v49, v64, 16, 1
	v_add_u32_e32 v68, s6, v33
	s_lshl_b32 s4, s7, 7
	v_add3_u32 v49, v64, v49, s14
	s_waitcnt lgkmcnt(0)
	v_bfe_u32 v50, v66, 16, 1
	v_ashrrev_i32_e32 v69, 31, v68
	v_lshl_add_u64 v[52:53], v[12:13], 0, s[4:5]
	v_lshrrev_b32_e32 v49, 16, v49
	v_add3_u32 v50, v66, v50, s14
	v_lshlrev_b64 v[68:69], 11, v[68:69]
	v_and_or_b32 v49, v50, s15, v49
	v_lshl_add_u64 v[68:69], v[52:53], 0, v[68:69]
	global_store_dwordx4 v[68:69], v[46:49], off nt
	v_bfe_u32 v50, v67, 16, 1
	v_add3_u32 v50, v67, v50, s14
	v_bfe_u32 v46, v51, 16, 1
	v_add3_u32 v46, v51, v46, s14
	v_bfe_u32 v47, v55, 16, 1
	v_lshrrev_b32_e32 v46, 16, v46
	v_add3_u32 v47, v55, v47, s14
	v_and_or_b32 v46, v47, s15, v46
	v_bfe_u32 v47, v57, 16, 1
	v_add3_u32 v47, v57, v47, s14
	v_bfe_u32 v48, v59, 16, 1
	v_lshrrev_b32_e32 v47, 16, v47
	v_add3_u32 v48, v59, v48, s14
	v_and_or_b32 v47, v48, s15, v47
	v_bfe_u32 v48, v61, 16, 1
	v_add3_u32 v48, v61, v48, s14
	v_bfe_u32 v49, v63, 16, 1
	v_lshrrev_b32_e32 v48, 16, v48
	v_add3_u32 v49, v63, v49, s14
	v_and_or_b32 v48, v49, s15, v48
	v_bfe_u32 v49, v65, 16, 1
	v_add3_u32 v49, v65, v49, s14
	v_lshrrev_b32_e32 v49, 16, v49
	v_and_or_b32 v49, v50, s15, v49
	v_add_u32_e32 v50, s6, v35
	v_ashrrev_i32_e32 v51, 31, v50
	v_lshlrev_b64 v[50:51], 11, v[50:51]
	ds_read2_b32 v[54:55], v34 offset0:16 offset1:24
	v_lshl_add_u64 v[50:51], v[52:53], 0, v[50:51]
	global_store_dwordx4 v[50:51], v[46:49], off nt
	ds_read2_b32 v[50:51], v34 offset0:49 offset1:57
	ds_read2_b32 v[56:57], v34 offset0:82 offset1:90
	ds_read2_b32 v[58:59], v34 offset0:115 offset1:123
	s_waitcnt lgkmcnt(3)
	v_bfe_u32 v46, v54, 16, 1
	v_add3_u32 v46, v54, v46, s14
	s_waitcnt lgkmcnt(2)
	v_bfe_u32 v47, v50, 16, 1
	ds_read2_b32 v[60:61], v34 offset0:148 offset1:156
	v_lshrrev_b32_e32 v46, 16, v46
	v_add3_u32 v47, v50, v47, s14
	ds_read2_b32 v[62:63], v34 offset0:181 offset1:189
	v_and_or_b32 v46, v47, s15, v46
	s_waitcnt lgkmcnt(3)
	v_bfe_u32 v47, v56, 16, 1
	v_add3_u32 v47, v56, v47, s14
	s_waitcnt lgkmcnt(2)
	v_bfe_u32 v48, v58, 16, 1
	ds_read2_b32 v[64:65], v34 offset0:214 offset1:222
	v_lshrrev_b32_e32 v47, 16, v47
	v_add3_u32 v48, v58, v48, s14
	ds_read2_b32 v[66:67], v34 offset0:247 offset1:255
	v_and_or_b32 v47, v48, s15, v47
	s_waitcnt lgkmcnt(3)
	v_bfe_u32 v48, v60, 16, 1
	v_add3_u32 v48, v60, v48, s14
	s_waitcnt lgkmcnt(2)
	v_bfe_u32 v49, v62, 16, 1
	v_lshrrev_b32_e32 v48, 16, v48
	v_add3_u32 v49, v62, v49, s14
	v_and_or_b32 v48, v49, s15, v48
	s_waitcnt lgkmcnt(1)
	v_bfe_u32 v49, v64, 16, 1
	v_add_u32_e32 v68, s6, v36
	v_add3_u32 v49, v64, v49, s14
	s_waitcnt lgkmcnt(0)
	v_bfe_u32 v50, v66, 16, 1
	v_ashrrev_i32_e32 v69, 31, v68
	v_lshrrev_b32_e32 v49, 16, v49
	v_add3_u32 v50, v66, v50, s14
	v_lshlrev_b64 v[68:69], 11, v[68:69]
	v_and_or_b32 v49, v50, s15, v49
	v_lshl_add_u64 v[68:69], v[52:53], 0, v[68:69]
	global_store_dwordx4 v[68:69], v[46:49], off nt
	v_bfe_u32 v50, v67, 16, 1
	v_add3_u32 v50, v67, v50, s14
	v_bfe_u32 v46, v55, 16, 1
	v_add3_u32 v46, v55, v46, s14
	v_bfe_u32 v47, v51, 16, 1
	v_lshrrev_b32_e32 v46, 16, v46
	v_add3_u32 v47, v51, v47, s14
	v_and_or_b32 v46, v47, s15, v46
	v_bfe_u32 v47, v57, 16, 1
	v_add3_u32 v47, v57, v47, s14
	v_bfe_u32 v48, v59, 16, 1
	v_lshrrev_b32_e32 v47, 16, v47
	v_add3_u32 v48, v59, v48, s14
	v_and_or_b32 v47, v48, s15, v47
	v_bfe_u32 v48, v61, 16, 1
	v_add3_u32 v48, v61, v48, s14
	v_bfe_u32 v49, v63, 16, 1
	v_lshrrev_b32_e32 v48, 16, v48
	v_add3_u32 v49, v63, v49, s14
	v_and_or_b32 v48, v49, s15, v48
	v_bfe_u32 v49, v65, 16, 1
	v_add3_u32 v49, v65, v49, s14
	v_lshrrev_b32_e32 v49, 16, v49
	v_and_or_b32 v49, v50, s15, v49
	v_add_u32_e32 v50, s6, v37
	v_ashrrev_i32_e32 v51, 31, v50
	v_lshlrev_b64 v[50:51], 11, v[50:51]
	v_lshl_add_u64 v[50:51], v[52:53], 0, v[50:51]
	global_store_dwordx4 v[50:51], v[46:49], off nt
	s_waitcnt lgkmcnt(0)

; __device__ __forceinline__ void tr_item(const float* W, int ld, int K, int nblk, int item, bf16* WT, bool gu, LAS float* scr, int lane) {
;     const int kb = item / nblk, nb = item % nblk, k0 = 64 * kb, n0 = 32 * nb;
;     int drow0 = n0;
;     if (gu) { const int bj = n0 / FF, j = n0 - bj * FF; drow0 = 256 * (j / 128) + 128 * bj + (j % 128); }
;     { float t_[32];
; #pragma unroll
;       for (int i = 0; i < 32; ++i) t_[i] = W[(size_t)(k0 + 2 * i + (lane >> 5)) * ld + n0 + (lane & 31)];
; __device__ __forceinline__ void convert_items(Frame& F, const Args& a, int lo, int hi, int w, int nw) {
;     ...
;         if (r < I_FO) { tr_item(a.in[9], D, D, 32, r, (bf16*)(F.ws + WS_WFOXOUT), false, scr, lane); continue; } r -= I_FO;
.LBB0_1180:
	s_andn2_b64 vcc, exec, s[6:7]
	s_cbranch_vccnz .LBB0_1182
	s_add_i32 s4, s11, 0x2a00
	s_and_b32 s7, s4, 0x1ffc0
	s_and_b32 s6, s10, 0x3e0
	v_add_u32_e32 v46, s7, v28
	s_lshl_b32 s4, s6, 2
	v_ashrrev_i32_e32 v47, 31, v46
	v_lshl_add_u64 v[48:49], v[14:15], 0, s[4:5]
	v_lshlrev_b64 v[46:47], 12, v[46:47]
	v_lshl_add_u64 v[46:47], v[48:49], 0, v[46:47]
	v_add_co_u32_e32 v48, vcc, 0x2000, v46
	s_lshl_b32 s4, s7, 1
	s_nop 0
	v_addc_co_u32_e32 v49, vcc, 0, v47, vcc
	v_add_co_u32_e32 v50, vcc, 0x4000, v46
	s_nop 1
	v_addc_co_u32_e32 v51, vcc, 0, v47, vcc
	v_add_co_u32_e32 v52, vcc, 0x6000, v46
	s_nop 1
	v_addc_co_u32_e32 v53, vcc, 0, v47, vcc
	v_add_co_u32_e32 v54, vcc, 0x8000, v46
	s_nop 1
	v_addc_co_u32_e32 v55, vcc, 0, v47, vcc
	v_add_co_u32_e32 v56, vcc, 0xa000, v46
	s_nop 1
	v_addc_co_u32_e32 v57, vcc, 0, v47, vcc
	v_add_co_u32_e32 v58, vcc, 0xc000, v46
	s_nop 1
	v_addc_co_u32_e32 v59, vcc, 0, v47, vcc
	v_add_co_u32_e32 v60, vcc, 0xe000, v46
	s_nop 1
	v_addc_co_u32_e32 v61, vcc, 0, v47, vcc
	global_load_dword v64, v[46:47], off nt
	global_load_dword v65, v[48:49], off nt
	global_load_dword v66, v[50:51], off nt
	global_load_dword v67, v[52:53], off nt
	global_load_dword v68, v[54:55], off nt
	global_load_dword v69, v[56:57], off nt
	global_load_dword v70, v[58:59], off nt
	global_load_dword v71, v[60:61], off nt
	v_add_co_u32_e32 v48, vcc, 0x10000, v46
	s_nop 1
	v_addc_co_u32_e32 v49, vcc, 0, v47, vcc
	v_add_co_u32_e32 v50, vcc, 0x12000, v46
	s_nop 1
	v_addc_co_u32_e32 v51, vcc, 0, v47, vcc
	v_add_co_u32_e32 v52, vcc, 0x14000, v46
	s_nop 1
	v_addc_co_u32_e32 v53, vcc, 0, v47, vcc
	v_add_co_u32_e32 v54, vcc, 0x16000, v46
	s_nop 1
	v_addc_co_u32_e32 v55, vcc, 0, v47, vcc
	v_add_co_u32_e32 v56, vcc, 0x18000, v46
	s_nop 1
	v_addc_co_u32_e32 v57, vcc, 0, v47, vcc
	v_add_co_u32_e32 v58, vcc, 0x1a000, v46
	s_nop 1
	v_addc_co_u32_e32 v59, vcc, 0, v47, vcc
	v_add_co_u32_e32 v60, vcc, 0x1c000, v46
	s_nop 1
	v_addc_co_u32_e32 v61, vcc, 0, v47, vcc
	v_add_co_u32_e32 v62, vcc, 0x1e000, v46
	s_nop 1
	v_addc_co_u32_e32 v63, vcc, 0, v47, vcc
	global_load_dword v72, v[48:49], off nt
	global_load_dword v73, v[50:51], off nt
	global_load_dword v74, v[52:53], off nt
	global_load_dword v75, v[54:55], off nt
	global_load_dword v76, v[56:57], off nt
	global_load_dword v77, v[58:59], off nt
	global_load_dword v78, v[60:61], off nt
	global_load_dword v79, v[62:63], off nt
	v_add_co_u32_e32 v48, vcc, 0x20000, v46
	s_nop 1
	v_addc_co_u32_e32 v49, vcc, 0, v47, vcc
	v_add_co_u32_e32 v50, vcc, 0x22000, v46
	s_nop 1
	v_addc_co_u32_e32 v51, vcc, 0, v47, vcc
	v_add_co_u32_e32 v52, vcc, 0x24000, v46
	s_nop 1
	v_addc_co_u32_e32 v53, vcc, 0, v47, vcc
	v_add_co_u32_e32 v54, vcc, 0x26000, v46
	s_nop 1
	v_addc_co_u32_e32 v55, vcc, 0, v47, vcc
	v_add_co_u32_e32 v56, vcc, 0x28000, v46
	s_nop 1
	v_addc_co_u32_e32 v57, vcc, 0, v47, vcc
	v_add_co_u32_e32 v58, vcc, 0x2a000, v46
	s_nop 1
	v_addc_co_u32_e32 v59, vcc, 0, v47, vcc
	v_add_co_u32_e32 v60, vcc, 0x2c000, v46
	s_nop 1
	v_addc_co_u32_e32 v61, vcc, 0, v47, vcc
	v_add_co_u32_e32 v62, vcc, 0x2e000, v46
	s_nop 1
	v_addc_co_u32_e32 v63, vcc, 0, v47, vcc
	global_load_dword v80, v[48:49], off nt
	global_load_dword v81, v[50:51], off nt
	global_load_dword v82, v[52:53], off nt
	global_load_dword v83, v[54:55], off nt
	global_load_dword v84, v[56:57], off nt
	global_load_dword v85, v[58:59], off nt
	global_load_dword v86, v[60:61], off nt
	s_nop 0
	global_load_dword v62, v[62:63], off nt
	v_add_co_u32_e32 v48, vcc, 0x30000, v46
	s_nop 1
	v_addc_co_u32_e32 v49, vcc, 0, v47, vcc
	v_add_co_u32_e32 v50, vcc, 0x32000, v46
	s_nop 1
	v_addc_co_u32_e32 v51, vcc, 0, v47, vcc
	v_add_co_u32_e32 v52, vcc, 0x34000, v46
	s_nop 1
	v_addc_co_u32_e32 v53, vcc, 0, v47, vcc
	v_add_co_u32_e32 v54, vcc, 0x36000, v46
	s_nop 1
	v_addc_co_u32_e32 v55, vcc, 0, v47, vcc
	v_add_co_u32_e32 v56, vcc, 0x38000, v46
	s_nop 1
	v_addc_co_u32_e32 v57, vcc, 0, v47, vcc
	v_add_co_u32_e32 v58, vcc, 0x3a000, v46
	s_nop 1
	v_addc_co_u32_e32 v59, vcc, 0, v47, vcc
	v_add_co_u32_e32 v60, vcc, 0x3c000, v46
	s_nop 1
	v_addc_co_u32_e32 v61, vcc, 0, v47, vcc
	v_add_co_u32_e32 v46, vcc, 0x3e000, v46
	s_nop 1
	v_addc_co_u32_e32 v47, vcc, 0, v47, vcc
	global_load_dword v48, v[48:49], off nt
	s_nop 0
	global_load_dword v49, v[50:51], off nt
	s_nop 0
	global_load_dword v50, v[52:53], off nt
	global_load_dword v51, v[54:55], off nt
	s_nop 0
	global_load_dword v52, v[56:57], off nt
	global_load_dword v53, v[58:59], off nt
	global_load_dword v54, v[60:61], off nt
	s_nop 0
	global_load_dword v46, v[46:47], off nt
	s_waitcnt vmcnt(0)
	ds_write2_b32 v29, v64, v65 offset1:66
	ds_write2_b32 v29, v66, v67 offset0:132 offset1:198
	ds_write2_b32 v38, v68, v69 offset0:8 offset1:74
	ds_write2_b32 v38, v70, v71 offset0:140 offset1:206
	ds_write2_b32 v39, v72, v73 offset0:16 offset1:82
	ds_write2_b32 v39, v74, v75 offset0:148 offset1:214
	ds_write2_b32 v40, v76, v77 offset0:24 offset1:90
	ds_write2_b32 v40, v78, v79 offset0:156 offset1:222
	ds_write2_b32 v41, v80, v81 offset0:32 offset1:98
	ds_write2_b32 v41, v82, v83 offset0:164 offset1:230
	ds_write2_b32 v42, v84, v85 offset0:40 offset1:106
	ds_write2_b32 v42, v86, v62 offset0:172 offset1:238
	ds_write2_b32 v43, v48, v49 offset0:48 offset1:114
	ds_write2_b32 v43, v50, v51 offset0:180 offset1:246
	ds_write2_b32 v44, v52, v53 offset0:56 offset1:122
	ds_write2_b32 v44, v54, v46 offset0:188 offset1:254
	s_waitcnt lgkmcnt(0)
; #define GAS __attribute__((address_space(1)))
; #define LAS __attribute__((address_space(3)))
; #define LDS_WAIT() asm volatile("s_waitcnt lgkmcnt(0)" ::: "memory")
; __device__ __forceinline__ unsigned pk2(float lo, float hi) { return f2bf(lo) | (f2bf(hi) << 16); }
; __device__ __forceinline__ void tr_item(const float* W, int ld, int K, int nblk, int item, bf16* WT, bool gu, LAS float* scr, int lane) {
;     ...
;     LDS_WAIT(); asm volatile("" ::: "memory");
;     const int c = lane & 7;
; #pragma unroll
;     for (int j = 0; j < 4; ++j) { const int n = (lane >> 3) + 8 * j; const LAS float* s = scr + (8 * c) * 33 + n;
;         v4u o; o.x = pk2(s[0 * 33], s[1 * 33]); o.y = pk2(s[2 * 33], s[3 * 33]); o.z = pk2(s[4 * 33], s[5 * 33]); o.w = pk2(s[6 * 33], s[7 * 33]);
;         *(GAS v4u*)(WT + (size_t)(drow0 + n) * K + k0 + 8 * c) = o; }
;     LDS_WAIT(); asm volatile("" ::: "memory");
	ds_read2_b32 v[50:51], v34 offset1:8
	ds_read2_b32 v[54:55], v34 offset0:33 offset1:41
	ds_read2_b32 v[56:57], v34 offset0:66 offset1:74
	ds_read2_b32 v[58:59], v34 offset0:99 offset1:107
	ds_read2_b32 v[60:61], v34 offset0:132 offset1:140
	s_waitcnt lgkmcnt(4)
	v_bfe_u32 v46, v50, 16, 1
	v_add3_u32 v46, v50, v46, s14
	s_waitcnt lgkmcnt(3)
	v_bfe_u32 v47, v54, 16, 1
	v_lshrrev_b32_e32 v46, 16, v46
	v_add3_u32 v47, v54, v47, s14
	ds_read2_b32 v[62:63], v34 offset0:165 offset1:173
	v_and_or_b32 v46, v47, s15, v46
	s_waitcnt lgkmcnt(3)
	v_bfe_u32 v47, v56, 16, 1
	v_add3_u32 v47, v56, v47, s14
	s_waitcnt lgkmcnt(2)
	v_bfe_u32 v48, v58, 16, 1
	ds_read2_b32 v[64:65], v34 offset0:198 offset1:206
	v_lshrrev_b32_e32 v47, 16, v47
	v_add3_u32 v48, v58, v48, s14
	ds_read2_b32 v[66:67], v34 offset0:231 offset1:239
	v_and_or_b32 v47, v48, s15, v47
	s_waitcnt lgkmcnt(3)
	v_bfe_u32 v48, v60, 16, 1
	v_add3_u32 v48, v60, v48, s14
	s_waitcnt lgkmcnt(2)
	v_bfe_u32 v49, v62, 16, 1
	v_lshrrev_b32_e32 v48, 16, v48
	v_add3_u32 v49, v62, v49, s14
	v_and_or_b32 v48, v49, s15, v48
	s_waitcnt lgkmcnt(1)
	v_bfe_u32 v49, v64, 16, 1
	v_add_u32_e32 v68, s6, v33
	v_add3_u32 v49, v64, v49, s14
	s_waitcnt lgkmcnt(0)
	v_bfe_u32 v50, v66, 16, 1
	v_ashrrev_i32_e32 v69, 31, v68
	v_lshl_add_u64 v[52:53], v[24:25], 0, s[4:5]
	v_lshrrev_b32_e32 v49, 16, v49
	v_add3_u32 v50, v66, v50, s14
	v_lshlrev_b64 v[68:69], 11, v[68:69]
	v_and_or_b32 v49, v50, s15, v49
	v_lshl_add_u64 v[68:69], v[52:53], 0, v[68:69]
	global_store_dwordx4 v[68:69], v[46:49], off nt
	v_bfe_u32 v50, v67, 16, 1
	v_add3_u32 v50, v67, v50, s14
	v_bfe_u32 v46, v51, 16, 1
	v_add3_u32 v46, v51, v46, s14
	v_bfe_u32 v47, v55, 16, 1
	v_lshrrev_b32_e32 v46, 16, v46
	v_add3_u32 v47, v55, v47, s14
	v_and_or_b32 v46, v47, s15, v46
	v_bfe_u32 v47, v57, 16, 1
	v_add3_u32 v47, v57, v47, s14
	v_bfe_u32 v48, v59, 16, 1
	v_lshrrev_b32_e32 v47, 16, v47
	v_add3_u32 v48, v59, v48, s14
	v_and_or_b32 v47, v48, s15, v47
	v_bfe_u32 v48, v61, 16, 1
	v_add3_u32 v48, v61, v48, s14
	v_bfe_u32 v49, v63, 16, 1
	v_lshrrev_b32_e32 v48, 16, v48
	v_add3_u32 v49, v63, v49, s14
	v_and_or_b32 v48, v49, s15, v48
	v_bfe_u32 v49, v65, 16, 1
	v_add3_u32 v49, v65, v49, s14
	v_lshrrev_b32_e32 v49, 16, v49
	v_and_or_b32 v49, v50, s15, v49
	v_add_u32_e32 v50, s6, v35
	v_ashrrev_i32_e32 v51, 31, v50
	v_lshlrev_b64 v[50:51], 11, v[50:51]
	ds_read2_b32 v[54:55], v34 offset0:16 offset1:24
	v_lshl_add_u64 v[50:51], v[52:53], 0, v[50:51]
	global_store_dwordx4 v[50:51], v[46:49], off nt
	ds_read2_b32 v[50:51], v34 offset0:49 offset1:57
	ds_read2_b32 v[56:57], v34 offset0:82 offset1:90
	ds_read2_b32 v[58:59], v34 offset0:115 offset1:123
	s_waitcnt lgkmcnt(3)
	v_bfe_u32 v46, v54, 16, 1
	v_add3_u32 v46, v54, v46, s14
	s_waitcnt lgkmcnt(2)
	v_bfe_u32 v47, v50, 16, 1
	ds_read2_b32 v[60:61], v34 offset0:148 offset1:156
	v_lshrrev_b32_e32 v46, 16, v46
	v_add3_u32 v47, v50, v47, s14
	ds_read2_b32 v[62:63], v34 offset0:181 offset1:189
	v_and_or_b32 v46, v47, s15, v46
	s_waitcnt lgkmcnt(3)
	v_bfe_u32 v47, v56, 16, 1
	v_add3_u32 v47, v56, v47, s14
	s_waitcnt lgkmcnt(2)
	v_bfe_u32 v48, v58, 16, 1
	ds_read2_b32 v[64:65], v34 offset0:214 offset1:222
	v_lshrrev_b32_e32 v47, 16, v47
	v_add3_u32 v48, v58, v48, s14
	ds_read2_b32 v[66:67], v34 offset0:247 offset1:255
	v_and_or_b32 v47, v48, s15, v47
	s_waitcnt lgkmcnt(3)
	v_bfe_u32 v48, v60, 16, 1
	v_add3_u32 v48, v60, v48, s14
	s_waitcnt lgkmcnt(2)
	v_bfe_u32 v49, v62, 16, 1
	v_lshrrev_b32_e32 v48, 16, v48
	v_add3_u32 v49, v62, v49, s14
	v_and_or_b32 v48, v49, s15, v48
	s_waitcnt lgkmcnt(1)
	v_bfe_u32 v49, v64, 16, 1
	v_add_u32_e32 v68, s6, v36
	v_add3_u32 v49, v64, v49, s14
	s_waitcnt lgkmcnt(0)
	v_bfe_u32 v50, v66, 16, 1
	v_ashrrev_i32_e32 v69, 31, v68
	v_lshrrev_b32_e32 v49, 16, v49
	v_add3_u32 v50, v66, v50, s14
	v_lshlrev_b64 v[68:69], 11, v[68:69]
	v_and_or_b32 v49, v50, s15, v49
	v_lshl_add_u64 v[68:69], v[52:53], 0, v[68:69]
	global_store_dwordx4 v[68:69], v[46:49], off nt
	v_bfe_u32 v50, v67, 16, 1
	v_add3_u32 v50, v67, v50, s14
	v_bfe_u32 v46, v55, 16, 1
	v_add3_u32 v46, v55, v46, s14
	v_bfe_u32 v47, v51, 16, 1
	v_lshrrev_b32_e32 v46, 16, v46
	v_add3_u32 v47, v51, v47, s14
	v_and_or_b32 v46, v47, s15, v46
	v_bfe_u32 v47, v57, 16, 1
	v_add3_u32 v47, v57, v47, s14
	v_bfe_u32 v48, v59, 16, 1
	v_lshrrev_b32_e32 v47, 16, v47
	v_add3_u32 v48, v59, v48, s14
	v_and_or_b32 v47, v48, s15, v47
	v_bfe_u32 v48, v61, 16, 1
	v_add3_u32 v48, v61, v48, s14
	v_bfe_u32 v49, v63, 16, 1
	v_lshrrev_b32_e32 v48, 16, v48
	v_add3_u32 v49, v63, v49, s14
	v_and_or_b32 v48, v49, s15, v48
	v_bfe_u32 v49, v65, 16, 1
	v_add3_u32 v49, v65, v49, s14
	v_lshrrev_b32_e32 v49, 16, v49
	v_and_or_b32 v49, v50, s15, v49
	v_add_u32_e32 v50, s6, v37
	v_ashrrev_i32_e32 v51, 31, v50
	v_lshlrev_b64 v[50:51], 11, v[50:51]
	v_lshl_add_u64 v[50:51], v[52:53], 0, v[50:51]
	global_store_dwordx4 v[50:51], v[46:49], off nt
	s_waitcnt lgkmcnt(0)

; #define LAS __attribute__((address_space(3)))
; #define LDS_WAIT() asm volatile("s_waitcnt lgkmcnt(0)" ::: "memory")
; __device__ __forceinline__ void tr_item(const float* W, int ld, int K, int nblk, int item, bf16* WT, bool gu, LAS float* scr, int lane) {
;     const int kb = item / nblk, nb = item % nblk, k0 = 64 * kb, n0 = 32 * nb;
;     int drow0 = n0;
;     if (gu) { const int bj = n0 / FF, j = n0 - bj * FF; drow0 = 256 * (j / 128) + 128 * bj + (j % 128); }
;     { float t_[32];
; #pragma unroll
;       for (int i = 0; i < 32; ++i) t_[i] = W[(size_t)(k0 + 2 * i + (lane >> 5)) * ld + n0 + (lane & 31)];
; #pragma unroll
;       for (int i = 0; i < 32; ++i) scr[(2 * i + (lane >> 5)) * 33 + (lane & 31)] = t_[i]; }
;     LDS_WAIT(); asm volatile("" ::: "memory");
; __device__ __forceinline__ void convert_items(Frame& F, const Args& a, int lo, int hi, int w, int nw) {
;     ...
;         if (r < I_FI) { tr_item(a.in[7], 3 * D + 16, D, 96, r, (bf16*)(F.ws + WS_WFOXIN), false, scr, lane); continue; } r -= I_FI;
.LBB0_1183:
	s_andn2_b64 vcc, exec, s[6:7]
	s_cbranch_vccnz .LBB0_1160
	s_mul_hi_i32 s4, s16, 0x2aaaaaab
	s_lshr_b32 s6, s4, 31
	s_ashr_i32 s4, s4, 4
	s_add_i32 s4, s4, s6
	s_lshl_b32 s8, s4, 6
	s_mulk_i32 s4, 0xf400
	s_add_i32 s6, s10, s4
	v_add_u32_e32 v64, s8, v28
	s_ashr_i32 s7, s6, 31
	v_lshl_add_u64 v[46:47], s[6:7], 2, v[16:17]
	v_add_u32_e32 v50, 2, v64
	v_add_u32_e32 v52, 4, v64
	v_add_u32_e32 v54, 6, v64
	v_add_u32_e32 v56, 8, v64
	v_add_u32_e32 v58, 10, v64
	v_add_u32_e32 v60, 12, v64
	v_add_u32_e32 v62, 14, v64
	v_mad_i64_i32 v[48:49], s[26:27], v64, s24, v[46:47]
	v_mad_i64_i32 v[50:51], s[26:27], v50, s24, v[46:47]
	v_mad_i64_i32 v[52:53], s[26:27], v52, s24, v[46:47]
	v_mad_i64_i32 v[54:55], s[26:27], v54, s24, v[46:47]
	v_mad_i64_i32 v[56:57], s[26:27], v56, s24, v[46:47]
	v_mad_i64_i32 v[58:59], s[26:27], v58, s24, v[46:47]
	v_mad_i64_i32 v[60:61], s[26:27], v60, s24, v[46:47]
	v_mad_i64_i32 v[62:63], s[26:27], v62, s24, v[46:47]
	global_load_dword v65, v[48:49], off nt
	global_load_dword v66, v[50:51], off nt
	global_load_dword v67, v[52:53], off nt
	global_load_dword v68, v[54:55], off nt
	global_load_dword v69, v[56:57], off nt
	global_load_dword v70, v[58:59], off nt
	global_load_dword v71, v[60:61], off nt
	global_load_dword v72, v[62:63], off nt
	v_add_u32_e32 v48, 16, v64
	v_add_u32_e32 v50, 18, v64
	v_add_u32_e32 v52, 20, v64
	v_add_u32_e32 v54, 22, v64
	v_add_u32_e32 v56, 24, v64
	v_add_u32_e32 v58, 26, v64
	v_add_u32_e32 v60, 28, v64
	v_add_u32_e32 v62, 30, v64
	v_mad_i64_i32 v[48:49], s[26:27], v48, s24, v[46:47]
	v_mad_i64_i32 v[50:51], s[26:27], v50, s24, v[46:47]
	v_mad_i64_i32 v[52:53], s[26:27], v52, s24, v[46:47]
	v_mad_i64_i32 v[54:55], s[26:27], v54, s24, v[46:47]
	v_mad_i64_i32 v[56:57], s[26:27], v56, s24, v[46:47]
	v_mad_i64_i32 v[58:59], s[26:27], v58, s24, v[46:47]
	v_mad_i64_i32 v[60:61], s[26:27], v60, s24, v[46:47]
	v_mad_i64_i32 v[62:63], s[26:27], v62, s24, v[46:47]
	global_load_dword v73, v[48:49], off nt
	global_load_dword v74, v[50:51], off nt
	global_load_dword v75, v[52:53], off nt
	global_load_dword v76, v[54:55], off nt
	global_load_dword v77, v[56:57], off nt
	global_load_dword v78, v[58:59], off nt
	global_load_dword v79, v[60:61], off nt
	global_load_dword v80, v[62:63], off nt
	v_add_u32_e32 v48, 32, v64
	v_add_u32_e32 v50, 34, v64
	v_add_u32_e32 v52, 36, v64
	v_add_u32_e32 v54, 38, v64
	v_add_u32_e32 v56, 40, v64
	v_add_u32_e32 v58, 42, v64
	v_add_u32_e32 v60, 44, v64
	v_add_u32_e32 v62, 46, v64
	v_mad_i64_i32 v[48:49], s[26:27], v48, s24, v[46:47]
	v_mad_i64_i32 v[50:51], s[26:27], v50, s24, v[46:47]
	v_mad_i64_i32 v[52:53], s[26:27], v52, s24, v[46:47]
	v_mad_i64_i32 v[54:55], s[26:27], v54, s24, v[46:47]
	v_mad_i64_i32 v[56:57], s[26:27], v56, s24, v[46:47]
	v_mad_i64_i32 v[58:59], s[26:27], v58, s24, v[46:47]
	v_mad_i64_i32 v[60:61], s[26:27], v60, s24, v[46:47]
	v_mad_i64_i32 v[62:63], s[26:27], v62, s24, v[46:47]
	global_load_dword v81, v[48:49], off nt
	global_load_dword v82, v[50:51], off nt
	global_load_dword v83, v[52:53], off nt
	global_load_dword v84, v[54:55], off nt
	global_load_dword v85, v[56:57], off nt
	global_load_dword v86, v[58:59], off nt
	global_load_dword v87, v[60:61], off nt
	s_nop 0
	global_load_dword v62, v[62:63], off nt
	v_add_u32_e32 v48, 48, v64
	v_add_u32_e32 v50, 50, v64
	v_add_u32_e32 v52, 52, v64
	v_add_u32_e32 v54, 54, v64
	v_add_u32_e32 v56, 56, v64
	v_add_u32_e32 v58, 58, v64
	v_add_u32_e32 v60, 60, v64
	v_add_u32_e32 v63, 62, v64
	v_mad_i64_i32 v[48:49], s[26:27], v48, s24, v[46:47]
	v_mad_i64_i32 v[50:51], s[26:27], v50, s24, v[46:47]
	v_mad_i64_i32 v[52:53], s[26:27], v52, s24, v[46:47]
	v_mad_i64_i32 v[54:55], s[26:27], v54, s24, v[46:47]
	v_mad_i64_i32 v[56:57], s[26:27], v56, s24, v[46:47]
	v_mad_i64_i32 v[58:59], s[26:27], v58, s24, v[46:47]
	v_mad_i64_i32 v[60:61], s[26:27], v60, s24, v[46:47]
	v_mad_i64_i32 v[46:47], s[26:27], v63, s24, v[46:47]
	global_load_dword v48, v[48:49], off nt
	s_nop 0
	global_load_dword v49, v[50:51], off nt
	s_nop 0
	global_load_dword v50, v[52:53], off nt
	global_load_dword v51, v[54:55], off nt
	s_nop 0
	global_load_dword v52, v[56:57], off nt
	global_load_dword v53, v[58:59], off nt
	global_load_dword v54, v[60:61], off nt
	s_nop 0
	global_load_dword v46, v[46:47], off nt
	s_waitcnt vmcnt(0)
	ds_write2_b32 v29, v65, v66 offset1:66
	ds_write2_b32 v29, v67, v68 offset0:132 offset1:198
	ds_write2_b32 v38, v69, v70 offset0:8 offset1:74
	ds_write2_b32 v38, v71, v72 offset0:140 offset1:206
	ds_write2_b32 v39, v73, v74 offset0:16 offset1:82
	ds_write2_b32 v39, v75, v76 offset0:148 offset1:214
	ds_write2_b32 v40, v77, v78 offset0:24 offset1:90
	ds_write2_b32 v40, v79, v80 offset0:156 offset1:222
	ds_write2_b32 v41, v81, v82 offset0:32 offset1:98
	ds_write2_b32 v41, v83, v84 offset0:164 offset1:230
	ds_write2_b32 v42, v85, v86 offset0:40 offset1:106
	ds_write2_b32 v42, v87, v62 offset0:172 offset1:238
	ds_write2_b32 v43, v48, v49 offset0:48 offset1:114
	ds_write2_b32 v43, v50, v51 offset0:180 offset1:246
	ds_write2_b32 v44, v52, v53 offset0:56 offset1:122
	ds_write2_b32 v44, v54, v46 offset0:188 offset1:254
	s_waitcnt lgkmcnt(0)
; #define GAS __attribute__((address_space(1)))
; #define LAS __attribute__((address_space(3)))
; #define LDS_WAIT() asm volatile("s_waitcnt lgkmcnt(0)" ::: "memory")
; __device__ __forceinline__ unsigned pk2(float lo, float hi) { return f2bf(lo) | (f2bf(hi) << 16); }
; __device__ __forceinline__ void tr_item(const float* W, int ld, int K, int nblk, int item, bf16* WT, bool gu, LAS float* scr, int lane) {
;     ...
;     LDS_WAIT(); asm volatile("" ::: "memory");
;     const int c = lane & 7;
; #pragma unroll
;     for (int j = 0; j < 4; ++j) { const int n = (lane >> 3) + 8 * j; const LAS float* s = scr + (8 * c) * 33 + n;
;         v4u o; o.x = pk2(s[0 * 33], s[1 * 33]); o.y = pk2(s[2 * 33], s[3 * 33]); o.z = pk2(s[4 * 33], s[5 * 33]); o.w = pk2(s[6 * 33], s[7 * 33]);
;         *(GAS v4u*)(WT + (size_t)(drow0 + n) * K + k0 + 8 * c) = o; }
;     LDS_WAIT(); asm volatile("" ::: "memory");
	ds_read2_b32 v[50:51], v34 offset1:8
	ds_read2_b32 v[54:55], v34 offset0:33 offset1:41
	ds_read2_b32 v[56:57], v34 offset0:66 offset1:74
	ds_read2_b32 v[58:59], v34 offset0:99 offset1:107
	ds_read2_b32 v[60:61], v34 offset0:132 offset1:140
	s_waitcnt lgkmcnt(4)
	v_bfe_u32 v46, v50, 16, 1
	v_add3_u32 v46, v50, v46, s14
	s_waitcnt lgkmcnt(3)
	v_bfe_u32 v47, v54, 16, 1
	v_lshrrev_b32_e32 v46, 16, v46
	v_add3_u32 v47, v54, v47, s14
	ds_read2_b32 v[62:63], v34 offset0:165 offset1:173
	v_and_or_b32 v46, v47, s15, v46
	s_waitcnt lgkmcnt(3)
	v_bfe_u32 v47, v56, 16, 1
	v_add3_u32 v47, v56, v47, s14
	s_waitcnt lgkmcnt(2)
	v_bfe_u32 v48, v58, 16, 1
	ds_read2_b32 v[64:65], v34 offset0:198 offset1:206
	v_lshrrev_b32_e32 v47, 16, v47
	v_add3_u32 v48, v58, v48, s14
	ds_read2_b32 v[66:67], v34 offset0:231 offset1:239
	v_and_or_b32 v47, v48, s15, v47
	s_waitcnt lgkmcnt(3)
	v_bfe_u32 v48, v60, 16, 1
	v_add3_u32 v48, v60, v48, s14
	s_waitcnt lgkmcnt(2)
	v_bfe_u32 v49, v62, 16, 1
	v_lshrrev_b32_e32 v48, 16, v48
	v_add3_u32 v49, v62, v49, s14
	v_and_or_b32 v48, v49, s15, v48
	s_waitcnt lgkmcnt(1)
	v_bfe_u32 v49, v64, 16, 1
	v_add_u32_e32 v68, s6, v33
	s_ashr_i32 s9, s8, 31
	v_add3_u32 v49, v64, v49, s14
	s_waitcnt lgkmcnt(0)
	v_bfe_u32 v50, v66, 16, 1
	v_ashrrev_i32_e32 v69, 31, v68
	v_lshl_add_u64 v[52:53], s[8:9], 1, v[26:27]
	v_lshrrev_b32_e32 v49, 16, v49
	v_add3_u32 v50, v66, v50, s14
	v_lshlrev_b64 v[70:71], 11, v[68:69]
	v_and_or_b32 v49, v50, s15, v49
	v_lshl_add_u64 v[70:71], v[52:53], 0, v[70:71]
	global_store_dwordx4 v[70:71], v[46:49], off nt
	v_bfe_u32 v50, v67, 16, 1
	v_add3_u32 v50, v67, v50, s14
	v_bfe_u32 v46, v51, 16, 1
	v_add3_u32 v46, v51, v46, s14
	v_bfe_u32 v47, v55, 16, 1
	v_lshrrev_b32_e32 v46, 16, v46
	v_add3_u32 v47, v55, v47, s14
	v_and_or_b32 v46, v47, s15, v46
	v_bfe_u32 v47, v57, 16, 1
	v_add3_u32 v47, v57, v47, s14
	v_bfe_u32 v48, v59, 16, 1
	v_lshrrev_b32_e32 v47, 16, v47
	v_add3_u32 v48, v59, v48, s14
	v_and_or_b32 v47, v48, s15, v47
	v_bfe_u32 v48, v61, 16, 1
	v_add3_u32 v48, v61, v48, s14
	v_bfe_u32 v49, v63, 16, 1
	v_lshrrev_b32_e32 v48, 16, v48
	v_add3_u32 v49, v63, v49, s14
	v_and_or_b32 v48, v49, s15, v48
	v_bfe_u32 v49, v65, 16, 1
	v_add3_u32 v49, v65, v49, s14
	v_lshrrev_b32_e32 v49, 16, v49
	v_and_or_b32 v49, v50, s15, v49
	v_add_u32_e32 v50, 8, v68
	v_ashrrev_i32_e32 v51, 31, v50
	v_lshlrev_b64 v[50:51], 11, v[50:51]
	ds_read2_b32 v[54:55], v34 offset0:16 offset1:24
	v_lshl_add_u64 v[50:51], v[52:53], 0, v[50:51]
	global_store_dwordx4 v[50:51], v[46:49], off nt
	ds_read2_b32 v[50:51], v34 offset0:49 offset1:57
	ds_read2_b32 v[56:57], v34 offset0:82 offset1:90
	ds_read2_b32 v[58:59], v34 offset0:115 offset1:123
	s_waitcnt lgkmcnt(3)
	v_bfe_u32 v46, v54, 16, 1
	v_add3_u32 v46, v54, v46, s14
	s_waitcnt lgkmcnt(2)
	v_bfe_u32 v47, v50, 16, 1
	ds_read2_b32 v[60:61], v34 offset0:148 offset1:156
	v_lshrrev_b32_e32 v46, 16, v46
	v_add3_u32 v47, v50, v47, s14
	ds_read2_b32 v[62:63], v34 offset0:181 offset1:189
	v_and_or_b32 v46, v47, s15, v46
	s_waitcnt lgkmcnt(3)
	v_bfe_u32 v47, v56, 16, 1
	v_add3_u32 v47, v56, v47, s14
	s_waitcnt lgkmcnt(2)
	v_bfe_u32 v48, v58, 16, 1
	ds_read2_b32 v[64:65], v34 offset0:214 offset1:222
	v_lshrrev_b32_e32 v47, 16, v47
	v_add3_u32 v48, v58, v48, s14
	ds_read2_b32 v[66:67], v34 offset0:247 offset1:255
	v_and_or_b32 v47, v48, s15, v47
	s_waitcnt lgkmcnt(3)
	v_bfe_u32 v48, v60, 16, 1
	v_add3_u32 v48, v60, v48, s14
	s_waitcnt lgkmcnt(2)
	v_bfe_u32 v49, v62, 16, 1
	v_lshrrev_b32_e32 v48, 16, v48
	v_add3_u32 v49, v62, v49, s14
	v_and_or_b32 v48, v49, s15, v48
	s_waitcnt lgkmcnt(1)
	v_bfe_u32 v49, v64, 16, 1
	v_add_u32_e32 v70, 16, v68
	v_add3_u32 v49, v64, v49, s14
	s_waitcnt lgkmcnt(0)
	v_bfe_u32 v50, v66, 16, 1
	v_ashrrev_i32_e32 v71, 31, v70
	v_lshrrev_b32_e32 v49, 16, v49
	v_add3_u32 v50, v66, v50, s14
	v_lshlrev_b64 v[70:71], 11, v[70:71]
	v_and_or_b32 v49, v50, s15, v49
	v_lshl_add_u64 v[70:71], v[52:53], 0, v[70:71]
	global_store_dwordx4 v[70:71], v[46:49], off nt
	v_bfe_u32 v50, v67, 16, 1
	v_add3_u32 v50, v67, v50, s14
	v_bfe_u32 v46, v55, 16, 1
	v_add3_u32 v46, v55, v46, s14
	v_bfe_u32 v47, v51, 16, 1
	v_lshrrev_b32_e32 v46, 16, v46
	v_add3_u32 v47, v51, v47, s14
	v_and_or_b32 v46, v47, s15, v46
	v_bfe_u32 v47, v57, 16, 1
	v_add3_u32 v47, v57, v47, s14
	v_bfe_u32 v48, v59, 16, 1
	v_lshrrev_b32_e32 v47, 16, v47
	v_add3_u32 v48, v59, v48, s14
	v_and_or_b32 v47, v48, s15, v47
	v_bfe_u32 v48, v61, 16, 1
	v_add3_u32 v48, v61, v48, s14
	v_bfe_u32 v49, v63, 16, 1
	v_lshrrev_b32_e32 v48, 16, v48
	v_add3_u32 v49, v63, v49, s14
	v_and_or_b32 v48, v49, s15, v48
	v_bfe_u32 v49, v65, 16, 1
	v_add3_u32 v49, v65, v49, s14
	v_lshrrev_b32_e32 v49, 16, v49
	v_and_or_b32 v49, v50, s15, v49
	v_add_u32_e32 v50, 24, v68
	v_ashrrev_i32_e32 v51, 31, v50
	v_lshlrev_b64 v[50:51], 11, v[50:51]
	v_lshl_add_u64 v[50:51], v[52:53], 0, v[50:51]
	global_store_dwordx4 v[50:51], v[46:49], off nt
	s_waitcnt lgkmcnt(0)
	s_branch .LBB0_1160

; #define LAS __attribute__((address_space(3)))
; __device__ __forceinline__ void tr_item8(const float* W, int ld, int K, int nblk, int item, unsigned char* WT, bool gu, float scale, LAS float* scr, int lane) {
;     const int kb = item / nblk, nb = item % nblk, k0 = 64 * kb, n0 = 32 * nb;
;     int drow0 = n0;
;     if (gu) { const int bj = n0 / FF, j = n0 - bj * FF; drow0 = 256 * (j / 128) + 128 * bj + (j % 128); }
;     { float t_[32];
; #pragma unroll
;       for (int i = 0; i < 32; ++i) t_[i] = W[(size_t)(k0 + 2 * i + (lane >> 5)) * ld + n0 + (lane & 31)];
; __device__ __forceinline__ void convert_items(Frame& F, const Args& a, int lo, int hi, int w, int nw) {
;     ...
;     for (int it = lo + w; it < hi; it += nw) {
;         int r = it;
;         if (r < I_FI) { tr_item(a.in[7], 3 * D + 16, D, 96, r, (bf16*)(F.ws + WS_WFOXIN), false, scr, lane); continue; } r -= I_FI;
;         if (r < I_FO) { tr_item(a.in[9], D, D, 32, r, (bf16*)(F.ws + WS_WFOXOUT), false, scr, lane); continue; } r -= I_FO;
;         if (r < I_SI) { tr_item(a.in[10], D + 512, D, 48, r, (bf16*)(F.ws + WS_WSWAIN), false, scr, lane); continue; } r -= I_SI;
;         if (r < I_SO) { tr_item(a.in[12], D, D, 32, r, (bf16*)(F.ws + WS_WSWAOUT), false, scr, lane); continue; } r -= I_SO;
;         if (r < I_GU) { tr_item8(a.in[14], 2 * FF, D, 224, r, F.ws + WS_WGU, true, WSC_GU, scr, lane); continue; } r -= I_GU;
;         if (r < I_DN) { tr_item8(a.in[15], D, FF, 32, r, F.ws + WS_WDN, false, WSC_DN, scr, lane); continue; } r -= I_DN;
;         if (r < NE * I_GU) { const int e = r / I_GU, rr = r % I_GU; tr_item8(a.in[18] + (size_t)e * D * 2 * FF, 2 * FF, D, 224, rr, F.ws + WS_WMGU + (size_t)e * 2 * FF * D, true, WSC_GU, scr, lane); continue; } r -= NE * I_GU;
;         { const int e = r / I_DN, rr = r % I_DN; tr_item8(a.in[19] + (size_t)e * FF * D, D, FF, 32, rr, F.ws + WS_WMDN + (size_t)e * D * FF, false, WSC_DN, scr, lane); }
.LBB0_1296:
	s_cmpk_gt_i32 s8, 0x5ff
	s_mov_b64 s[4:5], -1
	s_cbranch_scc0 .LBB0_1322
	s_cmpk_gt_u32 s8, 0x7ff
	s_cbranch_scc0 .LBB0_1319
	s_cmpk_gt_u32 s8, 0xaff
	s_cbranch_scc0 .LBB0_1316
	s_cmpk_gt_u32 s8, 0xcff
	s_cbranch_scc0 .LBB0_1313
	s_cmpk_gt_u32 s8, 0x1aff
	s_cbranch_scc0 .LBB0_1310
	s_cmpk_gt_u32 s8, 0x21ff
	s_cbranch_scc0 .LBB0_1307
	s_cmpk_gt_u32 s8, 0x91ff
	s_cbranch_scc0 .LBB0_1304
	s_add_i32 s0, s8, 0x6e00
	s_bfe_u32 s4, s0, 0x80008
	s_mulk_i32 s4, 0x2493
	s_lshr_b32 s4, s4, 16
	s_mul_i32 s5, s4, 0x700
	v_readlane_b32 s40, v254, 28
	s_sub_i32 s6, s0, s5
	s_mul_i32 s0, s4, 0xe00000
	v_readlane_b32 s46, v254, 34
	v_readlane_b32 s47, v254, 35
	s_add_u32 s7, s46, s0
	s_addc_u32 s31, s47, 0
	s_mul_i32 s4, s4, 0x380000
	s_add_u32 s4, s66, s4
	s_addc_u32 s5, s58, 0
	s_lshl_b32 s0, s6, 5
	s_and_b32 s0, s0, 0x3e0
	s_lshl_b32 s6, s6, 1
	s_and_b32 s6, s6, 0xfc0
	s_lshl_b32 s40, s0, 2
	v_readlane_b32 s41, v254, 29
	v_add_u32_e32 v28, s6, v30
	s_add_u32 s40, s7, s40
	s_addc_u32 s41, s31, 0
	v_ashrrev_i32_e32 v29, 31, v28
	v_lshl_add_u64 v[48:49], s[40:41], 0, v[0:1]
	v_lshlrev_b64 v[28:29], 12, v[28:29]
	v_lshl_add_u64 v[28:29], v[48:49], 0, v[28:29]
	s_movk_i32 s7, 0x2000
	v_add_co_u32_e32 v48, vcc, s7, v28
	s_movk_i32 s7, 0x4000
	s_nop 0
	v_addc_co_u32_e32 v49, vcc, 0, v29, vcc
	global_load_dword v50, v[28:29], off nt
	global_load_dword v51, v[48:49], off nt
	v_add_co_u32_e32 v48, vcc, s7, v28
	s_movk_i32 s7, 0x6000
	s_nop 0
	v_addc_co_u32_e32 v49, vcc, 0, v29, vcc
	global_load_dword v52, v[48:49], off nt
	v_add_co_u32_e32 v48, vcc, s7, v28
	s_mov_b32 s7, 0x8000
	s_nop 0
	v_addc_co_u32_e32 v49, vcc, 0, v29, vcc
	global_load_dword v53, v[48:49], off nt
	v_add_co_u32_e32 v48, vcc, s7, v28
	s_mov_b32 s7, 0xa000
	s_nop 0
	v_addc_co_u32_e32 v49, vcc, 0, v29, vcc
	global_load_dword v54, v[48:49], off nt
	v_add_co_u32_e32 v48, vcc, s7, v28
	s_mov_b32 s7, 0xc000
	s_nop 0
	v_addc_co_u32_e32 v49, vcc, 0, v29, vcc
	global_load_dword v55, v[48:49], off nt
	v_add_co_u32_e32 v48, vcc, s7, v28
	s_mov_b32 s7, 0xe000
	s_nop 0
	v_addc_co_u32_e32 v49, vcc, 0, v29, vcc
	global_load_dword v56, v[48:49], off nt
	v_add_co_u32_e32 v48, vcc, s7, v28
	s_mov_b32 s7, 0x10000
	s_nop 0
	v_addc_co_u32_e32 v49, vcc, 0, v29, vcc
	global_load_dword v57, v[48:49], off nt
	v_add_co_u32_e32 v48, vcc, s7, v28
	s_mov_b32 s7, 0x12000
	s_nop 0
	v_addc_co_u32_e32 v49, vcc, 0, v29, vcc
	global_load_dword v58, v[48:49], off nt
	v_add_co_u32_e32 v48, vcc, s7, v28
	s_mov_b32 s7, 0x14000
	s_nop 0
	v_addc_co_u32_e32 v49, vcc, 0, v29, vcc
	global_load_dword v59, v[48:49], off nt
	v_add_co_u32_e32 v48, vcc, s7, v28
	s_mov_b32 s7, 0x16000
	s_nop 0
	v_addc_co_u32_e32 v49, vcc, 0, v29, vcc
	global_load_dword v60, v[48:49], off nt
	v_add_co_u32_e32 v48, vcc, s7, v28
	s_mov_b32 s7, 0x18000
	s_nop 0
	v_addc_co_u32_e32 v49, vcc, 0, v29, vcc
	global_load_dword v61, v[48:49], off nt
	v_add_co_u32_e32 v48, vcc, s7, v28
	s_mov_b32 s7, 0x1a000
	s_nop 0
	v_addc_co_u32_e32 v49, vcc, 0, v29, vcc
	global_load_dword v62, v[48:49], off nt
	v_add_co_u32_e32 v48, vcc, s7, v28
	s_mov_b32 s7, 0x1c000
	s_nop 0
	v_addc_co_u32_e32 v49, vcc, 0, v29, vcc
	global_load_dword v63, v[48:49], off nt
	v_add_co_u32_e32 v48, vcc, s7, v28
	s_mov_b32 s7, 0x1e000
	s_nop 0
	v_addc_co_u32_e32 v49, vcc, 0, v29, vcc
	global_load_dword v64, v[48:49], off nt
	v_add_co_u32_e32 v48, vcc, s7, v28
	s_mov_b32 s7, 0x20000
	s_nop 0
	v_addc_co_u32_e32 v49, vcc, 0, v29, vcc
	global_load_dword v65, v[48:49], off nt
	v_add_co_u32_e32 v48, vcc, s7, v28
	s_mov_b32 s7, 0x22000
	s_nop 0
	v_addc_co_u32_e32 v49, vcc, 0, v29, vcc
	global_load_dword v66, v[48:49], off nt
	v_add_co_u32_e32 v48, vcc, s7, v28
	s_mov_b32 s7, 0x24000
	s_nop 0
	v_addc_co_u32_e32 v49, vcc, 0, v29, vcc
	global_load_dword v67, v[48:49], off nt
	v_add_co_u32_e32 v48, vcc, s7, v28
	s_mov_b32 s7, 0x26000
	s_nop 0
	v_addc_co_u32_e32 v49, vcc, 0, v29, vcc
	global_load_dword v68, v[48:49], off nt
	v_add_co_u32_e32 v48, vcc, s7, v28
	s_mov_b32 s7, 0x28000
	s_nop 0
	v_addc_co_u32_e32 v49, vcc, 0, v29, vcc
	global_load_dword v69, v[48:49], off nt
	v_add_co_u32_e32 v48, vcc, s7, v28
	s_mov_b32 s7, 0x2a000
	s_nop 0
	v_addc_co_u32_e32 v49, vcc, 0, v29, vcc
	global_load_dword v70, v[48:49], off nt
	v_add_co_u32_e32 v48, vcc, s7, v28
	s_mov_b32 s7, 0x2c000
	s_nop 0
	v_addc_co_u32_e32 v49, vcc, 0, v29, vcc
	global_load_dword v71, v[48:49], off nt
	v_add_co_u32_e32 v48, vcc, s7, v28
	s_mov_b32 s7, 0x2e000
	s_nop 0
	v_addc_co_u32_e32 v49, vcc, 0, v29, vcc
	global_load_dword v72, v[48:49], off nt
	v_add_co_u32_e32 v48, vcc, s7, v28
	s_mov_b32 s7, 0x30000
	s_nop 0
	v_addc_co_u32_e32 v49, vcc, 0, v29, vcc
	global_load_dword v73, v[48:49], off nt
	v_add_co_u32_e32 v48, vcc, s7, v28
	s_mov_b32 s7, 0x32000
	s_nop 0
	v_addc_co_u32_e32 v49, vcc, 0, v29, vcc
	global_load_dword v74, v[48:49], off nt
	v_add_co_u32_e32 v48, vcc, s7, v28
	s_mov_b32 s7, 0x34000
	s_nop 0
	v_addc_co_u32_e32 v49, vcc, 0, v29, vcc
	global_load_dword v75, v[48:49], off nt
	v_add_co_u32_e32 v48, vcc, s7, v28
	s_mov_b32 s7, 0x36000
	s_nop 0
	v_addc_co_u32_e32 v49, vcc, 0, v29, vcc
	global_load_dword v76, v[48:49], off nt
	v_add_co_u32_e32 v48, vcc, s7, v28
	s_mov_b32 s7, 0x38000
	s_nop 0
	v_addc_co_u32_e32 v49, vcc, 0, v29, vcc
	global_load_dword v77, v[48:49], off nt
	v_add_co_u32_e32 v48, vcc, s7, v28
	s_mov_b32 s7, 0x3a000
	s_nop 0
	v_addc_co_u32_e32 v49, vcc, 0, v29, vcc
	global_load_dword v78, v[48:49], off nt
	v_add_co_u32_e32 v48, vcc, s7, v28
	s_mov_b32 s7, 0x3c000
	s_nop 0
	v_addc_co_u32_e32 v49, vcc, 0, v29, vcc
	global_load_dword v79, v[48:49], off nt
	v_add_co_u32_e32 v48, vcc, s7, v28
	s_mov_b32 s7, 0x3e000
	s_nop 0
	v_addc_co_u32_e32 v49, vcc, 0, v29, vcc
	v_add_co_u32_e32 v28, vcc, s7, v28
	global_load_dword v48, v[48:49], off nt
	s_nop 0
	v_addc_co_u32_e32 v29, vcc, 0, v29, vcc
	global_load_dword v28, v[28:29], off nt
	s_waitcnt vmcnt(31)
; __device__ __forceinline__ unsigned cvt_pk4_fp8(float a, float b, float c, float d) { int w = 0; w = __builtin_amdgcn_cvt_pk_fp8_f32(a, b, w, false); w = __builtin_amdgcn_cvt_pk_fp8_f32(c, d, w, true); return (unsigned)w; }
; #define GAS __attribute__((address_space(1)))
; #define LAS __attribute__((address_space(3)))
; #define LDS_WAIT() asm volatile("s_waitcnt lgkmcnt(0)" ::: "memory")
; __device__ __forceinline__ void tr_item8(const float* W, int ld, int K, int nblk, int item, unsigned char* WT, bool gu, float scale, LAS float* scr, int lane) {
;     ...
; #pragma unroll
;       for (int i = 0; i < 32; ++i) scr[(2 * i + (lane >> 5)) * 33 + (lane & 31)] = t_[i] * scale; }
;     LDS_WAIT(); asm volatile("" ::: "memory");
;     const int c = lane & 3;
; #pragma unroll
;     for (int j = 0; j < 2; ++j) { const int n = (lane >> 2) + 16 * j; const LAS float* sp = scr + (16 * c) * 33 + n;
;         v4u o; o.x = pg8::cvt_pk4_fp8(sp[0 * 33], sp[1 * 33], sp[2 * 33], sp[3 * 33]); o.y = pg8::cvt_pk4_fp8(sp[4 * 33], sp[5 * 33], sp[6 * 33], sp[7 * 33]);
;         o.z = pg8::cvt_pk4_fp8(sp[8 * 33], sp[9 * 33], sp[10 * 33], sp[11 * 33]); o.w = pg8::cvt_pk4_fp8(sp[12 * 33], sp[13 * 33], sp[14 * 33], sp[15 * 33]);
;         *(GAS v4u*)(WT + (size_t)(drow0 + n) * K + k0 + 16 * c) = o; }
;     LDS_WAIT(); asm volatile("" ::: "memory");
	v_mul_f32_e32 v29, 0x43000000, v50
	s_waitcnt vmcnt(30)
	v_mul_f32_e32 v49, 0x43000000, v51
	ds_write2_b32 v31, v29, v49 offset1:66
	s_waitcnt vmcnt(29)
	v_mul_f32_e32 v29, 0x43000000, v52
	s_waitcnt vmcnt(28)
	v_mul_f32_e32 v49, 0x43000000, v53
	ds_write2_b32 v31, v29, v49 offset0:132 offset1:198
	s_waitcnt vmcnt(27)
	v_mul_f32_e32 v29, 0x43000000, v54
	s_waitcnt vmcnt(26)
	v_mul_f32_e32 v49, 0x43000000, v55
	ds_write2_b32 v40, v29, v49 offset0:8 offset1:74
	s_waitcnt vmcnt(25)
	v_mul_f32_e32 v29, 0x43000000, v56
	s_waitcnt vmcnt(24)
	v_mul_f32_e32 v49, 0x43000000, v57
	ds_write2_b32 v40, v29, v49 offset0:140 offset1:206
	s_waitcnt vmcnt(23)
	v_mul_f32_e32 v29, 0x43000000, v58
	s_waitcnt vmcnt(22)
	v_mul_f32_e32 v49, 0x43000000, v59
	ds_write2_b32 v41, v29, v49 offset0:16 offset1:82
	s_waitcnt vmcnt(21)
	v_mul_f32_e32 v29, 0x43000000, v60
	s_waitcnt vmcnt(20)
	v_mul_f32_e32 v49, 0x43000000, v61
	ds_write2_b32 v41, v29, v49 offset0:148 offset1:214
	s_waitcnt vmcnt(19)
	v_mul_f32_e32 v29, 0x43000000, v62
	s_waitcnt vmcnt(18)
	v_mul_f32_e32 v49, 0x43000000, v63
	ds_write2_b32 v42, v29, v49 offset0:24 offset1:90
	s_waitcnt vmcnt(17)
	v_mul_f32_e32 v29, 0x43000000, v64
	s_waitcnt vmcnt(16)
	v_mul_f32_e32 v49, 0x43000000, v65
	ds_write2_b32 v42, v29, v49 offset0:156 offset1:222
	s_waitcnt vmcnt(15)
	v_mul_f32_e32 v29, 0x43000000, v66
	s_waitcnt vmcnt(14)
	v_mul_f32_e32 v49, 0x43000000, v67
	ds_write2_b32 v43, v29, v49 offset0:32 offset1:98
	s_waitcnt vmcnt(13)
	v_mul_f32_e32 v29, 0x43000000, v68
	s_waitcnt vmcnt(12)
	v_mul_f32_e32 v49, 0x43000000, v69
	ds_write2_b32 v43, v29, v49 offset0:164 offset1:230
	s_waitcnt vmcnt(11)
	v_mul_f32_e32 v29, 0x43000000, v70
	s_waitcnt vmcnt(10)
	v_mul_f32_e32 v49, 0x43000000, v71
	ds_write2_b32 v44, v29, v49 offset0:40 offset1:106
	s_waitcnt vmcnt(9)
	v_mul_f32_e32 v29, 0x43000000, v72
	s_waitcnt vmcnt(8)
	v_mul_f32_e32 v49, 0x43000000, v73
	ds_write2_b32 v44, v29, v49 offset0:172 offset1:238
	v_mov_b32_e32 v50, v1
	v_mov_b32_e32 v51, v1
	s_waitcnt vmcnt(7)
	v_mul_f32_e32 v29, 0x43000000, v74
	s_add_u32 s4, s4, s6
	s_addc_u32 s5, s5, 0
	v_readlane_b32 s42, v254, 30
	v_readlane_b32 s43, v254, 31
	v_readlane_b32 s44, v254, 32
	s_waitcnt vmcnt(6)
	v_mul_f32_e32 v49, 0x43000000, v75
	ds_write2_b32 v45, v29, v49 offset0:48 offset1:114
	v_readlane_b32 s45, v254, 33
	s_waitcnt vmcnt(5)
	v_mul_f32_e32 v29, 0x43000000, v76
	s_waitcnt vmcnt(4)
	v_mul_f32_e32 v49, 0x43000000, v77
	ds_write2_b32 v45, v29, v49 offset0:180 offset1:246
	s_waitcnt vmcnt(3)
	v_mul_f32_e32 v29, 0x43000000, v78
	s_waitcnt vmcnt(2)
	v_mul_f32_e32 v49, 0x43000000, v79
	ds_write2_b32 v46, v29, v49 offset0:56 offset1:122
	v_mov_b32_e32 v49, v1
	s_waitcnt vmcnt(1)
	v_mul_f32_e32 v29, 0x43000000, v48
	v_mov_b32_e32 v48, v1
	s_waitcnt vmcnt(0)
	v_mul_f32_e32 v28, 0x43000000, v28
	ds_write2_b32 v46, v29, v28 offset0:188 offset1:254
	s_waitcnt lgkmcnt(0)
	ds_read2_b32 v[52:53], v33 offset1:16
	ds_read2_b32 v[54:55], v33 offset0:33 offset1:49
	ds_read2_b32 v[56:57], v33 offset0:66 offset1:82
	ds_read2_b32 v[58:59], v33 offset0:99 offset1:115
	ds_read2_b32 v[60:61], v33 offset0:132 offset1:148
	ds_read2_b32 v[62:63], v33 offset0:165 offset1:181
	ds_read2_b32 v[64:65], v33 offset0:198 offset1:214
	ds_read2_b32 v[66:67], v33 offset0:231 offset1:247
	ds_read2_b32 v[68:69], v47 offset0:8 offset1:24
	ds_read2_b32 v[70:71], v47 offset0:41 offset1:57
	ds_read2_b32 v[72:73], v47 offset0:74 offset1:90
	ds_read2_b32 v[74:75], v47 offset0:107 offset1:123
	ds_read2_b32 v[76:77], v47 offset0:140 offset1:156
	ds_read2_b32 v[78:79], v47 offset0:173 offset1:189
	ds_read2_b32 v[80:81], v47 offset0:206 offset1:222
	ds_read2_b32 v[82:83], v47 offset0:239 offset1:255
	s_waitcnt lgkmcnt(14)
	v_cvt_pk_fp8_f32 v48, v52, v54
	s_waitcnt lgkmcnt(10)
	v_cvt_pk_fp8_f32 v49, v60, v62
	s_waitcnt lgkmcnt(6)
	v_cvt_pk_fp8_f32 v50, v68, v70
	s_waitcnt lgkmcnt(2)
	v_cvt_pk_fp8_f32 v51, v76, v78
	v_cvt_pk_fp8_f32 v48, v56, v58 op_sel:[0,0,1]
	v_cvt_pk_fp8_f32 v49, v64, v66 op_sel:[0,0,1]
	v_cvt_pk_fp8_f32 v50, v72, v74 op_sel:[0,0,1]
	s_waitcnt lgkmcnt(0)
	v_cvt_pk_fp8_f32 v51, v80, v82 op_sel:[0,0,1]
	v_lshl_add_u64 v[28:29], s[4:5], 0, v[2:3]
	v_add_u32_e32 v52, s0, v32
	v_mad_i64_i32 v[84:85], s[4:5], v52, s13, v[28:29]
	global_store_dwordx4 v[84:85], v[48:51], off nt
	v_add_u32_e32 v52, s0, v34
	v_mad_i64_i32 v[28:29], s[4:5], v52, s13, v[28:29]
	v_mov_b32_e32 v48, v1
	v_mov_b32_e32 v49, v1
	v_mov_b32_e32 v50, v1
	v_mov_b32_e32 v51, v1
	v_cvt_pk_fp8_f32 v48, v53, v55
	v_cvt_pk_fp8_f32 v49, v61, v63
	v_cvt_pk_fp8_f32 v50, v69, v71
	v_cvt_pk_fp8_f32 v51, v77, v79
	v_cvt_pk_fp8_f32 v48, v57, v59 op_sel:[0,0,1]
	v_cvt_pk_fp8_f32 v49, v65, v67 op_sel:[0,0,1]
	v_cvt_pk_fp8_f32 v50, v73, v75 op_sel:[0,0,1]
	v_cvt_pk_fp8_f32 v51, v81, v83 op_sel:[0,0,1]
	s_mov_b64 s[4:5], 0
	global_store_dwordx4 v[28:29], v[48:51], off nt
	s_waitcnt lgkmcnt(0)
; #define LAS __attribute__((address_space(3)))
; __device__ __forceinline__ void tr_item8(const float* W, int ld, int K, int nblk, int item, unsigned char* WT, bool gu, float scale, LAS float* scr, int lane) {
;     const int kb = item / nblk, nb = item % nblk, k0 = 64 * kb, n0 = 32 * nb;
;     int drow0 = n0;
;     if (gu) { const int bj = n0 / FF, j = n0 - bj * FF; drow0 = 256 * (j / 128) + 128 * bj + (j % 128); }
;     { float t_[32];
; #pragma unroll
;       for (int i = 0; i < 32; ++i) t_[i] = W[(size_t)(k0 + 2 * i + (lane >> 5)) * ld + n0 + (lane & 31)];
; __device__ __forceinline__ void convert_items(Frame& F, const Args& a, int lo, int hi, int w, int nw) {
;     ...
;         if (r < NE * I_GU) { const int e = r / I_GU, rr = r % I_GU; tr_item8(a.in[18] + (size_t)e * D * 2 * FF, 2 * FF, D, 224, rr, F.ws + WS_WMGU + (size_t)e * 2 * FF * D, true, WSC_GU, scr, lane); continue; } r -= NE * I_GU;
.LBB0_1304:
	s_andn2_b64 vcc, exec, s[4:5]
	s_cbranch_vccnz .LBB0_1306
	s_add_i32 s0, s8, 0xde00
	s_bfe_u32 s4, s0, 0x70009
	s_mulk_i32 s4, 0x2493
	s_lshr_b32 s4, s4, 16
	s_mul_i32 s5, s4, 0xe00
	v_readlane_b32 s40, v254, 28
	s_sub_i32 s0, s0, s5
	s_mul_i32 s5, s4, 0x1c00000
	v_readlane_b32 s44, v254, 32
	v_readlane_b32 s45, v254, 33
	s_add_u32 s7, s44, s5
	s_addc_u32 s31, s45, 0
	s_mul_i32 s4, s4, 0x700000
	s_add_u32 s4, s36, s4
	s_addc_u32 s5, s37, 0
	s_bfe_u32 s6, s0, 0xb0005
	s_mulk_i32 s6, 0x2493
	s_lshr_b32 s6, s6, 16
	s_mul_i32 s40, s6, 0xe0
	v_readlane_b32 s41, v254, 29
	s_sub_i32 s40, s0, s40
	s_lshl_b32 s0, s40, 5
	s_and_b32 s41, s40, 0xffff
	s_cmpk_gt_u32 s41, 0x6f
	v_readlane_b32 s42, v254, 30
	s_cselect_b32 s41, 0xfffff200, 0
	s_cselect_b32 s42, 0x80, 0
	s_add_i32 s0, s41, s0
	s_sext_i32_i16 s41, s0
	s_bfe_u32 s41, s41, 0x70018
	v_readlane_b32 s43, v254, 31
	s_add_i32 s41, s0, s41
	s_sext_i32_i16 s43, s41
	s_and_b32 s41, s41, 0xff80
	s_sub_i32 s0, s0, s41
	s_lshl_b32 s43, s43, 1
	s_sext_i32_i16 s0, s0
	s_and_b32 s43, s43, 0xffffff00
	s_add_i32 s0, s42, s0
	s_lshl_b32 s40, s40, 7
	s_add_i32 s0, s0, s43
	s_lshl_b32 s6, s6, 6
	s_and_b32 s40, s40, 0x3ff80
	s_add_u32 s40, s7, s40
	s_addc_u32 s41, s31, 0
	v_add_u32_e32 v50, s6, v30
	v_lshl_add_u64 v[28:29], s[40:41], 0, v[0:1]
	v_mad_i64_i32 v[48:49], s[40:41], v50, s14, v[28:29]
	global_load_dword v51, v[48:49], off nt
	v_add_u32_e32 v48, 2, v50
	v_mad_i64_i32 v[48:49], s[40:41], v48, s14, v[28:29]
	global_load_dword v52, v[48:49], off nt
	v_add_u32_e32 v48, 4, v50
	v_mad_i64_i32 v[48:49], s[40:41], v48, s14, v[28:29]
	global_load_dword v53, v[48:49], off nt
	v_add_u32_e32 v48, 6, v50
	v_mad_i64_i32 v[48:49], s[40:41], v48, s14, v[28:29]
	global_load_dword v54, v[48:49], off nt
	v_add_u32_e32 v48, 8, v50
	v_mad_i64_i32 v[48:49], s[40:41], v48, s14, v[28:29]
	global_load_dword v55, v[48:49], off nt
	v_add_u32_e32 v48, 10, v50
	v_mad_i64_i32 v[48:49], s[40:41], v48, s14, v[28:29]
	global_load_dword v56, v[48:49], off nt
	v_add_u32_e32 v48, 12, v50
	v_mad_i64_i32 v[48:49], s[40:41], v48, s14, v[28:29]
	global_load_dword v57, v[48:49], off nt
	v_add_u32_e32 v48, 14, v50
	v_mad_i64_i32 v[48:49], s[40:41], v48, s14, v[28:29]
	global_load_dword v58, v[48:49], off nt
	v_add_u32_e32 v48, 16, v50
	v_mad_i64_i32 v[48:49], s[40:41], v48, s14, v[28:29]
	global_load_dword v59, v[48:49], off nt
	v_add_u32_e32 v48, 18, v50
	v_mad_i64_i32 v[48:49], s[40:41], v48, s14, v[28:29]
	global_load_dword v60, v[48:49], off nt
	v_add_u32_e32 v48, 20, v50
	v_mad_i64_i32 v[48:49], s[40:41], v48, s14, v[28:29]
	global_load_dword v61, v[48:49], off nt
	v_add_u32_e32 v48, 22, v50
	v_mad_i64_i32 v[48:49], s[40:41], v48, s14, v[28:29]
	global_load_dword v62, v[48:49], off nt
	v_add_u32_e32 v48, 24, v50
	v_mad_i64_i32 v[48:49], s[40:41], v48, s14, v[28:29]
	global_load_dword v63, v[48:49], off nt
	v_add_u32_e32 v48, 26, v50
	v_mad_i64_i32 v[48:49], s[40:41], v48, s14, v[28:29]
	global_load_dword v64, v[48:49], off nt
	v_add_u32_e32 v48, 28, v50
	v_mad_i64_i32 v[48:49], s[40:41], v48, s14, v[28:29]
	global_load_dword v65, v[48:49], off nt
	v_add_u32_e32 v48, 30, v50
	v_mad_i64_i32 v[48:49], s[40:41], v48, s14, v[28:29]
	global_load_dword v66, v[48:49], off nt
	v_add_u32_e32 v48, 32, v50
	v_mad_i64_i32 v[48:49], s[40:41], v48, s14, v[28:29]
	global_load_dword v67, v[48:49], off nt
	v_add_u32_e32 v48, 34, v50
	v_mad_i64_i32 v[48:49], s[40:41], v48, s14, v[28:29]
	global_load_dword v68, v[48:49], off nt
	v_add_u32_e32 v48, 36, v50
	v_mad_i64_i32 v[48:49], s[40:41], v48, s14, v[28:29]
	global_load_dword v69, v[48:49], off nt
	v_add_u32_e32 v48, 38, v50
	v_mad_i64_i32 v[48:49], s[40:41], v48, s14, v[28:29]
	global_load_dword v70, v[48:49], off nt
	v_add_u32_e32 v48, 40, v50
	v_mad_i64_i32 v[48:49], s[40:41], v48, s14, v[28:29]
	global_load_dword v71, v[48:49], off nt
	v_add_u32_e32 v48, 42, v50
	v_mad_i64_i32 v[48:49], s[40:41], v48, s14, v[28:29]
	global_load_dword v72, v[48:49], off nt
	v_add_u32_e32 v48, 44, v50
	v_mad_i64_i32 v[48:49], s[40:41], v48, s14, v[28:29]
	global_load_dword v73, v[48:49], off nt
	v_add_u32_e32 v48, 46, v50
	v_mad_i64_i32 v[48:49], s[40:41], v48, s14, v[28:29]
	global_load_dword v74, v[48:49], off nt
	v_add_u32_e32 v48, 48, v50
	v_mad_i64_i32 v[48:49], s[40:41], v48, s14, v[28:29]
	global_load_dword v75, v[48:49], off nt
	v_add_u32_e32 v48, 50, v50
	v_mad_i64_i32 v[48:49], s[40:41], v48, s14, v[28:29]
	global_load_dword v76, v[48:49], off nt
	v_add_u32_e32 v48, 52, v50
	v_mad_i64_i32 v[48:49], s[40:41], v48, s14, v[28:29]
	global_load_dword v77, v[48:49], off nt
	v_add_u32_e32 v48, 54, v50
	v_mad_i64_i32 v[48:49], s[40:41], v48, s14, v[28:29]
	global_load_dword v78, v[48:49], off nt
	v_add_u32_e32 v48, 56, v50
	v_mad_i64_i32 v[48:49], s[40:41], v48, s14, v[28:29]
	global_load_dword v79, v[48:49], off nt
	v_add_u32_e32 v48, 58, v50
	v_mad_i64_i32 v[48:49], s[40:41], v48, s14, v[28:29]
	global_load_dword v80, v[48:49], off nt
	v_add_u32_e32 v48, 60, v50
	v_mad_i64_i32 v[48:49], s[40:41], v48, s14, v[28:29]
	global_load_dword v48, v[48:49], off nt
	v_add_u32_e32 v49, 62, v50
	v_mad_i64_i32 v[28:29], s[40:41], v49, s14, v[28:29]
	global_load_dword v28, v[28:29], off nt
	s_waitcnt vmcnt(31)
; __device__ __forceinline__ unsigned cvt_pk4_fp8(float a, float b, float c, float d) { int w = 0; w = __builtin_amdgcn_cvt_pk_fp8_f32(a, b, w, false); w = __builtin_amdgcn_cvt_pk_fp8_f32(c, d, w, true); return (unsigned)w; }
; #define GAS __attribute__((address_space(1)))
; #define LAS __attribute__((address_space(3)))
; #define LDS_WAIT() asm volatile("s_waitcnt lgkmcnt(0)" ::: "memory")
; __device__ __forceinline__ void tr_item8(const float* W, int ld, int K, int nblk, int item, unsigned char* WT, bool gu, float scale, LAS float* scr, int lane) {
;     ...
; #pragma unroll
;       for (int i = 0; i < 32; ++i) scr[(2 * i + (lane >> 5)) * 33 + (lane & 31)] = t_[i] * scale; }
;     LDS_WAIT(); asm volatile("" ::: "memory");
;     const int c = lane & 3;
; #pragma unroll
;     for (int j = 0; j < 2; ++j) { const int n = (lane >> 2) + 16 * j; const LAS float* sp = scr + (16 * c) * 33 + n;
;         v4u o; o.x = pg8::cvt_pk4_fp8(sp[0 * 33], sp[1 * 33], sp[2 * 33], sp[3 * 33]); o.y = pg8::cvt_pk4_fp8(sp[4 * 33], sp[5 * 33], sp[6 * 33], sp[7 * 33]);
;         o.z = pg8::cvt_pk4_fp8(sp[8 * 33], sp[9 * 33], sp[10 * 33], sp[11 * 33]); o.w = pg8::cvt_pk4_fp8(sp[12 * 33], sp[13 * 33], sp[14 * 33], sp[15 * 33]);
;         *(GAS v4u*)(WT + (size_t)(drow0 + n) * K + k0 + 16 * c) = o; }
;     LDS_WAIT(); asm volatile("" ::: "memory");
	v_mul_f32_e32 v29, 0x42800000, v51
	s_waitcnt vmcnt(30)
	v_mul_f32_e32 v49, 0x42800000, v52
	ds_write2_b32 v31, v29, v49 offset1:66
	s_waitcnt vmcnt(29)
	v_mul_f32_e32 v29, 0x42800000, v53
	s_waitcnt vmcnt(28)
	v_mul_f32_e32 v49, 0x42800000, v54
	ds_write2_b32 v31, v29, v49 offset0:132 offset1:198
	s_waitcnt vmcnt(27)
	v_mul_f32_e32 v29, 0x42800000, v55
	s_waitcnt vmcnt(26)
	v_mul_f32_e32 v49, 0x42800000, v56
	ds_write2_b32 v40, v29, v49 offset0:8 offset1:74
	s_waitcnt vmcnt(25)
	v_mul_f32_e32 v29, 0x42800000, v57
	s_waitcnt vmcnt(24)
	v_mul_f32_e32 v49, 0x42800000, v58
	ds_write2_b32 v40, v29, v49 offset0:140 offset1:206
	s_waitcnt vmcnt(23)
	v_mul_f32_e32 v29, 0x42800000, v59
	s_waitcnt vmcnt(22)
	v_mul_f32_e32 v49, 0x42800000, v60
	ds_write2_b32 v41, v29, v49 offset0:16 offset1:82
	s_waitcnt vmcnt(21)
	v_mul_f32_e32 v29, 0x42800000, v61
	s_waitcnt vmcnt(20)
	v_mul_f32_e32 v49, 0x42800000, v62
	ds_write2_b32 v41, v29, v49 offset0:148 offset1:214
	s_waitcnt vmcnt(19)
	v_mul_f32_e32 v29, 0x42800000, v63
	s_waitcnt vmcnt(18)
	v_mul_f32_e32 v49, 0x42800000, v64
	ds_write2_b32 v42, v29, v49 offset0:24 offset1:90
	s_waitcnt vmcnt(17)
	v_mul_f32_e32 v29, 0x42800000, v65
	s_waitcnt vmcnt(16)
	v_mul_f32_e32 v49, 0x42800000, v66
	ds_write2_b32 v42, v29, v49 offset0:156 offset1:222
	s_waitcnt vmcnt(15)
	v_mul_f32_e32 v29, 0x42800000, v67
	s_waitcnt vmcnt(14)
	v_mul_f32_e32 v49, 0x42800000, v68
	ds_write2_b32 v43, v29, v49 offset0:32 offset1:98
	s_waitcnt vmcnt(13)
	v_mul_f32_e32 v29, 0x42800000, v69
	v_mov_b32_e32 v50, v1
	v_mov_b32_e32 v51, v1
	s_add_u32 s4, s4, s6
	s_waitcnt vmcnt(12)
	v_mul_f32_e32 v49, 0x42800000, v70
	ds_write2_b32 v43, v29, v49 offset0:164 offset1:230
	v_add_u32_e32 v84, s0, v32
	s_addc_u32 s5, s5, 0
	s_waitcnt vmcnt(11)
	v_mul_f32_e32 v29, 0x42800000, v71
	v_ashrrev_i32_e32 v85, 31, v84
	v_lshlrev_b64 v[84:85], 10, v[84:85]
	v_readlane_b32 s46, v254, 34
	s_waitcnt vmcnt(10)
	v_mul_f32_e32 v49, 0x42800000, v72
	ds_write2_b32 v44, v29, v49 offset0:40 offset1:106
	v_readlane_b32 s47, v254, 35
	s_waitcnt vmcnt(9)
	v_mul_f32_e32 v29, 0x42800000, v73
	s_waitcnt vmcnt(8)
	v_mul_f32_e32 v49, 0x42800000, v74
	ds_write2_b32 v44, v29, v49 offset0:172 offset1:238
	s_waitcnt vmcnt(7)
	v_mul_f32_e32 v29, 0x42800000, v75
	s_waitcnt vmcnt(6)
	v_mul_f32_e32 v49, 0x42800000, v76
	ds_write2_b32 v45, v29, v49 offset0:48 offset1:114
	s_waitcnt vmcnt(5)
	v_mul_f32_e32 v29, 0x42800000, v77
	s_waitcnt vmcnt(4)
	v_mul_f32_e32 v49, 0x42800000, v78
	ds_write2_b32 v45, v29, v49 offset0:180 offset1:246
	s_waitcnt vmcnt(3)
	v_mul_f32_e32 v29, 0x42800000, v79
	s_waitcnt vmcnt(2)
	v_mul_f32_e32 v49, 0x42800000, v80
	ds_write2_b32 v46, v29, v49 offset0:56 offset1:122
	v_mov_b32_e32 v49, v1
	s_waitcnt vmcnt(1)
	v_mul_f32_e32 v29, 0x42800000, v48
	v_mov_b32_e32 v48, v1
	s_waitcnt vmcnt(0)
	v_mul_f32_e32 v28, 0x42800000, v28
	ds_write2_b32 v46, v29, v28 offset0:188 offset1:254
	s_waitcnt lgkmcnt(0)
	ds_read2_b32 v[52:53], v33 offset1:16
	ds_read2_b32 v[54:55], v33 offset0:33 offset1:49
	ds_read2_b32 v[56:57], v33 offset0:66 offset1:82
	ds_read2_b32 v[58:59], v33 offset0:99 offset1:115
	ds_read2_b32 v[60:61], v33 offset0:132 offset1:148
	ds_read2_b32 v[62:63], v33 offset0:165 offset1:181
	ds_read2_b32 v[64:65], v33 offset0:198 offset1:214
	ds_read2_b32 v[66:67], v33 offset0:231 offset1:247
	ds_read2_b32 v[68:69], v47 offset0:8 offset1:24
	ds_read2_b32 v[70:71], v47 offset0:41 offset1:57
	ds_read2_b32 v[72:73], v47 offset0:74 offset1:90
	ds_read2_b32 v[74:75], v47 offset0:107 offset1:123
	ds_read2_b32 v[76:77], v47 offset0:140 offset1:156
	ds_read2_b32 v[78:79], v47 offset0:173 offset1:189
	ds_read2_b32 v[80:81], v47 offset0:206 offset1:222
	ds_read2_b32 v[82:83], v47 offset0:239 offset1:255
	s_waitcnt lgkmcnt(14)
	v_cvt_pk_fp8_f32 v48, v52, v54
	s_waitcnt lgkmcnt(10)
	v_cvt_pk_fp8_f32 v49, v60, v62
	s_waitcnt lgkmcnt(6)
	v_cvt_pk_fp8_f32 v50, v68, v70
	s_waitcnt lgkmcnt(2)
	v_cvt_pk_fp8_f32 v51, v76, v78
	v_cvt_pk_fp8_f32 v48, v56, v58 op_sel:[0,0,1]
	v_cvt_pk_fp8_f32 v49, v64, v66 op_sel:[0,0,1]
	v_cvt_pk_fp8_f32 v50, v72, v74 op_sel:[0,0,1]
	s_waitcnt lgkmcnt(0)
	v_cvt_pk_fp8_f32 v51, v80, v82 op_sel:[0,0,1]
	v_lshl_add_u64 v[28:29], s[4:5], 0, v[2:3]
	v_lshl_add_u64 v[84:85], v[28:29], 0, v[84:85]
	v_add_u32_e32 v52, s0, v34
	global_store_dwordx4 v[84:85], v[48:51], off nt
	s_nop 1
	v_mov_b32_e32 v48, v1
	v_mov_b32_e32 v49, v1
	v_mov_b32_e32 v50, v1
	v_mov_b32_e32 v51, v1
	v_cvt_pk_fp8_f32 v48, v53, v55
	v_cvt_pk_fp8_f32 v49, v61, v63
	v_cvt_pk_fp8_f32 v50, v69, v71
	v_cvt_pk_fp8_f32 v51, v77, v79
	v_cvt_pk_fp8_f32 v48, v57, v59 op_sel:[0,0,1]
	v_cvt_pk_fp8_f32 v49, v65, v67 op_sel:[0,0,1]
	v_cvt_pk_fp8_f32 v50, v73, v75 op_sel:[0,0,1]
	v_cvt_pk_fp8_f32 v51, v81, v83 op_sel:[0,0,1]
	v_ashrrev_i32_e32 v53, 31, v52
	v_lshlrev_b64 v[52:53], 10, v[52:53]
	v_lshl_add_u64 v[28:29], v[28:29], 0, v[52:53]
	global_store_dwordx4 v[28:29], v[48:51], off nt
	s_waitcnt lgkmcnt(0)

; #define LAS __attribute__((address_space(3)))
; __device__ __forceinline__ void tr_item8(const float* W, int ld, int K, int nblk, int item, unsigned char* WT, bool gu, float scale, LAS float* scr, int lane) {
;     const int kb = item / nblk, nb = item % nblk, k0 = 64 * kb, n0 = 32 * nb;
;     int drow0 = n0;
;     if (gu) { const int bj = n0 / FF, j = n0 - bj * FF; drow0 = 256 * (j / 128) + 128 * bj + (j % 128); }
;     { float t_[32];
; #pragma unroll
;       for (int i = 0; i < 32; ++i) t_[i] = W[(size_t)(k0 + 2 * i + (lane >> 5)) * ld + n0 + (lane & 31)];
; __device__ __forceinline__ void convert_items(Frame& F, const Args& a, int lo, int hi, int w, int nw) {
;     ...
;         if (r < I_DN) { tr_item8(a.in[15], D, FF, 32, r, F.ws + WS_WDN, false, WSC_DN, scr, lane); continue; } r -= I_DN;
.LBB0_1307:
	s_andn2_b64 vcc, exec, s[4:5]
	s_cbranch_vccnz .LBB0_1309
	s_lshl_b32 s0, s8, 5
	s_and_b32 s4, s11, 0x1ffc0
	s_and_b32 s6, s0, 0x3e0
	v_add_u32_e32 v28, s4, v30
	s_lshl_b32 s0, s6, 2
	v_ashrrev_i32_e32 v29, 31, v28
	v_lshl_add_u64 v[48:49], v[4:5], 0, s[0:1]
	v_lshlrev_b64 v[28:29], 12, v[28:29]
	v_lshl_add_u64 v[28:29], v[48:49], 0, v[28:29]
	v_add_co_u32_e32 v48, vcc, 0x2000, v28
	global_load_dword v50, v[28:29], off nt
	s_nop 0
	v_addc_co_u32_e32 v49, vcc, 0, v29, vcc
	global_load_dword v51, v[48:49], off nt
	v_add_co_u32_e32 v48, vcc, 0x4000, v28
	s_mov_b32 s5, s1
	s_nop 0
	v_addc_co_u32_e32 v49, vcc, 0, v29, vcc
	global_load_dword v52, v[48:49], off nt
	v_add_co_u32_e32 v48, vcc, 0x6000, v28
	s_nop 1
	v_addc_co_u32_e32 v49, vcc, 0, v29, vcc
	global_load_dword v53, v[48:49], off nt
	v_add_co_u32_e32 v48, vcc, 0x8000, v28
	s_nop 1
	v_addc_co_u32_e32 v49, vcc, 0, v29, vcc
	global_load_dword v54, v[48:49], off nt
	v_add_co_u32_e32 v48, vcc, 0xa000, v28
	s_nop 1
	v_addc_co_u32_e32 v49, vcc, 0, v29, vcc
	global_load_dword v55, v[48:49], off nt
	v_add_co_u32_e32 v48, vcc, 0xc000, v28
	s_nop 1
	v_addc_co_u32_e32 v49, vcc, 0, v29, vcc
	global_load_dword v56, v[48:49], off nt
	v_add_co_u32_e32 v48, vcc, 0xe000, v28
	s_nop 1
	v_addc_co_u32_e32 v49, vcc, 0, v29, vcc
	global_load_dword v57, v[48:49], off nt
	v_add_co_u32_e32 v48, vcc, 0x10000, v28
	s_nop 1
	v_addc_co_u32_e32 v49, vcc, 0, v29, vcc
	global_load_dword v58, v[48:49], off nt
	v_add_co_u32_e32 v48, vcc, 0x12000, v28
	s_nop 1
	v_addc_co_u32_e32 v49, vcc, 0, v29, vcc
	global_load_dword v59, v[48:49], off nt
	v_add_co_u32_e32 v48, vcc, 0x14000, v28
	s_nop 1
	v_addc_co_u32_e32 v49, vcc, 0, v29, vcc
	global_load_dword v60, v[48:49], off nt
	v_add_co_u32_e32 v48, vcc, 0x16000, v28
	s_nop 1
	v_addc_co_u32_e32 v49, vcc, 0, v29, vcc
	global_load_dword v61, v[48:49], off nt
	v_add_co_u32_e32 v48, vcc, 0x18000, v28
	s_nop 1
	v_addc_co_u32_e32 v49, vcc, 0, v29, vcc
	global_load_dword v62, v[48:49], off nt
	v_add_co_u32_e32 v48, vcc, 0x1a000, v28
	s_nop 1
	v_addc_co_u32_e32 v49, vcc, 0, v29, vcc
	global_load_dword v63, v[48:49], off nt
	v_add_co_u32_e32 v48, vcc, 0x1c000, v28
	s_nop 1
	v_addc_co_u32_e32 v49, vcc, 0, v29, vcc
	global_load_dword v64, v[48:49], off nt
	v_add_co_u32_e32 v48, vcc, 0x1e000, v28
	s_nop 1
	v_addc_co_u32_e32 v49, vcc, 0, v29, vcc
	global_load_dword v65, v[48:49], off nt
	v_add_co_u32_e32 v48, vcc, 0x20000, v28
	s_nop 1
	v_addc_co_u32_e32 v49, vcc, 0, v29, vcc
	global_load_dword v66, v[48:49], off nt
	v_add_co_u32_e32 v48, vcc, 0x22000, v28
	s_nop 1
	v_addc_co_u32_e32 v49, vcc, 0, v29, vcc
	global_load_dword v67, v[48:49], off nt
	v_add_co_u32_e32 v48, vcc, 0x24000, v28
	s_nop 1
	v_addc_co_u32_e32 v49, vcc, 0, v29, vcc
	global_load_dword v68, v[48:49], off nt
	v_add_co_u32_e32 v48, vcc, 0x26000, v28
	s_nop 1
	v_addc_co_u32_e32 v49, vcc, 0, v29, vcc
	global_load_dword v69, v[48:49], off nt
	v_add_co_u32_e32 v48, vcc, 0x28000, v28
	s_nop 1
	v_addc_co_u32_e32 v49, vcc, 0, v29, vcc
	global_load_dword v70, v[48:49], off nt
	v_add_co_u32_e32 v48, vcc, 0x2a000, v28
	s_nop 1
	v_addc_co_u32_e32 v49, vcc, 0, v29, vcc
	global_load_dword v71, v[48:49], off nt
	v_add_co_u32_e32 v48, vcc, 0x2c000, v28
	s_nop 1
	v_addc_co_u32_e32 v49, vcc, 0, v29, vcc
	global_load_dword v72, v[48:49], off nt
	v_add_co_u32_e32 v48, vcc, 0x2e000, v28
	s_nop 1
	v_addc_co_u32_e32 v49, vcc, 0, v29, vcc
	global_load_dword v73, v[48:49], off nt
	v_add_co_u32_e32 v48, vcc, 0x30000, v28
	s_nop 1
	v_addc_co_u32_e32 v49, vcc, 0, v29, vcc
	global_load_dword v74, v[48:49], off nt
	v_add_co_u32_e32 v48, vcc, 0x32000, v28
	s_nop 1
	v_addc_co_u32_e32 v49, vcc, 0, v29, vcc
	global_load_dword v75, v[48:49], off nt
	v_add_co_u32_e32 v48, vcc, 0x34000, v28
	s_nop 1
	v_addc_co_u32_e32 v49, vcc, 0, v29, vcc
	global_load_dword v76, v[48:49], off nt
	v_add_co_u32_e32 v48, vcc, 0x36000, v28
	s_nop 1
	v_addc_co_u32_e32 v49, vcc, 0, v29, vcc
	global_load_dword v77, v[48:49], off nt
	v_add_co_u32_e32 v48, vcc, 0x38000, v28
	s_nop 1
	v_addc_co_u32_e32 v49, vcc, 0, v29, vcc
	global_load_dword v78, v[48:49], off nt
	v_add_co_u32_e32 v48, vcc, 0x3a000, v28
	s_nop 1
	v_addc_co_u32_e32 v49, vcc, 0, v29, vcc
	global_load_dword v79, v[48:49], off nt
	v_add_co_u32_e32 v48, vcc, 0x3c000, v28
	s_nop 1
	v_addc_co_u32_e32 v49, vcc, 0, v29, vcc
	v_add_co_u32_e32 v28, vcc, 0x3e000, v28
	global_load_dword v48, v[48:49], off nt
	s_nop 0
	v_addc_co_u32_e32 v29, vcc, 0, v29, vcc
	global_load_dword v28, v[28:29], off nt
	s_waitcnt vmcnt(31)
	v_mul_f32_e32 v29, 0x43000000, v50
	s_waitcnt vmcnt(30)
; __device__ __forceinline__ unsigned cvt_pk4_fp8(float a, float b, float c, float d) { int w = 0; w = __builtin_amdgcn_cvt_pk_fp8_f32(a, b, w, false); w = __builtin_amdgcn_cvt_pk_fp8_f32(c, d, w, true); return (unsigned)w; }
; #define GAS __attribute__((address_space(1)))
; #define LAS __attribute__((address_space(3)))
; #define LDS_WAIT() asm volatile("s_waitcnt lgkmcnt(0)" ::: "memory")
; __device__ __forceinline__ void tr_item8(const float* W, int ld, int K, int nblk, int item, unsigned char* WT, bool gu, float scale, LAS float* scr, int lane) {
;     ...
; #pragma unroll
;       for (int i = 0; i < 32; ++i) scr[(2 * i + (lane >> 5)) * 33 + (lane & 31)] = t_[i] * scale; }
;     LDS_WAIT(); asm volatile("" ::: "memory");
;     const int c = lane & 3;
; #pragma unroll
;     for (int j = 0; j < 2; ++j) { const int n = (lane >> 2) + 16 * j; const LAS float* sp = scr + (16 * c) * 33 + n;
;         v4u o; o.x = pg8::cvt_pk4_fp8(sp[0 * 33], sp[1 * 33], sp[2 * 33], sp[3 * 33]); o.y = pg8::cvt_pk4_fp8(sp[4 * 33], sp[5 * 33], sp[6 * 33], sp[7 * 33]);
;         o.z = pg8::cvt_pk4_fp8(sp[8 * 33], sp[9 * 33], sp[10 * 33], sp[11 * 33]); o.w = pg8::cvt_pk4_fp8(sp[12 * 33], sp[13 * 33], sp[14 * 33], sp[15 * 33]);
;         *(GAS v4u*)(WT + (size_t)(drow0 + n) * K + k0 + 16 * c) = o; }
;     LDS_WAIT(); asm volatile("" ::: "memory");
	v_mul_f32_e32 v49, 0x43000000, v51
	ds_write2_b32 v31, v29, v49 offset1:66
	s_waitcnt vmcnt(29)
	v_mul_f32_e32 v29, 0x43000000, v52
	s_waitcnt vmcnt(28)
	v_mul_f32_e32 v49, 0x43000000, v53
	ds_write2_b32 v31, v29, v49 offset0:132 offset1:198
	s_waitcnt vmcnt(27)
	v_mul_f32_e32 v29, 0x43000000, v54
	s_waitcnt vmcnt(26)
	v_mul_f32_e32 v49, 0x43000000, v55
	ds_write2_b32 v40, v29, v49 offset0:8 offset1:74
	s_waitcnt vmcnt(25)
	v_mul_f32_e32 v29, 0x43000000, v56
	s_waitcnt vmcnt(24)
	v_mul_f32_e32 v49, 0x43000000, v57
	ds_write2_b32 v40, v29, v49 offset0:140 offset1:206
	s_waitcnt vmcnt(23)
	v_mul_f32_e32 v29, 0x43000000, v58
	s_waitcnt vmcnt(22)
	v_mul_f32_e32 v49, 0x43000000, v59
	ds_write2_b32 v41, v29, v49 offset0:16 offset1:82
	s_waitcnt vmcnt(21)
	v_mul_f32_e32 v29, 0x43000000, v60
	s_waitcnt vmcnt(20)
	v_mul_f32_e32 v49, 0x43000000, v61
	ds_write2_b32 v41, v29, v49 offset0:148 offset1:214
	s_waitcnt vmcnt(19)
	v_mul_f32_e32 v29, 0x43000000, v62
	s_waitcnt vmcnt(18)
	v_mul_f32_e32 v49, 0x43000000, v63
	ds_write2_b32 v42, v29, v49 offset0:24 offset1:90
	s_waitcnt vmcnt(17)
	v_mul_f32_e32 v29, 0x43000000, v64
	s_waitcnt vmcnt(16)
	v_mul_f32_e32 v49, 0x43000000, v65
	ds_write2_b32 v42, v29, v49 offset0:156 offset1:222
	s_waitcnt vmcnt(15)
	v_mul_f32_e32 v29, 0x43000000, v66
	s_waitcnt vmcnt(14)
	v_mul_f32_e32 v49, 0x43000000, v67
	ds_write2_b32 v43, v29, v49 offset0:32 offset1:98
	s_waitcnt vmcnt(13)
	v_mul_f32_e32 v29, 0x43000000, v68
	s_waitcnt vmcnt(12)
	v_mul_f32_e32 v49, 0x43000000, v69
	ds_write2_b32 v43, v29, v49 offset0:164 offset1:230
	s_waitcnt vmcnt(11)
	v_mul_f32_e32 v29, 0x43000000, v70
	s_waitcnt vmcnt(10)
	v_mul_f32_e32 v49, 0x43000000, v71
	ds_write2_b32 v44, v29, v49 offset0:40 offset1:106
	s_waitcnt vmcnt(9)
	v_mul_f32_e32 v29, 0x43000000, v72
	s_waitcnt vmcnt(8)
	v_mul_f32_e32 v49, 0x43000000, v73
	ds_write2_b32 v44, v29, v49 offset0:172 offset1:238
	v_mov_b32_e32 v50, 0
	v_mov_b32_e32 v51, 0
	s_waitcnt vmcnt(7)
	v_mul_f32_e32 v29, 0x43000000, v74
	s_waitcnt vmcnt(6)
	v_mul_f32_e32 v49, 0x43000000, v75
	ds_write2_b32 v45, v29, v49 offset0:48 offset1:114
	s_waitcnt vmcnt(5)
	v_mul_f32_e32 v29, 0x43000000, v76
	s_waitcnt vmcnt(4)
	v_mul_f32_e32 v49, 0x43000000, v77
	ds_write2_b32 v45, v29, v49 offset0:180 offset1:246
	s_waitcnt vmcnt(3)
	v_mul_f32_e32 v29, 0x43000000, v78
	s_waitcnt vmcnt(2)
	v_mul_f32_e32 v49, 0x43000000, v79
	ds_write2_b32 v46, v29, v49 offset0:56 offset1:122
	v_mov_b32_e32 v49, 0
	s_waitcnt vmcnt(1)
	v_mul_f32_e32 v29, 0x43000000, v48
	v_mov_b32_e32 v48, 0
	s_waitcnt vmcnt(0)
	v_mul_f32_e32 v28, 0x43000000, v28
	ds_write2_b32 v46, v29, v28 offset0:188 offset1:254
	s_waitcnt lgkmcnt(0)
	ds_read2_b32 v[52:53], v33 offset1:16
	ds_read2_b32 v[54:55], v33 offset0:33 offset1:49
	ds_read2_b32 v[56:57], v33 offset0:66 offset1:82
	ds_read2_b32 v[58:59], v33 offset0:99 offset1:115
	ds_read2_b32 v[60:61], v33 offset0:132 offset1:148
	ds_read2_b32 v[62:63], v33 offset0:165 offset1:181
	ds_read2_b32 v[64:65], v33 offset0:198 offset1:214
	ds_read2_b32 v[66:67], v33 offset0:231 offset1:247
	ds_read2_b32 v[68:69], v47 offset0:8 offset1:24
	ds_read2_b32 v[70:71], v47 offset0:41 offset1:57
	ds_read2_b32 v[72:73], v47 offset0:74 offset1:90
	ds_read2_b32 v[74:75], v47 offset0:107 offset1:123
	ds_read2_b32 v[76:77], v47 offset0:140 offset1:156
	ds_read2_b32 v[78:79], v47 offset0:173 offset1:189
	ds_read2_b32 v[80:81], v47 offset0:206 offset1:222
	ds_read2_b32 v[82:83], v47 offset0:239 offset1:255
	s_waitcnt lgkmcnt(14)
	v_cvt_pk_fp8_f32 v48, v52, v54
	s_waitcnt lgkmcnt(10)
	v_cvt_pk_fp8_f32 v49, v60, v62
	s_waitcnt lgkmcnt(6)
	v_cvt_pk_fp8_f32 v50, v68, v70
	s_waitcnt lgkmcnt(2)
	v_cvt_pk_fp8_f32 v51, v76, v78
	v_cvt_pk_fp8_f32 v48, v56, v58 op_sel:[0,0,1]
	v_cvt_pk_fp8_f32 v49, v64, v66 op_sel:[0,0,1]
	v_cvt_pk_fp8_f32 v50, v72, v74 op_sel:[0,0,1]
	s_waitcnt lgkmcnt(0)
	v_cvt_pk_fp8_f32 v51, v80, v82 op_sel:[0,0,1]
	v_lshl_add_u64 v[28:29], v[16:17], 0, s[4:5]
	v_add_u32_e32 v52, s6, v32
	v_mad_i64_i32 v[84:85], s[4:5], v52, s13, v[28:29]
	global_store_dwordx4 v[84:85], v[48:51], off nt
	v_add_u32_e32 v52, s6, v34
	v_mad_i64_i32 v[28:29], s[4:5], v52, s13, v[28:29]
	v_mov_b32_e32 v48, 0
	v_mov_b32_e32 v49, 0
	v_mov_b32_e32 v50, 0
	v_mov_b32_e32 v51, 0
	v_cvt_pk_fp8_f32 v48, v53, v55
	v_cvt_pk_fp8_f32 v49, v61, v63
	v_cvt_pk_fp8_f32 v50, v69, v71
	v_cvt_pk_fp8_f32 v51, v77, v79
	v_cvt_pk_fp8_f32 v48, v57, v59 op_sel:[0,0,1]
	v_cvt_pk_fp8_f32 v49, v65, v67 op_sel:[0,0,1]
	v_cvt_pk_fp8_f32 v50, v73, v75 op_sel:[0,0,1]
	v_cvt_pk_fp8_f32 v51, v81, v83 op_sel:[0,0,1]
	global_store_dwordx4 v[28:29], v[48:51], off nt
	s_waitcnt lgkmcnt(0)

; #define LAS __attribute__((address_space(3)))
; __device__ __forceinline__ void tr_item8(const float* W, int ld, int K, int nblk, int item, unsigned char* WT, bool gu, float scale, LAS float* scr, int lane) {
;     const int kb = item / nblk, nb = item % nblk, k0 = 64 * kb, n0 = 32 * nb;
;     int drow0 = n0;
;     if (gu) { const int bj = n0 / FF, j = n0 - bj * FF; drow0 = 256 * (j / 128) + 128 * bj + (j % 128); }
;     { float t_[32];
; #pragma unroll
;       for (int i = 0; i < 32; ++i) t_[i] = W[(size_t)(k0 + 2 * i + (lane >> 5)) * ld + n0 + (lane & 31)];
; __device__ __forceinline__ void convert_items(Frame& F, const Args& a, int lo, int hi, int w, int nw) {
;     ...
;         if (r < I_GU) { tr_item8(a.in[14], 2 * FF, D, 224, r, F.ws + WS_WGU, true, WSC_GU, scr, lane); continue; } r -= I_GU;
.LBB0_1310:
	s_andn2_b64 vcc, exec, s[4:5]
	s_cbranch_vccnz .LBB0_1312
	s_add_i32 s0, s8, 0xf300
	s_bfe_u32 s4, s0, 0xb0005
	s_mulk_i32 s4, 0x2493
	s_lshr_b32 s4, s4, 16
	s_mul_i32 s5, s4, 0xe0
	s_sub_i32 s0, s0, s5
	s_lshl_b32 s5, s0, 5
	s_and_b32 s6, s0, 0xffff
	s_cmpk_gt_u32 s6, 0x6f
	s_cselect_b32 s31, 0xfffff200, 0
	s_cselect_b32 s40, 0x80, 0
	s_lshl_b32 s0, s0, 7
	s_lshl_b32 s4, s4, 6
	s_and_b32 s0, s0, 0x3ff80
	v_add_u32_e32 v64, s4, v30
	v_lshl_add_u64 v[28:29], v[6:7], 0, s[0:1]
	v_mad_i64_i32 v[48:49], s[6:7], v64, s14, v[28:29]
	v_add_u32_e32 v50, 2, v64
	v_add_u32_e32 v52, 4, v64
	v_add_u32_e32 v54, 6, v64
	v_add_u32_e32 v56, 8, v64
	v_add_u32_e32 v58, 10, v64
	v_add_u32_e32 v60, 12, v64
	v_add_u32_e32 v62, 14, v64
	v_mad_i64_i32 v[50:51], s[6:7], v50, s14, v[28:29]
	v_mad_i64_i32 v[52:53], s[6:7], v52, s14, v[28:29]
	v_mad_i64_i32 v[54:55], s[6:7], v54, s14, v[28:29]
	v_mad_i64_i32 v[56:57], s[6:7], v56, s14, v[28:29]
	v_mad_i64_i32 v[58:59], s[6:7], v58, s14, v[28:29]
	v_mad_i64_i32 v[60:61], s[6:7], v60, s14, v[28:29]
	v_mad_i64_i32 v[62:63], s[6:7], v62, s14, v[28:29]
	global_load_dword v65, v[48:49], off nt
	global_load_dword v66, v[50:51], off nt
	global_load_dword v67, v[52:53], off nt
	global_load_dword v68, v[54:55], off nt
	global_load_dword v69, v[56:57], off nt
	global_load_dword v70, v[58:59], off nt
	global_load_dword v71, v[60:61], off nt
	global_load_dword v72, v[62:63], off nt
	v_add_u32_e32 v48, 16, v64
	v_mad_i64_i32 v[48:49], s[6:7], v48, s14, v[28:29]
	v_add_u32_e32 v50, 18, v64
	v_add_u32_e32 v52, 20, v64
	v_add_u32_e32 v54, 22, v64
	v_add_u32_e32 v56, 24, v64
	v_add_u32_e32 v58, 26, v64
	v_add_u32_e32 v60, 28, v64
	v_add_u32_e32 v62, 30, v64
	v_mad_i64_i32 v[50:51], s[6:7], v50, s14, v[28:29]
	v_mad_i64_i32 v[52:53], s[6:7], v52, s14, v[28:29]
	v_mad_i64_i32 v[54:55], s[6:7], v54, s14, v[28:29]
	v_mad_i64_i32 v[56:57], s[6:7], v56, s14, v[28:29]
	v_mad_i64_i32 v[58:59], s[6:7], v58, s14, v[28:29]
	v_mad_i64_i32 v[60:61], s[6:7], v60, s14, v[28:29]
	v_mad_i64_i32 v[62:63], s[6:7], v62, s14, v[28:29]
	global_load_dword v73, v[48:49], off nt
	global_load_dword v74, v[50:51], off nt
	global_load_dword v75, v[52:53], off nt
	global_load_dword v76, v[54:55], off nt
	global_load_dword v77, v[56:57], off nt
	global_load_dword v78, v[58:59], off nt
	global_load_dword v79, v[60:61], off nt
	global_load_dword v80, v[62:63], off nt
	v_add_u32_e32 v48, 32, v64
	v_add_u32_e32 v50, 34, v64
	v_add_u32_e32 v52, 36, v64
	v_add_u32_e32 v54, 38, v64
	v_add_u32_e32 v60, 44, v64
	v_mad_i64_i32 v[48:49], s[6:7], v48, s14, v[28:29]
	v_mad_i64_i32 v[50:51], s[6:7], v50, s14, v[28:29]
	v_mad_i64_i32 v[52:53], s[6:7], v52, s14, v[28:29]
	v_mad_i64_i32 v[54:55], s[6:7], v54, s14, v[28:29]
	v_add_u32_e32 v56, 40, v64
	v_add_u32_e32 v58, 42, v64
	v_mad_i64_i32 v[60:61], s[6:7], v60, s14, v[28:29]
	v_add_u32_e32 v62, 46, v64
	v_mad_i64_i32 v[56:57], s[6:7], v56, s14, v[28:29]
	v_mad_i64_i32 v[58:59], s[6:7], v58, s14, v[28:29]
	v_mad_i64_i32 v[62:63], s[6:7], v62, s14, v[28:29]
	global_load_dword v81, v[48:49], off nt
	global_load_dword v82, v[50:51], off nt
	global_load_dword v83, v[52:53], off nt
	global_load_dword v84, v[54:55], off nt
	global_load_dword v85, v[56:57], off nt
	global_load_dword v86, v[58:59], off nt
	s_nop 0
	global_load_dword v60, v[60:61], off nt
	s_nop 0
	global_load_dword v61, v[62:63], off nt
	v_add_u32_e32 v48, 48, v64
	v_add_u32_e32 v50, 50, v64
	v_add_u32_e32 v52, 52, v64
	v_add_u32_e32 v54, 54, v64
	v_mad_i64_i32 v[48:49], s[6:7], v48, s14, v[28:29]
	v_mad_i64_i32 v[50:51], s[6:7], v50, s14, v[28:29]
	v_mad_i64_i32 v[52:53], s[6:7], v52, s14, v[28:29]
	v_mad_i64_i32 v[54:55], s[6:7], v54, s14, v[28:29]
	v_add_u32_e32 v56, 56, v64
	v_add_u32_e32 v58, 58, v64
	v_mad_i64_i32 v[56:57], s[6:7], v56, s14, v[28:29]
	v_mad_i64_i32 v[58:59], s[6:7], v58, s14, v[28:29]
	global_load_dword v62, v[48:49], off nt
	s_nop 0
	global_load_dword v50, v[50:51], off nt
	s_nop 0
	global_load_dword v51, v[52:53], off nt
	s_nop 0
	global_load_dword v52, v[54:55], off nt
	global_load_dword v53, v[56:57], off nt
	s_nop 0
	global_load_dword v54, v[58:59], off nt
	v_add_u32_e32 v48, 60, v64
	v_add_u32_e32 v55, 62, v64
	v_mad_i64_i32 v[48:49], s[6:7], v48, s14, v[28:29]
	v_mad_i64_i32 v[28:29], s[6:7], v55, s14, v[28:29]
	global_load_dword v48, v[48:49], off nt
	s_nop 0
	global_load_dword v28, v[28:29], off nt
	s_waitcnt vmcnt(31)
	v_mul_f32_e32 v29, 0x42800000, v65
	s_waitcnt vmcnt(30)
	v_mul_f32_e32 v49, 0x42800000, v66
	ds_write2_b32 v31, v29, v49 offset1:66
	s_waitcnt vmcnt(29)
	v_mul_f32_e32 v29, 0x42800000, v67
	s_waitcnt vmcnt(28)
	v_mul_f32_e32 v49, 0x42800000, v68
	ds_write2_b32 v31, v29, v49 offset0:132 offset1:198
	s_waitcnt vmcnt(27)
	v_mul_f32_e32 v29, 0x42800000, v69
	s_waitcnt vmcnt(26)
; __device__ __forceinline__ unsigned cvt_pk4_fp8(float a, float b, float c, float d) { int w = 0; w = __builtin_amdgcn_cvt_pk_fp8_f32(a, b, w, false); w = __builtin_amdgcn_cvt_pk_fp8_f32(c, d, w, true); return (unsigned)w; }
; #define GAS __attribute__((address_space(1)))
; #define LAS __attribute__((address_space(3)))
; #define LDS_WAIT() asm volatile("s_waitcnt lgkmcnt(0)" ::: "memory")
; __device__ __forceinline__ void tr_item8(const float* W, int ld, int K, int nblk, int item, unsigned char* WT, bool gu, float scale, LAS float* scr, int lane) {
;     ...
; #pragma unroll
;       for (int i = 0; i < 32; ++i) scr[(2 * i + (lane >> 5)) * 33 + (lane & 31)] = t_[i] * scale; }
;     LDS_WAIT(); asm volatile("" ::: "memory");
;     const int c = lane & 3;
; #pragma unroll
;     for (int j = 0; j < 2; ++j) { const int n = (lane >> 2) + 16 * j; const LAS float* sp = scr + (16 * c) * 33 + n;
;         v4u o; o.x = pg8::cvt_pk4_fp8(sp[0 * 33], sp[1 * 33], sp[2 * 33], sp[3 * 33]); o.y = pg8::cvt_pk4_fp8(sp[4 * 33], sp[5 * 33], sp[6 * 33], sp[7 * 33]);
;         o.z = pg8::cvt_pk4_fp8(sp[8 * 33], sp[9 * 33], sp[10 * 33], sp[11 * 33]); o.w = pg8::cvt_pk4_fp8(sp[12 * 33], sp[13 * 33], sp[14 * 33], sp[15 * 33]);
;         *(GAS v4u*)(WT + (size_t)(drow0 + n) * K + k0 + 16 * c) = o; }
;     LDS_WAIT(); asm volatile("" ::: "memory");
	v_mul_f32_e32 v49, 0x42800000, v70
	ds_write2_b32 v40, v29, v49 offset0:8 offset1:74
	s_waitcnt vmcnt(25)
	v_mul_f32_e32 v29, 0x42800000, v71
	s_waitcnt vmcnt(24)
	v_mul_f32_e32 v49, 0x42800000, v72
	ds_write2_b32 v40, v29, v49 offset0:140 offset1:206
	s_add_i32 s0, s31, s5
	s_sext_i32_i16 s5, s0
	s_bfe_u32 s5, s5, 0x70018
	s_add_i32 s5, s0, s5
	s_sext_i32_i16 s6, s5
	s_and_b32 s5, s5, 0xff80
	s_sub_i32 s0, s0, s5
	s_lshl_b32 s6, s6, 1
	s_sext_i32_i16 s0, s0
	s_waitcnt vmcnt(23)
	v_mul_f32_e32 v29, 0x42800000, v73
	s_waitcnt vmcnt(22)
	v_mul_f32_e32 v49, 0x42800000, v74
	ds_write2_b32 v41, v29, v49 offset0:16 offset1:82
	s_waitcnt vmcnt(21)
	v_mul_f32_e32 v29, 0x42800000, v75
	s_waitcnt vmcnt(20)
	v_mul_f32_e32 v49, 0x42800000, v76
	ds_write2_b32 v41, v29, v49 offset0:148 offset1:214
	s_waitcnt vmcnt(19)
	v_mul_f32_e32 v29, 0x42800000, v77
	s_waitcnt vmcnt(18)
	v_mul_f32_e32 v49, 0x42800000, v78
	ds_write2_b32 v42, v29, v49 offset0:24 offset1:90
	s_waitcnt vmcnt(17)
	v_mul_f32_e32 v29, 0x42800000, v79
	s_waitcnt vmcnt(16)
	v_mul_f32_e32 v49, 0x42800000, v80
	ds_write2_b32 v42, v29, v49 offset0:156 offset1:222
	s_and_b32 s6, s6, 0xffffff00
	s_add_i32 s0, s40, s0
	s_add_i32 s0, s0, s6
	s_mov_b32 s5, s1
	s_waitcnt vmcnt(15)
	v_mul_f32_e32 v29, 0x42800000, v81
	s_waitcnt vmcnt(14)
	v_mul_f32_e32 v49, 0x42800000, v82
	ds_write2_b32 v43, v29, v49 offset0:32 offset1:98
	s_waitcnt vmcnt(13)
	v_mul_f32_e32 v29, 0x42800000, v83
	s_waitcnt vmcnt(12)
	v_mul_f32_e32 v49, 0x42800000, v84
	ds_write2_b32 v43, v29, v49 offset0:164 offset1:230
	s_waitcnt vmcnt(11)
	v_mul_f32_e32 v29, 0x42800000, v85
	s_waitcnt vmcnt(10)
	v_mul_f32_e32 v49, 0x42800000, v86
	ds_write2_b32 v44, v29, v49 offset0:40 offset1:106
	s_waitcnt vmcnt(9)
	v_mul_f32_e32 v29, 0x42800000, v60
	s_waitcnt vmcnt(8)
	v_mul_f32_e32 v49, 0x42800000, v61
	ds_write2_b32 v44, v29, v49 offset0:172 offset1:238
	v_add_u32_e32 v84, s0, v32
	v_ashrrev_i32_e32 v85, 31, v84
	v_lshlrev_b64 v[84:85], 10, v[84:85]
	s_waitcnt vmcnt(7)
	v_mul_f32_e32 v29, 0x42800000, v62
	s_waitcnt vmcnt(6)
	v_mul_f32_e32 v49, 0x42800000, v50
	ds_write2_b32 v45, v29, v49 offset0:48 offset1:114
	s_waitcnt vmcnt(5)
	v_mul_f32_e32 v29, 0x42800000, v51
	s_waitcnt vmcnt(4)
	v_mul_f32_e32 v49, 0x42800000, v52
	ds_write2_b32 v45, v29, v49 offset0:180 offset1:246
	s_waitcnt vmcnt(3)
	v_mul_f32_e32 v29, 0x42800000, v53
	s_waitcnt vmcnt(2)
	v_mul_f32_e32 v49, 0x42800000, v54
	ds_write2_b32 v46, v29, v49 offset0:56 offset1:122
	v_mov_b32_e32 v49, 0
	v_mov_b32_e32 v50, 0
	s_waitcnt vmcnt(1)
	v_mul_f32_e32 v29, 0x42800000, v48
	s_waitcnt vmcnt(0)
	v_mul_f32_e32 v28, 0x42800000, v28
	ds_write2_b32 v46, v29, v28 offset0:188 offset1:254
	s_waitcnt lgkmcnt(0)
	ds_read2_b32 v[52:53], v33 offset1:16
	ds_read2_b32 v[54:55], v33 offset0:33 offset1:49
	ds_read2_b32 v[56:57], v33 offset0:66 offset1:82
	ds_read2_b32 v[58:59], v33 offset0:99 offset1:115
	ds_read2_b32 v[60:61], v33 offset0:132 offset1:148
	ds_read2_b32 v[62:63], v33 offset0:165 offset1:181
	ds_read2_b32 v[64:65], v33 offset0:198 offset1:214
	ds_read2_b32 v[66:67], v33 offset0:231 offset1:247
	ds_read2_b32 v[68:69], v47 offset0:8 offset1:24
	ds_read2_b32 v[70:71], v47 offset0:41 offset1:57
	ds_read2_b32 v[72:73], v47 offset0:74 offset1:90
	ds_read2_b32 v[74:75], v47 offset0:107 offset1:123
	ds_read2_b32 v[76:77], v47 offset0:140 offset1:156
	ds_read2_b32 v[78:79], v47 offset0:173 offset1:189
	v_mov_b32_e32 v48, 0
	ds_read2_b32 v[80:81], v47 offset0:206 offset1:222
	ds_read2_b32 v[82:83], v47 offset0:239 offset1:255
	v_mov_b32_e32 v51, 0
	s_waitcnt lgkmcnt(14)
	v_cvt_pk_fp8_f32 v48, v52, v54
	s_waitcnt lgkmcnt(10)
	v_cvt_pk_fp8_f32 v49, v60, v62
	s_waitcnt lgkmcnt(6)
	v_cvt_pk_fp8_f32 v50, v68, v70
	s_waitcnt lgkmcnt(2)
	v_cvt_pk_fp8_f32 v51, v76, v78
	v_cvt_pk_fp8_f32 v48, v56, v58 op_sel:[0,0,1]
	v_cvt_pk_fp8_f32 v49, v64, v66 op_sel:[0,0,1]
	v_cvt_pk_fp8_f32 v50, v72, v74 op_sel:[0,0,1]
	s_waitcnt lgkmcnt(0)
	v_cvt_pk_fp8_f32 v51, v80, v82 op_sel:[0,0,1]
	v_lshl_add_u64 v[28:29], v[18:19], 0, s[4:5]
	v_lshl_add_u64 v[84:85], v[28:29], 0, v[84:85]
	v_add_u32_e32 v52, s0, v34
	global_store_dwordx4 v[84:85], v[48:51], off nt
	s_nop 1
	v_mov_b32_e32 v48, 0
	v_mov_b32_e32 v49, 0
	v_mov_b32_e32 v50, 0
	v_mov_b32_e32 v51, 0
	v_cvt_pk_fp8_f32 v48, v53, v55
	v_cvt_pk_fp8_f32 v49, v61, v63
	v_cvt_pk_fp8_f32 v50, v69, v71
	v_cvt_pk_fp8_f32 v51, v77, v79
	v_cvt_pk_fp8_f32 v48, v57, v59 op_sel:[0,0,1]
	v_cvt_pk_fp8_f32 v49, v65, v67 op_sel:[0,0,1]
	v_cvt_pk_fp8_f32 v50, v73, v75 op_sel:[0,0,1]
	v_cvt_pk_fp8_f32 v51, v81, v83 op_sel:[0,0,1]
	v_ashrrev_i32_e32 v53, 31, v52
	v_lshlrev_b64 v[52:53], 10, v[52:53]
	v_lshl_add_u64 v[28:29], v[28:29], 0, v[52:53]
	global_store_dwordx4 v[28:29], v[48:51], off nt
	s_waitcnt lgkmcnt(0)

; #define LAS __attribute__((address_space(3)))
; __device__ __forceinline__ void tr_item(const float* W, int ld, int K, int nblk, int item, bf16* WT, bool gu, LAS float* scr, int lane) {
;     const int kb = item / nblk, nb = item % nblk, k0 = 64 * kb, n0 = 32 * nb;
;     int drow0 = n0;
;     if (gu) { const int bj = n0 / FF, j = n0 - bj * FF; drow0 = 256 * (j / 128) + 128 * bj + (j % 128); }
;     { float t_[32];
; #pragma unroll
;       for (int i = 0; i < 32; ++i) t_[i] = W[(size_t)(k0 + 2 * i + (lane >> 5)) * ld + n0 + (lane & 31)];
; #pragma unroll
;       for (int i = 0; i < 32; ++i) scr[(2 * i + (lane >> 5)) * 33 + (lane & 31)] = t_[i]; }
; __device__ __forceinline__ void convert_items(Frame& F, const Args& a, int lo, int hi, int w, int nw) {
;     ...
;         if (r < I_SO) { tr_item(a.in[12], D, D, 32, r, (bf16*)(F.ws + WS_WSWAOUT), false, scr, lane); continue; } r -= I_SO;
.LBB0_1313:
	s_andn2_b64 vcc, exec, s[4:5]
	s_cbranch_vccnz .LBB0_1315
	s_add_i32 s0, s11, 0x2000
	s_and_b32 s5, s0, 0x1ffc0
	s_and_b32 s4, s9, 0x3e0
	v_add_u32_e32 v28, s5, v30
	s_lshl_b32 s0, s4, 2
	v_ashrrev_i32_e32 v29, 31, v28
	v_lshl_add_u64 v[48:49], v[8:9], 0, s[0:1]
	v_lshlrev_b64 v[28:29], 12, v[28:29]
	v_lshl_add_u64 v[28:29], v[48:49], 0, v[28:29]
	v_add_co_u32_e32 v48, vcc, 0x2000, v28
	global_load_dword v50, v[28:29], off nt
	s_nop 0
	v_addc_co_u32_e32 v49, vcc, 0, v29, vcc
	global_load_dword v51, v[48:49], off nt
	v_add_co_u32_e32 v48, vcc, 0x4000, v28
	s_lshl_b32 s0, s5, 1
	s_nop 0
	v_addc_co_u32_e32 v49, vcc, 0, v29, vcc
	global_load_dword v52, v[48:49], off nt
	v_add_co_u32_e32 v48, vcc, 0x6000, v28
	s_nop 1
	v_addc_co_u32_e32 v49, vcc, 0, v29, vcc
	global_load_dword v53, v[48:49], off nt
	v_add_co_u32_e32 v48, vcc, 0x8000, v28
	s_nop 1
	v_addc_co_u32_e32 v49, vcc, 0, v29, vcc
	global_load_dword v54, v[48:49], off nt
	v_add_co_u32_e32 v48, vcc, 0xa000, v28
	s_nop 1
	v_addc_co_u32_e32 v49, vcc, 0, v29, vcc
	global_load_dword v55, v[48:49], off nt
	v_add_co_u32_e32 v48, vcc, 0xc000, v28
	s_nop 1
	v_addc_co_u32_e32 v49, vcc, 0, v29, vcc
	global_load_dword v56, v[48:49], off nt
	v_add_co_u32_e32 v48, vcc, 0xe000, v28
	s_nop 1
	v_addc_co_u32_e32 v49, vcc, 0, v29, vcc
	global_load_dword v57, v[48:49], off nt
	v_add_co_u32_e32 v48, vcc, 0x10000, v28
	s_nop 1
	v_addc_co_u32_e32 v49, vcc, 0, v29, vcc
	global_load_dword v58, v[48:49], off nt
	v_add_co_u32_e32 v48, vcc, 0x12000, v28
	s_nop 1
	v_addc_co_u32_e32 v49, vcc, 0, v29, vcc
	global_load_dword v59, v[48:49], off nt
	v_add_co_u32_e32 v48, vcc, 0x14000, v28
	s_nop 1
	v_addc_co_u32_e32 v49, vcc, 0, v29, vcc
	global_load_dword v60, v[48:49], off nt
	v_add_co_u32_e32 v48, vcc, 0x16000, v28
	s_nop 1
	v_addc_co_u32_e32 v49, vcc, 0, v29, vcc
	global_load_dword v61, v[48:49], off nt
	v_add_co_u32_e32 v48, vcc, 0x18000, v28
	s_nop 1
	v_addc_co_u32_e32 v49, vcc, 0, v29, vcc
	global_load_dword v62, v[48:49], off nt
	v_add_co_u32_e32 v48, vcc, 0x1a000, v28
	s_nop 1
	v_addc_co_u32_e32 v49, vcc, 0, v29, vcc
	global_load_dword v63, v[48:49], off nt
	v_add_co_u32_e32 v48, vcc, 0x1c000, v28
	s_nop 1
	v_addc_co_u32_e32 v49, vcc, 0, v29, vcc
	global_load_dword v64, v[48:49], off nt
	v_add_co_u32_e32 v48, vcc, 0x1e000, v28
	s_nop 1
	v_addc_co_u32_e32 v49, vcc, 0, v29, vcc
	global_load_dword v65, v[48:49], off nt
	v_add_co_u32_e32 v48, vcc, 0x20000, v28
	s_nop 1
	v_addc_co_u32_e32 v49, vcc, 0, v29, vcc
	global_load_dword v66, v[48:49], off nt
	v_add_co_u32_e32 v48, vcc, 0x22000, v28
	s_nop 1
	v_addc_co_u32_e32 v49, vcc, 0, v29, vcc
	global_load_dword v67, v[48:49], off nt
	v_add_co_u32_e32 v48, vcc, 0x24000, v28
	s_nop 1
	v_addc_co_u32_e32 v49, vcc, 0, v29, vcc
	global_load_dword v68, v[48:49], off nt
	v_add_co_u32_e32 v48, vcc, 0x26000, v28
	s_nop 1
	v_addc_co_u32_e32 v49, vcc, 0, v29, vcc
	global_load_dword v69, v[48:49], off nt
	v_add_co_u32_e32 v48, vcc, 0x28000, v28
	s_nop 1
	v_addc_co_u32_e32 v49, vcc, 0, v29, vcc
	global_load_dword v70, v[48:49], off nt
	v_add_co_u32_e32 v48, vcc, 0x2a000, v28
	s_nop 1
	v_addc_co_u32_e32 v49, vcc, 0, v29, vcc
	global_load_dword v71, v[48:49], off nt
	v_add_co_u32_e32 v48, vcc, 0x2c000, v28
	s_nop 1
	v_addc_co_u32_e32 v49, vcc, 0, v29, vcc
	global_load_dword v72, v[48:49], off nt
	v_add_co_u32_e32 v48, vcc, 0x2e000, v28
	s_nop 1
	v_addc_co_u32_e32 v49, vcc, 0, v29, vcc
	global_load_dword v73, v[48:49], off nt
	v_add_co_u32_e32 v48, vcc, 0x30000, v28
	s_nop 1
	v_addc_co_u32_e32 v49, vcc, 0, v29, vcc
	global_load_dword v74, v[48:49], off nt
	v_add_co_u32_e32 v48, vcc, 0x32000, v28
	s_nop 1
	v_addc_co_u32_e32 v49, vcc, 0, v29, vcc
	global_load_dword v75, v[48:49], off nt
	v_add_co_u32_e32 v48, vcc, 0x34000, v28
	s_nop 1
	v_addc_co_u32_e32 v49, vcc, 0, v29, vcc
	global_load_dword v76, v[48:49], off nt
	v_add_co_u32_e32 v48, vcc, 0x36000, v28
	s_nop 1
	v_addc_co_u32_e32 v49, vcc, 0, v29, vcc
	global_load_dword v77, v[48:49], off nt
	v_add_co_u32_e32 v48, vcc, 0x38000, v28
	s_nop 1
	v_addc_co_u32_e32 v49, vcc, 0, v29, vcc
	global_load_dword v78, v[48:49], off nt
	v_add_co_u32_e32 v48, vcc, 0x3a000, v28
	s_nop 1
	v_addc_co_u32_e32 v49, vcc, 0, v29, vcc
	global_load_dword v79, v[48:49], off nt
	v_add_co_u32_e32 v48, vcc, 0x3c000, v28
	s_nop 1
	v_addc_co_u32_e32 v49, vcc, 0, v29, vcc
	v_add_co_u32_e32 v28, vcc, 0x3e000, v28
	global_load_dword v48, v[48:49], off nt
	s_nop 0
	v_addc_co_u32_e32 v29, vcc, 0, v29, vcc
	global_load_dword v28, v[28:29], off nt
	s_waitcnt vmcnt(30)
	ds_write2_b32 v31, v50, v51 offset1:66
	s_waitcnt vmcnt(28)
	ds_write2_b32 v31, v52, v53 offset0:132 offset1:198
	s_waitcnt vmcnt(26)
	ds_write2_b32 v40, v54, v55 offset0:8 offset1:74
	s_waitcnt vmcnt(24)
	ds_write2_b32 v40, v56, v57 offset0:140 offset1:206
	s_waitcnt vmcnt(22)
	ds_write2_b32 v41, v58, v59 offset0:16 offset1:82
	s_waitcnt vmcnt(20)
	ds_write2_b32 v41, v60, v61 offset0:148 offset1:214
	s_waitcnt vmcnt(18)
	ds_write2_b32 v42, v62, v63 offset0:24 offset1:90
	s_waitcnt vmcnt(16)
	ds_write2_b32 v42, v64, v65 offset0:156 offset1:222
	s_waitcnt vmcnt(14)
	ds_write2_b32 v43, v66, v67 offset0:32 offset1:98
	s_waitcnt vmcnt(12)
	ds_write2_b32 v43, v68, v69 offset0:164 offset1:230
	s_waitcnt vmcnt(10)
	ds_write2_b32 v44, v70, v71 offset0:40 offset1:106
	s_waitcnt vmcnt(8)
; #define GAS __attribute__((address_space(1)))
; #define LAS __attribute__((address_space(3)))
; #define LDS_WAIT() asm volatile("s_waitcnt lgkmcnt(0)" ::: "memory")
; __device__ __forceinline__ unsigned pk2(float lo, float hi) { return f2bf(lo) | (f2bf(hi) << 16); }
; __device__ __forceinline__ void tr_item(const float* W, int ld, int K, int nblk, int item, bf16* WT, bool gu, LAS float* scr, int lane) {
;     ...
;       for (int i = 0; i < 32; ++i) scr[(2 * i + (lane >> 5)) * 33 + (lane & 31)] = t_[i]; }
;     LDS_WAIT(); asm volatile("" ::: "memory");
;     const int c = lane & 7;
; #pragma unroll
;     for (int j = 0; j < 4; ++j) { const int n = (lane >> 3) + 8 * j; const LAS float* s = scr + (8 * c) * 33 + n;
;         v4u o; o.x = pk2(s[0 * 33], s[1 * 33]); o.y = pk2(s[2 * 33], s[3 * 33]); o.z = pk2(s[4 * 33], s[5 * 33]); o.w = pk2(s[6 * 33], s[7 * 33]);
;         *(GAS v4u*)(WT + (size_t)(drow0 + n) * K + k0 + 8 * c) = o; }
;     LDS_WAIT(); asm volatile("" ::: "memory");
	ds_write2_b32 v44, v72, v73 offset0:172 offset1:238
	s_waitcnt vmcnt(6)
	ds_write2_b32 v45, v74, v75 offset0:48 offset1:114
	s_waitcnt vmcnt(4)
	ds_write2_b32 v45, v76, v77 offset0:180 offset1:246
	s_waitcnt vmcnt(2)
	ds_write2_b32 v46, v78, v79 offset0:56 offset1:122
	s_waitcnt vmcnt(0)
	ds_write2_b32 v46, v48, v28 offset0:188 offset1:254
	s_waitcnt lgkmcnt(0)
	ds_read2_b32 v[52:53], v36 offset0:33 offset1:41
	ds_read2_b32 v[54:55], v36 offset1:8
	ds_read2_b32 v[56:57], v36 offset0:66 offset1:74
	ds_read2_b32 v[58:59], v36 offset0:99 offset1:107
	ds_read2_b32 v[60:61], v36 offset0:132 offset1:140
	ds_read2_b32 v[62:63], v36 offset0:165 offset1:173
	ds_read2_b32 v[64:65], v36 offset0:198 offset1:206
	ds_read2_b32 v[66:67], v36 offset0:231 offset1:239
	s_waitcnt lgkmcnt(7)
	v_bfe_u32 v49, v52, 16, 1
	s_waitcnt lgkmcnt(6)
	v_bfe_u32 v48, v54, 16, 1
	v_add3_u32 v48, v54, v48, s15
	v_lshrrev_b32_e32 v48, 16, v48
	v_add3_u32 v49, v52, v49, s15
	v_and_or_b32 v48, v49, s16, v48
	s_waitcnt lgkmcnt(5)
	v_bfe_u32 v49, v56, 16, 1
	v_add3_u32 v49, v56, v49, s15
	s_waitcnt lgkmcnt(4)
	v_bfe_u32 v50, v58, 16, 1
	v_lshrrev_b32_e32 v49, 16, v49
	v_add3_u32 v50, v58, v50, s15
	v_and_or_b32 v49, v50, s16, v49
	s_waitcnt lgkmcnt(3)
	v_bfe_u32 v50, v60, 16, 1
	v_add3_u32 v50, v60, v50, s15
	s_waitcnt lgkmcnt(2)
	v_bfe_u32 v51, v62, 16, 1
	v_lshrrev_b32_e32 v50, 16, v50
	v_add3_u32 v51, v62, v51, s15
	v_and_or_b32 v50, v51, s16, v50
	s_waitcnt lgkmcnt(1)
	v_bfe_u32 v51, v64, 16, 1
	v_add_u32_e32 v68, s4, v35
	v_add3_u32 v51, v64, v51, s15
	s_waitcnt lgkmcnt(0)
	v_bfe_u32 v52, v66, 16, 1
	v_ashrrev_i32_e32 v69, 31, v68
	v_lshl_add_u64 v[28:29], v[20:21], 0, s[0:1]
	v_lshrrev_b32_e32 v51, 16, v51
	v_add3_u32 v52, v66, v52, s15
	v_lshlrev_b64 v[68:69], 11, v[68:69]
	v_and_or_b32 v51, v52, s16, v51
	v_lshl_add_u64 v[68:69], v[28:29], 0, v[68:69]
	global_store_dwordx4 v[68:69], v[48:51], off nt
	v_bfe_u32 v52, v67, 16, 1
	v_add3_u32 v52, v67, v52, s15
	v_bfe_u32 v48, v55, 16, 1
	v_add3_u32 v48, v55, v48, s15
	v_bfe_u32 v49, v53, 16, 1
	v_lshrrev_b32_e32 v48, 16, v48
	v_add3_u32 v49, v53, v49, s15
	v_and_or_b32 v48, v49, s16, v48
	v_bfe_u32 v49, v57, 16, 1
	v_add3_u32 v49, v57, v49, s15
	v_bfe_u32 v50, v59, 16, 1
	v_lshrrev_b32_e32 v49, 16, v49
	v_add3_u32 v50, v59, v50, s15
	v_and_or_b32 v49, v50, s16, v49
	v_bfe_u32 v50, v61, 16, 1
	v_add3_u32 v50, v61, v50, s15
	v_bfe_u32 v51, v63, 16, 1
	v_lshrrev_b32_e32 v50, 16, v50
	v_add3_u32 v51, v63, v51, s15
	v_and_or_b32 v50, v51, s16, v50
	v_bfe_u32 v51, v65, 16, 1
	v_add3_u32 v51, v65, v51, s15
	v_lshrrev_b32_e32 v51, 16, v51
	v_and_or_b32 v51, v52, s16, v51
	v_add_u32_e32 v52, s4, v37
	v_ashrrev_i32_e32 v53, 31, v52
	v_lshlrev_b64 v[52:53], 11, v[52:53]
	v_lshl_add_u64 v[52:53], v[28:29], 0, v[52:53]
	global_store_dwordx4 v[52:53], v[48:51], off nt
	ds_read2_b32 v[52:53], v36 offset0:49 offset1:57
	ds_read2_b32 v[54:55], v36 offset0:16 offset1:24
	ds_read2_b32 v[56:57], v36 offset0:82 offset1:90
	ds_read2_b32 v[58:59], v36 offset0:115 offset1:123
	ds_read2_b32 v[60:61], v36 offset0:148 offset1:156
	ds_read2_b32 v[62:63], v36 offset0:181 offset1:189
	ds_read2_b32 v[64:65], v36 offset0:214 offset1:222
	ds_read2_b32 v[66:67], v36 offset0:247 offset1:255
	s_waitcnt lgkmcnt(7)
	v_bfe_u32 v49, v52, 16, 1
	s_waitcnt lgkmcnt(6)
	v_bfe_u32 v48, v54, 16, 1
	v_add3_u32 v48, v54, v48, s15
	v_lshrrev_b32_e32 v48, 16, v48
	v_add3_u32 v49, v52, v49, s15
	v_and_or_b32 v48, v49, s16, v48
	s_waitcnt lgkmcnt(5)
	v_bfe_u32 v49, v56, 16, 1
	v_add3_u32 v49, v56, v49, s15
	s_waitcnt lgkmcnt(4)
	v_bfe_u32 v50, v58, 16, 1
	v_lshrrev_b32_e32 v49, 16, v49
	v_add3_u32 v50, v58, v50, s15
	v_and_or_b32 v49, v50, s16, v49
	s_waitcnt lgkmcnt(3)
	v_bfe_u32 v50, v60, 16, 1
	v_add3_u32 v50, v60, v50, s15
	s_waitcnt lgkmcnt(2)
	v_bfe_u32 v51, v62, 16, 1
	v_lshrrev_b32_e32 v50, 16, v50
	v_add3_u32 v51, v62, v51, s15
	v_and_or_b32 v50, v51, s16, v50
	s_waitcnt lgkmcnt(1)
	v_bfe_u32 v51, v64, 16, 1
	v_add_u32_e32 v68, s4, v38
	v_add3_u32 v51, v64, v51, s15
	s_waitcnt lgkmcnt(0)
	v_bfe_u32 v52, v66, 16, 1
	v_ashrrev_i32_e32 v69, 31, v68
	v_lshrrev_b32_e32 v51, 16, v51
	v_add3_u32 v52, v66, v52, s15
	v_lshlrev_b64 v[68:69], 11, v[68:69]
	v_and_or_b32 v51, v52, s16, v51
	v_lshl_add_u64 v[68:69], v[28:29], 0, v[68:69]
	global_store_dwordx4 v[68:69], v[48:51], off nt
	v_bfe_u32 v52, v67, 16, 1
	v_add3_u32 v52, v67, v52, s15
	v_bfe_u32 v48, v55, 16, 1
	v_add3_u32 v48, v55, v48, s15
	v_bfe_u32 v49, v53, 16, 1
	v_lshrrev_b32_e32 v48, 16, v48
	v_add3_u32 v49, v53, v49, s15
	v_and_or_b32 v48, v49, s16, v48
	v_bfe_u32 v49, v57, 16, 1
	v_add3_u32 v49, v57, v49, s15
	v_bfe_u32 v50, v59, 16, 1
	v_lshrrev_b32_e32 v49, 16, v49
	v_add3_u32 v50, v59, v50, s15
	v_and_or_b32 v49, v50, s16, v49
	v_bfe_u32 v50, v61, 16, 1
	v_add3_u32 v50, v61, v50, s15
	v_bfe_u32 v51, v63, 16, 1
	v_lshrrev_b32_e32 v50, 16, v50
	v_add3_u32 v51, v63, v51, s15
	v_and_or_b32 v50, v51, s16, v50
	v_bfe_u32 v51, v65, 16, 1
	v_add3_u32 v51, v65, v51, s15
	v_lshrrev_b32_e32 v51, 16, v51
	v_and_or_b32 v51, v52, s16, v51
	v_add_u32_e32 v52, s4, v39
	v_ashrrev_i32_e32 v53, 31, v52
	v_lshlrev_b64 v[52:53], 11, v[52:53]
	v_lshl_add_u64 v[28:29], v[28:29], 0, v[52:53]
	global_store_dwordx4 v[28:29], v[48:51], off nt
	s_waitcnt lgkmcnt(0)

; #define LAS __attribute__((address_space(3)))
; __device__ __forceinline__ void tr_item(const float* W, int ld, int K, int nblk, int item, bf16* WT, bool gu, LAS float* scr, int lane) {
;     const int kb = item / nblk, nb = item % nblk, k0 = 64 * kb, n0 = 32 * nb;
;     int drow0 = n0;
;     if (gu) { const int bj = n0 / FF, j = n0 - bj * FF; drow0 = 256 * (j / 128) + 128 * bj + (j % 128); }
;     { float t_[32];
; #pragma unroll
;       for (int i = 0; i < 32; ++i) t_[i] = W[(size_t)(k0 + 2 * i + (lane >> 5)) * ld + n0 + (lane & 31)];
; #pragma unroll
;       for (int i = 0; i < 32; ++i) scr[(2 * i + (lane >> 5)) * 33 + (lane & 31)] = t_[i]; }
; __device__ __forceinline__ void convert_items(Frame& F, const Args& a, int lo, int hi, int w, int nw) {
;     ...
;         if (r < I_SI) { tr_item(a.in[10], D + 512, D, 48, r, (bf16*)(F.ws + WS_WSWAIN), false, scr, lane); continue; } r -= I_SI;
.LBB0_1316:
	s_andn2_b64 vcc, exec, s[4:5]
	s_cbranch_vccnz .LBB0_1318
	s_add_i32 s0, s8, 0xf800
	s_and_b32 s4, s0, 0xffff
	s_mul_i32 s4, s4, 0xaaab
	s_lshr_b32 s5, s4, 21
	s_mul_i32 s4, s5, 48
	s_sub_i32 s0, s0, s4
	s_lshl_b32 s0, s0, 5
	s_and_b32 s4, s0, 0xffe0
	s_lshl_b32 s0, s4, 2
	v_lshl_add_u32 v50, s5, 6, v30
	v_lshl_add_u64 v[28:29], v[10:11], 0, s[0:1]
	v_mad_i64_i32 v[48:49], s[6:7], v50, s17, v[28:29]
	global_load_dword v51, v[48:49], off nt
	v_add_u32_e32 v48, 2, v50
	v_mad_i64_i32 v[48:49], s[6:7], v48, s17, v[28:29]
	global_load_dword v52, v[48:49], off nt
	v_add_u32_e32 v48, 4, v50
	v_mad_i64_i32 v[48:49], s[6:7], v48, s17, v[28:29]
	global_load_dword v53, v[48:49], off nt
	v_add_u32_e32 v48, 6, v50
	v_mad_i64_i32 v[48:49], s[6:7], v48, s17, v[28:29]
	global_load_dword v54, v[48:49], off nt
	v_add_u32_e32 v48, 8, v50
	v_mad_i64_i32 v[48:49], s[6:7], v48, s17, v[28:29]
	global_load_dword v55, v[48:49], off nt
	v_add_u32_e32 v48, 10, v50
	v_mad_i64_i32 v[48:49], s[6:7], v48, s17, v[28:29]
	global_load_dword v56, v[48:49], off nt
	v_add_u32_e32 v48, 12, v50
	v_mad_i64_i32 v[48:49], s[6:7], v48, s17, v[28:29]
	global_load_dword v57, v[48:49], off nt
	v_add_u32_e32 v48, 14, v50
	v_mad_i64_i32 v[48:49], s[6:7], v48, s17, v[28:29]
	global_load_dword v58, v[48:49], off nt
	v_add_u32_e32 v48, 16, v50
	v_mad_i64_i32 v[48:49], s[6:7], v48, s17, v[28:29]
	global_load_dword v59, v[48:49], off nt
	v_add_u32_e32 v48, 18, v50
	v_mad_i64_i32 v[48:49], s[6:7], v48, s17, v[28:29]
	global_load_dword v60, v[48:49], off nt
	v_add_u32_e32 v48, 20, v50
	v_mad_i64_i32 v[48:49], s[6:7], v48, s17, v[28:29]
	global_load_dword v61, v[48:49], off nt
	v_add_u32_e32 v48, 22, v50
	v_mad_i64_i32 v[48:49], s[6:7], v48, s17, v[28:29]
	global_load_dword v62, v[48:49], off nt
	v_add_u32_e32 v48, 24, v50
	v_mad_i64_i32 v[48:49], s[6:7], v48, s17, v[28:29]
	global_load_dword v63, v[48:49], off nt
	v_add_u32_e32 v48, 26, v50
	v_mad_i64_i32 v[48:49], s[6:7], v48, s17, v[28:29]
	global_load_dword v64, v[48:49], off nt
	v_add_u32_e32 v48, 28, v50
	v_mad_i64_i32 v[48:49], s[6:7], v48, s17, v[28:29]
	global_load_dword v65, v[48:49], off nt
	v_add_u32_e32 v48, 30, v50
	v_mad_i64_i32 v[48:49], s[6:7], v48, s17, v[28:29]
	global_load_dword v66, v[48:49], off nt
	v_add_u32_e32 v48, 32, v50
	v_mad_i64_i32 v[48:49], s[6:7], v48, s17, v[28:29]
	global_load_dword v67, v[48:49], off nt
	v_add_u32_e32 v48, 34, v50
	v_mad_i64_i32 v[48:49], s[6:7], v48, s17, v[28:29]
	global_load_dword v68, v[48:49], off nt
	v_add_u32_e32 v48, 36, v50
	v_mad_i64_i32 v[48:49], s[6:7], v48, s17, v[28:29]
	global_load_dword v69, v[48:49], off nt
	v_add_u32_e32 v48, 38, v50
	v_mad_i64_i32 v[48:49], s[6:7], v48, s17, v[28:29]
	global_load_dword v70, v[48:49], off nt
	v_add_u32_e32 v48, 40, v50
	v_mad_i64_i32 v[48:49], s[6:7], v48, s17, v[28:29]
	global_load_dword v71, v[48:49], off nt
	v_add_u32_e32 v48, 42, v50
	v_mad_i64_i32 v[48:49], s[6:7], v48, s17, v[28:29]
	global_load_dword v72, v[48:49], off nt
	v_add_u32_e32 v48, 44, v50
	v_mad_i64_i32 v[48:49], s[6:7], v48, s17, v[28:29]
	global_load_dword v73, v[48:49], off nt
	v_add_u32_e32 v48, 46, v50
	v_mad_i64_i32 v[48:49], s[6:7], v48, s17, v[28:29]
	global_load_dword v74, v[48:49], off nt
	v_add_u32_e32 v48, 48, v50
	v_mad_i64_i32 v[48:49], s[6:7], v48, s17, v[28:29]
	global_load_dword v75, v[48:49], off nt
	v_add_u32_e32 v48, 50, v50
	v_mad_i64_i32 v[48:49], s[6:7], v48, s17, v[28:29]
	global_load_dword v76, v[48:49], off nt
	v_add_u32_e32 v48, 52, v50
	v_mad_i64_i32 v[48:49], s[6:7], v48, s17, v[28:29]
	global_load_dword v77, v[48:49], off nt
	v_add_u32_e32 v48, 54, v50
	v_mad_i64_i32 v[48:49], s[6:7], v48, s17, v[28:29]
	global_load_dword v78, v[48:49], off nt
	v_add_u32_e32 v48, 56, v50
	v_mad_i64_i32 v[48:49], s[6:7], v48, s17, v[28:29]
	global_load_dword v79, v[48:49], off nt
	v_add_u32_e32 v48, 58, v50
	v_mad_i64_i32 v[48:49], s[6:7], v48, s17, v[28:29]
	global_load_dword v80, v[48:49], off nt
	v_add_u32_e32 v48, 60, v50
	v_mad_i64_i32 v[48:49], s[6:7], v48, s17, v[28:29]
	global_load_dword v48, v[48:49], off nt
	v_add_u32_e32 v49, 62, v50
	v_mad_i64_i32 v[28:29], s[6:7], v49, s17, v[28:29]
	global_load_dword v28, v[28:29], off nt
	s_waitcnt vmcnt(30)
	ds_write2_b32 v31, v51, v52 offset1:66
	s_waitcnt vmcnt(28)
	ds_write2_b32 v31, v53, v54 offset0:132 offset1:198
	s_waitcnt vmcnt(26)
	ds_write2_b32 v40, v55, v56 offset0:8 offset1:74
	s_waitcnt vmcnt(24)
	ds_write2_b32 v40, v57, v58 offset0:140 offset1:206
	s_waitcnt vmcnt(22)
	ds_write2_b32 v41, v59, v60 offset0:16 offset1:82
	s_waitcnt vmcnt(20)
	ds_write2_b32 v41, v61, v62 offset0:148 offset1:214
	s_waitcnt vmcnt(18)
	ds_write2_b32 v42, v63, v64 offset0:24 offset1:90
	s_waitcnt vmcnt(16)
	ds_write2_b32 v42, v65, v66 offset0:156 offset1:222
	s_waitcnt vmcnt(14)
	ds_write2_b32 v43, v67, v68 offset0:32 offset1:98
	s_waitcnt vmcnt(12)
	ds_write2_b32 v43, v69, v70 offset0:164 offset1:230
	s_waitcnt vmcnt(10)
	ds_write2_b32 v44, v71, v72 offset0:40 offset1:106
	s_waitcnt vmcnt(8)
	ds_write2_b32 v44, v73, v74 offset0:172 offset1:238
	s_waitcnt vmcnt(6)
	ds_write2_b32 v45, v75, v76 offset0:48 offset1:114
	s_waitcnt vmcnt(4)
; #define GAS __attribute__((address_space(1)))
; #define LAS __attribute__((address_space(3)))
; #define LDS_WAIT() asm volatile("s_waitcnt lgkmcnt(0)" ::: "memory")
; __device__ __forceinline__ unsigned pk2(float lo, float hi) { return f2bf(lo) | (f2bf(hi) << 16); }
; __device__ __forceinline__ void tr_item(const float* W, int ld, int K, int nblk, int item, bf16* WT, bool gu, LAS float* scr, int lane) {
;     ...
;       for (int i = 0; i < 32; ++i) scr[(2 * i + (lane >> 5)) * 33 + (lane & 31)] = t_[i]; }
;     LDS_WAIT(); asm volatile("" ::: "memory");
;     const int c = lane & 7;
; #pragma unroll
;     for (int j = 0; j < 4; ++j) { const int n = (lane >> 3) + 8 * j; const LAS float* s = scr + (8 * c) * 33 + n;
;         v4u o; o.x = pk2(s[0 * 33], s[1 * 33]); o.y = pk2(s[2 * 33], s[3 * 33]); o.z = pk2(s[4 * 33], s[5 * 33]); o.w = pk2(s[6 * 33], s[7 * 33]);
;         *(GAS v4u*)(WT + (size_t)(drow0 + n) * K + k0 + 8 * c) = o; }
;     LDS_WAIT(); asm volatile("" ::: "memory");
	ds_write2_b32 v45, v77, v78 offset0:180 offset1:246
	s_waitcnt vmcnt(2)
	ds_write2_b32 v46, v79, v80 offset0:56 offset1:122
	s_waitcnt vmcnt(0)
	ds_write2_b32 v46, v48, v28 offset0:188 offset1:254
	s_waitcnt lgkmcnt(0)
	ds_read2_b32 v[52:53], v36 offset0:33 offset1:41
	ds_read2_b32 v[54:55], v36 offset1:8
	ds_read2_b32 v[56:57], v36 offset0:66 offset1:74
	ds_read2_b32 v[58:59], v36 offset0:99 offset1:107
	ds_read2_b32 v[60:61], v36 offset0:132 offset1:140
	ds_read2_b32 v[62:63], v36 offset0:165 offset1:173
	ds_read2_b32 v[64:65], v36 offset0:198 offset1:206
	ds_read2_b32 v[66:67], v36 offset0:231 offset1:239
	s_waitcnt lgkmcnt(7)
	v_bfe_u32 v49, v52, 16, 1
	s_waitcnt lgkmcnt(6)
	v_bfe_u32 v48, v54, 16, 1
	v_add3_u32 v48, v54, v48, s15
	v_lshrrev_b32_e32 v48, 16, v48
	v_add3_u32 v49, v52, v49, s15
	v_and_or_b32 v48, v49, s16, v48
	s_waitcnt lgkmcnt(5)
	v_bfe_u32 v49, v56, 16, 1
	v_add3_u32 v49, v56, v49, s15
	s_waitcnt lgkmcnt(4)
	v_bfe_u32 v50, v58, 16, 1
	v_lshrrev_b32_e32 v49, 16, v49
	v_add3_u32 v50, v58, v50, s15
	v_and_or_b32 v49, v50, s16, v49
	s_waitcnt lgkmcnt(3)
	v_bfe_u32 v50, v60, 16, 1
	v_add3_u32 v50, v60, v50, s15
	s_waitcnt lgkmcnt(2)
	v_bfe_u32 v51, v62, 16, 1
	v_lshrrev_b32_e32 v50, 16, v50
	v_add3_u32 v51, v62, v51, s15
	v_and_or_b32 v50, v51, s16, v50
	s_waitcnt lgkmcnt(1)
	v_bfe_u32 v51, v64, 16, 1
	v_add_u32_e32 v68, s4, v35
	s_lshl_b32 s0, s5, 7
	v_add3_u32 v51, v64, v51, s15
	s_waitcnt lgkmcnt(0)
	v_bfe_u32 v52, v66, 16, 1
	v_ashrrev_i32_e32 v69, 31, v68
	v_lshl_add_u64 v[28:29], v[22:23], 0, s[0:1]
	v_lshrrev_b32_e32 v51, 16, v51
	v_add3_u32 v52, v66, v52, s15
	v_lshlrev_b64 v[68:69], 11, v[68:69]
	v_and_or_b32 v51, v52, s16, v51
	v_lshl_add_u64 v[68:69], v[28:29], 0, v[68:69]
	global_store_dwordx4 v[68:69], v[48:51], off nt
	v_bfe_u32 v52, v67, 16, 1
	v_add3_u32 v52, v67, v52, s15
	v_bfe_u32 v48, v55, 16, 1
	v_add3_u32 v48, v55, v48, s15
	v_bfe_u32 v49, v53, 16, 1
	v_lshrrev_b32_e32 v48, 16, v48
	v_add3_u32 v49, v53, v49, s15
	v_and_or_b32 v48, v49, s16, v48
	v_bfe_u32 v49, v57, 16, 1
	v_add3_u32 v49, v57, v49, s15
	v_bfe_u32 v50, v59, 16, 1
	v_lshrrev_b32_e32 v49, 16, v49
	v_add3_u32 v50, v59, v50, s15
	v_and_or_b32 v49, v50, s16, v49
	v_bfe_u32 v50, v61, 16, 1
	v_add3_u32 v50, v61, v50, s15
	v_bfe_u32 v51, v63, 16, 1
	v_lshrrev_b32_e32 v50, 16, v50
	v_add3_u32 v51, v63, v51, s15
	v_and_or_b32 v50, v51, s16, v50
	v_bfe_u32 v51, v65, 16, 1
	v_add3_u32 v51, v65, v51, s15
	v_lshrrev_b32_e32 v51, 16, v51
	v_and_or_b32 v51, v52, s16, v51
	v_add_u32_e32 v52, s4, v37
	v_ashrrev_i32_e32 v53, 31, v52
	v_lshlrev_b64 v[52:53], 11, v[52:53]
	v_lshl_add_u64 v[52:53], v[28:29], 0, v[52:53]
	global_store_dwordx4 v[52:53], v[48:51], off nt
	ds_read2_b32 v[52:53], v36 offset0:49 offset1:57
	ds_read2_b32 v[54:55], v36 offset0:16 offset1:24
	ds_read2_b32 v[56:57], v36 offset0:82 offset1:90
	ds_read2_b32 v[58:59], v36 offset0:115 offset1:123
	ds_read2_b32 v[60:61], v36 offset0:148 offset1:156
	ds_read2_b32 v[62:63], v36 offset0:181 offset1:189
	ds_read2_b32 v[64:65], v36 offset0:214 offset1:222
	ds_read2_b32 v[66:67], v36 offset0:247 offset1:255
	s_waitcnt lgkmcnt(7)
	v_bfe_u32 v49, v52, 16, 1
	s_waitcnt lgkmcnt(6)
	v_bfe_u32 v48, v54, 16, 1
	v_add3_u32 v48, v54, v48, s15
	v_lshrrev_b32_e32 v48, 16, v48
	v_add3_u32 v49, v52, v49, s15
	v_and_or_b32 v48, v49, s16, v48
	s_waitcnt lgkmcnt(5)
	v_bfe_u32 v49, v56, 16, 1
	v_add3_u32 v49, v56, v49, s15
	s_waitcnt lgkmcnt(4)
	v_bfe_u32 v50, v58, 16, 1
	v_lshrrev_b32_e32 v49, 16, v49
	v_add3_u32 v50, v58, v50, s15
	v_and_or_b32 v49, v50, s16, v49
	s_waitcnt lgkmcnt(3)
	v_bfe_u32 v50, v60, 16, 1
	v_add3_u32 v50, v60, v50, s15
	s_waitcnt lgkmcnt(2)
	v_bfe_u32 v51, v62, 16, 1
	v_lshrrev_b32_e32 v50, 16, v50
	v_add3_u32 v51, v62, v51, s15
	v_and_or_b32 v50, v51, s16, v50
	s_waitcnt lgkmcnt(1)
	v_bfe_u32 v51, v64, 16, 1
	v_add_u32_e32 v68, s4, v38
	v_add3_u32 v51, v64, v51, s15
	s_waitcnt lgkmcnt(0)
	v_bfe_u32 v52, v66, 16, 1
	v_ashrrev_i32_e32 v69, 31, v68
	v_lshrrev_b32_e32 v51, 16, v51
	v_add3_u32 v52, v66, v52, s15
	v_lshlrev_b64 v[68:69], 11, v[68:69]
	v_and_or_b32 v51, v52, s16, v51
	v_lshl_add_u64 v[68:69], v[28:29], 0, v[68:69]
	global_store_dwordx4 v[68:69], v[48:51], off nt
	v_bfe_u32 v52, v67, 16, 1
	v_add3_u32 v52, v67, v52, s15
	v_bfe_u32 v48, v55, 16, 1
	v_add3_u32 v48, v55, v48, s15
	v_bfe_u32 v49, v53, 16, 1
	v_lshrrev_b32_e32 v48, 16, v48
	v_add3_u32 v49, v53, v49, s15
	v_and_or_b32 v48, v49, s16, v48
	v_bfe_u32 v49, v57, 16, 1
	v_add3_u32 v49, v57, v49, s15
	v_bfe_u32 v50, v59, 16, 1
	v_lshrrev_b32_e32 v49, 16, v49
	v_add3_u32 v50, v59, v50, s15
	v_and_or_b32 v49, v50, s16, v49
	v_bfe_u32 v50, v61, 16, 1
	v_add3_u32 v50, v61, v50, s15
	v_bfe_u32 v51, v63, 16, 1
	v_lshrrev_b32_e32 v50, 16, v50
	v_add3_u32 v51, v63, v51, s15
	v_and_or_b32 v50, v51, s16, v50
	v_bfe_u32 v51, v65, 16, 1
	v_add3_u32 v51, v65, v51, s15
	v_lshrrev_b32_e32 v51, 16, v51
	v_and_or_b32 v51, v52, s16, v51
	v_add_u32_e32 v52, s4, v39
	v_ashrrev_i32_e32 v53, 31, v52
	v_lshlrev_b64 v[52:53], 11, v[52:53]
	v_lshl_add_u64 v[28:29], v[28:29], 0, v[52:53]
	global_store_dwordx4 v[28:29], v[48:51], off nt
	s_waitcnt lgkmcnt(0)

; #define LAS __attribute__((address_space(3)))
; __device__ __forceinline__ void tr_item(const float* W, int ld, int K, int nblk, int item, bf16* WT, bool gu, LAS float* scr, int lane) {
;     const int kb = item / nblk, nb = item % nblk, k0 = 64 * kb, n0 = 32 * nb;
;     int drow0 = n0;
;     if (gu) { const int bj = n0 / FF, j = n0 - bj * FF; drow0 = 256 * (j / 128) + 128 * bj + (j % 128); }
;     { float t_[32];
; #pragma unroll
;       for (int i = 0; i < 32; ++i) t_[i] = W[(size_t)(k0 + 2 * i + (lane >> 5)) * ld + n0 + (lane & 31)];
; #pragma unroll
;       for (int i = 0; i < 32; ++i) scr[(2 * i + (lane >> 5)) * 33 + (lane & 31)] = t_[i]; }
; __device__ __forceinline__ void convert_items(Frame& F, const Args& a, int lo, int hi, int w, int nw) {
;     ...
;         if (r < I_FO) { tr_item(a.in[9], D, D, 32, r, (bf16*)(F.ws + WS_WFOXOUT), false, scr, lane); continue; } r -= I_FO;
.LBB0_1319:
	s_andn2_b64 vcc, exec, s[4:5]
	s_cbranch_vccnz .LBB0_1321
	s_add_i32 s0, s11, 0x2a00
	s_and_b32 s5, s0, 0x1ffc0
	s_and_b32 s4, s9, 0x3e0
	v_add_u32_e32 v28, s5, v30
	s_lshl_b32 s0, s4, 2
	v_ashrrev_i32_e32 v29, 31, v28
	v_lshl_add_u64 v[48:49], v[12:13], 0, s[0:1]
	v_lshlrev_b64 v[28:29], 12, v[28:29]
	v_lshl_add_u64 v[28:29], v[48:49], 0, v[28:29]
	v_add_co_u32_e32 v48, vcc, 0x2000, v28
	global_load_dword v50, v[28:29], off nt
	s_nop 0
	v_addc_co_u32_e32 v49, vcc, 0, v29, vcc
	global_load_dword v51, v[48:49], off nt
	v_add_co_u32_e32 v48, vcc, 0x4000, v28
	s_lshl_b32 s0, s5, 1
	s_nop 0
	v_addc_co_u32_e32 v49, vcc, 0, v29, vcc
	global_load_dword v52, v[48:49], off nt
	v_add_co_u32_e32 v48, vcc, 0x6000, v28
	s_nop 1
	v_addc_co_u32_e32 v49, vcc, 0, v29, vcc
	global_load_dword v53, v[48:49], off nt
	v_add_co_u32_e32 v48, vcc, 0x8000, v28
	s_nop 1
	v_addc_co_u32_e32 v49, vcc, 0, v29, vcc
	global_load_dword v54, v[48:49], off nt
	v_add_co_u32_e32 v48, vcc, 0xa000, v28
	s_nop 1
	v_addc_co_u32_e32 v49, vcc, 0, v29, vcc
	global_load_dword v55, v[48:49], off nt
	v_add_co_u32_e32 v48, vcc, 0xc000, v28
	s_nop 1
	v_addc_co_u32_e32 v49, vcc, 0, v29, vcc
	global_load_dword v56, v[48:49], off nt
	v_add_co_u32_e32 v48, vcc, 0xe000, v28
	s_nop 1
	v_addc_co_u32_e32 v49, vcc, 0, v29, vcc
	global_load_dword v57, v[48:49], off nt
	v_add_co_u32_e32 v48, vcc, 0x10000, v28
	s_nop 1
	v_addc_co_u32_e32 v49, vcc, 0, v29, vcc
	global_load_dword v58, v[48:49], off nt
	v_add_co_u32_e32 v48, vcc, 0x12000, v28
	s_nop 1
	v_addc_co_u32_e32 v49, vcc, 0, v29, vcc
	global_load_dword v59, v[48:49], off nt
	v_add_co_u32_e32 v48, vcc, 0x14000, v28
	s_nop 1
	v_addc_co_u32_e32 v49, vcc, 0, v29, vcc
	global_load_dword v60, v[48:49], off nt
	v_add_co_u32_e32 v48, vcc, 0x16000, v28
	s_nop 1
	v_addc_co_u32_e32 v49, vcc, 0, v29, vcc
	global_load_dword v61, v[48:49], off nt
	v_add_co_u32_e32 v48, vcc, 0x18000, v28
	s_nop 1
	v_addc_co_u32_e32 v49, vcc, 0, v29, vcc
	global_load_dword v62, v[48:49], off nt
	v_add_co_u32_e32 v48, vcc, 0x1a000, v28
	s_nop 1
	v_addc_co_u32_e32 v49, vcc, 0, v29, vcc
	global_load_dword v63, v[48:49], off nt
	v_add_co_u32_e32 v48, vcc, 0x1c000, v28
	s_nop 1
	v_addc_co_u32_e32 v49, vcc, 0, v29, vcc
	global_load_dword v64, v[48:49], off nt
	v_add_co_u32_e32 v48, vcc, 0x1e000, v28
	s_nop 1
	v_addc_co_u32_e32 v49, vcc, 0, v29, vcc
	global_load_dword v65, v[48:49], off nt
	v_add_co_u32_e32 v48, vcc, 0x20000, v28
	s_nop 1
	v_addc_co_u32_e32 v49, vcc, 0, v29, vcc
	global_load_dword v66, v[48:49], off nt
	v_add_co_u32_e32 v48, vcc, 0x22000, v28
	s_nop 1
	v_addc_co_u32_e32 v49, vcc, 0, v29, vcc
	global_load_dword v67, v[48:49], off nt
	v_add_co_u32_e32 v48, vcc, 0x24000, v28
	s_nop 1
	v_addc_co_u32_e32 v49, vcc, 0, v29, vcc
	global_load_dword v68, v[48:49], off nt
	v_add_co_u32_e32 v48, vcc, 0x26000, v28
	s_nop 1
	v_addc_co_u32_e32 v49, vcc, 0, v29, vcc
	global_load_dword v69, v[48:49], off nt
	v_add_co_u32_e32 v48, vcc, 0x28000, v28
	s_nop 1
	v_addc_co_u32_e32 v49, vcc, 0, v29, vcc
	global_load_dword v70, v[48:49], off nt
	v_add_co_u32_e32 v48, vcc, 0x2a000, v28
	s_nop 1
	v_addc_co_u32_e32 v49, vcc, 0, v29, vcc
	global_load_dword v71, v[48:49], off nt
	v_add_co_u32_e32 v48, vcc, 0x2c000, v28
	s_nop 1
	v_addc_co_u32_e32 v49, vcc, 0, v29, vcc
	global_load_dword v72, v[48:49], off nt
	v_add_co_u32_e32 v48, vcc, 0x2e000, v28
	s_nop 1
	v_addc_co_u32_e32 v49, vcc, 0, v29, vcc
	global_load_dword v73, v[48:49], off nt
	v_add_co_u32_e32 v48, vcc, 0x30000, v28
	s_nop 1
	v_addc_co_u32_e32 v49, vcc, 0, v29, vcc
	global_load_dword v74, v[48:49], off nt
	v_add_co_u32_e32 v48, vcc, 0x32000, v28
	s_nop 1
	v_addc_co_u32_e32 v49, vcc, 0, v29, vcc
	global_load_dword v75, v[48:49], off nt
	v_add_co_u32_e32 v48, vcc, 0x34000, v28
	s_nop 1
	v_addc_co_u32_e32 v49, vcc, 0, v29, vcc
	global_load_dword v76, v[48:49], off nt
	v_add_co_u32_e32 v48, vcc, 0x36000, v28
	s_nop 1
	v_addc_co_u32_e32 v49, vcc, 0, v29, vcc
	global_load_dword v77, v[48:49], off nt
	v_add_co_u32_e32 v48, vcc, 0x38000, v28
	s_nop 1
	v_addc_co_u32_e32 v49, vcc, 0, v29, vcc
	global_load_dword v78, v[48:49], off nt
	v_add_co_u32_e32 v48, vcc, 0x3a000, v28
	s_nop 1
	v_addc_co_u32_e32 v49, vcc, 0, v29, vcc
	global_load_dword v79, v[48:49], off nt
	v_add_co_u32_e32 v48, vcc, 0x3c000, v28
	s_nop 1
	v_addc_co_u32_e32 v49, vcc, 0, v29, vcc
	v_add_co_u32_e32 v28, vcc, 0x3e000, v28
	global_load_dword v48, v[48:49], off nt
	s_nop 0
	v_addc_co_u32_e32 v29, vcc, 0, v29, vcc
	global_load_dword v28, v[28:29], off nt
	s_waitcnt vmcnt(30)
	ds_write2_b32 v31, v50, v51 offset1:66
	s_waitcnt vmcnt(28)
	ds_write2_b32 v31, v52, v53 offset0:132 offset1:198
	s_waitcnt vmcnt(26)
	ds_write2_b32 v40, v54, v55 offset0:8 offset1:74
	s_waitcnt vmcnt(24)
	ds_write2_b32 v40, v56, v57 offset0:140 offset1:206
	s_waitcnt vmcnt(22)
	ds_write2_b32 v41, v58, v59 offset0:16 offset1:82
	s_waitcnt vmcnt(20)
	ds_write2_b32 v41, v60, v61 offset0:148 offset1:214
	s_waitcnt vmcnt(18)
	ds_write2_b32 v42, v62, v63 offset0:24 offset1:90
	s_waitcnt vmcnt(16)
	ds_write2_b32 v42, v64, v65 offset0:156 offset1:222
	s_waitcnt vmcnt(14)
	ds_write2_b32 v43, v66, v67 offset0:32 offset1:98
	s_waitcnt vmcnt(12)
	ds_write2_b32 v43, v68, v69 offset0:164 offset1:230
	s_waitcnt vmcnt(10)
	ds_write2_b32 v44, v70, v71 offset0:40 offset1:106
	s_waitcnt vmcnt(8)
; #define GAS __attribute__((address_space(1)))
; #define LAS __attribute__((address_space(3)))
; #define LDS_WAIT() asm volatile("s_waitcnt lgkmcnt(0)" ::: "memory")
; __device__ __forceinline__ unsigned pk2(float lo, float hi) { return f2bf(lo) | (f2bf(hi) << 16); }
; __device__ __forceinline__ void tr_item(const float* W, int ld, int K, int nblk, int item, bf16* WT, bool gu, LAS float* scr, int lane) {
;     ...
;       for (int i = 0; i < 32; ++i) scr[(2 * i + (lane >> 5)) * 33 + (lane & 31)] = t_[i]; }
;     LDS_WAIT(); asm volatile("" ::: "memory");
;     const int c = lane & 7;
; #pragma unroll
;     for (int j = 0; j < 4; ++j) { const int n = (lane >> 3) + 8 * j; const LAS float* s = scr + (8 * c) * 33 + n;
;         v4u o; o.x = pk2(s[0 * 33], s[1 * 33]); o.y = pk2(s[2 * 33], s[3 * 33]); o.z = pk2(s[4 * 33], s[5 * 33]); o.w = pk2(s[6 * 33], s[7 * 33]);
;         *(GAS v4u*)(WT + (size_t)(drow0 + n) * K + k0 + 8 * c) = o; }
;     LDS_WAIT(); asm volatile("" ::: "memory");
	ds_write2_b32 v44, v72, v73 offset0:172 offset1:238
	s_waitcnt vmcnt(6)
	ds_write2_b32 v45, v74, v75 offset0:48 offset1:114
	s_waitcnt vmcnt(4)
	ds_write2_b32 v45, v76, v77 offset0:180 offset1:246
	s_waitcnt vmcnt(2)
	ds_write2_b32 v46, v78, v79 offset0:56 offset1:122
	s_waitcnt vmcnt(0)
	ds_write2_b32 v46, v48, v28 offset0:188 offset1:254
	s_waitcnt lgkmcnt(0)
	ds_read2_b32 v[52:53], v36 offset0:33 offset1:41
	ds_read2_b32 v[54:55], v36 offset1:8
	ds_read2_b32 v[56:57], v36 offset0:66 offset1:74
	ds_read2_b32 v[58:59], v36 offset0:99 offset1:107
	ds_read2_b32 v[60:61], v36 offset0:132 offset1:140
	ds_read2_b32 v[62:63], v36 offset0:165 offset1:173
	ds_read2_b32 v[64:65], v36 offset0:198 offset1:206
	ds_read2_b32 v[66:67], v36 offset0:231 offset1:239
	s_waitcnt lgkmcnt(7)
	v_bfe_u32 v49, v52, 16, 1
	s_waitcnt lgkmcnt(6)
	v_bfe_u32 v48, v54, 16, 1
	v_add3_u32 v48, v54, v48, s15
	v_lshrrev_b32_e32 v48, 16, v48
	v_add3_u32 v49, v52, v49, s15
	v_and_or_b32 v48, v49, s16, v48
	s_waitcnt lgkmcnt(5)
	v_bfe_u32 v49, v56, 16, 1
	v_add3_u32 v49, v56, v49, s15
	s_waitcnt lgkmcnt(4)
	v_bfe_u32 v50, v58, 16, 1
	v_lshrrev_b32_e32 v49, 16, v49
	v_add3_u32 v50, v58, v50, s15
	v_and_or_b32 v49, v50, s16, v49
	s_waitcnt lgkmcnt(3)
	v_bfe_u32 v50, v60, 16, 1
	v_add3_u32 v50, v60, v50, s15
	s_waitcnt lgkmcnt(2)
	v_bfe_u32 v51, v62, 16, 1
	v_lshrrev_b32_e32 v50, 16, v50
	v_add3_u32 v51, v62, v51, s15
	v_and_or_b32 v50, v51, s16, v50
	s_waitcnt lgkmcnt(1)
	v_bfe_u32 v51, v64, 16, 1
	v_add_u32_e32 v68, s4, v35
	v_add3_u32 v51, v64, v51, s15
	s_waitcnt lgkmcnt(0)
	v_bfe_u32 v52, v66, 16, 1
	v_ashrrev_i32_e32 v69, 31, v68
	v_lshl_add_u64 v[28:29], v[24:25], 0, s[0:1]
	v_lshrrev_b32_e32 v51, 16, v51
	v_add3_u32 v52, v66, v52, s15
	v_lshlrev_b64 v[68:69], 11, v[68:69]
	v_and_or_b32 v51, v52, s16, v51
	v_lshl_add_u64 v[68:69], v[28:29], 0, v[68:69]
	global_store_dwordx4 v[68:69], v[48:51], off nt
	v_bfe_u32 v52, v67, 16, 1
	v_add3_u32 v52, v67, v52, s15
	v_bfe_u32 v48, v55, 16, 1
	v_add3_u32 v48, v55, v48, s15
	v_bfe_u32 v49, v53, 16, 1
	v_lshrrev_b32_e32 v48, 16, v48
	v_add3_u32 v49, v53, v49, s15
	v_and_or_b32 v48, v49, s16, v48
	v_bfe_u32 v49, v57, 16, 1
	v_add3_u32 v49, v57, v49, s15
	v_bfe_u32 v50, v59, 16, 1
	v_lshrrev_b32_e32 v49, 16, v49
	v_add3_u32 v50, v59, v50, s15
	v_and_or_b32 v49, v50, s16, v49
	v_bfe_u32 v50, v61, 16, 1
	v_add3_u32 v50, v61, v50, s15
	v_bfe_u32 v51, v63, 16, 1
	v_lshrrev_b32_e32 v50, 16, v50
	v_add3_u32 v51, v63, v51, s15
	v_and_or_b32 v50, v51, s16, v50
	v_bfe_u32 v51, v65, 16, 1
	v_add3_u32 v51, v65, v51, s15
	v_lshrrev_b32_e32 v51, 16, v51
	v_and_or_b32 v51, v52, s16, v51
	v_add_u32_e32 v52, s4, v37
	v_ashrrev_i32_e32 v53, 31, v52
	v_lshlrev_b64 v[52:53], 11, v[52:53]
	v_lshl_add_u64 v[52:53], v[28:29], 0, v[52:53]
	global_store_dwordx4 v[52:53], v[48:51], off nt
	ds_read2_b32 v[52:53], v36 offset0:49 offset1:57
	ds_read2_b32 v[54:55], v36 offset0:16 offset1:24
	ds_read2_b32 v[56:57], v36 offset0:82 offset1:90
	ds_read2_b32 v[58:59], v36 offset0:115 offset1:123
	ds_read2_b32 v[60:61], v36 offset0:148 offset1:156
	ds_read2_b32 v[62:63], v36 offset0:181 offset1:189
	ds_read2_b32 v[64:65], v36 offset0:214 offset1:222
	ds_read2_b32 v[66:67], v36 offset0:247 offset1:255
	s_waitcnt lgkmcnt(7)
	v_bfe_u32 v49, v52, 16, 1
	s_waitcnt lgkmcnt(6)
	v_bfe_u32 v48, v54, 16, 1
	v_add3_u32 v48, v54, v48, s15
	v_lshrrev_b32_e32 v48, 16, v48
	v_add3_u32 v49, v52, v49, s15
	v_and_or_b32 v48, v49, s16, v48
	s_waitcnt lgkmcnt(5)
	v_bfe_u32 v49, v56, 16, 1
	v_add3_u32 v49, v56, v49, s15
	s_waitcnt lgkmcnt(4)
	v_bfe_u32 v50, v58, 16, 1
	v_lshrrev_b32_e32 v49, 16, v49
	v_add3_u32 v50, v58, v50, s15
	v_and_or_b32 v49, v50, s16, v49
	s_waitcnt lgkmcnt(3)
	v_bfe_u32 v50, v60, 16, 1
	v_add3_u32 v50, v60, v50, s15
	s_waitcnt lgkmcnt(2)
	v_bfe_u32 v51, v62, 16, 1
	v_lshrrev_b32_e32 v50, 16, v50
	v_add3_u32 v51, v62, v51, s15
	v_and_or_b32 v50, v51, s16, v50
	s_waitcnt lgkmcnt(1)
	v_bfe_u32 v51, v64, 16, 1
	v_add_u32_e32 v68, s4, v38
	v_add3_u32 v51, v64, v51, s15
	s_waitcnt lgkmcnt(0)
	v_bfe_u32 v52, v66, 16, 1
	v_ashrrev_i32_e32 v69, 31, v68
	v_lshrrev_b32_e32 v51, 16, v51
	v_add3_u32 v52, v66, v52, s15
	v_lshlrev_b64 v[68:69], 11, v[68:69]
	v_and_or_b32 v51, v52, s16, v51
	v_lshl_add_u64 v[68:69], v[28:29], 0, v[68:69]
	global_store_dwordx4 v[68:69], v[48:51], off nt
	v_bfe_u32 v52, v67, 16, 1
	v_add3_u32 v52, v67, v52, s15
	v_bfe_u32 v48, v55, 16, 1
	v_add3_u32 v48, v55, v48, s15
	v_bfe_u32 v49, v53, 16, 1
	v_lshrrev_b32_e32 v48, 16, v48
	v_add3_u32 v49, v53, v49, s15
	v_and_or_b32 v48, v49, s16, v48
	v_bfe_u32 v49, v57, 16, 1
	v_add3_u32 v49, v57, v49, s15
	v_bfe_u32 v50, v59, 16, 1
	v_lshrrev_b32_e32 v49, 16, v49
	v_add3_u32 v50, v59, v50, s15
	v_and_or_b32 v49, v50, s16, v49
	v_bfe_u32 v50, v61, 16, 1
	v_add3_u32 v50, v61, v50, s15
	v_bfe_u32 v51, v63, 16, 1
	v_lshrrev_b32_e32 v50, 16, v50
	v_add3_u32 v51, v63, v51, s15
	v_and_or_b32 v50, v51, s16, v50
	v_bfe_u32 v51, v65, 16, 1
	v_add3_u32 v51, v65, v51, s15
	v_lshrrev_b32_e32 v51, 16, v51
	v_and_or_b32 v51, v52, s16, v51
	v_add_u32_e32 v52, s4, v39
	v_ashrrev_i32_e32 v53, 31, v52
	v_lshlrev_b64 v[52:53], 11, v[52:53]
	v_lshl_add_u64 v[28:29], v[28:29], 0, v[52:53]
	global_store_dwordx4 v[28:29], v[48:51], off nt
	s_waitcnt lgkmcnt(0)

; #define LAS __attribute__((address_space(3)))
; __device__ __forceinline__ void tr_item(const float* W, int ld, int K, int nblk, int item, bf16* WT, bool gu, LAS float* scr, int lane) {
;     const int kb = item / nblk, nb = item % nblk, k0 = 64 * kb, n0 = 32 * nb;
;     int drow0 = n0;
;     if (gu) { const int bj = n0 / FF, j = n0 - bj * FF; drow0 = 256 * (j / 128) + 128 * bj + (j % 128); }
;     { float t_[32];
; #pragma unroll
;       for (int i = 0; i < 32; ++i) t_[i] = W[(size_t)(k0 + 2 * i + (lane >> 5)) * ld + n0 + (lane & 31)];
; #pragma unroll
;       for (int i = 0; i < 32; ++i) scr[(2 * i + (lane >> 5)) * 33 + (lane & 31)] = t_[i]; }
; __device__ __forceinline__ void convert_items(Frame& F, const Args& a, int lo, int hi, int w, int nw) {
;     ...
;         if (r < I_FI) { tr_item(a.in[7], 3 * D + 16, D, 96, r, (bf16*)(F.ws + WS_WFOXIN), false, scr, lane); continue; } r -= I_FI;
.LBB0_1322:
	s_andn2_b64 vcc, exec, s[4:5]
	s_cbranch_vccnz .LBB0_1295
	s_mul_hi_i32 s0, s8, 0x2aaaaaab
	s_lshr_b32 s4, s0, 31
	s_ashr_i32 s0, s0, 4
	s_add_i32 s0, s0, s4
	s_lshl_b32 s6, s0, 6
	s_mulk_i32 s0, 0xf400
	s_add_i32 s4, s9, s0
	s_ashr_i32 s5, s4, 31
	v_add_u32_e32 v50, s6, v30
	v_lshl_add_u64 v[28:29], s[4:5], 2, v[14:15]
	v_mad_i64_i32 v[48:49], s[40:41], v50, s30, v[28:29]
	global_load_dword v51, v[48:49], off nt
	v_add_u32_e32 v48, 2, v50
	v_mad_i64_i32 v[48:49], s[40:41], v48, s30, v[28:29]
	global_load_dword v52, v[48:49], off nt
	v_add_u32_e32 v48, 4, v50
	v_mad_i64_i32 v[48:49], s[40:41], v48, s30, v[28:29]
	global_load_dword v53, v[48:49], off nt
	v_add_u32_e32 v48, 6, v50
	v_mad_i64_i32 v[48:49], s[40:41], v48, s30, v[28:29]
	global_load_dword v54, v[48:49], off nt
	v_add_u32_e32 v48, 8, v50
	v_mad_i64_i32 v[48:49], s[40:41], v48, s30, v[28:29]
	global_load_dword v55, v[48:49], off nt
	v_add_u32_e32 v48, 10, v50
	v_mad_i64_i32 v[48:49], s[40:41], v48, s30, v[28:29]
	global_load_dword v56, v[48:49], off nt
	v_add_u32_e32 v48, 12, v50
	v_mad_i64_i32 v[48:49], s[40:41], v48, s30, v[28:29]
	global_load_dword v57, v[48:49], off nt
	v_add_u32_e32 v48, 14, v50
	v_mad_i64_i32 v[48:49], s[40:41], v48, s30, v[28:29]
	global_load_dword v58, v[48:49], off nt
	v_add_u32_e32 v48, 16, v50
	v_mad_i64_i32 v[48:49], s[40:41], v48, s30, v[28:29]
	global_load_dword v59, v[48:49], off nt
	v_add_u32_e32 v48, 18, v50
	v_mad_i64_i32 v[48:49], s[40:41], v48, s30, v[28:29]
	global_load_dword v60, v[48:49], off nt
	v_add_u32_e32 v48, 20, v50
	v_mad_i64_i32 v[48:49], s[40:41], v48, s30, v[28:29]
	global_load_dword v61, v[48:49], off nt
	v_add_u32_e32 v48, 22, v50
	v_mad_i64_i32 v[48:49], s[40:41], v48, s30, v[28:29]
	global_load_dword v62, v[48:49], off nt
	v_add_u32_e32 v48, 24, v50
	v_mad_i64_i32 v[48:49], s[40:41], v48, s30, v[28:29]
	global_load_dword v63, v[48:49], off nt
	v_add_u32_e32 v48, 26, v50
	v_mad_i64_i32 v[48:49], s[40:41], v48, s30, v[28:29]
	global_load_dword v64, v[48:49], off nt
	v_add_u32_e32 v48, 28, v50
	v_mad_i64_i32 v[48:49], s[40:41], v48, s30, v[28:29]
	global_load_dword v65, v[48:49], off nt
	v_add_u32_e32 v48, 30, v50
	v_mad_i64_i32 v[48:49], s[40:41], v48, s30, v[28:29]
	global_load_dword v66, v[48:49], off nt
	v_add_u32_e32 v48, 32, v50
	v_mad_i64_i32 v[48:49], s[40:41], v48, s30, v[28:29]
	global_load_dword v67, v[48:49], off nt
	v_add_u32_e32 v48, 34, v50
	v_mad_i64_i32 v[48:49], s[40:41], v48, s30, v[28:29]
	global_load_dword v68, v[48:49], off nt
	v_add_u32_e32 v48, 36, v50
	v_mad_i64_i32 v[48:49], s[40:41], v48, s30, v[28:29]
	global_load_dword v69, v[48:49], off nt
	v_add_u32_e32 v48, 38, v50
	v_mad_i64_i32 v[48:49], s[40:41], v48, s30, v[28:29]
	global_load_dword v70, v[48:49], off nt
	v_add_u32_e32 v48, 40, v50
	v_mad_i64_i32 v[48:49], s[40:41], v48, s30, v[28:29]
	global_load_dword v71, v[48:49], off nt
	v_add_u32_e32 v48, 42, v50
	v_mad_i64_i32 v[48:49], s[40:41], v48, s30, v[28:29]
	global_load_dword v72, v[48:49], off nt
	v_add_u32_e32 v48, 44, v50
	v_mad_i64_i32 v[48:49], s[40:41], v48, s30, v[28:29]
	global_load_dword v73, v[48:49], off nt
	v_add_u32_e32 v48, 46, v50
	v_mad_i64_i32 v[48:49], s[40:41], v48, s30, v[28:29]
	global_load_dword v74, v[48:49], off nt
	v_add_u32_e32 v48, 48, v50
	v_mad_i64_i32 v[48:49], s[40:41], v48, s30, v[28:29]
	global_load_dword v75, v[48:49], off nt
	v_add_u32_e32 v48, 50, v50
	v_mad_i64_i32 v[48:49], s[40:41], v48, s30, v[28:29]
	global_load_dword v76, v[48:49], off nt
	v_add_u32_e32 v48, 52, v50
	v_mad_i64_i32 v[48:49], s[40:41], v48, s30, v[28:29]
	global_load_dword v77, v[48:49], off nt
	v_add_u32_e32 v48, 54, v50
	v_mad_i64_i32 v[48:49], s[40:41], v48, s30, v[28:29]
	global_load_dword v78, v[48:49], off nt
	v_add_u32_e32 v48, 56, v50
	v_mad_i64_i32 v[48:49], s[40:41], v48, s30, v[28:29]
	global_load_dword v79, v[48:49], off nt
	v_add_u32_e32 v48, 58, v50
	v_mad_i64_i32 v[48:49], s[40:41], v48, s30, v[28:29]
	global_load_dword v80, v[48:49], off nt
	v_add_u32_e32 v48, 60, v50
	v_mad_i64_i32 v[48:49], s[40:41], v48, s30, v[28:29]
	global_load_dword v48, v[48:49], off nt
	v_add_u32_e32 v49, 62, v50
	v_mad_i64_i32 v[28:29], s[40:41], v49, s30, v[28:29]
	global_load_dword v28, v[28:29], off nt
	s_waitcnt vmcnt(30)
	ds_write2_b32 v31, v51, v52 offset1:66
	s_waitcnt vmcnt(28)
	ds_write2_b32 v31, v53, v54 offset0:132 offset1:198
	s_waitcnt vmcnt(26)
	ds_write2_b32 v40, v55, v56 offset0:8 offset1:74
	s_waitcnt vmcnt(24)
	ds_write2_b32 v40, v57, v58 offset0:140 offset1:206
	s_waitcnt vmcnt(22)
	ds_write2_b32 v41, v59, v60 offset0:16 offset1:82
	s_waitcnt vmcnt(20)
	ds_write2_b32 v41, v61, v62 offset0:148 offset1:214
	s_waitcnt vmcnt(18)
	ds_write2_b32 v42, v63, v64 offset0:24 offset1:90
	s_waitcnt vmcnt(16)
	ds_write2_b32 v42, v65, v66 offset0:156 offset1:222
	s_waitcnt vmcnt(14)
	ds_write2_b32 v43, v67, v68 offset0:32 offset1:98
	s_waitcnt vmcnt(12)
	ds_write2_b32 v43, v69, v70 offset0:164 offset1:230
	s_waitcnt vmcnt(10)
	ds_write2_b32 v44, v71, v72 offset0:40 offset1:106
	s_waitcnt vmcnt(8)
	ds_write2_b32 v44, v73, v74 offset0:172 offset1:238
	s_waitcnt vmcnt(6)
	ds_write2_b32 v45, v75, v76 offset0:48 offset1:114
	s_waitcnt vmcnt(4)
; #define GAS __attribute__((address_space(1)))
; #define LAS __attribute__((address_space(3)))
; #define LDS_WAIT() asm volatile("s_waitcnt lgkmcnt(0)" ::: "memory")
; __device__ __forceinline__ unsigned pk2(float lo, float hi) { return f2bf(lo) | (f2bf(hi) << 16); }
; __device__ __forceinline__ void tr_item(const float* W, int ld, int K, int nblk, int item, bf16* WT, bool gu, LAS float* scr, int lane) {
;     ...
;       for (int i = 0; i < 32; ++i) scr[(2 * i + (lane >> 5)) * 33 + (lane & 31)] = t_[i]; }
;     LDS_WAIT(); asm volatile("" ::: "memory");
;     const int c = lane & 7;
; #pragma unroll
;     for (int j = 0; j < 4; ++j) { const int n = (lane >> 3) + 8 * j; const LAS float* s = scr + (8 * c) * 33 + n;
;         v4u o; o.x = pk2(s[0 * 33], s[1 * 33]); o.y = pk2(s[2 * 33], s[3 * 33]); o.z = pk2(s[4 * 33], s[5 * 33]); o.w = pk2(s[6 * 33], s[7 * 33]);
;         *(GAS v4u*)(WT + (size_t)(drow0 + n) * K + k0 + 8 * c) = o; }
;     LDS_WAIT(); asm volatile("" ::: "memory");
	ds_write2_b32 v45, v77, v78 offset0:180 offset1:246
	s_waitcnt vmcnt(2)
	ds_write2_b32 v46, v79, v80 offset0:56 offset1:122
	s_waitcnt vmcnt(0)
	ds_write2_b32 v46, v48, v28 offset0:188 offset1:254
	s_waitcnt lgkmcnt(0)
	ds_read2_b32 v[52:53], v36 offset0:33 offset1:41
	ds_read2_b32 v[54:55], v36 offset1:8
	ds_read2_b32 v[56:57], v36 offset0:66 offset1:74
	ds_read2_b32 v[58:59], v36 offset0:99 offset1:107
	ds_read2_b32 v[60:61], v36 offset0:132 offset1:140
	ds_read2_b32 v[62:63], v36 offset0:165 offset1:173
	ds_read2_b32 v[64:65], v36 offset0:198 offset1:206
	ds_read2_b32 v[66:67], v36 offset0:231 offset1:239
	s_waitcnt lgkmcnt(7)
	v_bfe_u32 v49, v52, 16, 1
	s_waitcnt lgkmcnt(6)
	v_bfe_u32 v48, v54, 16, 1
	v_add3_u32 v48, v54, v48, s15
	v_lshrrev_b32_e32 v48, 16, v48
	v_add3_u32 v49, v52, v49, s15
	v_and_or_b32 v48, v49, s16, v48
	s_waitcnt lgkmcnt(5)
	v_bfe_u32 v49, v56, 16, 1
	v_add3_u32 v49, v56, v49, s15
	s_waitcnt lgkmcnt(4)
	v_bfe_u32 v50, v58, 16, 1
	v_lshrrev_b32_e32 v49, 16, v49
	v_add3_u32 v50, v58, v50, s15
	v_and_or_b32 v49, v50, s16, v49
	s_waitcnt lgkmcnt(3)
	v_bfe_u32 v50, v60, 16, 1
	v_add3_u32 v50, v60, v50, s15
	s_waitcnt lgkmcnt(2)
	v_bfe_u32 v51, v62, 16, 1
	v_lshrrev_b32_e32 v50, 16, v50
	v_add3_u32 v51, v62, v51, s15
	v_and_or_b32 v50, v51, s16, v50
	s_waitcnt lgkmcnt(1)
	v_bfe_u32 v51, v64, 16, 1
	v_add_u32_e32 v68, s4, v35
	s_ashr_i32 s7, s6, 31
	v_add3_u32 v51, v64, v51, s15
	s_waitcnt lgkmcnt(0)
	v_bfe_u32 v52, v66, 16, 1
	v_ashrrev_i32_e32 v69, 31, v68
	v_lshl_add_u64 v[28:29], s[6:7], 1, v[26:27]
	v_lshrrev_b32_e32 v51, 16, v51
	v_add3_u32 v52, v66, v52, s15
	v_lshlrev_b64 v[70:71], 11, v[68:69]
	v_and_or_b32 v51, v52, s16, v51
	v_lshl_add_u64 v[70:71], v[28:29], 0, v[70:71]
	global_store_dwordx4 v[70:71], v[48:51], off nt
	v_bfe_u32 v52, v67, 16, 1
	v_add3_u32 v52, v67, v52, s15
	v_bfe_u32 v48, v55, 16, 1
	v_add3_u32 v48, v55, v48, s15
	v_bfe_u32 v49, v53, 16, 1
	v_lshrrev_b32_e32 v48, 16, v48
	v_add3_u32 v49, v53, v49, s15
	v_and_or_b32 v48, v49, s16, v48
	v_bfe_u32 v49, v57, 16, 1
	v_add3_u32 v49, v57, v49, s15
	v_bfe_u32 v50, v59, 16, 1
	v_lshrrev_b32_e32 v49, 16, v49
	v_add3_u32 v50, v59, v50, s15
	v_and_or_b32 v49, v50, s16, v49
	v_bfe_u32 v50, v61, 16, 1
	v_add3_u32 v50, v61, v50, s15
	v_bfe_u32 v51, v63, 16, 1
	v_lshrrev_b32_e32 v50, 16, v50
	v_add3_u32 v51, v63, v51, s15
	v_and_or_b32 v50, v51, s16, v50
	v_bfe_u32 v51, v65, 16, 1
	v_add3_u32 v51, v65, v51, s15
	v_lshrrev_b32_e32 v51, 16, v51
	v_and_or_b32 v51, v52, s16, v51
	v_add_u32_e32 v52, 8, v68
	v_ashrrev_i32_e32 v53, 31, v52
	v_lshlrev_b64 v[52:53], 11, v[52:53]
	v_lshl_add_u64 v[52:53], v[28:29], 0, v[52:53]
	global_store_dwordx4 v[52:53], v[48:51], off nt
	ds_read2_b32 v[52:53], v36 offset0:49 offset1:57
	ds_read2_b32 v[54:55], v36 offset0:16 offset1:24
	ds_read2_b32 v[56:57], v36 offset0:82 offset1:90
	ds_read2_b32 v[58:59], v36 offset0:115 offset1:123
	ds_read2_b32 v[60:61], v36 offset0:148 offset1:156
	ds_read2_b32 v[62:63], v36 offset0:181 offset1:189
	ds_read2_b32 v[64:65], v36 offset0:214 offset1:222
	ds_read2_b32 v[66:67], v36 offset0:247 offset1:255
	s_waitcnt lgkmcnt(7)
	v_bfe_u32 v49, v52, 16, 1
	s_waitcnt lgkmcnt(6)
	v_bfe_u32 v48, v54, 16, 1
	v_add3_u32 v48, v54, v48, s15
	v_lshrrev_b32_e32 v48, 16, v48
	v_add3_u32 v49, v52, v49, s15
	v_and_or_b32 v48, v49, s16, v48
	s_waitcnt lgkmcnt(5)
	v_bfe_u32 v49, v56, 16, 1
	v_add3_u32 v49, v56, v49, s15
	s_waitcnt lgkmcnt(4)
	v_bfe_u32 v50, v58, 16, 1
	v_lshrrev_b32_e32 v49, 16, v49
	v_add3_u32 v50, v58, v50, s15
	v_and_or_b32 v49, v50, s16, v49
	s_waitcnt lgkmcnt(3)
	v_bfe_u32 v50, v60, 16, 1
	v_add3_u32 v50, v60, v50, s15
	s_waitcnt lgkmcnt(2)
	v_bfe_u32 v51, v62, 16, 1
	v_lshrrev_b32_e32 v50, 16, v50
	v_add3_u32 v51, v62, v51, s15
	v_and_or_b32 v50, v51, s16, v50
	s_waitcnt lgkmcnt(1)
	v_bfe_u32 v51, v64, 16, 1
	v_add_u32_e32 v70, 16, v68
	v_add3_u32 v51, v64, v51, s15
	s_waitcnt lgkmcnt(0)
	v_bfe_u32 v52, v66, 16, 1
	v_ashrrev_i32_e32 v71, 31, v70
	v_lshrrev_b32_e32 v51, 16, v51
	v_add3_u32 v52, v66, v52, s15
	v_lshlrev_b64 v[70:71], 11, v[70:71]
	v_and_or_b32 v51, v52, s16, v51
	v_lshl_add_u64 v[70:71], v[28:29], 0, v[70:71]
	global_store_dwordx4 v[70:71], v[48:51], off nt
	v_bfe_u32 v52, v67, 16, 1
	v_add3_u32 v52, v67, v52, s15
	v_bfe_u32 v48, v55, 16, 1
	v_add3_u32 v48, v55, v48, s15
	v_bfe_u32 v49, v53, 16, 1
	v_lshrrev_b32_e32 v48, 16, v48
	v_add3_u32 v49, v53, v49, s15
	v_and_or_b32 v48, v49, s16, v48
	v_bfe_u32 v49, v57, 16, 1
	v_add3_u32 v49, v57, v49, s15
	v_bfe_u32 v50, v59, 16, 1
	v_lshrrev_b32_e32 v49, 16, v49
	v_add3_u32 v50, v59, v50, s15
	v_and_or_b32 v49, v50, s16, v49
	v_bfe_u32 v50, v61, 16, 1
	v_add3_u32 v50, v61, v50, s15
	v_bfe_u32 v51, v63, 16, 1
	v_lshrrev_b32_e32 v50, 16, v50
	v_add3_u32 v51, v63, v51, s15
	v_and_or_b32 v50, v51, s16, v50
	v_bfe_u32 v51, v65, 16, 1
	v_add3_u32 v51, v65, v51, s15
	v_lshrrev_b32_e32 v51, 16, v51
	v_and_or_b32 v51, v52, s16, v51
	v_add_u32_e32 v52, 24, v68
	v_ashrrev_i32_e32 v53, 31, v52
	v_lshlrev_b64 v[52:53], 11, v[52:53]
	v_lshl_add_u64 v[28:29], v[28:29], 0, v[52:53]
	global_store_dwordx4 v[28:29], v[48:51], off nt
	s_waitcnt lgkmcnt(0)
	s_branch .LBB0_1295

; #define LAS __attribute__((address_space(3)))
; __device__ __forceinline__ void tr_item8(const float* W, int ld, int K, int nblk, int item, unsigned char* WT, bool gu, float scale, LAS float* scr, int lane) {
;     const int kb = item / nblk, nb = item % nblk, k0 = 64 * kb, n0 = 32 * nb;
;     int drow0 = n0;
;     if (gu) { const int bj = n0 / FF, j = n0 - bj * FF; drow0 = 256 * (j / 128) + 128 * bj + (j % 128); }
;     { float t_[32];
; #pragma unroll
;       for (int i = 0; i < 32; ++i) t_[i] = W[(size_t)(k0 + 2 * i + (lane >> 5)) * ld + n0 + (lane & 31)];
; __device__ __forceinline__ void convert_items(Frame& F, const Args& a, int lo, int hi, int w, int nw) {
;     ...
;     for (int it = lo + w; it < hi; it += nw) {
;         int r = it;
;         if (r < I_FI) { tr_item(a.in[7], 3 * D + 16, D, 96, r, (bf16*)(F.ws + WS_WFOXIN), false, scr, lane); continue; } r -= I_FI;
;         if (r < I_FO) { tr_item(a.in[9], D, D, 32, r, (bf16*)(F.ws + WS_WFOXOUT), false, scr, lane); continue; } r -= I_FO;
;         if (r < I_SI) { tr_item(a.in[10], D + 512, D, 48, r, (bf16*)(F.ws + WS_WSWAIN), false, scr, lane); continue; } r -= I_SI;
;         if (r < I_SO) { tr_item(a.in[12], D, D, 32, r, (bf16*)(F.ws + WS_WSWAOUT), false, scr, lane); continue; } r -= I_SO;
;         if (r < I_GU) { tr_item8(a.in[14], 2 * FF, D, 224, r, F.ws + WS_WGU, true, WSC_GU, scr, lane); continue; } r -= I_GU;
;         if (r < I_DN) { tr_item8(a.in[15], D, FF, 32, r, F.ws + WS_WDN, false, WSC_DN, scr, lane); continue; } r -= I_DN;
;         if (r < NE * I_GU) { const int e = r / I_GU, rr = r % I_GU; tr_item8(a.in[18] + (size_t)e * D * 2 * FF, 2 * FF, D, 224, rr, F.ws + WS_WMGU + (size_t)e * 2 * FF * D, true, WSC_GU, scr, lane); continue; } r -= NE * I_GU;
;         { const int e = r / I_DN, rr = r % I_DN; tr_item8(a.in[19] + (size_t)e * FF * D, D, FF, 32, rr, F.ws + WS_WMDN + (size_t)e * D * FF, false, WSC_DN, scr, lane); }
.LBB0_1330:
	s_cmpk_gt_i32 s8, 0x5ff
	s_mov_b64 s[4:5], -1
	s_cbranch_scc0 .LBB0_1356
	s_cmpk_gt_u32 s8, 0x7ff
	s_cbranch_scc0 .LBB0_1353
	s_cmpk_gt_u32 s8, 0xaff
	s_cbranch_scc0 .LBB0_1350
	s_cmpk_gt_u32 s8, 0xcff
	s_cbranch_scc0 .LBB0_1347
	s_cmpk_gt_u32 s8, 0x1aff
	s_cbranch_scc0 .LBB0_1344
	s_cmpk_gt_u32 s8, 0x21ff
	s_cbranch_scc0 .LBB0_1341
	s_cmpk_gt_u32 s8, 0x91ff
	s_cbranch_scc0 .LBB0_1338
	s_add_i32 s0, s8, 0x6e00
	s_bfe_u32 s4, s0, 0x80008
	s_mulk_i32 s4, 0x2493
	s_lshr_b32 s4, s4, 16
	s_mul_i32 s5, s4, 0x700
	v_readlane_b32 s40, v254, 28
	s_sub_i32 s6, s0, s5
	s_mul_i32 s0, s4, 0xe00000
	v_readlane_b32 s46, v254, 34
	v_readlane_b32 s47, v254, 35
	s_add_u32 s7, s46, s0
	s_addc_u32 s31, s47, 0
	s_mul_i32 s4, s4, 0x380000
	s_add_u32 s4, s66, s4
	s_addc_u32 s5, s58, 0
	s_lshl_b32 s0, s6, 5
	s_and_b32 s0, s0, 0x3e0
	s_lshl_b32 s6, s6, 1
	s_and_b32 s6, s6, 0xfc0
	s_lshl_b32 s40, s0, 2
	v_readlane_b32 s41, v254, 29
	v_add_u32_e32 v28, s6, v30
	s_add_u32 s40, s7, s40
	s_addc_u32 s41, s31, 0
	v_ashrrev_i32_e32 v29, 31, v28
	v_lshl_add_u64 v[48:49], s[40:41], 0, v[0:1]
	v_lshlrev_b64 v[28:29], 12, v[28:29]
	v_lshl_add_u64 v[28:29], v[48:49], 0, v[28:29]
	s_movk_i32 s7, 0x2000
	v_add_co_u32_e32 v48, vcc, s7, v28
	s_movk_i32 s7, 0x4000
	s_nop 0
	v_addc_co_u32_e32 v49, vcc, 0, v29, vcc
	global_load_dword v50, v[28:29], off nt
	global_load_dword v51, v[48:49], off nt
	v_add_co_u32_e32 v48, vcc, s7, v28
	s_movk_i32 s7, 0x6000
	s_nop 0
	v_addc_co_u32_e32 v49, vcc, 0, v29, vcc
	global_load_dword v52, v[48:49], off nt
	v_add_co_u32_e32 v48, vcc, s7, v28
	s_mov_b32 s7, 0x8000
	s_nop 0
	v_addc_co_u32_e32 v49, vcc, 0, v29, vcc
	global_load_dword v53, v[48:49], off nt
	v_add_co_u32_e32 v48, vcc, s7, v28
	s_mov_b32 s7, 0xa000
	s_nop 0
	v_addc_co_u32_e32 v49, vcc, 0, v29, vcc
	global_load_dword v54, v[48:49], off nt
	v_add_co_u32_e32 v48, vcc, s7, v28
	s_mov_b32 s7, 0xc000
	s_nop 0
	v_addc_co_u32_e32 v49, vcc, 0, v29, vcc
	global_load_dword v55, v[48:49], off nt
	v_add_co_u32_e32 v48, vcc, s7, v28
	s_mov_b32 s7, 0xe000
	s_nop 0
	v_addc_co_u32_e32 v49, vcc, 0, v29, vcc
	global_load_dword v56, v[48:49], off nt
	v_add_co_u32_e32 v48, vcc, s7, v28
	s_mov_b32 s7, 0x10000
	s_nop 0
	v_addc_co_u32_e32 v49, vcc, 0, v29, vcc
	global_load_dword v57, v[48:49], off nt
	v_add_co_u32_e32 v48, vcc, s7, v28
	s_mov_b32 s7, 0x12000
	s_nop 0
	v_addc_co_u32_e32 v49, vcc, 0, v29, vcc
	global_load_dword v58, v[48:49], off nt
	v_add_co_u32_e32 v48, vcc, s7, v28
	s_mov_b32 s7, 0x14000
	s_nop 0
	v_addc_co_u32_e32 v49, vcc, 0, v29, vcc
	global_load_dword v59, v[48:49], off nt
	v_add_co_u32_e32 v48, vcc, s7, v28
	s_mov_b32 s7, 0x16000
	s_nop 0
	v_addc_co_u32_e32 v49, vcc, 0, v29, vcc
	global_load_dword v60, v[48:49], off nt
	v_add_co_u32_e32 v48, vcc, s7, v28
	s_mov_b32 s7, 0x18000
	s_nop 0
	v_addc_co_u32_e32 v49, vcc, 0, v29, vcc
	global_load_dword v61, v[48:49], off nt
	v_add_co_u32_e32 v48, vcc, s7, v28
	s_mov_b32 s7, 0x1a000
	s_nop 0
	v_addc_co_u32_e32 v49, vcc, 0, v29, vcc
	global_load_dword v62, v[48:49], off nt
	v_add_co_u32_e32 v48, vcc, s7, v28
	s_mov_b32 s7, 0x1c000
	s_nop 0
	v_addc_co_u32_e32 v49, vcc, 0, v29, vcc
	global_load_dword v63, v[48:49], off nt
	v_add_co_u32_e32 v48, vcc, s7, v28
	s_mov_b32 s7, 0x1e000
	s_nop 0
	v_addc_co_u32_e32 v49, vcc, 0, v29, vcc
	global_load_dword v64, v[48:49], off nt
	v_add_co_u32_e32 v48, vcc, s7, v28
	s_mov_b32 s7, 0x20000
	s_nop 0
	v_addc_co_u32_e32 v49, vcc, 0, v29, vcc
	global_load_dword v65, v[48:49], off nt
	v_add_co_u32_e32 v48, vcc, s7, v28
	s_mov_b32 s7, 0x22000
	s_nop 0
	v_addc_co_u32_e32 v49, vcc, 0, v29, vcc
	global_load_dword v66, v[48:49], off nt
	v_add_co_u32_e32 v48, vcc, s7, v28
	s_mov_b32 s7, 0x24000
	s_nop 0
	v_addc_co_u32_e32 v49, vcc, 0, v29, vcc
	global_load_dword v67, v[48:49], off nt
	v_add_co_u32_e32 v48, vcc, s7, v28
	s_mov_b32 s7, 0x26000
	s_nop 0
	v_addc_co_u32_e32 v49, vcc, 0, v29, vcc
	global_load_dword v68, v[48:49], off nt
	v_add_co_u32_e32 v48, vcc, s7, v28
	s_mov_b32 s7, 0x28000
	s_nop 0
	v_addc_co_u32_e32 v49, vcc, 0, v29, vcc
	global_load_dword v69, v[48:49], off nt
	v_add_co_u32_e32 v48, vcc, s7, v28
	s_mov_b32 s7, 0x2a000
	s_nop 0
	v_addc_co_u32_e32 v49, vcc, 0, v29, vcc
	global_load_dword v70, v[48:49], off nt
	v_add_co_u32_e32 v48, vcc, s7, v28
	s_mov_b32 s7, 0x2c000
	s_nop 0
	v_addc_co_u32_e32 v49, vcc, 0, v29, vcc
	global_load_dword v71, v[48:49], off nt
	v_add_co_u32_e32 v48, vcc, s7, v28
	s_mov_b32 s7, 0x2e000
	s_nop 0
	v_addc_co_u32_e32 v49, vcc, 0, v29, vcc
	global_load_dword v72, v[48:49], off nt
	v_add_co_u32_e32 v48, vcc, s7, v28
	s_mov_b32 s7, 0x30000
	s_nop 0
	v_addc_co_u32_e32 v49, vcc, 0, v29, vcc
	global_load_dword v73, v[48:49], off nt
	v_add_co_u32_e32 v48, vcc, s7, v28
	s_mov_b32 s7, 0x32000
	s_nop 0
	v_addc_co_u32_e32 v49, vcc, 0, v29, vcc
	global_load_dword v74, v[48:49], off nt
	v_add_co_u32_e32 v48, vcc, s7, v28
	s_mov_b32 s7, 0x34000
	s_nop 0
	v_addc_co_u32_e32 v49, vcc, 0, v29, vcc
	global_load_dword v75, v[48:49], off nt
	v_add_co_u32_e32 v48, vcc, s7, v28
	s_mov_b32 s7, 0x36000
	s_nop 0
	v_addc_co_u32_e32 v49, vcc, 0, v29, vcc
	global_load_dword v76, v[48:49], off nt
	v_add_co_u32_e32 v48, vcc, s7, v28
	s_mov_b32 s7, 0x38000
	s_nop 0
	v_addc_co_u32_e32 v49, vcc, 0, v29, vcc
	global_load_dword v77, v[48:49], off nt
	v_add_co_u32_e32 v48, vcc, s7, v28
	s_mov_b32 s7, 0x3a000
	s_nop 0
	v_addc_co_u32_e32 v49, vcc, 0, v29, vcc
	global_load_dword v78, v[48:49], off nt
	v_add_co_u32_e32 v48, vcc, s7, v28
	s_mov_b32 s7, 0x3c000
	s_nop 0
	v_addc_co_u32_e32 v49, vcc, 0, v29, vcc
	global_load_dword v79, v[48:49], off nt
	v_add_co_u32_e32 v48, vcc, s7, v28
	s_mov_b32 s7, 0x3e000
	s_nop 0
	v_addc_co_u32_e32 v49, vcc, 0, v29, vcc
	v_add_co_u32_e32 v28, vcc, s7, v28
	global_load_dword v48, v[48:49], off nt
	s_nop 0
	v_addc_co_u32_e32 v29, vcc, 0, v29, vcc
	global_load_dword v28, v[28:29], off nt
	s_waitcnt vmcnt(0)
; __device__ __forceinline__ unsigned cvt_pk4_fp8(float a, float b, float c, float d) { int w = 0; w = __builtin_amdgcn_cvt_pk_fp8_f32(a, b, w, false); w = __builtin_amdgcn_cvt_pk_fp8_f32(c, d, w, true); return (unsigned)w; }
; #define GAS __attribute__((address_space(1)))
; #define LAS __attribute__((address_space(3)))
; #define LDS_WAIT() asm volatile("s_waitcnt lgkmcnt(0)" ::: "memory")
; __device__ __forceinline__ void tr_item8(const float* W, int ld, int K, int nblk, int item, unsigned char* WT, bool gu, float scale, LAS float* scr, int lane) {
;     ...
; #pragma unroll
;       for (int i = 0; i < 32; ++i) scr[(2 * i + (lane >> 5)) * 33 + (lane & 31)] = t_[i] * scale; }
;     LDS_WAIT(); asm volatile("" ::: "memory");
;     const int c = lane & 3;
; #pragma unroll
;     for (int j = 0; j < 2; ++j) { const int n = (lane >> 2) + 16 * j; const LAS float* sp = scr + (16 * c) * 33 + n;
;         v4u o; o.x = pg8::cvt_pk4_fp8(sp[0 * 33], sp[1 * 33], sp[2 * 33], sp[3 * 33]); o.y = pg8::cvt_pk4_fp8(sp[4 * 33], sp[5 * 33], sp[6 * 33], sp[7 * 33]);
;         o.z = pg8::cvt_pk4_fp8(sp[8 * 33], sp[9 * 33], sp[10 * 33], sp[11 * 33]); o.w = pg8::cvt_pk4_fp8(sp[12 * 33], sp[13 * 33], sp[14 * 33], sp[15 * 33]);
;         *(GAS v4u*)(WT + (size_t)(drow0 + n) * K + k0 + 16 * c) = o; }
;     LDS_WAIT(); asm volatile("" ::: "memory");
	v_mul_f32_e32 v29, 0x43000000, v50
	v_mul_f32_e32 v49, 0x43000000, v51
	ds_write2_b32 v31, v29, v49 offset1:66
	v_mul_f32_e32 v29, 0x43000000, v52
	v_mul_f32_e32 v49, 0x43000000, v53
	ds_write2_b32 v31, v29, v49 offset0:132 offset1:198
	v_mul_f32_e32 v29, 0x43000000, v54
	v_mul_f32_e32 v49, 0x43000000, v55
	ds_write2_b32 v40, v29, v49 offset0:8 offset1:74
	v_mul_f32_e32 v29, 0x43000000, v56
	v_mul_f32_e32 v49, 0x43000000, v57
	ds_write2_b32 v40, v29, v49 offset0:140 offset1:206
	v_mul_f32_e32 v29, 0x43000000, v58
	v_mul_f32_e32 v49, 0x43000000, v59
	ds_write2_b32 v41, v29, v49 offset0:16 offset1:82
	v_mul_f32_e32 v29, 0x43000000, v60
	v_mul_f32_e32 v49, 0x43000000, v61
	ds_write2_b32 v41, v29, v49 offset0:148 offset1:214
	v_mul_f32_e32 v29, 0x43000000, v62
	v_mul_f32_e32 v49, 0x43000000, v63
	ds_write2_b32 v42, v29, v49 offset0:24 offset1:90
	v_mul_f32_e32 v29, 0x43000000, v64
	v_mul_f32_e32 v49, 0x43000000, v65
	ds_write2_b32 v42, v29, v49 offset0:156 offset1:222
	v_mul_f32_e32 v29, 0x43000000, v66
	v_mul_f32_e32 v49, 0x43000000, v67
	ds_write2_b32 v43, v29, v49 offset0:32 offset1:98
	v_mul_f32_e32 v29, 0x43000000, v68
	v_mul_f32_e32 v49, 0x43000000, v69
	ds_write2_b32 v43, v29, v49 offset0:164 offset1:230
	v_mul_f32_e32 v29, 0x43000000, v70
	v_mul_f32_e32 v49, 0x43000000, v71
	ds_write2_b32 v44, v29, v49 offset0:40 offset1:106
	v_mul_f32_e32 v29, 0x43000000, v72
	v_mul_f32_e32 v49, 0x43000000, v73
	ds_write2_b32 v44, v29, v49 offset0:172 offset1:238
	v_mov_b32_e32 v50, v1
	v_mov_b32_e32 v51, v1
	v_mul_f32_e32 v29, 0x43000000, v74
	s_add_u32 s4, s4, s6
	s_addc_u32 s5, s5, 0
	v_readlane_b32 s42, v254, 30
	v_readlane_b32 s43, v254, 31
	v_readlane_b32 s44, v254, 32
	v_mul_f32_e32 v49, 0x43000000, v75
	ds_write2_b32 v45, v29, v49 offset0:48 offset1:114
	v_readlane_b32 s45, v254, 33
	v_mul_f32_e32 v29, 0x43000000, v76
	v_mul_f32_e32 v49, 0x43000000, v77
	ds_write2_b32 v45, v29, v49 offset0:180 offset1:246
	v_mul_f32_e32 v29, 0x43000000, v78
	v_mul_f32_e32 v49, 0x43000000, v79
	ds_write2_b32 v46, v29, v49 offset0:56 offset1:122
	v_mov_b32_e32 v49, v1
	v_mul_f32_e32 v29, 0x43000000, v48
	v_mov_b32_e32 v48, v1
	v_mul_f32_e32 v28, 0x43000000, v28
	ds_write2_b32 v46, v29, v28 offset0:188 offset1:254
	s_waitcnt lgkmcnt(0)
	ds_read2_b32 v[52:53], v33 offset1:16
	ds_read2_b32 v[54:55], v33 offset0:33 offset1:49
	ds_read2_b32 v[56:57], v33 offset0:66 offset1:82
	ds_read2_b32 v[58:59], v33 offset0:99 offset1:115
	ds_read2_b32 v[60:61], v33 offset0:132 offset1:148
	ds_read2_b32 v[62:63], v33 offset0:165 offset1:181
	ds_read2_b32 v[64:65], v33 offset0:198 offset1:214
	ds_read2_b32 v[66:67], v33 offset0:231 offset1:247
	ds_read2_b32 v[68:69], v47 offset0:8 offset1:24
	ds_read2_b32 v[70:71], v47 offset0:41 offset1:57
	ds_read2_b32 v[72:73], v47 offset0:74 offset1:90
	ds_read2_b32 v[74:75], v47 offset0:107 offset1:123
	ds_read2_b32 v[76:77], v47 offset0:140 offset1:156
	ds_read2_b32 v[78:79], v47 offset0:173 offset1:189
	ds_read2_b32 v[80:81], v47 offset0:206 offset1:222
	ds_read2_b32 v[82:83], v47 offset0:239 offset1:255
	s_waitcnt lgkmcnt(14)
	v_cvt_pk_fp8_f32 v48, v52, v54
	s_waitcnt lgkmcnt(10)
	v_cvt_pk_fp8_f32 v49, v60, v62
	s_waitcnt lgkmcnt(6)
	v_cvt_pk_fp8_f32 v50, v68, v70
	s_waitcnt lgkmcnt(2)
	v_cvt_pk_fp8_f32 v51, v76, v78
	v_cvt_pk_fp8_f32 v48, v56, v58 op_sel:[0,0,1]
	v_cvt_pk_fp8_f32 v49, v64, v66 op_sel:[0,0,1]
	v_cvt_pk_fp8_f32 v50, v72, v74 op_sel:[0,0,1]
	s_waitcnt lgkmcnt(0)
	v_cvt_pk_fp8_f32 v51, v80, v82 op_sel:[0,0,1]
	v_lshl_add_u64 v[28:29], s[4:5], 0, v[2:3]
	v_add_u32_e32 v52, s0, v32
	v_mad_i64_i32 v[84:85], s[4:5], v52, s13, v[28:29]
	global_store_dwordx4 v[84:85], v[48:51], off nt
	v_add_u32_e32 v52, s0, v34
	v_mad_i64_i32 v[28:29], s[4:5], v52, s13, v[28:29]
	v_mov_b32_e32 v48, v1
	v_mov_b32_e32 v49, v1
	v_mov_b32_e32 v50, v1
	v_mov_b32_e32 v51, v1
	v_cvt_pk_fp8_f32 v48, v53, v55
	v_cvt_pk_fp8_f32 v49, v61, v63
	v_cvt_pk_fp8_f32 v50, v69, v71
	v_cvt_pk_fp8_f32 v51, v77, v79
	v_cvt_pk_fp8_f32 v48, v57, v59 op_sel:[0,0,1]
	v_cvt_pk_fp8_f32 v49, v65, v67 op_sel:[0,0,1]
	v_cvt_pk_fp8_f32 v50, v73, v75 op_sel:[0,0,1]
	v_cvt_pk_fp8_f32 v51, v81, v83 op_sel:[0,0,1]
	s_mov_b64 s[4:5], 0
	global_store_dwordx4 v[28:29], v[48:51], off nt
	s_waitcnt lgkmcnt(0)
; #define LAS __attribute__((address_space(3)))
; __device__ __forceinline__ void tr_item8(const float* W, int ld, int K, int nblk, int item, unsigned char* WT, bool gu, float scale, LAS float* scr, int lane) {
;     const int kb = item / nblk, nb = item % nblk, k0 = 64 * kb, n0 = 32 * nb;
;     int drow0 = n0;
;     if (gu) { const int bj = n0 / FF, j = n0 - bj * FF; drow0 = 256 * (j / 128) + 128 * bj + (j % 128); }
;     { float t_[32];
; #pragma unroll
;       for (int i = 0; i < 32; ++i) t_[i] = W[(size_t)(k0 + 2 * i + (lane >> 5)) * ld + n0 + (lane & 31)];
; __device__ __forceinline__ void convert_items(Frame& F, const Args& a, int lo, int hi, int w, int nw) {
;     ...
;         if (r < NE * I_GU) { const int e = r / I_GU, rr = r % I_GU; tr_item8(a.in[18] + (size_t)e * D * 2 * FF, 2 * FF, D, 224, rr, F.ws + WS_WMGU + (size_t)e * 2 * FF * D, true, WSC_GU, scr, lane); continue; } r -= NE * I_GU;
.LBB0_1338:
	s_andn2_b64 vcc, exec, s[4:5]
	s_cbranch_vccnz .LBB0_1340
	s_add_i32 s0, s8, 0xde00
	s_bfe_u32 s4, s0, 0x70009
	s_mulk_i32 s4, 0x2493
	s_lshr_b32 s4, s4, 16
	s_mul_i32 s5, s4, 0xe00
	v_readlane_b32 s40, v254, 28
	s_sub_i32 s0, s0, s5
	s_mul_i32 s5, s4, 0x1c00000
	v_readlane_b32 s44, v254, 32
	v_readlane_b32 s45, v254, 33
	s_add_u32 s7, s44, s5
	s_addc_u32 s31, s45, 0
	s_mul_i32 s4, s4, 0x700000
	s_add_u32 s4, s36, s4
	s_addc_u32 s5, s37, 0
	s_bfe_u32 s6, s0, 0xb0005
	s_mulk_i32 s6, 0x2493
	s_lshr_b32 s6, s6, 16
	s_mul_i32 s40, s6, 0xe0
	v_readlane_b32 s41, v254, 29
	s_sub_i32 s40, s0, s40
	s_lshl_b32 s0, s40, 5
	s_and_b32 s41, s40, 0xffff
	s_cmpk_gt_u32 s41, 0x6f
	v_readlane_b32 s42, v254, 30
	s_cselect_b32 s41, 0xfffff200, 0
	s_cselect_b32 s42, 0x80, 0
	s_add_i32 s0, s41, s0
	s_sext_i32_i16 s41, s0
	s_bfe_u32 s41, s41, 0x70018
	v_readlane_b32 s43, v254, 31
	s_add_i32 s41, s0, s41
	s_sext_i32_i16 s43, s41
	s_and_b32 s41, s41, 0xff80
	s_sub_i32 s0, s0, s41
	s_lshl_b32 s43, s43, 1
	s_sext_i32_i16 s0, s0
	s_and_b32 s43, s43, 0xffffff00
	s_add_i32 s0, s42, s0
	s_lshl_b32 s40, s40, 7
	s_add_i32 s0, s0, s43
	s_lshl_b32 s6, s6, 6
	s_and_b32 s40, s40, 0x3ff80
	s_add_u32 s40, s7, s40
	s_addc_u32 s41, s31, 0
	v_add_u32_e32 v50, s6, v30
	v_lshl_add_u64 v[28:29], s[40:41], 0, v[0:1]
	v_mad_i64_i32 v[48:49], s[40:41], v50, s14, v[28:29]
	global_load_dword v51, v[48:49], off nt
	v_add_u32_e32 v48, 2, v50
	v_mad_i64_i32 v[48:49], s[40:41], v48, s14, v[28:29]
	global_load_dword v52, v[48:49], off nt
	v_add_u32_e32 v48, 4, v50
	v_mad_i64_i32 v[48:49], s[40:41], v48, s14, v[28:29]
	global_load_dword v53, v[48:49], off nt
	v_add_u32_e32 v48, 6, v50
	v_mad_i64_i32 v[48:49], s[40:41], v48, s14, v[28:29]
	global_load_dword v54, v[48:49], off nt
	v_add_u32_e32 v48, 8, v50
	v_mad_i64_i32 v[48:49], s[40:41], v48, s14, v[28:29]
	global_load_dword v55, v[48:49], off nt
	v_add_u32_e32 v48, 10, v50
	v_mad_i64_i32 v[48:49], s[40:41], v48, s14, v[28:29]
	global_load_dword v56, v[48:49], off nt
	v_add_u32_e32 v48, 12, v50
	v_mad_i64_i32 v[48:49], s[40:41], v48, s14, v[28:29]
	global_load_dword v57, v[48:49], off nt
	v_add_u32_e32 v48, 14, v50
	v_mad_i64_i32 v[48:49], s[40:41], v48, s14, v[28:29]
	global_load_dword v58, v[48:49], off nt
	v_add_u32_e32 v48, 16, v50
	v_mad_i64_i32 v[48:49], s[40:41], v48, s14, v[28:29]
	global_load_dword v59, v[48:49], off nt
	v_add_u32_e32 v48, 18, v50
	v_mad_i64_i32 v[48:49], s[40:41], v48, s14, v[28:29]
	global_load_dword v60, v[48:49], off nt
	v_add_u32_e32 v48, 20, v50
	v_mad_i64_i32 v[48:49], s[40:41], v48, s14, v[28:29]
	global_load_dword v61, v[48:49], off nt
	v_add_u32_e32 v48, 22, v50
	v_mad_i64_i32 v[48:49], s[40:41], v48, s14, v[28:29]
	global_load_dword v62, v[48:49], off nt
	v_add_u32_e32 v48, 24, v50
	v_mad_i64_i32 v[48:49], s[40:41], v48, s14, v[28:29]
	global_load_dword v63, v[48:49], off nt
	v_add_u32_e32 v48, 26, v50
	v_mad_i64_i32 v[48:49], s[40:41], v48, s14, v[28:29]
	global_load_dword v64, v[48:49], off nt
	v_add_u32_e32 v48, 28, v50
	v_mad_i64_i32 v[48:49], s[40:41], v48, s14, v[28:29]
	global_load_dword v65, v[48:49], off nt
	v_add_u32_e32 v48, 30, v50
	v_mad_i64_i32 v[48:49], s[40:41], v48, s14, v[28:29]
	global_load_dword v66, v[48:49], off nt
	v_add_u32_e32 v48, 32, v50
	v_mad_i64_i32 v[48:49], s[40:41], v48, s14, v[28:29]
	global_load_dword v67, v[48:49], off nt
	v_add_u32_e32 v48, 34, v50
	v_mad_i64_i32 v[48:49], s[40:41], v48, s14, v[28:29]
	global_load_dword v68, v[48:49], off nt
	v_add_u32_e32 v48, 36, v50
	v_mad_i64_i32 v[48:49], s[40:41], v48, s14, v[28:29]
	global_load_dword v69, v[48:49], off nt
	v_add_u32_e32 v48, 38, v50
	v_mad_i64_i32 v[48:49], s[40:41], v48, s14, v[28:29]
	global_load_dword v70, v[48:49], off nt
	v_add_u32_e32 v48, 40, v50
	v_mad_i64_i32 v[48:49], s[40:41], v48, s14, v[28:29]
	global_load_dword v71, v[48:49], off nt
	v_add_u32_e32 v48, 42, v50
	v_mad_i64_i32 v[48:49], s[40:41], v48, s14, v[28:29]
	global_load_dword v72, v[48:49], off nt
	v_add_u32_e32 v48, 44, v50
	v_mad_i64_i32 v[48:49], s[40:41], v48, s14, v[28:29]
	global_load_dword v73, v[48:49], off nt
	v_add_u32_e32 v48, 46, v50
	v_mad_i64_i32 v[48:49], s[40:41], v48, s14, v[28:29]
	global_load_dword v74, v[48:49], off nt
	v_add_u32_e32 v48, 48, v50
	v_mad_i64_i32 v[48:49], s[40:41], v48, s14, v[28:29]
	global_load_dword v75, v[48:49], off nt
	v_add_u32_e32 v48, 50, v50
	v_mad_i64_i32 v[48:49], s[40:41], v48, s14, v[28:29]
	global_load_dword v76, v[48:49], off nt
	v_add_u32_e32 v48, 52, v50
	v_mad_i64_i32 v[48:49], s[40:41], v48, s14, v[28:29]
	global_load_dword v77, v[48:49], off nt
	v_add_u32_e32 v48, 54, v50
	v_mad_i64_i32 v[48:49], s[40:41], v48, s14, v[28:29]
	global_load_dword v78, v[48:49], off nt
	v_add_u32_e32 v48, 56, v50
	v_mad_i64_i32 v[48:49], s[40:41], v48, s14, v[28:29]
	global_load_dword v79, v[48:49], off nt
	v_add_u32_e32 v48, 58, v50
	v_mad_i64_i32 v[48:49], s[40:41], v48, s14, v[28:29]
	global_load_dword v80, v[48:49], off nt
	v_add_u32_e32 v48, 60, v50
	v_mad_i64_i32 v[48:49], s[40:41], v48, s14, v[28:29]
	global_load_dword v48, v[48:49], off nt
	v_add_u32_e32 v49, 62, v50
	v_mad_i64_i32 v[28:29], s[40:41], v49, s14, v[28:29]
	global_load_dword v28, v[28:29], off nt
	s_waitcnt vmcnt(0)
; __device__ __forceinline__ unsigned cvt_pk4_fp8(float a, float b, float c, float d) { int w = 0; w = __builtin_amdgcn_cvt_pk_fp8_f32(a, b, w, false); w = __builtin_amdgcn_cvt_pk_fp8_f32(c, d, w, true); return (unsigned)w; }
; #define GAS __attribute__((address_space(1)))
; #define LAS __attribute__((address_space(3)))
; #define LDS_WAIT() asm volatile("s_waitcnt lgkmcnt(0)" ::: "memory")
; __device__ __forceinline__ void tr_item8(const float* W, int ld, int K, int nblk, int item, unsigned char* WT, bool gu, float scale, LAS float* scr, int lane) {
;     ...
;       for (int i = 0; i < 32; ++i) scr[(2 * i + (lane >> 5)) * 33 + (lane & 31)] = t_[i] * scale; }
;     LDS_WAIT(); asm volatile("" ::: "memory");
;     const int c = lane & 3;
; #pragma unroll
;     for (int j = 0; j < 2; ++j) { const int n = (lane >> 2) + 16 * j; const LAS float* sp = scr + (16 * c) * 33 + n;
;         v4u o; o.x = pg8::cvt_pk4_fp8(sp[0 * 33], sp[1 * 33], sp[2 * 33], sp[3 * 33]); o.y = pg8::cvt_pk4_fp8(sp[4 * 33], sp[5 * 33], sp[6 * 33], sp[7 * 33]);
;         o.z = pg8::cvt_pk4_fp8(sp[8 * 33], sp[9 * 33], sp[10 * 33], sp[11 * 33]); o.w = pg8::cvt_pk4_fp8(sp[12 * 33], sp[13 * 33], sp[14 * 33], sp[15 * 33]);
;         *(GAS v4u*)(WT + (size_t)(drow0 + n) * K + k0 + 16 * c) = o; }
;     LDS_WAIT(); asm volatile("" ::: "memory");
	v_mul_f32_e32 v29, 0x42800000, v51
	v_mul_f32_e32 v49, 0x42800000, v52
	ds_write2_b32 v31, v29, v49 offset1:66
	v_mul_f32_e32 v29, 0x42800000, v53
	v_mul_f32_e32 v49, 0x42800000, v54
	ds_write2_b32 v31, v29, v49 offset0:132 offset1:198
	v_mul_f32_e32 v29, 0x42800000, v55
	v_mul_f32_e32 v49, 0x42800000, v56
	ds_write2_b32 v40, v29, v49 offset0:8 offset1:74
	v_mul_f32_e32 v29, 0x42800000, v57
	v_mul_f32_e32 v49, 0x42800000, v58
	ds_write2_b32 v40, v29, v49 offset0:140 offset1:206
	v_mul_f32_e32 v29, 0x42800000, v59
	v_mul_f32_e32 v49, 0x42800000, v60
	ds_write2_b32 v41, v29, v49 offset0:16 offset1:82
	v_mul_f32_e32 v29, 0x42800000, v61
	v_mul_f32_e32 v49, 0x42800000, v62
	ds_write2_b32 v41, v29, v49 offset0:148 offset1:214
	v_mul_f32_e32 v29, 0x42800000, v63
	v_mul_f32_e32 v49, 0x42800000, v64
	ds_write2_b32 v42, v29, v49 offset0:24 offset1:90
	v_mul_f32_e32 v29, 0x42800000, v65
	v_mul_f32_e32 v49, 0x42800000, v66
	ds_write2_b32 v42, v29, v49 offset0:156 offset1:222
	v_mul_f32_e32 v29, 0x42800000, v67
	v_mul_f32_e32 v49, 0x42800000, v68
	ds_write2_b32 v43, v29, v49 offset0:32 offset1:98
	v_mul_f32_e32 v29, 0x42800000, v69
	v_mov_b32_e32 v50, v1
	v_mov_b32_e32 v51, v1
	s_add_u32 s4, s4, s6
	v_mul_f32_e32 v49, 0x42800000, v70
	ds_write2_b32 v43, v29, v49 offset0:164 offset1:230
	v_add_u32_e32 v84, s0, v32
	s_addc_u32 s5, s5, 0
	v_mul_f32_e32 v29, 0x42800000, v71
	v_ashrrev_i32_e32 v85, 31, v84
	v_lshlrev_b64 v[84:85], 10, v[84:85]
	v_readlane_b32 s46, v254, 34
	v_mul_f32_e32 v49, 0x42800000, v72
	ds_write2_b32 v44, v29, v49 offset0:40 offset1:106
	v_readlane_b32 s47, v254, 35
	v_mul_f32_e32 v29, 0x42800000, v73
	v_mul_f32_e32 v49, 0x42800000, v74
	ds_write2_b32 v44, v29, v49 offset0:172 offset1:238
	v_mul_f32_e32 v29, 0x42800000, v75
	v_mul_f32_e32 v49, 0x42800000, v76
	ds_write2_b32 v45, v29, v49 offset0:48 offset1:114
	v_mul_f32_e32 v29, 0x42800000, v77
	v_mul_f32_e32 v49, 0x42800000, v78
	ds_write2_b32 v45, v29, v49 offset0:180 offset1:246
	v_mul_f32_e32 v29, 0x42800000, v79
	v_mul_f32_e32 v49, 0x42800000, v80
	ds_write2_b32 v46, v29, v49 offset0:56 offset1:122
	v_mov_b32_e32 v49, v1
	v_mul_f32_e32 v29, 0x42800000, v48
	v_mov_b32_e32 v48, v1
	v_mul_f32_e32 v28, 0x42800000, v28
	ds_write2_b32 v46, v29, v28 offset0:188 offset1:254
	s_waitcnt lgkmcnt(0)
	ds_read2_b32 v[52:53], v33 offset1:16
	ds_read2_b32 v[54:55], v33 offset0:33 offset1:49
	ds_read2_b32 v[56:57], v33 offset0:66 offset1:82
	ds_read2_b32 v[58:59], v33 offset0:99 offset1:115
	ds_read2_b32 v[60:61], v33 offset0:132 offset1:148
	ds_read2_b32 v[62:63], v33 offset0:165 offset1:181
	ds_read2_b32 v[64:65], v33 offset0:198 offset1:214
	ds_read2_b32 v[66:67], v33 offset0:231 offset1:247
	ds_read2_b32 v[68:69], v47 offset0:8 offset1:24
	ds_read2_b32 v[70:71], v47 offset0:41 offset1:57
	ds_read2_b32 v[72:73], v47 offset0:74 offset1:90
	ds_read2_b32 v[74:75], v47 offset0:107 offset1:123
	ds_read2_b32 v[76:77], v47 offset0:140 offset1:156
	ds_read2_b32 v[78:79], v47 offset0:173 offset1:189
	ds_read2_b32 v[80:81], v47 offset0:206 offset1:222
	ds_read2_b32 v[82:83], v47 offset0:239 offset1:255
	s_waitcnt lgkmcnt(14)
	v_cvt_pk_fp8_f32 v48, v52, v54
	s_waitcnt lgkmcnt(10)
	v_cvt_pk_fp8_f32 v49, v60, v62
	s_waitcnt lgkmcnt(6)
	v_cvt_pk_fp8_f32 v50, v68, v70
	s_waitcnt lgkmcnt(2)
	v_cvt_pk_fp8_f32 v51, v76, v78
	v_cvt_pk_fp8_f32 v48, v56, v58 op_sel:[0,0,1]
	v_cvt_pk_fp8_f32 v49, v64, v66 op_sel:[0,0,1]
	v_cvt_pk_fp8_f32 v50, v72, v74 op_sel:[0,0,1]
	s_waitcnt lgkmcnt(0)
	v_cvt_pk_fp8_f32 v51, v80, v82 op_sel:[0,0,1]
	v_lshl_add_u64 v[28:29], s[4:5], 0, v[2:3]
	v_lshl_add_u64 v[84:85], v[28:29], 0, v[84:85]
	v_add_u32_e32 v52, s0, v34
	global_store_dwordx4 v[84:85], v[48:51], off nt
	s_nop 1
	v_mov_b32_e32 v48, v1
	v_mov_b32_e32 v49, v1
	v_mov_b32_e32 v50, v1
	v_mov_b32_e32 v51, v1
	v_cvt_pk_fp8_f32 v48, v53, v55
	v_cvt_pk_fp8_f32 v49, v61, v63
	v_cvt_pk_fp8_f32 v50, v69, v71
	v_cvt_pk_fp8_f32 v51, v77, v79
	v_cvt_pk_fp8_f32 v48, v57, v59 op_sel:[0,0,1]
	v_cvt_pk_fp8_f32 v49, v65, v67 op_sel:[0,0,1]
	v_cvt_pk_fp8_f32 v50, v73, v75 op_sel:[0,0,1]
	v_cvt_pk_fp8_f32 v51, v81, v83 op_sel:[0,0,1]
	v_ashrrev_i32_e32 v53, 31, v52
	v_lshlrev_b64 v[52:53], 10, v[52:53]
	v_lshl_add_u64 v[28:29], v[28:29], 0, v[52:53]
	global_store_dwordx4 v[28:29], v[48:51], off nt
	s_waitcnt lgkmcnt(0)

; __device__ __forceinline__ void tr_item8(const float* W, int ld, int K, int nblk, int item, unsigned char* WT, bool gu, float scale, LAS float* scr, int lane) {
;     const int kb = item / nblk, nb = item % nblk, k0 = 64 * kb, n0 = 32 * nb;
;     int drow0 = n0;
;     if (gu) { const int bj = n0 / FF, j = n0 - bj * FF; drow0 = 256 * (j / 128) + 128 * bj + (j % 128); }
;     { float t_[32];
; #pragma unroll
;       for (int i = 0; i < 32; ++i) t_[i] = W[(size_t)(k0 + 2 * i + (lane >> 5)) * ld + n0 + (lane & 31)];
; __device__ __forceinline__ void convert_items(Frame& F, const Args& a, int lo, int hi, int w, int nw) {
;     ...
;         if (r < I_DN) { tr_item8(a.in[15], D, FF, 32, r, F.ws + WS_WDN, false, WSC_DN, scr, lane); continue; } r -= I_DN;
.LBB0_1341:
	s_andn2_b64 vcc, exec, s[4:5]
	s_cbranch_vccnz .LBB0_1343
	s_lshl_b32 s0, s8, 5
	s_and_b32 s4, s12, 0x1ffc0
	s_and_b32 s6, s0, 0x3e0
	v_add_u32_e32 v28, s4, v30
	s_lshl_b32 s0, s6, 2
	v_ashrrev_i32_e32 v29, 31, v28
	v_lshl_add_u64 v[48:49], v[4:5], 0, s[0:1]
	v_lshlrev_b64 v[28:29], 12, v[28:29]
	v_lshl_add_u64 v[28:29], v[48:49], 0, v[28:29]
	v_add_co_u32_e32 v48, vcc, 0x2000, v28
	global_load_dword v50, v[28:29], off nt
	s_nop 0
	v_addc_co_u32_e32 v49, vcc, 0, v29, vcc
	global_load_dword v51, v[48:49], off nt
	v_add_co_u32_e32 v48, vcc, 0x4000, v28
	s_mov_b32 s5, s1
	s_nop 0
	v_addc_co_u32_e32 v49, vcc, 0, v29, vcc
	global_load_dword v52, v[48:49], off nt
	v_add_co_u32_e32 v48, vcc, 0x6000, v28
	s_nop 1
	v_addc_co_u32_e32 v49, vcc, 0, v29, vcc
	global_load_dword v53, v[48:49], off nt
	v_add_co_u32_e32 v48, vcc, 0x8000, v28
	s_nop 1
	v_addc_co_u32_e32 v49, vcc, 0, v29, vcc
	global_load_dword v54, v[48:49], off nt
	v_add_co_u32_e32 v48, vcc, 0xa000, v28
	s_nop 1
	v_addc_co_u32_e32 v49, vcc, 0, v29, vcc
	global_load_dword v55, v[48:49], off nt
	v_add_co_u32_e32 v48, vcc, 0xc000, v28
	s_nop 1
	v_addc_co_u32_e32 v49, vcc, 0, v29, vcc
	global_load_dword v56, v[48:49], off nt
	v_add_co_u32_e32 v48, vcc, 0xe000, v28
	s_nop 1
	v_addc_co_u32_e32 v49, vcc, 0, v29, vcc
	global_load_dword v57, v[48:49], off nt
	v_add_co_u32_e32 v48, vcc, 0x10000, v28
	s_nop 1
	v_addc_co_u32_e32 v49, vcc, 0, v29, vcc
	global_load_dword v58, v[48:49], off nt
	v_add_co_u32_e32 v48, vcc, 0x12000, v28
	s_nop 1
	v_addc_co_u32_e32 v49, vcc, 0, v29, vcc
	global_load_dword v59, v[48:49], off nt
	v_add_co_u32_e32 v48, vcc, 0x14000, v28
	s_nop 1
	v_addc_co_u32_e32 v49, vcc, 0, v29, vcc
	global_load_dword v60, v[48:49], off nt
	v_add_co_u32_e32 v48, vcc, 0x16000, v28
	s_nop 1
	v_addc_co_u32_e32 v49, vcc, 0, v29, vcc
	global_load_dword v61, v[48:49], off nt
	v_add_co_u32_e32 v48, vcc, 0x18000, v28
	s_nop 1
	v_addc_co_u32_e32 v49, vcc, 0, v29, vcc
	global_load_dword v62, v[48:49], off nt
	v_add_co_u32_e32 v48, vcc, 0x1a000, v28
	s_nop 1
	v_addc_co_u32_e32 v49, vcc, 0, v29, vcc
	global_load_dword v63, v[48:49], off nt
	v_add_co_u32_e32 v48, vcc, 0x1c000, v28
	s_nop 1
	v_addc_co_u32_e32 v49, vcc, 0, v29, vcc
	global_load_dword v64, v[48:49], off nt
	v_add_co_u32_e32 v48, vcc, 0x1e000, v28
	s_nop 1
	v_addc_co_u32_e32 v49, vcc, 0, v29, vcc
	global_load_dword v65, v[48:49], off nt
	v_add_co_u32_e32 v48, vcc, 0x20000, v28
	s_nop 1
	v_addc_co_u32_e32 v49, vcc, 0, v29, vcc
	global_load_dword v66, v[48:49], off nt
	v_add_co_u32_e32 v48, vcc, 0x22000, v28
	s_nop 1
	v_addc_co_u32_e32 v49, vcc, 0, v29, vcc
	global_load_dword v67, v[48:49], off nt
	v_add_co_u32_e32 v48, vcc, 0x24000, v28
	s_nop 1
	v_addc_co_u32_e32 v49, vcc, 0, v29, vcc
	global_load_dword v68, v[48:49], off nt
	v_add_co_u32_e32 v48, vcc, 0x26000, v28
	s_nop 1
	v_addc_co_u32_e32 v49, vcc, 0, v29, vcc
	global_load_dword v69, v[48:49], off nt
	v_add_co_u32_e32 v48, vcc, 0x28000, v28
	s_nop 1
	v_addc_co_u32_e32 v49, vcc, 0, v29, vcc
	global_load_dword v70, v[48:49], off nt
	v_add_co_u32_e32 v48, vcc, 0x2a000, v28
	s_nop 1
	v_addc_co_u32_e32 v49, vcc, 0, v29, vcc
	global_load_dword v71, v[48:49], off nt
	v_add_co_u32_e32 v48, vcc, 0x2c000, v28
	s_nop 1
	v_addc_co_u32_e32 v49, vcc, 0, v29, vcc
	global_load_dword v72, v[48:49], off nt
	v_add_co_u32_e32 v48, vcc, 0x2e000, v28
	s_nop 1
	v_addc_co_u32_e32 v49, vcc, 0, v29, vcc
	global_load_dword v73, v[48:49], off nt
	v_add_co_u32_e32 v48, vcc, 0x30000, v28
	s_nop 1
	v_addc_co_u32_e32 v49, vcc, 0, v29, vcc
	global_load_dword v74, v[48:49], off nt
	v_add_co_u32_e32 v48, vcc, 0x32000, v28
	s_nop 1
	v_addc_co_u32_e32 v49, vcc, 0, v29, vcc
	global_load_dword v75, v[48:49], off nt
	v_add_co_u32_e32 v48, vcc, 0x34000, v28
	s_nop 1
	v_addc_co_u32_e32 v49, vcc, 0, v29, vcc
	global_load_dword v76, v[48:49], off nt
	v_add_co_u32_e32 v48, vcc, 0x36000, v28
	s_nop 1
	v_addc_co_u32_e32 v49, vcc, 0, v29, vcc
	global_load_dword v77, v[48:49], off nt
	v_add_co_u32_e32 v48, vcc, 0x38000, v28
	s_nop 1
	v_addc_co_u32_e32 v49, vcc, 0, v29, vcc
	global_load_dword v78, v[48:49], off nt
	v_add_co_u32_e32 v48, vcc, 0x3a000, v28
	s_nop 1
	v_addc_co_u32_e32 v49, vcc, 0, v29, vcc
	global_load_dword v79, v[48:49], off nt
	v_add_co_u32_e32 v48, vcc, 0x3c000, v28
	s_nop 1
	v_addc_co_u32_e32 v49, vcc, 0, v29, vcc
	v_add_co_u32_e32 v28, vcc, 0x3e000, v28
	global_load_dword v48, v[48:49], off nt
	s_nop 0
	v_addc_co_u32_e32 v29, vcc, 0, v29, vcc
	global_load_dword v28, v[28:29], off nt
	s_waitcnt vmcnt(0)
; __device__ __forceinline__ unsigned cvt_pk4_fp8(float a, float b, float c, float d) { int w = 0; w = __builtin_amdgcn_cvt_pk_fp8_f32(a, b, w, false); w = __builtin_amdgcn_cvt_pk_fp8_f32(c, d, w, true); return (unsigned)w; }
; #define GAS __attribute__((address_space(1)))
; #define LAS __attribute__((address_space(3)))
; #define LDS_WAIT() asm volatile("s_waitcnt lgkmcnt(0)" ::: "memory")
; __device__ __forceinline__ void tr_item8(const float* W, int ld, int K, int nblk, int item, unsigned char* WT, bool gu, float scale, LAS float* scr, int lane) {
;     ...
;       for (int i = 0; i < 32; ++i) scr[(2 * i + (lane >> 5)) * 33 + (lane & 31)] = t_[i] * scale; }
;     LDS_WAIT(); asm volatile("" ::: "memory");
;     const int c = lane & 3;
; #pragma unroll
;     for (int j = 0; j < 2; ++j) { const int n = (lane >> 2) + 16 * j; const LAS float* sp = scr + (16 * c) * 33 + n;
;         v4u o; o.x = pg8::cvt_pk4_fp8(sp[0 * 33], sp[1 * 33], sp[2 * 33], sp[3 * 33]); o.y = pg8::cvt_pk4_fp8(sp[4 * 33], sp[5 * 33], sp[6 * 33], sp[7 * 33]);
;         o.z = pg8::cvt_pk4_fp8(sp[8 * 33], sp[9 * 33], sp[10 * 33], sp[11 * 33]); o.w = pg8::cvt_pk4_fp8(sp[12 * 33], sp[13 * 33], sp[14 * 33], sp[15 * 33]);
;         *(GAS v4u*)(WT + (size_t)(drow0 + n) * K + k0 + 16 * c) = o; }
;     LDS_WAIT(); asm volatile("" ::: "memory");
	v_mul_f32_e32 v29, 0x43000000, v50
	v_mul_f32_e32 v49, 0x43000000, v51
	ds_write2_b32 v31, v29, v49 offset1:66
	v_mul_f32_e32 v29, 0x43000000, v52
	v_mul_f32_e32 v49, 0x43000000, v53
	ds_write2_b32 v31, v29, v49 offset0:132 offset1:198
	v_mul_f32_e32 v29, 0x43000000, v54
	v_mul_f32_e32 v49, 0x43000000, v55
	ds_write2_b32 v40, v29, v49 offset0:8 offset1:74
	v_mul_f32_e32 v29, 0x43000000, v56
	v_mul_f32_e32 v49, 0x43000000, v57
	ds_write2_b32 v40, v29, v49 offset0:140 offset1:206
	v_mul_f32_e32 v29, 0x43000000, v58
	v_mul_f32_e32 v49, 0x43000000, v59
	ds_write2_b32 v41, v29, v49 offset0:16 offset1:82
	v_mul_f32_e32 v29, 0x43000000, v60
	v_mul_f32_e32 v49, 0x43000000, v61
	ds_write2_b32 v41, v29, v49 offset0:148 offset1:214
	v_mul_f32_e32 v29, 0x43000000, v62
	v_mul_f32_e32 v49, 0x43000000, v63
	ds_write2_b32 v42, v29, v49 offset0:24 offset1:90
	v_mul_f32_e32 v29, 0x43000000, v64
	v_mul_f32_e32 v49, 0x43000000, v65
	ds_write2_b32 v42, v29, v49 offset0:156 offset1:222
	v_mul_f32_e32 v29, 0x43000000, v66
	v_mul_f32_e32 v49, 0x43000000, v67
	ds_write2_b32 v43, v29, v49 offset0:32 offset1:98
	v_mul_f32_e32 v29, 0x43000000, v68
	v_mul_f32_e32 v49, 0x43000000, v69
	ds_write2_b32 v43, v29, v49 offset0:164 offset1:230
	v_mul_f32_e32 v29, 0x43000000, v70
	v_mul_f32_e32 v49, 0x43000000, v71
	ds_write2_b32 v44, v29, v49 offset0:40 offset1:106
	v_mul_f32_e32 v29, 0x43000000, v72
	v_mul_f32_e32 v49, 0x43000000, v73
	ds_write2_b32 v44, v29, v49 offset0:172 offset1:238
	v_mov_b32_e32 v50, 0
	v_mov_b32_e32 v51, 0
	v_mul_f32_e32 v29, 0x43000000, v74
	v_mul_f32_e32 v49, 0x43000000, v75
	ds_write2_b32 v45, v29, v49 offset0:48 offset1:114
	v_mul_f32_e32 v29, 0x43000000, v76
	v_mul_f32_e32 v49, 0x43000000, v77
	ds_write2_b32 v45, v29, v49 offset0:180 offset1:246
	v_mul_f32_e32 v29, 0x43000000, v78
	v_mul_f32_e32 v49, 0x43000000, v79
	ds_write2_b32 v46, v29, v49 offset0:56 offset1:122
	v_mov_b32_e32 v49, 0
	v_mul_f32_e32 v29, 0x43000000, v48
	v_mov_b32_e32 v48, 0
	v_mul_f32_e32 v28, 0x43000000, v28
	ds_write2_b32 v46, v29, v28 offset0:188 offset1:254
	s_waitcnt lgkmcnt(0)
	ds_read2_b32 v[52:53], v33 offset1:16
	ds_read2_b32 v[54:55], v33 offset0:33 offset1:49
	ds_read2_b32 v[56:57], v33 offset0:66 offset1:82
	ds_read2_b32 v[58:59], v33 offset0:99 offset1:115
	ds_read2_b32 v[60:61], v33 offset0:132 offset1:148
	ds_read2_b32 v[62:63], v33 offset0:165 offset1:181
	ds_read2_b32 v[64:65], v33 offset0:198 offset1:214
	ds_read2_b32 v[66:67], v33 offset0:231 offset1:247
	ds_read2_b32 v[68:69], v47 offset0:8 offset1:24
	ds_read2_b32 v[70:71], v47 offset0:41 offset1:57
	ds_read2_b32 v[72:73], v47 offset0:74 offset1:90
	ds_read2_b32 v[74:75], v47 offset0:107 offset1:123
	ds_read2_b32 v[76:77], v47 offset0:140 offset1:156
	ds_read2_b32 v[78:79], v47 offset0:173 offset1:189
	ds_read2_b32 v[80:81], v47 offset0:206 offset1:222
	ds_read2_b32 v[82:83], v47 offset0:239 offset1:255
	s_waitcnt lgkmcnt(14)
	v_cvt_pk_fp8_f32 v48, v52, v54
	s_waitcnt lgkmcnt(10)
	v_cvt_pk_fp8_f32 v49, v60, v62
	s_waitcnt lgkmcnt(6)
	v_cvt_pk_fp8_f32 v50, v68, v70
	s_waitcnt lgkmcnt(2)
	v_cvt_pk_fp8_f32 v51, v76, v78
	v_cvt_pk_fp8_f32 v48, v56, v58 op_sel:[0,0,1]
	v_cvt_pk_fp8_f32 v49, v64, v66 op_sel:[0,0,1]
	v_cvt_pk_fp8_f32 v50, v72, v74 op_sel:[0,0,1]
	s_waitcnt lgkmcnt(0)
	v_cvt_pk_fp8_f32 v51, v80, v82 op_sel:[0,0,1]
	v_lshl_add_u64 v[28:29], v[16:17], 0, s[4:5]
	v_add_u32_e32 v52, s6, v32
	v_mad_i64_i32 v[84:85], s[4:5], v52, s13, v[28:29]
	global_store_dwordx4 v[84:85], v[48:51], off nt
	v_add_u32_e32 v52, s6, v34
	v_mad_i64_i32 v[28:29], s[4:5], v52, s13, v[28:29]
	v_mov_b32_e32 v48, 0
	v_mov_b32_e32 v49, 0
	v_mov_b32_e32 v50, 0
	v_mov_b32_e32 v51, 0
	v_cvt_pk_fp8_f32 v48, v53, v55
	v_cvt_pk_fp8_f32 v49, v61, v63
	v_cvt_pk_fp8_f32 v50, v69, v71
	v_cvt_pk_fp8_f32 v51, v77, v79
	v_cvt_pk_fp8_f32 v48, v57, v59 op_sel:[0,0,1]
	v_cvt_pk_fp8_f32 v49, v65, v67 op_sel:[0,0,1]
	v_cvt_pk_fp8_f32 v50, v73, v75 op_sel:[0,0,1]
	v_cvt_pk_fp8_f32 v51, v81, v83 op_sel:[0,0,1]
	global_store_dwordx4 v[28:29], v[48:51], off nt
	s_waitcnt lgkmcnt(0)

; __device__ __forceinline__ void tr_item8(const float* W, int ld, int K, int nblk, int item, unsigned char* WT, bool gu, float scale, LAS float* scr, int lane) {
;     const int kb = item / nblk, nb = item % nblk, k0 = 64 * kb, n0 = 32 * nb;
;     int drow0 = n0;
;     if (gu) { const int bj = n0 / FF, j = n0 - bj * FF; drow0 = 256 * (j / 128) + 128 * bj + (j % 128); }
;     { float t_[32];
; #pragma unroll
;       for (int i = 0; i < 32; ++i) t_[i] = W[(size_t)(k0 + 2 * i + (lane >> 5)) * ld + n0 + (lane & 31)];
; __device__ __forceinline__ void convert_items(Frame& F, const Args& a, int lo, int hi, int w, int nw) {
;     ...
;         if (r < I_GU) { tr_item8(a.in[14], 2 * FF, D, 224, r, F.ws + WS_WGU, true, WSC_GU, scr, lane); continue; } r -= I_GU;
.LBB0_1344:
	s_andn2_b64 vcc, exec, s[4:5]
	s_cbranch_vccnz .LBB0_1346
	s_add_i32 s0, s8, 0xf300
	s_bfe_u32 s4, s0, 0xb0005
	s_mulk_i32 s4, 0x2493
	s_lshr_b32 s4, s4, 16
	s_mul_i32 s5, s4, 0xe0
	s_sub_i32 s0, s0, s5
	s_lshl_b32 s5, s0, 5
	s_and_b32 s6, s0, 0xffff
	s_cmpk_gt_u32 s6, 0x6f
	s_cselect_b32 s31, 0xfffff200, 0
	s_cselect_b32 s40, 0x80, 0
	s_lshl_b32 s0, s0, 7
	s_lshl_b32 s4, s4, 6
	s_and_b32 s0, s0, 0x3ff80
	v_add_u32_e32 v64, s4, v30
	v_lshl_add_u64 v[28:29], v[6:7], 0, s[0:1]
	v_mad_i64_i32 v[48:49], s[6:7], v64, s14, v[28:29]
	v_add_u32_e32 v50, 2, v64
	v_add_u32_e32 v52, 4, v64
	v_add_u32_e32 v54, 6, v64
	v_add_u32_e32 v56, 8, v64
	v_add_u32_e32 v58, 10, v64
	v_add_u32_e32 v60, 12, v64
	v_add_u32_e32 v62, 14, v64
	v_mad_i64_i32 v[50:51], s[6:7], v50, s14, v[28:29]
	v_mad_i64_i32 v[52:53], s[6:7], v52, s14, v[28:29]
	v_mad_i64_i32 v[54:55], s[6:7], v54, s14, v[28:29]
	v_mad_i64_i32 v[56:57], s[6:7], v56, s14, v[28:29]
	v_mad_i64_i32 v[58:59], s[6:7], v58, s14, v[28:29]
	v_mad_i64_i32 v[60:61], s[6:7], v60, s14, v[28:29]
	v_mad_i64_i32 v[62:63], s[6:7], v62, s14, v[28:29]
	global_load_dword v65, v[48:49], off nt
	global_load_dword v66, v[50:51], off nt
	global_load_dword v67, v[52:53], off nt
	global_load_dword v68, v[54:55], off nt
	global_load_dword v69, v[56:57], off nt
	global_load_dword v70, v[58:59], off nt
	global_load_dword v71, v[60:61], off nt
	global_load_dword v72, v[62:63], off nt
	v_add_u32_e32 v48, 16, v64
	v_mad_i64_i32 v[48:49], s[6:7], v48, s14, v[28:29]
	v_add_u32_e32 v50, 18, v64
	v_add_u32_e32 v52, 20, v64
	v_add_u32_e32 v54, 22, v64
	v_add_u32_e32 v56, 24, v64
	v_add_u32_e32 v58, 26, v64
	v_add_u32_e32 v60, 28, v64
	v_add_u32_e32 v62, 30, v64
	v_mad_i64_i32 v[50:51], s[6:7], v50, s14, v[28:29]
	v_mad_i64_i32 v[52:53], s[6:7], v52, s14, v[28:29]
	v_mad_i64_i32 v[54:55], s[6:7], v54, s14, v[28:29]
	v_mad_i64_i32 v[56:57], s[6:7], v56, s14, v[28:29]
	v_mad_i64_i32 v[58:59], s[6:7], v58, s14, v[28:29]
	v_mad_i64_i32 v[60:61], s[6:7], v60, s14, v[28:29]
	v_mad_i64_i32 v[62:63], s[6:7], v62, s14, v[28:29]
	global_load_dword v73, v[48:49], off nt
	global_load_dword v74, v[50:51], off nt
	global_load_dword v75, v[52:53], off nt
	global_load_dword v76, v[54:55], off nt
	global_load_dword v77, v[56:57], off nt
	global_load_dword v78, v[58:59], off nt
	global_load_dword v79, v[60:61], off nt
	global_load_dword v80, v[62:63], off nt
	v_add_u32_e32 v48, 32, v64
	v_add_u32_e32 v50, 34, v64
	v_add_u32_e32 v52, 36, v64
	v_add_u32_e32 v54, 38, v64
	v_add_u32_e32 v60, 44, v64
	v_mad_i64_i32 v[48:49], s[6:7], v48, s14, v[28:29]
	v_mad_i64_i32 v[50:51], s[6:7], v50, s14, v[28:29]
	v_mad_i64_i32 v[52:53], s[6:7], v52, s14, v[28:29]
	v_mad_i64_i32 v[54:55], s[6:7], v54, s14, v[28:29]
	v_add_u32_e32 v56, 40, v64
	v_add_u32_e32 v58, 42, v64
	v_mad_i64_i32 v[60:61], s[6:7], v60, s14, v[28:29]
	v_add_u32_e32 v62, 46, v64
	v_mad_i64_i32 v[56:57], s[6:7], v56, s14, v[28:29]
	v_mad_i64_i32 v[58:59], s[6:7], v58, s14, v[28:29]
	v_mad_i64_i32 v[62:63], s[6:7], v62, s14, v[28:29]
	global_load_dword v81, v[48:49], off nt
	global_load_dword v82, v[50:51], off nt
	global_load_dword v83, v[52:53], off nt
	global_load_dword v84, v[54:55], off nt
	global_load_dword v85, v[56:57], off nt
	global_load_dword v86, v[58:59], off nt
	s_nop 0
	global_load_dword v60, v[60:61], off nt
	s_nop 0
	global_load_dword v61, v[62:63], off nt
	v_add_u32_e32 v48, 48, v64
	v_add_u32_e32 v50, 50, v64
	v_add_u32_e32 v52, 52, v64
	v_add_u32_e32 v54, 54, v64
	v_mad_i64_i32 v[48:49], s[6:7], v48, s14, v[28:29]
	v_mad_i64_i32 v[50:51], s[6:7], v50, s14, v[28:29]
	v_mad_i64_i32 v[52:53], s[6:7], v52, s14, v[28:29]
	v_mad_i64_i32 v[54:55], s[6:7], v54, s14, v[28:29]
	v_add_u32_e32 v56, 56, v64
	v_add_u32_e32 v58, 58, v64
	v_mad_i64_i32 v[56:57], s[6:7], v56, s14, v[28:29]
	v_mad_i64_i32 v[58:59], s[6:7], v58, s14, v[28:29]
	global_load_dword v62, v[48:49], off nt
	s_nop 0
	global_load_dword v50, v[50:51], off nt
	s_nop 0
	global_load_dword v51, v[52:53], off nt
	s_nop 0
	global_load_dword v52, v[54:55], off nt
	global_load_dword v53, v[56:57], off nt
	s_nop 0
	global_load_dword v54, v[58:59], off nt
	v_add_u32_e32 v48, 60, v64
	v_add_u32_e32 v55, 62, v64
	v_mad_i64_i32 v[48:49], s[6:7], v48, s14, v[28:29]
	v_mad_i64_i32 v[28:29], s[6:7], v55, s14, v[28:29]
	global_load_dword v48, v[48:49], off nt
	s_nop 0
	global_load_dword v28, v[28:29], off nt
	s_waitcnt vmcnt(0)
; __device__ __forceinline__ unsigned cvt_pk4_fp8(float a, float b, float c, float d) { int w = 0; w = __builtin_amdgcn_cvt_pk_fp8_f32(a, b, w, false); w = __builtin_amdgcn_cvt_pk_fp8_f32(c, d, w, true); return (unsigned)w; }
; #define GAS __attribute__((address_space(1)))
; #define LAS __attribute__((address_space(3)))
; #define LDS_WAIT() asm volatile("s_waitcnt lgkmcnt(0)" ::: "memory")
; __device__ __forceinline__ void tr_item8(const float* W, int ld, int K, int nblk, int item, unsigned char* WT, bool gu, float scale, LAS float* scr, int lane) {
;     ...
;       for (int i = 0; i < 32; ++i) scr[(2 * i + (lane >> 5)) * 33 + (lane & 31)] = t_[i] * scale; }
;     LDS_WAIT(); asm volatile("" ::: "memory");
;     const int c = lane & 3;
; #pragma unroll
;     for (int j = 0; j < 2; ++j) { const int n = (lane >> 2) + 16 * j; const LAS float* sp = scr + (16 * c) * 33 + n;
;         v4u o; o.x = pg8::cvt_pk4_fp8(sp[0 * 33], sp[1 * 33], sp[2 * 33], sp[3 * 33]); o.y = pg8::cvt_pk4_fp8(sp[4 * 33], sp[5 * 33], sp[6 * 33], sp[7 * 33]);
;         o.z = pg8::cvt_pk4_fp8(sp[8 * 33], sp[9 * 33], sp[10 * 33], sp[11 * 33]); o.w = pg8::cvt_pk4_fp8(sp[12 * 33], sp[13 * 33], sp[14 * 33], sp[15 * 33]);
;         *(GAS v4u*)(WT + (size_t)(drow0 + n) * K + k0 + 16 * c) = o; }
;     LDS_WAIT(); asm volatile("" ::: "memory");
	v_mul_f32_e32 v29, 0x42800000, v65
	v_mul_f32_e32 v49, 0x42800000, v66
	ds_write2_b32 v31, v29, v49 offset1:66
	v_mul_f32_e32 v29, 0x42800000, v67
	v_mul_f32_e32 v49, 0x42800000, v68
	ds_write2_b32 v31, v29, v49 offset0:132 offset1:198
	v_mul_f32_e32 v29, 0x42800000, v69
	v_mul_f32_e32 v49, 0x42800000, v70
	ds_write2_b32 v40, v29, v49 offset0:8 offset1:74
	v_mul_f32_e32 v29, 0x42800000, v71
	v_mul_f32_e32 v49, 0x42800000, v72
	ds_write2_b32 v40, v29, v49 offset0:140 offset1:206
	s_add_i32 s0, s31, s5
	s_sext_i32_i16 s5, s0
	s_bfe_u32 s5, s5, 0x70018
	s_add_i32 s5, s0, s5
	s_sext_i32_i16 s6, s5
	s_and_b32 s5, s5, 0xff80
	s_sub_i32 s0, s0, s5
	s_lshl_b32 s6, s6, 1
	s_sext_i32_i16 s0, s0
	v_mul_f32_e32 v29, 0x42800000, v73
	v_mul_f32_e32 v49, 0x42800000, v74
	ds_write2_b32 v41, v29, v49 offset0:16 offset1:82
	v_mul_f32_e32 v29, 0x42800000, v75
	v_mul_f32_e32 v49, 0x42800000, v76
	ds_write2_b32 v41, v29, v49 offset0:148 offset1:214
	v_mul_f32_e32 v29, 0x42800000, v77
	v_mul_f32_e32 v49, 0x42800000, v78
	ds_write2_b32 v42, v29, v49 offset0:24 offset1:90
	v_mul_f32_e32 v29, 0x42800000, v79
	v_mul_f32_e32 v49, 0x42800000, v80
	ds_write2_b32 v42, v29, v49 offset0:156 offset1:222
	s_and_b32 s6, s6, 0xffffff00
	s_add_i32 s0, s40, s0
	s_add_i32 s0, s0, s6
	s_mov_b32 s5, s1
	v_mul_f32_e32 v29, 0x42800000, v81
	v_mul_f32_e32 v49, 0x42800000, v82
	ds_write2_b32 v43, v29, v49 offset0:32 offset1:98
	v_mul_f32_e32 v29, 0x42800000, v83
	v_mul_f32_e32 v49, 0x42800000, v84
	ds_write2_b32 v43, v29, v49 offset0:164 offset1:230
	v_mul_f32_e32 v29, 0x42800000, v85
	v_mul_f32_e32 v49, 0x42800000, v86
	ds_write2_b32 v44, v29, v49 offset0:40 offset1:106
	v_mul_f32_e32 v29, 0x42800000, v60
	v_mul_f32_e32 v49, 0x42800000, v61
	ds_write2_b32 v44, v29, v49 offset0:172 offset1:238
	v_add_u32_e32 v84, s0, v32
	v_ashrrev_i32_e32 v85, 31, v84
	v_lshlrev_b64 v[84:85], 10, v[84:85]
	v_mul_f32_e32 v29, 0x42800000, v62
	v_mul_f32_e32 v49, 0x42800000, v50
	ds_write2_b32 v45, v29, v49 offset0:48 offset1:114
	v_mul_f32_e32 v29, 0x42800000, v51
	v_mul_f32_e32 v49, 0x42800000, v52
	ds_write2_b32 v45, v29, v49 offset0:180 offset1:246
	v_mul_f32_e32 v29, 0x42800000, v53
	v_mul_f32_e32 v49, 0x42800000, v54
	ds_write2_b32 v46, v29, v49 offset0:56 offset1:122
	v_mov_b32_e32 v49, 0
	v_mov_b32_e32 v50, 0
	v_mul_f32_e32 v29, 0x42800000, v48
	v_mul_f32_e32 v28, 0x42800000, v28
	ds_write2_b32 v46, v29, v28 offset0:188 offset1:254
	s_waitcnt lgkmcnt(0)
	ds_read2_b32 v[52:53], v33 offset1:16
	ds_read2_b32 v[54:55], v33 offset0:33 offset1:49
	ds_read2_b32 v[56:57], v33 offset0:66 offset1:82
	ds_read2_b32 v[58:59], v33 offset0:99 offset1:115
	ds_read2_b32 v[60:61], v33 offset0:132 offset1:148
	ds_read2_b32 v[62:63], v33 offset0:165 offset1:181
	ds_read2_b32 v[64:65], v33 offset0:198 offset1:214
	ds_read2_b32 v[66:67], v33 offset0:231 offset1:247
	ds_read2_b32 v[68:69], v47 offset0:8 offset1:24
	ds_read2_b32 v[70:71], v47 offset0:41 offset1:57
	ds_read2_b32 v[72:73], v47 offset0:74 offset1:90
	ds_read2_b32 v[74:75], v47 offset0:107 offset1:123
	ds_read2_b32 v[76:77], v47 offset0:140 offset1:156
	ds_read2_b32 v[78:79], v47 offset0:173 offset1:189
	v_mov_b32_e32 v48, 0
	ds_read2_b32 v[80:81], v47 offset0:206 offset1:222
	ds_read2_b32 v[82:83], v47 offset0:239 offset1:255
	v_mov_b32_e32 v51, 0
	s_waitcnt lgkmcnt(14)
	v_cvt_pk_fp8_f32 v48, v52, v54
	s_waitcnt lgkmcnt(10)
	v_cvt_pk_fp8_f32 v49, v60, v62
	s_waitcnt lgkmcnt(6)
	v_cvt_pk_fp8_f32 v50, v68, v70
	s_waitcnt lgkmcnt(2)
	v_cvt_pk_fp8_f32 v51, v76, v78
	v_cvt_pk_fp8_f32 v48, v56, v58 op_sel:[0,0,1]
	v_cvt_pk_fp8_f32 v49, v64, v66 op_sel:[0,0,1]
	v_cvt_pk_fp8_f32 v50, v72, v74 op_sel:[0,0,1]
	s_waitcnt lgkmcnt(0)
	v_cvt_pk_fp8_f32 v51, v80, v82 op_sel:[0,0,1]
	v_lshl_add_u64 v[28:29], v[18:19], 0, s[4:5]
	v_lshl_add_u64 v[84:85], v[28:29], 0, v[84:85]
	v_add_u32_e32 v52, s0, v34
	global_store_dwordx4 v[84:85], v[48:51], off nt
	s_nop 1
	v_mov_b32_e32 v48, 0
	v_mov_b32_e32 v49, 0
	v_mov_b32_e32 v50, 0
	v_mov_b32_e32 v51, 0
	v_cvt_pk_fp8_f32 v48, v53, v55
	v_cvt_pk_fp8_f32 v49, v61, v63
	v_cvt_pk_fp8_f32 v50, v69, v71
	v_cvt_pk_fp8_f32 v51, v77, v79
	v_cvt_pk_fp8_f32 v48, v57, v59 op_sel:[0,0,1]
	v_cvt_pk_fp8_f32 v49, v65, v67 op_sel:[0,0,1]
	v_cvt_pk_fp8_f32 v50, v73, v75 op_sel:[0,0,1]
	v_cvt_pk_fp8_f32 v51, v81, v83 op_sel:[0,0,1]
	v_ashrrev_i32_e32 v53, 31, v52
	v_lshlrev_b64 v[52:53], 10, v[52:53]
	v_lshl_add_u64 v[28:29], v[28:29], 0, v[52:53]
	global_store_dwordx4 v[28:29], v[48:51], off nt
	s_waitcnt lgkmcnt(0)

; #define LDS_WAIT() asm volatile("s_waitcnt lgkmcnt(0)" ::: "memory")
; __device__ __forceinline__ void tr_item(const float* W, int ld, int K, int nblk, int item, bf16* WT, bool gu, LAS float* scr, int lane) {
;     const int kb = item / nblk, nb = item % nblk, k0 = 64 * kb, n0 = 32 * nb;
;     int drow0 = n0;
;     if (gu) { const int bj = n0 / FF, j = n0 - bj * FF; drow0 = 256 * (j / 128) + 128 * bj + (j % 128); }
;     { float t_[32];
; #pragma unroll
;       for (int i = 0; i < 32; ++i) t_[i] = W[(size_t)(k0 + 2 * i + (lane >> 5)) * ld + n0 + (lane & 31)];
; #pragma unroll
;       for (int i = 0; i < 32; ++i) scr[(2 * i + (lane >> 5)) * 33 + (lane & 31)] = t_[i]; }
;     LDS_WAIT(); asm volatile("" ::: "memory");
; __device__ __forceinline__ void convert_items(Frame& F, const Args& a, int lo, int hi, int w, int nw) {
;     ...
;         if (r < I_SO) { tr_item(a.in[12], D, D, 32, r, (bf16*)(F.ws + WS_WSWAOUT), false, scr, lane); continue; } r -= I_SO;
.LBB0_1347:
	s_andn2_b64 vcc, exec, s[4:5]
	s_cbranch_vccnz .LBB0_1349
	s_add_i32 s0, s12, 0x2000
	s_and_b32 s5, s0, 0x1ffc0
	s_and_b32 s4, s9, 0x3e0
	v_add_u32_e32 v28, s5, v30
	s_lshl_b32 s0, s4, 2
	v_ashrrev_i32_e32 v29, 31, v28
	v_lshl_add_u64 v[48:49], v[8:9], 0, s[0:1]
	v_lshlrev_b64 v[28:29], 12, v[28:29]
	v_lshl_add_u64 v[28:29], v[48:49], 0, v[28:29]
	v_add_co_u32_e32 v48, vcc, 0x2000, v28
	global_load_dword v50, v[28:29], off nt
	s_nop 0
	v_addc_co_u32_e32 v49, vcc, 0, v29, vcc
	global_load_dword v51, v[48:49], off nt
	v_add_co_u32_e32 v48, vcc, 0x4000, v28
	s_lshl_b32 s0, s5, 1
	s_nop 0
	v_addc_co_u32_e32 v49, vcc, 0, v29, vcc
	global_load_dword v52, v[48:49], off nt
	v_add_co_u32_e32 v48, vcc, 0x6000, v28
	s_nop 1
	v_addc_co_u32_e32 v49, vcc, 0, v29, vcc
	global_load_dword v53, v[48:49], off nt
	v_add_co_u32_e32 v48, vcc, 0x8000, v28
	s_nop 1
	v_addc_co_u32_e32 v49, vcc, 0, v29, vcc
	global_load_dword v54, v[48:49], off nt
	v_add_co_u32_e32 v48, vcc, 0xa000, v28
	s_nop 1
	v_addc_co_u32_e32 v49, vcc, 0, v29, vcc
	global_load_dword v55, v[48:49], off nt
	v_add_co_u32_e32 v48, vcc, 0xc000, v28
	s_nop 1
	v_addc_co_u32_e32 v49, vcc, 0, v29, vcc
	global_load_dword v56, v[48:49], off nt
	v_add_co_u32_e32 v48, vcc, 0xe000, v28
	s_nop 1
	v_addc_co_u32_e32 v49, vcc, 0, v29, vcc
	global_load_dword v57, v[48:49], off nt
	v_add_co_u32_e32 v48, vcc, 0x10000, v28
	s_nop 1
	v_addc_co_u32_e32 v49, vcc, 0, v29, vcc
	global_load_dword v58, v[48:49], off nt
	v_add_co_u32_e32 v48, vcc, 0x12000, v28
	s_nop 1
	v_addc_co_u32_e32 v49, vcc, 0, v29, vcc
	global_load_dword v59, v[48:49], off nt
	v_add_co_u32_e32 v48, vcc, 0x14000, v28
	s_nop 1
	v_addc_co_u32_e32 v49, vcc, 0, v29, vcc
	global_load_dword v60, v[48:49], off nt
	v_add_co_u32_e32 v48, vcc, 0x16000, v28
	s_nop 1
	v_addc_co_u32_e32 v49, vcc, 0, v29, vcc
	global_load_dword v61, v[48:49], off nt
	v_add_co_u32_e32 v48, vcc, 0x18000, v28
	s_nop 1
	v_addc_co_u32_e32 v49, vcc, 0, v29, vcc
	global_load_dword v62, v[48:49], off nt
	v_add_co_u32_e32 v48, vcc, 0x1a000, v28
	s_nop 1
	v_addc_co_u32_e32 v49, vcc, 0, v29, vcc
	global_load_dword v63, v[48:49], off nt
	v_add_co_u32_e32 v48, vcc, 0x1c000, v28
	s_nop 1
	v_addc_co_u32_e32 v49, vcc, 0, v29, vcc
	global_load_dword v64, v[48:49], off nt
	v_add_co_u32_e32 v48, vcc, 0x1e000, v28
	s_nop 1
	v_addc_co_u32_e32 v49, vcc, 0, v29, vcc
	global_load_dword v65, v[48:49], off nt
	v_add_co_u32_e32 v48, vcc, 0x20000, v28
	s_nop 1
	v_addc_co_u32_e32 v49, vcc, 0, v29, vcc
	global_load_dword v66, v[48:49], off nt
	v_add_co_u32_e32 v48, vcc, 0x22000, v28
	s_nop 1
	v_addc_co_u32_e32 v49, vcc, 0, v29, vcc
	global_load_dword v67, v[48:49], off nt
	v_add_co_u32_e32 v48, vcc, 0x24000, v28
	s_nop 1
	v_addc_co_u32_e32 v49, vcc, 0, v29, vcc
	global_load_dword v68, v[48:49], off nt
	v_add_co_u32_e32 v48, vcc, 0x26000, v28
	s_nop 1
	v_addc_co_u32_e32 v49, vcc, 0, v29, vcc
	global_load_dword v69, v[48:49], off nt
	v_add_co_u32_e32 v48, vcc, 0x28000, v28
	s_nop 1
	v_addc_co_u32_e32 v49, vcc, 0, v29, vcc
	global_load_dword v70, v[48:49], off nt
	v_add_co_u32_e32 v48, vcc, 0x2a000, v28
	s_nop 1
	v_addc_co_u32_e32 v49, vcc, 0, v29, vcc
	global_load_dword v71, v[48:49], off nt
	v_add_co_u32_e32 v48, vcc, 0x2c000, v28
	s_nop 1
	v_addc_co_u32_e32 v49, vcc, 0, v29, vcc
	global_load_dword v72, v[48:49], off nt
	v_add_co_u32_e32 v48, vcc, 0x2e000, v28
	s_nop 1
	v_addc_co_u32_e32 v49, vcc, 0, v29, vcc
	global_load_dword v73, v[48:49], off nt
	v_add_co_u32_e32 v48, vcc, 0x30000, v28
	s_nop 1
	v_addc_co_u32_e32 v49, vcc, 0, v29, vcc
	global_load_dword v74, v[48:49], off nt
	v_add_co_u32_e32 v48, vcc, 0x32000, v28
	s_nop 1
	v_addc_co_u32_e32 v49, vcc, 0, v29, vcc
	global_load_dword v75, v[48:49], off nt
	v_add_co_u32_e32 v48, vcc, 0x34000, v28
	s_nop 1
	v_addc_co_u32_e32 v49, vcc, 0, v29, vcc
	global_load_dword v76, v[48:49], off nt
	v_add_co_u32_e32 v48, vcc, 0x36000, v28
	s_nop 1
	v_addc_co_u32_e32 v49, vcc, 0, v29, vcc
	global_load_dword v77, v[48:49], off nt
	v_add_co_u32_e32 v48, vcc, 0x38000, v28
	s_nop 1
	v_addc_co_u32_e32 v49, vcc, 0, v29, vcc
	global_load_dword v78, v[48:49], off nt
	v_add_co_u32_e32 v48, vcc, 0x3a000, v28
	s_nop 1
	v_addc_co_u32_e32 v49, vcc, 0, v29, vcc
	global_load_dword v79, v[48:49], off nt
	v_add_co_u32_e32 v48, vcc, 0x3c000, v28
	s_nop 1
	v_addc_co_u32_e32 v49, vcc, 0, v29, vcc
	v_add_co_u32_e32 v28, vcc, 0x3e000, v28
	global_load_dword v48, v[48:49], off nt
	s_nop 0
	v_addc_co_u32_e32 v29, vcc, 0, v29, vcc
	global_load_dword v28, v[28:29], off nt
	s_waitcnt vmcnt(0)
	ds_write2_b32 v31, v50, v51 offset1:66
	ds_write2_b32 v31, v52, v53 offset0:132 offset1:198
	ds_write2_b32 v40, v54, v55 offset0:8 offset1:74
	ds_write2_b32 v40, v56, v57 offset0:140 offset1:206
	ds_write2_b32 v41, v58, v59 offset0:16 offset1:82
	ds_write2_b32 v41, v60, v61 offset0:148 offset1:214
	ds_write2_b32 v42, v62, v63 offset0:24 offset1:90
	ds_write2_b32 v42, v64, v65 offset0:156 offset1:222
	ds_write2_b32 v43, v66, v67 offset0:32 offset1:98
	ds_write2_b32 v43, v68, v69 offset0:164 offset1:230
	ds_write2_b32 v44, v70, v71 offset0:40 offset1:106
	ds_write2_b32 v44, v72, v73 offset0:172 offset1:238
	ds_write2_b32 v45, v74, v75 offset0:48 offset1:114
	ds_write2_b32 v45, v76, v77 offset0:180 offset1:246
	ds_write2_b32 v46, v78, v79 offset0:56 offset1:122
	ds_write2_b32 v46, v48, v28 offset0:188 offset1:254
	s_waitcnt lgkmcnt(0)
; #define GAS __attribute__((address_space(1)))
; #define LAS __attribute__((address_space(3)))
; #define LDS_WAIT() asm volatile("s_waitcnt lgkmcnt(0)" ::: "memory")
; __device__ __forceinline__ unsigned pk2(float lo, float hi) { return f2bf(lo) | (f2bf(hi) << 16); }
; __device__ __forceinline__ void tr_item(const float* W, int ld, int K, int nblk, int item, bf16* WT, bool gu, LAS float* scr, int lane) {
;     ...
;     const int c = lane & 7;
; #pragma unroll
;     for (int j = 0; j < 4; ++j) { const int n = (lane >> 3) + 8 * j; const LAS float* s = scr + (8 * c) * 33 + n;
;         v4u o; o.x = pk2(s[0 * 33], s[1 * 33]); o.y = pk2(s[2 * 33], s[3 * 33]); o.z = pk2(s[4 * 33], s[5 * 33]); o.w = pk2(s[6 * 33], s[7 * 33]);
;         *(GAS v4u*)(WT + (size_t)(drow0 + n) * K + k0 + 8 * c) = o; }
;     LDS_WAIT(); asm volatile("" ::: "memory");
	ds_read2_b32 v[52:53], v36 offset0:33 offset1:41
	ds_read2_b32 v[54:55], v36 offset1:8
	ds_read2_b32 v[56:57], v36 offset0:66 offset1:74
	ds_read2_b32 v[58:59], v36 offset0:99 offset1:107
	ds_read2_b32 v[60:61], v36 offset0:132 offset1:140
	ds_read2_b32 v[62:63], v36 offset0:165 offset1:173
	ds_read2_b32 v[64:65], v36 offset0:198 offset1:206
	ds_read2_b32 v[66:67], v36 offset0:231 offset1:239
	s_waitcnt lgkmcnt(7)
	v_bfe_u32 v49, v52, 16, 1
	s_waitcnt lgkmcnt(6)
	v_bfe_u32 v48, v54, 16, 1
	v_add3_u32 v48, v54, v48, s15
	v_lshrrev_b32_e32 v48, 16, v48
	v_add3_u32 v49, v52, v49, s15
	v_and_or_b32 v48, v49, s16, v48
	s_waitcnt lgkmcnt(5)
	v_bfe_u32 v49, v56, 16, 1
	v_add3_u32 v49, v56, v49, s15
	s_waitcnt lgkmcnt(4)
	v_bfe_u32 v50, v58, 16, 1
	v_lshrrev_b32_e32 v49, 16, v49
	v_add3_u32 v50, v58, v50, s15
	v_and_or_b32 v49, v50, s16, v49
	s_waitcnt lgkmcnt(3)
	v_bfe_u32 v50, v60, 16, 1
	v_add3_u32 v50, v60, v50, s15
	s_waitcnt lgkmcnt(2)
	v_bfe_u32 v51, v62, 16, 1
	v_lshrrev_b32_e32 v50, 16, v50
	v_add3_u32 v51, v62, v51, s15
	v_and_or_b32 v50, v51, s16, v50
	s_waitcnt lgkmcnt(1)
	v_bfe_u32 v51, v64, 16, 1
	v_add_u32_e32 v68, s4, v35
	v_add3_u32 v51, v64, v51, s15
	s_waitcnt lgkmcnt(0)
	v_bfe_u32 v52, v66, 16, 1
	v_ashrrev_i32_e32 v69, 31, v68
	v_lshl_add_u64 v[28:29], v[20:21], 0, s[0:1]
	v_lshrrev_b32_e32 v51, 16, v51
	v_add3_u32 v52, v66, v52, s15
	v_lshlrev_b64 v[68:69], 11, v[68:69]
	v_and_or_b32 v51, v52, s16, v51
	v_lshl_add_u64 v[68:69], v[28:29], 0, v[68:69]
	global_store_dwordx4 v[68:69], v[48:51], off nt
	v_bfe_u32 v52, v67, 16, 1
	v_add3_u32 v52, v67, v52, s15
	v_bfe_u32 v48, v55, 16, 1
	v_add3_u32 v48, v55, v48, s15
	v_bfe_u32 v49, v53, 16, 1
	v_lshrrev_b32_e32 v48, 16, v48
	v_add3_u32 v49, v53, v49, s15
	v_and_or_b32 v48, v49, s16, v48
	v_bfe_u32 v49, v57, 16, 1
	v_add3_u32 v49, v57, v49, s15
	v_bfe_u32 v50, v59, 16, 1
	v_lshrrev_b32_e32 v49, 16, v49
	v_add3_u32 v50, v59, v50, s15
	v_and_or_b32 v49, v50, s16, v49
	v_bfe_u32 v50, v61, 16, 1
	v_add3_u32 v50, v61, v50, s15
	v_bfe_u32 v51, v63, 16, 1
	v_lshrrev_b32_e32 v50, 16, v50
	v_add3_u32 v51, v63, v51, s15
	v_and_or_b32 v50, v51, s16, v50
	v_bfe_u32 v51, v65, 16, 1
	v_add3_u32 v51, v65, v51, s15
	v_lshrrev_b32_e32 v51, 16, v51
	v_and_or_b32 v51, v52, s16, v51
	v_add_u32_e32 v52, s4, v37
	v_ashrrev_i32_e32 v53, 31, v52
	v_lshlrev_b64 v[52:53], 11, v[52:53]
	v_lshl_add_u64 v[52:53], v[28:29], 0, v[52:53]
	global_store_dwordx4 v[52:53], v[48:51], off nt
	ds_read2_b32 v[52:53], v36 offset0:49 offset1:57
	ds_read2_b32 v[54:55], v36 offset0:16 offset1:24
	ds_read2_b32 v[56:57], v36 offset0:82 offset1:90
	ds_read2_b32 v[58:59], v36 offset0:115 offset1:123
	ds_read2_b32 v[60:61], v36 offset0:148 offset1:156
	ds_read2_b32 v[62:63], v36 offset0:181 offset1:189
	ds_read2_b32 v[64:65], v36 offset0:214 offset1:222
	ds_read2_b32 v[66:67], v36 offset0:247 offset1:255
	s_waitcnt lgkmcnt(7)
	v_bfe_u32 v49, v52, 16, 1
	s_waitcnt lgkmcnt(6)
	v_bfe_u32 v48, v54, 16, 1
	v_add3_u32 v48, v54, v48, s15
	v_lshrrev_b32_e32 v48, 16, v48
	v_add3_u32 v49, v52, v49, s15
	v_and_or_b32 v48, v49, s16, v48
	s_waitcnt lgkmcnt(5)
	v_bfe_u32 v49, v56, 16, 1
	v_add3_u32 v49, v56, v49, s15
	s_waitcnt lgkmcnt(4)
	v_bfe_u32 v50, v58, 16, 1
	v_lshrrev_b32_e32 v49, 16, v49
	v_add3_u32 v50, v58, v50, s15
	v_and_or_b32 v49, v50, s16, v49
	s_waitcnt lgkmcnt(3)
	v_bfe_u32 v50, v60, 16, 1
	v_add3_u32 v50, v60, v50, s15
	s_waitcnt lgkmcnt(2)
	v_bfe_u32 v51, v62, 16, 1
	v_lshrrev_b32_e32 v50, 16, v50
	v_add3_u32 v51, v62, v51, s15
	v_and_or_b32 v50, v51, s16, v50
	s_waitcnt lgkmcnt(1)
	v_bfe_u32 v51, v64, 16, 1
	v_add_u32_e32 v68, s4, v38
	v_add3_u32 v51, v64, v51, s15
	s_waitcnt lgkmcnt(0)
	v_bfe_u32 v52, v66, 16, 1
	v_ashrrev_i32_e32 v69, 31, v68
	v_lshrrev_b32_e32 v51, 16, v51
	v_add3_u32 v52, v66, v52, s15
	v_lshlrev_b64 v[68:69], 11, v[68:69]
	v_and_or_b32 v51, v52, s16, v51
	v_lshl_add_u64 v[68:69], v[28:29], 0, v[68:69]
	global_store_dwordx4 v[68:69], v[48:51], off nt
	v_bfe_u32 v52, v67, 16, 1
	v_add3_u32 v52, v67, v52, s15
	v_bfe_u32 v48, v55, 16, 1
	v_add3_u32 v48, v55, v48, s15
	v_bfe_u32 v49, v53, 16, 1
	v_lshrrev_b32_e32 v48, 16, v48
	v_add3_u32 v49, v53, v49, s15
	v_and_or_b32 v48, v49, s16, v48
	v_bfe_u32 v49, v57, 16, 1
	v_add3_u32 v49, v57, v49, s15
	v_bfe_u32 v50, v59, 16, 1
	v_lshrrev_b32_e32 v49, 16, v49
	v_add3_u32 v50, v59, v50, s15
	v_and_or_b32 v49, v50, s16, v49
	v_bfe_u32 v50, v61, 16, 1
	v_add3_u32 v50, v61, v50, s15
	v_bfe_u32 v51, v63, 16, 1
	v_lshrrev_b32_e32 v50, 16, v50
	v_add3_u32 v51, v63, v51, s15
	v_and_or_b32 v50, v51, s16, v50
	v_bfe_u32 v51, v65, 16, 1
	v_add3_u32 v51, v65, v51, s15
	v_lshrrev_b32_e32 v51, 16, v51
	v_and_or_b32 v51, v52, s16, v51
	v_add_u32_e32 v52, s4, v39
	v_ashrrev_i32_e32 v53, 31, v52
	v_lshlrev_b64 v[52:53], 11, v[52:53]
	v_lshl_add_u64 v[28:29], v[28:29], 0, v[52:53]
	global_store_dwordx4 v[28:29], v[48:51], off nt
	s_waitcnt lgkmcnt(0)

; #define LDS_WAIT() asm volatile("s_waitcnt lgkmcnt(0)" ::: "memory")
; __device__ __forceinline__ void tr_item(const float* W, int ld, int K, int nblk, int item, bf16* WT, bool gu, LAS float* scr, int lane) {
;     const int kb = item / nblk, nb = item % nblk, k0 = 64 * kb, n0 = 32 * nb;
;     int drow0 = n0;
;     if (gu) { const int bj = n0 / FF, j = n0 - bj * FF; drow0 = 256 * (j / 128) + 128 * bj + (j % 128); }
;     { float t_[32];
; #pragma unroll
;       for (int i = 0; i < 32; ++i) t_[i] = W[(size_t)(k0 + 2 * i + (lane >> 5)) * ld + n0 + (lane & 31)];
; #pragma unroll
;       for (int i = 0; i < 32; ++i) scr[(2 * i + (lane >> 5)) * 33 + (lane & 31)] = t_[i]; }
;     LDS_WAIT(); asm volatile("" ::: "memory");
; __device__ __forceinline__ void convert_items(Frame& F, const Args& a, int lo, int hi, int w, int nw) {
;     ...
;         if (r < I_SI) { tr_item(a.in[10], D + 512, D, 48, r, (bf16*)(F.ws + WS_WSWAIN), false, scr, lane); continue; } r -= I_SI;
.LBB0_1350:
	s_andn2_b64 vcc, exec, s[4:5]
	s_cbranch_vccnz .LBB0_1352
	s_add_i32 s0, s8, 0xf800
	s_and_b32 s4, s0, 0xffff
	s_mul_i32 s4, s4, 0xaaab
	s_lshr_b32 s5, s4, 21
	s_mul_i32 s4, s5, 48
	s_sub_i32 s0, s0, s4
	s_lshl_b32 s0, s0, 5
	s_and_b32 s4, s0, 0xffe0
	s_lshl_b32 s0, s4, 2
	v_lshl_add_u32 v50, s5, 6, v30
	v_lshl_add_u64 v[28:29], v[10:11], 0, s[0:1]
	v_mad_i64_i32 v[48:49], s[6:7], v50, s17, v[28:29]
	global_load_dword v51, v[48:49], off nt
	v_add_u32_e32 v48, 2, v50
	v_mad_i64_i32 v[48:49], s[6:7], v48, s17, v[28:29]
	global_load_dword v52, v[48:49], off nt
	v_add_u32_e32 v48, 4, v50
	v_mad_i64_i32 v[48:49], s[6:7], v48, s17, v[28:29]
	global_load_dword v53, v[48:49], off nt
	v_add_u32_e32 v48, 6, v50
	v_mad_i64_i32 v[48:49], s[6:7], v48, s17, v[28:29]
	global_load_dword v54, v[48:49], off nt
	v_add_u32_e32 v48, 8, v50
	v_mad_i64_i32 v[48:49], s[6:7], v48, s17, v[28:29]
	global_load_dword v55, v[48:49], off nt
	v_add_u32_e32 v48, 10, v50
	v_mad_i64_i32 v[48:49], s[6:7], v48, s17, v[28:29]
	global_load_dword v56, v[48:49], off nt
	v_add_u32_e32 v48, 12, v50
	v_mad_i64_i32 v[48:49], s[6:7], v48, s17, v[28:29]
	global_load_dword v57, v[48:49], off nt
	v_add_u32_e32 v48, 14, v50
	v_mad_i64_i32 v[48:49], s[6:7], v48, s17, v[28:29]
	global_load_dword v58, v[48:49], off nt
	v_add_u32_e32 v48, 16, v50
	v_mad_i64_i32 v[48:49], s[6:7], v48, s17, v[28:29]
	global_load_dword v59, v[48:49], off nt
	v_add_u32_e32 v48, 18, v50
	v_mad_i64_i32 v[48:49], s[6:7], v48, s17, v[28:29]
	global_load_dword v60, v[48:49], off nt
	v_add_u32_e32 v48, 20, v50
	v_mad_i64_i32 v[48:49], s[6:7], v48, s17, v[28:29]
	global_load_dword v61, v[48:49], off nt
	v_add_u32_e32 v48, 22, v50
	v_mad_i64_i32 v[48:49], s[6:7], v48, s17, v[28:29]
	global_load_dword v62, v[48:49], off nt
	v_add_u32_e32 v48, 24, v50
	v_mad_i64_i32 v[48:49], s[6:7], v48, s17, v[28:29]
	global_load_dword v63, v[48:49], off nt
	v_add_u32_e32 v48, 26, v50
	v_mad_i64_i32 v[48:49], s[6:7], v48, s17, v[28:29]
	global_load_dword v64, v[48:49], off nt
	v_add_u32_e32 v48, 28, v50
	v_mad_i64_i32 v[48:49], s[6:7], v48, s17, v[28:29]
	global_load_dword v65, v[48:49], off nt
	v_add_u32_e32 v48, 30, v50
	v_mad_i64_i32 v[48:49], s[6:7], v48, s17, v[28:29]
	global_load_dword v66, v[48:49], off nt
	v_add_u32_e32 v48, 32, v50
	v_mad_i64_i32 v[48:49], s[6:7], v48, s17, v[28:29]
	global_load_dword v67, v[48:49], off nt
	v_add_u32_e32 v48, 34, v50
	v_mad_i64_i32 v[48:49], s[6:7], v48, s17, v[28:29]
	global_load_dword v68, v[48:49], off nt
	v_add_u32_e32 v48, 36, v50
	v_mad_i64_i32 v[48:49], s[6:7], v48, s17, v[28:29]
	global_load_dword v69, v[48:49], off nt
	v_add_u32_e32 v48, 38, v50
	v_mad_i64_i32 v[48:49], s[6:7], v48, s17, v[28:29]
	global_load_dword v70, v[48:49], off nt
	v_add_u32_e32 v48, 40, v50
	v_mad_i64_i32 v[48:49], s[6:7], v48, s17, v[28:29]
	global_load_dword v71, v[48:49], off nt
	v_add_u32_e32 v48, 42, v50
	v_mad_i64_i32 v[48:49], s[6:7], v48, s17, v[28:29]
	global_load_dword v72, v[48:49], off nt
	v_add_u32_e32 v48, 44, v50
	v_mad_i64_i32 v[48:49], s[6:7], v48, s17, v[28:29]
	global_load_dword v73, v[48:49], off nt
	v_add_u32_e32 v48, 46, v50
	v_mad_i64_i32 v[48:49], s[6:7], v48, s17, v[28:29]
	global_load_dword v74, v[48:49], off nt
	v_add_u32_e32 v48, 48, v50
	v_mad_i64_i32 v[48:49], s[6:7], v48, s17, v[28:29]
	global_load_dword v75, v[48:49], off nt
	v_add_u32_e32 v48, 50, v50
	v_mad_i64_i32 v[48:49], s[6:7], v48, s17, v[28:29]
	global_load_dword v76, v[48:49], off nt
	v_add_u32_e32 v48, 52, v50
	v_mad_i64_i32 v[48:49], s[6:7], v48, s17, v[28:29]
	global_load_dword v77, v[48:49], off nt
	v_add_u32_e32 v48, 54, v50
	v_mad_i64_i32 v[48:49], s[6:7], v48, s17, v[28:29]
	global_load_dword v78, v[48:49], off nt
	v_add_u32_e32 v48, 56, v50
	v_mad_i64_i32 v[48:49], s[6:7], v48, s17, v[28:29]
	global_load_dword v79, v[48:49], off nt
	v_add_u32_e32 v48, 58, v50
	v_mad_i64_i32 v[48:49], s[6:7], v48, s17, v[28:29]
	global_load_dword v80, v[48:49], off nt
	v_add_u32_e32 v48, 60, v50
	v_mad_i64_i32 v[48:49], s[6:7], v48, s17, v[28:29]
	global_load_dword v48, v[48:49], off nt
	v_add_u32_e32 v49, 62, v50
	v_mad_i64_i32 v[28:29], s[6:7], v49, s17, v[28:29]
	global_load_dword v28, v[28:29], off nt
	s_waitcnt vmcnt(0)
	ds_write2_b32 v31, v51, v52 offset1:66
	ds_write2_b32 v31, v53, v54 offset0:132 offset1:198
	ds_write2_b32 v40, v55, v56 offset0:8 offset1:74
	ds_write2_b32 v40, v57, v58 offset0:140 offset1:206
	ds_write2_b32 v41, v59, v60 offset0:16 offset1:82
	ds_write2_b32 v41, v61, v62 offset0:148 offset1:214
	ds_write2_b32 v42, v63, v64 offset0:24 offset1:90
	ds_write2_b32 v42, v65, v66 offset0:156 offset1:222
	ds_write2_b32 v43, v67, v68 offset0:32 offset1:98
	ds_write2_b32 v43, v69, v70 offset0:164 offset1:230
	ds_write2_b32 v44, v71, v72 offset0:40 offset1:106
	ds_write2_b32 v44, v73, v74 offset0:172 offset1:238
	ds_write2_b32 v45, v75, v76 offset0:48 offset1:114
	ds_write2_b32 v45, v77, v78 offset0:180 offset1:246
	ds_write2_b32 v46, v79, v80 offset0:56 offset1:122
	ds_write2_b32 v46, v48, v28 offset0:188 offset1:254
	s_waitcnt lgkmcnt(0)
; #define GAS __attribute__((address_space(1)))
; #define LAS __attribute__((address_space(3)))
; #define LDS_WAIT() asm volatile("s_waitcnt lgkmcnt(0)" ::: "memory")
; __device__ __forceinline__ unsigned pk2(float lo, float hi) { return f2bf(lo) | (f2bf(hi) << 16); }
; __device__ __forceinline__ void tr_item(const float* W, int ld, int K, int nblk, int item, bf16* WT, bool gu, LAS float* scr, int lane) {
;     ...
;     const int c = lane & 7;
; #pragma unroll
;     for (int j = 0; j < 4; ++j) { const int n = (lane >> 3) + 8 * j; const LAS float* s = scr + (8 * c) * 33 + n;
;         v4u o; o.x = pk2(s[0 * 33], s[1 * 33]); o.y = pk2(s[2 * 33], s[3 * 33]); o.z = pk2(s[4 * 33], s[5 * 33]); o.w = pk2(s[6 * 33], s[7 * 33]);
;         *(GAS v4u*)(WT + (size_t)(drow0 + n) * K + k0 + 8 * c) = o; }
;     LDS_WAIT(); asm volatile("" ::: "memory");
	ds_read2_b32 v[52:53], v36 offset0:33 offset1:41
	ds_read2_b32 v[54:55], v36 offset1:8
	ds_read2_b32 v[56:57], v36 offset0:66 offset1:74
	ds_read2_b32 v[58:59], v36 offset0:99 offset1:107
	ds_read2_b32 v[60:61], v36 offset0:132 offset1:140
	ds_read2_b32 v[62:63], v36 offset0:165 offset1:173
	ds_read2_b32 v[64:65], v36 offset0:198 offset1:206
	ds_read2_b32 v[66:67], v36 offset0:231 offset1:239
	s_waitcnt lgkmcnt(7)
	v_bfe_u32 v49, v52, 16, 1
	s_waitcnt lgkmcnt(6)
	v_bfe_u32 v48, v54, 16, 1
	v_add3_u32 v48, v54, v48, s15
	v_lshrrev_b32_e32 v48, 16, v48
	v_add3_u32 v49, v52, v49, s15
	v_and_or_b32 v48, v49, s16, v48
	s_waitcnt lgkmcnt(5)
	v_bfe_u32 v49, v56, 16, 1
	v_add3_u32 v49, v56, v49, s15
	s_waitcnt lgkmcnt(4)
	v_bfe_u32 v50, v58, 16, 1
	v_lshrrev_b32_e32 v49, 16, v49
	v_add3_u32 v50, v58, v50, s15
	v_and_or_b32 v49, v50, s16, v49
	s_waitcnt lgkmcnt(3)
	v_bfe_u32 v50, v60, 16, 1
	v_add3_u32 v50, v60, v50, s15
	s_waitcnt lgkmcnt(2)
	v_bfe_u32 v51, v62, 16, 1
	v_lshrrev_b32_e32 v50, 16, v50
	v_add3_u32 v51, v62, v51, s15
	v_and_or_b32 v50, v51, s16, v50
	s_waitcnt lgkmcnt(1)
	v_bfe_u32 v51, v64, 16, 1
	v_add_u32_e32 v68, s4, v35
	s_lshl_b32 s0, s5, 7
	v_add3_u32 v51, v64, v51, s15
	s_waitcnt lgkmcnt(0)
	v_bfe_u32 v52, v66, 16, 1
	v_ashrrev_i32_e32 v69, 31, v68
	v_lshl_add_u64 v[28:29], v[22:23], 0, s[0:1]
	v_lshrrev_b32_e32 v51, 16, v51
	v_add3_u32 v52, v66, v52, s15
	v_lshlrev_b64 v[68:69], 11, v[68:69]
	v_and_or_b32 v51, v52, s16, v51
	v_lshl_add_u64 v[68:69], v[28:29], 0, v[68:69]
	global_store_dwordx4 v[68:69], v[48:51], off nt
	v_bfe_u32 v52, v67, 16, 1
	v_add3_u32 v52, v67, v52, s15
	v_bfe_u32 v48, v55, 16, 1
	v_add3_u32 v48, v55, v48, s15
	v_bfe_u32 v49, v53, 16, 1
	v_lshrrev_b32_e32 v48, 16, v48
	v_add3_u32 v49, v53, v49, s15
	v_and_or_b32 v48, v49, s16, v48
	v_bfe_u32 v49, v57, 16, 1
	v_add3_u32 v49, v57, v49, s15
	v_bfe_u32 v50, v59, 16, 1
	v_lshrrev_b32_e32 v49, 16, v49
	v_add3_u32 v50, v59, v50, s15
	v_and_or_b32 v49, v50, s16, v49
	v_bfe_u32 v50, v61, 16, 1
	v_add3_u32 v50, v61, v50, s15
	v_bfe_u32 v51, v63, 16, 1
	v_lshrrev_b32_e32 v50, 16, v50
	v_add3_u32 v51, v63, v51, s15
	v_and_or_b32 v50, v51, s16, v50
	v_bfe_u32 v51, v65, 16, 1
	v_add3_u32 v51, v65, v51, s15
	v_lshrrev_b32_e32 v51, 16, v51
	v_and_or_b32 v51, v52, s16, v51
	v_add_u32_e32 v52, s4, v37
	v_ashrrev_i32_e32 v53, 31, v52
	v_lshlrev_b64 v[52:53], 11, v[52:53]
	v_lshl_add_u64 v[52:53], v[28:29], 0, v[52:53]
	global_store_dwordx4 v[52:53], v[48:51], off nt
	ds_read2_b32 v[52:53], v36 offset0:49 offset1:57
	ds_read2_b32 v[54:55], v36 offset0:16 offset1:24
	ds_read2_b32 v[56:57], v36 offset0:82 offset1:90
	ds_read2_b32 v[58:59], v36 offset0:115 offset1:123
	ds_read2_b32 v[60:61], v36 offset0:148 offset1:156
	ds_read2_b32 v[62:63], v36 offset0:181 offset1:189
	ds_read2_b32 v[64:65], v36 offset0:214 offset1:222
	ds_read2_b32 v[66:67], v36 offset0:247 offset1:255
	s_waitcnt lgkmcnt(7)
	v_bfe_u32 v49, v52, 16, 1
	s_waitcnt lgkmcnt(6)
	v_bfe_u32 v48, v54, 16, 1
	v_add3_u32 v48, v54, v48, s15
	v_lshrrev_b32_e32 v48, 16, v48
	v_add3_u32 v49, v52, v49, s15
	v_and_or_b32 v48, v49, s16, v48
	s_waitcnt lgkmcnt(5)
	v_bfe_u32 v49, v56, 16, 1
	v_add3_u32 v49, v56, v49, s15
	s_waitcnt lgkmcnt(4)
	v_bfe_u32 v50, v58, 16, 1
	v_lshrrev_b32_e32 v49, 16, v49
	v_add3_u32 v50, v58, v50, s15
	v_and_or_b32 v49, v50, s16, v49
	s_waitcnt lgkmcnt(3)
	v_bfe_u32 v50, v60, 16, 1
	v_add3_u32 v50, v60, v50, s15
	s_waitcnt lgkmcnt(2)
	v_bfe_u32 v51, v62, 16, 1
	v_lshrrev_b32_e32 v50, 16, v50
	v_add3_u32 v51, v62, v51, s15
	v_and_or_b32 v50, v51, s16, v50
	s_waitcnt lgkmcnt(1)
	v_bfe_u32 v51, v64, 16, 1
	v_add_u32_e32 v68, s4, v38
	v_add3_u32 v51, v64, v51, s15
	s_waitcnt lgkmcnt(0)
	v_bfe_u32 v52, v66, 16, 1
	v_ashrrev_i32_e32 v69, 31, v68
	v_lshrrev_b32_e32 v51, 16, v51
	v_add3_u32 v52, v66, v52, s15
	v_lshlrev_b64 v[68:69], 11, v[68:69]
	v_and_or_b32 v51, v52, s16, v51
	v_lshl_add_u64 v[68:69], v[28:29], 0, v[68:69]
	global_store_dwordx4 v[68:69], v[48:51], off nt
	v_bfe_u32 v52, v67, 16, 1
	v_add3_u32 v52, v67, v52, s15
	v_bfe_u32 v48, v55, 16, 1
	v_add3_u32 v48, v55, v48, s15
	v_bfe_u32 v49, v53, 16, 1
	v_lshrrev_b32_e32 v48, 16, v48
	v_add3_u32 v49, v53, v49, s15
	v_and_or_b32 v48, v49, s16, v48
	v_bfe_u32 v49, v57, 16, 1
	v_add3_u32 v49, v57, v49, s15
	v_bfe_u32 v50, v59, 16, 1
	v_lshrrev_b32_e32 v49, 16, v49
	v_add3_u32 v50, v59, v50, s15
	v_and_or_b32 v49, v50, s16, v49
	v_bfe_u32 v50, v61, 16, 1
	v_add3_u32 v50, v61, v50, s15
	v_bfe_u32 v51, v63, 16, 1
	v_lshrrev_b32_e32 v50, 16, v50
	v_add3_u32 v51, v63, v51, s15
	v_and_or_b32 v50, v51, s16, v50
	v_bfe_u32 v51, v65, 16, 1
	v_add3_u32 v51, v65, v51, s15
	v_lshrrev_b32_e32 v51, 16, v51
	v_and_or_b32 v51, v52, s16, v51
	v_add_u32_e32 v52, s4, v39
	v_ashrrev_i32_e32 v53, 31, v52
	v_lshlrev_b64 v[52:53], 11, v[52:53]
	v_lshl_add_u64 v[28:29], v[28:29], 0, v[52:53]
	global_store_dwordx4 v[28:29], v[48:51], off nt
	s_waitcnt lgkmcnt(0)

; #define LDS_WAIT() asm volatile("s_waitcnt lgkmcnt(0)" ::: "memory")
; __device__ __forceinline__ void tr_item(const float* W, int ld, int K, int nblk, int item, bf16* WT, bool gu, LAS float* scr, int lane) {
;     const int kb = item / nblk, nb = item % nblk, k0 = 64 * kb, n0 = 32 * nb;
;     int drow0 = n0;
;     if (gu) { const int bj = n0 / FF, j = n0 - bj * FF; drow0 = 256 * (j / 128) + 128 * bj + (j % 128); }
;     { float t_[32];
; #pragma unroll
;       for (int i = 0; i < 32; ++i) t_[i] = W[(size_t)(k0 + 2 * i + (lane >> 5)) * ld + n0 + (lane & 31)];
; #pragma unroll
;       for (int i = 0; i < 32; ++i) scr[(2 * i + (lane >> 5)) * 33 + (lane & 31)] = t_[i]; }
;     LDS_WAIT(); asm volatile("" ::: "memory");
; __device__ __forceinline__ void convert_items(Frame& F, const Args& a, int lo, int hi, int w, int nw) {
;     ...
;         if (r < I_FO) { tr_item(a.in[9], D, D, 32, r, (bf16*)(F.ws + WS_WFOXOUT), false, scr, lane); continue; } r -= I_FO;
.LBB0_1353:
	s_andn2_b64 vcc, exec, s[4:5]
	s_cbranch_vccnz .LBB0_1355
	s_add_i32 s0, s12, 0x2a00
	s_and_b32 s5, s0, 0x1ffc0
	s_and_b32 s4, s9, 0x3e0
	v_add_u32_e32 v28, s5, v30
	s_lshl_b32 s0, s4, 2
	v_ashrrev_i32_e32 v29, 31, v28
	v_lshl_add_u64 v[48:49], v[12:13], 0, s[0:1]
	v_lshlrev_b64 v[28:29], 12, v[28:29]
	v_lshl_add_u64 v[28:29], v[48:49], 0, v[28:29]
	v_add_co_u32_e32 v48, vcc, 0x2000, v28
	global_load_dword v50, v[28:29], off nt
	s_nop 0
	v_addc_co_u32_e32 v49, vcc, 0, v29, vcc
	global_load_dword v51, v[48:49], off nt
	v_add_co_u32_e32 v48, vcc, 0x4000, v28
	s_lshl_b32 s0, s5, 1
	s_nop 0
	v_addc_co_u32_e32 v49, vcc, 0, v29, vcc
	global_load_dword v52, v[48:49], off nt
	v_add_co_u32_e32 v48, vcc, 0x6000, v28
	s_nop 1
	v_addc_co_u32_e32 v49, vcc, 0, v29, vcc
	global_load_dword v53, v[48:49], off nt
	v_add_co_u32_e32 v48, vcc, 0x8000, v28
	s_nop 1
	v_addc_co_u32_e32 v49, vcc, 0, v29, vcc
	global_load_dword v54, v[48:49], off nt
	v_add_co_u32_e32 v48, vcc, 0xa000, v28
	s_nop 1
	v_addc_co_u32_e32 v49, vcc, 0, v29, vcc
	global_load_dword v55, v[48:49], off nt
	v_add_co_u32_e32 v48, vcc, 0xc000, v28
	s_nop 1
	v_addc_co_u32_e32 v49, vcc, 0, v29, vcc
	global_load_dword v56, v[48:49], off nt
	v_add_co_u32_e32 v48, vcc, 0xe000, v28
	s_nop 1
	v_addc_co_u32_e32 v49, vcc, 0, v29, vcc
	global_load_dword v57, v[48:49], off nt
	v_add_co_u32_e32 v48, vcc, 0x10000, v28
	s_nop 1
	v_addc_co_u32_e32 v49, vcc, 0, v29, vcc
	global_load_dword v58, v[48:49], off nt
	v_add_co_u32_e32 v48, vcc, 0x12000, v28
	s_nop 1
	v_addc_co_u32_e32 v49, vcc, 0, v29, vcc
	global_load_dword v59, v[48:49], off nt
	v_add_co_u32_e32 v48, vcc, 0x14000, v28
	s_nop 1
	v_addc_co_u32_e32 v49, vcc, 0, v29, vcc
	global_load_dword v60, v[48:49], off nt
	v_add_co_u32_e32 v48, vcc, 0x16000, v28
	s_nop 1
	v_addc_co_u32_e32 v49, vcc, 0, v29, vcc
	global_load_dword v61, v[48:49], off nt
	v_add_co_u32_e32 v48, vcc, 0x18000, v28
	s_nop 1
	v_addc_co_u32_e32 v49, vcc, 0, v29, vcc
	global_load_dword v62, v[48:49], off nt
	v_add_co_u32_e32 v48, vcc, 0x1a000, v28
	s_nop 1
	v_addc_co_u32_e32 v49, vcc, 0, v29, vcc
	global_load_dword v63, v[48:49], off nt
	v_add_co_u32_e32 v48, vcc, 0x1c000, v28
	s_nop 1
	v_addc_co_u32_e32 v49, vcc, 0, v29, vcc
	global_load_dword v64, v[48:49], off nt
	v_add_co_u32_e32 v48, vcc, 0x1e000, v28
	s_nop 1
	v_addc_co_u32_e32 v49, vcc, 0, v29, vcc
	global_load_dword v65, v[48:49], off nt
	v_add_co_u32_e32 v48, vcc, 0x20000, v28
	s_nop 1
	v_addc_co_u32_e32 v49, vcc, 0, v29, vcc
	global_load_dword v66, v[48:49], off nt
	v_add_co_u32_e32 v48, vcc, 0x22000, v28
	s_nop 1
	v_addc_co_u32_e32 v49, vcc, 0, v29, vcc
	global_load_dword v67, v[48:49], off nt
	v_add_co_u32_e32 v48, vcc, 0x24000, v28
	s_nop 1
	v_addc_co_u32_e32 v49, vcc, 0, v29, vcc
	global_load_dword v68, v[48:49], off nt
	v_add_co_u32_e32 v48, vcc, 0x26000, v28
	s_nop 1
	v_addc_co_u32_e32 v49, vcc, 0, v29, vcc
	global_load_dword v69, v[48:49], off nt
	v_add_co_u32_e32 v48, vcc, 0x28000, v28
	s_nop 1
	v_addc_co_u32_e32 v49, vcc, 0, v29, vcc
	global_load_dword v70, v[48:49], off nt
	v_add_co_u32_e32 v48, vcc, 0x2a000, v28
	s_nop 1
	v_addc_co_u32_e32 v49, vcc, 0, v29, vcc
	global_load_dword v71, v[48:49], off nt
	v_add_co_u32_e32 v48, vcc, 0x2c000, v28
	s_nop 1
	v_addc_co_u32_e32 v49, vcc, 0, v29, vcc
	global_load_dword v72, v[48:49], off nt
	v_add_co_u32_e32 v48, vcc, 0x2e000, v28
	s_nop 1
	v_addc_co_u32_e32 v49, vcc, 0, v29, vcc
	global_load_dword v73, v[48:49], off nt
	v_add_co_u32_e32 v48, vcc, 0x30000, v28
	s_nop 1
	v_addc_co_u32_e32 v49, vcc, 0, v29, vcc
	global_load_dword v74, v[48:49], off nt
	v_add_co_u32_e32 v48, vcc, 0x32000, v28
	s_nop 1
	v_addc_co_u32_e32 v49, vcc, 0, v29, vcc
	global_load_dword v75, v[48:49], off nt
	v_add_co_u32_e32 v48, vcc, 0x34000, v28
	s_nop 1
	v_addc_co_u32_e32 v49, vcc, 0, v29, vcc
	global_load_dword v76, v[48:49], off nt
	v_add_co_u32_e32 v48, vcc, 0x36000, v28
	s_nop 1
	v_addc_co_u32_e32 v49, vcc, 0, v29, vcc
	global_load_dword v77, v[48:49], off nt
	v_add_co_u32_e32 v48, vcc, 0x38000, v28
	s_nop 1
	v_addc_co_u32_e32 v49, vcc, 0, v29, vcc
	global_load_dword v78, v[48:49], off nt
	v_add_co_u32_e32 v48, vcc, 0x3a000, v28
	s_nop 1
	v_addc_co_u32_e32 v49, vcc, 0, v29, vcc
	global_load_dword v79, v[48:49], off nt
	v_add_co_u32_e32 v48, vcc, 0x3c000, v28
	s_nop 1
	v_addc_co_u32_e32 v49, vcc, 0, v29, vcc
	v_add_co_u32_e32 v28, vcc, 0x3e000, v28
	global_load_dword v48, v[48:49], off nt
	s_nop 0
	v_addc_co_u32_e32 v29, vcc, 0, v29, vcc
	global_load_dword v28, v[28:29], off nt
	s_waitcnt vmcnt(0)
	ds_write2_b32 v31, v50, v51 offset1:66
	ds_write2_b32 v31, v52, v53 offset0:132 offset1:198
	ds_write2_b32 v40, v54, v55 offset0:8 offset1:74
	ds_write2_b32 v40, v56, v57 offset0:140 offset1:206
	ds_write2_b32 v41, v58, v59 offset0:16 offset1:82
	ds_write2_b32 v41, v60, v61 offset0:148 offset1:214
	ds_write2_b32 v42, v62, v63 offset0:24 offset1:90
	ds_write2_b32 v42, v64, v65 offset0:156 offset1:222
	ds_write2_b32 v43, v66, v67 offset0:32 offset1:98
	ds_write2_b32 v43, v68, v69 offset0:164 offset1:230
	ds_write2_b32 v44, v70, v71 offset0:40 offset1:106
	ds_write2_b32 v44, v72, v73 offset0:172 offset1:238
	ds_write2_b32 v45, v74, v75 offset0:48 offset1:114
	ds_write2_b32 v45, v76, v77 offset0:180 offset1:246
	ds_write2_b32 v46, v78, v79 offset0:56 offset1:122
	ds_write2_b32 v46, v48, v28 offset0:188 offset1:254
	s_waitcnt lgkmcnt(0)
; #define GAS __attribute__((address_space(1)))
; #define LAS __attribute__((address_space(3)))
; #define LDS_WAIT() asm volatile("s_waitcnt lgkmcnt(0)" ::: "memory")
; __device__ __forceinline__ unsigned pk2(float lo, float hi) { return f2bf(lo) | (f2bf(hi) << 16); }
; __device__ __forceinline__ void tr_item(const float* W, int ld, int K, int nblk, int item, bf16* WT, bool gu, LAS float* scr, int lane) {
;     ...
;     const int c = lane & 7;
; #pragma unroll
;     for (int j = 0; j < 4; ++j) { const int n = (lane >> 3) + 8 * j; const LAS float* s = scr + (8 * c) * 33 + n;
;         v4u o; o.x = pk2(s[0 * 33], s[1 * 33]); o.y = pk2(s[2 * 33], s[3 * 33]); o.z = pk2(s[4 * 33], s[5 * 33]); o.w = pk2(s[6 * 33], s[7 * 33]);
;         *(GAS v4u*)(WT + (size_t)(drow0 + n) * K + k0 + 8 * c) = o; }
;     LDS_WAIT(); asm volatile("" ::: "memory");
	ds_read2_b32 v[52:53], v36 offset0:33 offset1:41
	ds_read2_b32 v[54:55], v36 offset1:8
	ds_read2_b32 v[56:57], v36 offset0:66 offset1:74
	ds_read2_b32 v[58:59], v36 offset0:99 offset1:107
	ds_read2_b32 v[60:61], v36 offset0:132 offset1:140
	ds_read2_b32 v[62:63], v36 offset0:165 offset1:173
	ds_read2_b32 v[64:65], v36 offset0:198 offset1:206
	ds_read2_b32 v[66:67], v36 offset0:231 offset1:239
	s_waitcnt lgkmcnt(7)
	v_bfe_u32 v49, v52, 16, 1
	s_waitcnt lgkmcnt(6)
	v_bfe_u32 v48, v54, 16, 1
	v_add3_u32 v48, v54, v48, s15
	v_lshrrev_b32_e32 v48, 16, v48
	v_add3_u32 v49, v52, v49, s15
	v_and_or_b32 v48, v49, s16, v48
	s_waitcnt lgkmcnt(5)
	v_bfe_u32 v49, v56, 16, 1
	v_add3_u32 v49, v56, v49, s15
	s_waitcnt lgkmcnt(4)
	v_bfe_u32 v50, v58, 16, 1
	v_lshrrev_b32_e32 v49, 16, v49
	v_add3_u32 v50, v58, v50, s15
	v_and_or_b32 v49, v50, s16, v49
	s_waitcnt lgkmcnt(3)
	v_bfe_u32 v50, v60, 16, 1
	v_add3_u32 v50, v60, v50, s15
	s_waitcnt lgkmcnt(2)
	v_bfe_u32 v51, v62, 16, 1
	v_lshrrev_b32_e32 v50, 16, v50
	v_add3_u32 v51, v62, v51, s15
	v_and_or_b32 v50, v51, s16, v50
	s_waitcnt lgkmcnt(1)
	v_bfe_u32 v51, v64, 16, 1
	v_add_u32_e32 v68, s4, v35
	v_add3_u32 v51, v64, v51, s15
	s_waitcnt lgkmcnt(0)
	v_bfe_u32 v52, v66, 16, 1
	v_ashrrev_i32_e32 v69, 31, v68
	v_lshl_add_u64 v[28:29], v[24:25], 0, s[0:1]
	v_lshrrev_b32_e32 v51, 16, v51
	v_add3_u32 v52, v66, v52, s15
	v_lshlrev_b64 v[68:69], 11, v[68:69]
	v_and_or_b32 v51, v52, s16, v51
	v_lshl_add_u64 v[68:69], v[28:29], 0, v[68:69]
	global_store_dwordx4 v[68:69], v[48:51], off nt
	v_bfe_u32 v52, v67, 16, 1
	v_add3_u32 v52, v67, v52, s15
	v_bfe_u32 v48, v55, 16, 1
	v_add3_u32 v48, v55, v48, s15
	v_bfe_u32 v49, v53, 16, 1
	v_lshrrev_b32_e32 v48, 16, v48
	v_add3_u32 v49, v53, v49, s15
	v_and_or_b32 v48, v49, s16, v48
	v_bfe_u32 v49, v57, 16, 1
	v_add3_u32 v49, v57, v49, s15
	v_bfe_u32 v50, v59, 16, 1
	v_lshrrev_b32_e32 v49, 16, v49
	v_add3_u32 v50, v59, v50, s15
	v_and_or_b32 v49, v50, s16, v49
	v_bfe_u32 v50, v61, 16, 1
	v_add3_u32 v50, v61, v50, s15
	v_bfe_u32 v51, v63, 16, 1
	v_lshrrev_b32_e32 v50, 16, v50
	v_add3_u32 v51, v63, v51, s15
	v_and_or_b32 v50, v51, s16, v50
	v_bfe_u32 v51, v65, 16, 1
	v_add3_u32 v51, v65, v51, s15
	v_lshrrev_b32_e32 v51, 16, v51
	v_and_or_b32 v51, v52, s16, v51
	v_add_u32_e32 v52, s4, v37
	v_ashrrev_i32_e32 v53, 31, v52
	v_lshlrev_b64 v[52:53], 11, v[52:53]
	v_lshl_add_u64 v[52:53], v[28:29], 0, v[52:53]
	global_store_dwordx4 v[52:53], v[48:51], off nt
	ds_read2_b32 v[52:53], v36 offset0:49 offset1:57
	ds_read2_b32 v[54:55], v36 offset0:16 offset1:24
	ds_read2_b32 v[56:57], v36 offset0:82 offset1:90
	ds_read2_b32 v[58:59], v36 offset0:115 offset1:123
	ds_read2_b32 v[60:61], v36 offset0:148 offset1:156
	ds_read2_b32 v[62:63], v36 offset0:181 offset1:189
	ds_read2_b32 v[64:65], v36 offset0:214 offset1:222
	ds_read2_b32 v[66:67], v36 offset0:247 offset1:255
	s_waitcnt lgkmcnt(7)
	v_bfe_u32 v49, v52, 16, 1
	s_waitcnt lgkmcnt(6)
	v_bfe_u32 v48, v54, 16, 1
	v_add3_u32 v48, v54, v48, s15
	v_lshrrev_b32_e32 v48, 16, v48
	v_add3_u32 v49, v52, v49, s15
	v_and_or_b32 v48, v49, s16, v48
	s_waitcnt lgkmcnt(5)
	v_bfe_u32 v49, v56, 16, 1
	v_add3_u32 v49, v56, v49, s15
	s_waitcnt lgkmcnt(4)
	v_bfe_u32 v50, v58, 16, 1
	v_lshrrev_b32_e32 v49, 16, v49
	v_add3_u32 v50, v58, v50, s15
	v_and_or_b32 v49, v50, s16, v49
	s_waitcnt lgkmcnt(3)
	v_bfe_u32 v50, v60, 16, 1
	v_add3_u32 v50, v60, v50, s15
	s_waitcnt lgkmcnt(2)
	v_bfe_u32 v51, v62, 16, 1
	v_lshrrev_b32_e32 v50, 16, v50
	v_add3_u32 v51, v62, v51, s15
	v_and_or_b32 v50, v51, s16, v50
	s_waitcnt lgkmcnt(1)
	v_bfe_u32 v51, v64, 16, 1
	v_add_u32_e32 v68, s4, v38
	v_add3_u32 v51, v64, v51, s15
	s_waitcnt lgkmcnt(0)
	v_bfe_u32 v52, v66, 16, 1
	v_ashrrev_i32_e32 v69, 31, v68
	v_lshrrev_b32_e32 v51, 16, v51
	v_add3_u32 v52, v66, v52, s15
	v_lshlrev_b64 v[68:69], 11, v[68:69]
	v_and_or_b32 v51, v52, s16, v51
	v_lshl_add_u64 v[68:69], v[28:29], 0, v[68:69]
	global_store_dwordx4 v[68:69], v[48:51], off nt
	v_bfe_u32 v52, v67, 16, 1
	v_add3_u32 v52, v67, v52, s15
	v_bfe_u32 v48, v55, 16, 1
	v_add3_u32 v48, v55, v48, s15
	v_bfe_u32 v49, v53, 16, 1
	v_lshrrev_b32_e32 v48, 16, v48
	v_add3_u32 v49, v53, v49, s15
	v_and_or_b32 v48, v49, s16, v48
	v_bfe_u32 v49, v57, 16, 1
	v_add3_u32 v49, v57, v49, s15
	v_bfe_u32 v50, v59, 16, 1
	v_lshrrev_b32_e32 v49, 16, v49
	v_add3_u32 v50, v59, v50, s15
	v_and_or_b32 v49, v50, s16, v49
	v_bfe_u32 v50, v61, 16, 1
	v_add3_u32 v50, v61, v50, s15
	v_bfe_u32 v51, v63, 16, 1
	v_lshrrev_b32_e32 v50, 16, v50
	v_add3_u32 v51, v63, v51, s15
	v_and_or_b32 v50, v51, s16, v50
	v_bfe_u32 v51, v65, 16, 1
	v_add3_u32 v51, v65, v51, s15
	v_lshrrev_b32_e32 v51, 16, v51
	v_and_or_b32 v51, v52, s16, v51
	v_add_u32_e32 v52, s4, v39
	v_ashrrev_i32_e32 v53, 31, v52
	v_lshlrev_b64 v[52:53], 11, v[52:53]
	v_lshl_add_u64 v[28:29], v[28:29], 0, v[52:53]
	global_store_dwordx4 v[28:29], v[48:51], off nt
	s_waitcnt lgkmcnt(0)

; #define LDS_WAIT() asm volatile("s_waitcnt lgkmcnt(0)" ::: "memory")
; __device__ __forceinline__ void tr_item(const float* W, int ld, int K, int nblk, int item, bf16* WT, bool gu, LAS float* scr, int lane) {
;     const int kb = item / nblk, nb = item % nblk, k0 = 64 * kb, n0 = 32 * nb;
;     int drow0 = n0;
;     if (gu) { const int bj = n0 / FF, j = n0 - bj * FF; drow0 = 256 * (j / 128) + 128 * bj + (j % 128); }
;     { float t_[32];
; #pragma unroll
;       for (int i = 0; i < 32; ++i) t_[i] = W[(size_t)(k0 + 2 * i + (lane >> 5)) * ld + n0 + (lane & 31)];
; #pragma unroll
;       for (int i = 0; i < 32; ++i) scr[(2 * i + (lane >> 5)) * 33 + (lane & 31)] = t_[i]; }
;     LDS_WAIT(); asm volatile("" ::: "memory");
; __device__ __forceinline__ void convert_items(Frame& F, const Args& a, int lo, int hi, int w, int nw) {
;     ...
;         if (r < I_FI) { tr_item(a.in[7], 3 * D + 16, D, 96, r, (bf16*)(F.ws + WS_WFOXIN), false, scr, lane); continue; } r -= I_FI;
.LBB0_1356:
	s_andn2_b64 vcc, exec, s[4:5]
	s_cbranch_vccnz .LBB0_1329
	s_mul_hi_i32 s0, s8, 0x2aaaaaab
	s_lshr_b32 s4, s0, 31
	s_ashr_i32 s0, s0, 4
	s_add_i32 s0, s0, s4
	s_lshl_b32 s6, s0, 6
	s_mulk_i32 s0, 0xf400
	s_add_i32 s4, s9, s0
	s_ashr_i32 s5, s4, 31
	v_add_u32_e32 v50, s6, v30
	v_lshl_add_u64 v[28:29], s[4:5], 2, v[14:15]
	v_mad_i64_i32 v[48:49], s[40:41], v50, s30, v[28:29]
	global_load_dword v51, v[48:49], off nt
	v_add_u32_e32 v48, 2, v50
	v_mad_i64_i32 v[48:49], s[40:41], v48, s30, v[28:29]
	global_load_dword v52, v[48:49], off nt
	v_add_u32_e32 v48, 4, v50
	v_mad_i64_i32 v[48:49], s[40:41], v48, s30, v[28:29]
	global_load_dword v53, v[48:49], off nt
	v_add_u32_e32 v48, 6, v50
	v_mad_i64_i32 v[48:49], s[40:41], v48, s30, v[28:29]
	global_load_dword v54, v[48:49], off nt
	v_add_u32_e32 v48, 8, v50
	v_mad_i64_i32 v[48:49], s[40:41], v48, s30, v[28:29]
	global_load_dword v55, v[48:49], off nt
	v_add_u32_e32 v48, 10, v50
	v_mad_i64_i32 v[48:49], s[40:41], v48, s30, v[28:29]
	global_load_dword v56, v[48:49], off nt
	v_add_u32_e32 v48, 12, v50
	v_mad_i64_i32 v[48:49], s[40:41], v48, s30, v[28:29]
	global_load_dword v57, v[48:49], off nt
	v_add_u32_e32 v48, 14, v50
	v_mad_i64_i32 v[48:49], s[40:41], v48, s30, v[28:29]
	global_load_dword v58, v[48:49], off nt
	v_add_u32_e32 v48, 16, v50
	v_mad_i64_i32 v[48:49], s[40:41], v48, s30, v[28:29]
	global_load_dword v59, v[48:49], off nt
	v_add_u32_e32 v48, 18, v50
	v_mad_i64_i32 v[48:49], s[40:41], v48, s30, v[28:29]
	global_load_dword v60, v[48:49], off nt
	v_add_u32_e32 v48, 20, v50
	v_mad_i64_i32 v[48:49], s[40:41], v48, s30, v[28:29]
	global_load_dword v61, v[48:49], off nt
	v_add_u32_e32 v48, 22, v50
	v_mad_i64_i32 v[48:49], s[40:41], v48, s30, v[28:29]
	global_load_dword v62, v[48:49], off nt
	v_add_u32_e32 v48, 24, v50
	v_mad_i64_i32 v[48:49], s[40:41], v48, s30, v[28:29]
	global_load_dword v63, v[48:49], off nt
	v_add_u32_e32 v48, 26, v50
	v_mad_i64_i32 v[48:49], s[40:41], v48, s30, v[28:29]
	global_load_dword v64, v[48:49], off nt
	v_add_u32_e32 v48, 28, v50
	v_mad_i64_i32 v[48:49], s[40:41], v48, s30, v[28:29]
	global_load_dword v65, v[48:49], off nt
	v_add_u32_e32 v48, 30, v50
	v_mad_i64_i32 v[48:49], s[40:41], v48, s30, v[28:29]
	global_load_dword v66, v[48:49], off nt
	v_add_u32_e32 v48, 32, v50
	v_mad_i64_i32 v[48:49], s[40:41], v48, s30, v[28:29]
	global_load_dword v67, v[48:49], off nt
	v_add_u32_e32 v48, 34, v50
	v_mad_i64_i32 v[48:49], s[40:41], v48, s30, v[28:29]
	global_load_dword v68, v[48:49], off nt
	v_add_u32_e32 v48, 36, v50
	v_mad_i64_i32 v[48:49], s[40:41], v48, s30, v[28:29]
	global_load_dword v69, v[48:49], off nt
	v_add_u32_e32 v48, 38, v50
	v_mad_i64_i32 v[48:49], s[40:41], v48, s30, v[28:29]
	global_load_dword v70, v[48:49], off nt
	v_add_u32_e32 v48, 40, v50
	v_mad_i64_i32 v[48:49], s[40:41], v48, s30, v[28:29]
	global_load_dword v71, v[48:49], off nt
	v_add_u32_e32 v48, 42, v50
	v_mad_i64_i32 v[48:49], s[40:41], v48, s30, v[28:29]
	global_load_dword v72, v[48:49], off nt
	v_add_u32_e32 v48, 44, v50
	v_mad_i64_i32 v[48:49], s[40:41], v48, s30, v[28:29]
	global_load_dword v73, v[48:49], off nt
	v_add_u32_e32 v48, 46, v50
	v_mad_i64_i32 v[48:49], s[40:41], v48, s30, v[28:29]
	global_load_dword v74, v[48:49], off nt
	v_add_u32_e32 v48, 48, v50
	v_mad_i64_i32 v[48:49], s[40:41], v48, s30, v[28:29]
	global_load_dword v75, v[48:49], off nt
	v_add_u32_e32 v48, 50, v50
	v_mad_i64_i32 v[48:49], s[40:41], v48, s30, v[28:29]
	global_load_dword v76, v[48:49], off nt
	v_add_u32_e32 v48, 52, v50
	v_mad_i64_i32 v[48:49], s[40:41], v48, s30, v[28:29]
	global_load_dword v77, v[48:49], off nt
	v_add_u32_e32 v48, 54, v50
	v_mad_i64_i32 v[48:49], s[40:41], v48, s30, v[28:29]
	global_load_dword v78, v[48:49], off nt
	v_add_u32_e32 v48, 56, v50
	v_mad_i64_i32 v[48:49], s[40:41], v48, s30, v[28:29]
	global_load_dword v79, v[48:49], off nt
	v_add_u32_e32 v48, 58, v50
	v_mad_i64_i32 v[48:49], s[40:41], v48, s30, v[28:29]
	global_load_dword v80, v[48:49], off nt
	v_add_u32_e32 v48, 60, v50
	v_mad_i64_i32 v[48:49], s[40:41], v48, s30, v[28:29]
	global_load_dword v48, v[48:49], off nt
	v_add_u32_e32 v49, 62, v50
	v_mad_i64_i32 v[28:29], s[40:41], v49, s30, v[28:29]
	global_load_dword v28, v[28:29], off nt
	s_waitcnt vmcnt(0)
	ds_write2_b32 v31, v51, v52 offset1:66
	ds_write2_b32 v31, v53, v54 offset0:132 offset1:198
	ds_write2_b32 v40, v55, v56 offset0:8 offset1:74
	ds_write2_b32 v40, v57, v58 offset0:140 offset1:206
	ds_write2_b32 v41, v59, v60 offset0:16 offset1:82
	ds_write2_b32 v41, v61, v62 offset0:148 offset1:214
	ds_write2_b32 v42, v63, v64 offset0:24 offset1:90
	ds_write2_b32 v42, v65, v66 offset0:156 offset1:222
	ds_write2_b32 v43, v67, v68 offset0:32 offset1:98
	ds_write2_b32 v43, v69, v70 offset0:164 offset1:230
	ds_write2_b32 v44, v71, v72 offset0:40 offset1:106
	ds_write2_b32 v44, v73, v74 offset0:172 offset1:238
	ds_write2_b32 v45, v75, v76 offset0:48 offset1:114
	ds_write2_b32 v45, v77, v78 offset0:180 offset1:246
	ds_write2_b32 v46, v79, v80 offset0:56 offset1:122
	ds_write2_b32 v46, v48, v28 offset0:188 offset1:254
	s_waitcnt lgkmcnt(0)
; #define GAS __attribute__((address_space(1)))
; #define LAS __attribute__((address_space(3)))
; #define LDS_WAIT() asm volatile("s_waitcnt lgkmcnt(0)" ::: "memory")
; __device__ __forceinline__ unsigned pk2(float lo, float hi) { return f2bf(lo) | (f2bf(hi) << 16); }
; __device__ __forceinline__ void tr_item(const float* W, int ld, int K, int nblk, int item, bf16* WT, bool gu, LAS float* scr, int lane) {
;     ...
;     const int c = lane & 7;
; #pragma unroll
;     for (int j = 0; j < 4; ++j) { const int n = (lane >> 3) + 8 * j; const LAS float* s = scr + (8 * c) * 33 + n;
;         v4u o; o.x = pk2(s[0 * 33], s[1 * 33]); o.y = pk2(s[2 * 33], s[3 * 33]); o.z = pk2(s[4 * 33], s[5 * 33]); o.w = pk2(s[6 * 33], s[7 * 33]);
;         *(GAS v4u*)(WT + (size_t)(drow0 + n) * K + k0 + 8 * c) = o; }
;     LDS_WAIT(); asm volatile("" ::: "memory");
	ds_read2_b32 v[52:53], v36 offset0:33 offset1:41
	ds_read2_b32 v[54:55], v36 offset1:8
	ds_read2_b32 v[56:57], v36 offset0:66 offset1:74
	ds_read2_b32 v[58:59], v36 offset0:99 offset1:107
	ds_read2_b32 v[60:61], v36 offset0:132 offset1:140
	ds_read2_b32 v[62:63], v36 offset0:165 offset1:173
	ds_read2_b32 v[64:65], v36 offset0:198 offset1:206
	ds_read2_b32 v[66:67], v36 offset0:231 offset1:239
	s_waitcnt lgkmcnt(7)
	v_bfe_u32 v49, v52, 16, 1
	s_waitcnt lgkmcnt(6)
	v_bfe_u32 v48, v54, 16, 1
	v_add3_u32 v48, v54, v48, s15
	v_lshrrev_b32_e32 v48, 16, v48
	v_add3_u32 v49, v52, v49, s15
	v_and_or_b32 v48, v49, s16, v48
	s_waitcnt lgkmcnt(5)
	v_bfe_u32 v49, v56, 16, 1
	v_add3_u32 v49, v56, v49, s15
	s_waitcnt lgkmcnt(4)
	v_bfe_u32 v50, v58, 16, 1
	v_lshrrev_b32_e32 v49, 16, v49
	v_add3_u32 v50, v58, v50, s15
	v_and_or_b32 v49, v50, s16, v49
	s_waitcnt lgkmcnt(3)
	v_bfe_u32 v50, v60, 16, 1
	v_add3_u32 v50, v60, v50, s15
	s_waitcnt lgkmcnt(2)
	v_bfe_u32 v51, v62, 16, 1
	v_lshrrev_b32_e32 v50, 16, v50
	v_add3_u32 v51, v62, v51, s15
	v_and_or_b32 v50, v51, s16, v50
	s_waitcnt lgkmcnt(1)
	v_bfe_u32 v51, v64, 16, 1
	v_add_u32_e32 v68, s4, v35
	s_ashr_i32 s7, s6, 31
	v_add3_u32 v51, v64, v51, s15
	s_waitcnt lgkmcnt(0)
	v_bfe_u32 v52, v66, 16, 1
	v_ashrrev_i32_e32 v69, 31, v68
	v_lshl_add_u64 v[28:29], s[6:7], 1, v[26:27]
	v_lshrrev_b32_e32 v51, 16, v51
	v_add3_u32 v52, v66, v52, s15
	v_lshlrev_b64 v[70:71], 11, v[68:69]
	v_and_or_b32 v51, v52, s16, v51
	v_lshl_add_u64 v[70:71], v[28:29], 0, v[70:71]
	global_store_dwordx4 v[70:71], v[48:51], off nt
	v_bfe_u32 v52, v67, 16, 1
	v_add3_u32 v52, v67, v52, s15
	v_bfe_u32 v48, v55, 16, 1
	v_add3_u32 v48, v55, v48, s15
	v_bfe_u32 v49, v53, 16, 1
	v_lshrrev_b32_e32 v48, 16, v48
	v_add3_u32 v49, v53, v49, s15
	v_and_or_b32 v48, v49, s16, v48
	v_bfe_u32 v49, v57, 16, 1
	v_add3_u32 v49, v57, v49, s15
	v_bfe_u32 v50, v59, 16, 1
	v_lshrrev_b32_e32 v49, 16, v49
	v_add3_u32 v50, v59, v50, s15
	v_and_or_b32 v49, v50, s16, v49
	v_bfe_u32 v50, v61, 16, 1
	v_add3_u32 v50, v61, v50, s15
	v_bfe_u32 v51, v63, 16, 1
	v_lshrrev_b32_e32 v50, 16, v50
	v_add3_u32 v51, v63, v51, s15
	v_and_or_b32 v50, v51, s16, v50
	v_bfe_u32 v51, v65, 16, 1
	v_add3_u32 v51, v65, v51, s15
	v_lshrrev_b32_e32 v51, 16, v51
	v_and_or_b32 v51, v52, s16, v51
	v_add_u32_e32 v52, 8, v68
	v_ashrrev_i32_e32 v53, 31, v52
	v_lshlrev_b64 v[52:53], 11, v[52:53]
	v_lshl_add_u64 v[52:53], v[28:29], 0, v[52:53]
	global_store_dwordx4 v[52:53], v[48:51], off nt
	ds_read2_b32 v[52:53], v36 offset0:49 offset1:57
	ds_read2_b32 v[54:55], v36 offset0:16 offset1:24
	ds_read2_b32 v[56:57], v36 offset0:82 offset1:90
	ds_read2_b32 v[58:59], v36 offset0:115 offset1:123
	ds_read2_b32 v[60:61], v36 offset0:148 offset1:156
	ds_read2_b32 v[62:63], v36 offset0:181 offset1:189
	ds_read2_b32 v[64:65], v36 offset0:214 offset1:222
	ds_read2_b32 v[66:67], v36 offset0:247 offset1:255
	s_waitcnt lgkmcnt(7)
	v_bfe_u32 v49, v52, 16, 1
	s_waitcnt lgkmcnt(6)
	v_bfe_u32 v48, v54, 16, 1
	v_add3_u32 v48, v54, v48, s15
	v_lshrrev_b32_e32 v48, 16, v48
	v_add3_u32 v49, v52, v49, s15
	v_and_or_b32 v48, v49, s16, v48
	s_waitcnt lgkmcnt(5)
	v_bfe_u32 v49, v56, 16, 1
	v_add3_u32 v49, v56, v49, s15
	s_waitcnt lgkmcnt(4)
	v_bfe_u32 v50, v58, 16, 1
	v_lshrrev_b32_e32 v49, 16, v49
	v_add3_u32 v50, v58, v50, s15
	v_and_or_b32 v49, v50, s16, v49
	s_waitcnt lgkmcnt(3)
	v_bfe_u32 v50, v60, 16, 1
	v_add3_u32 v50, v60, v50, s15
	s_waitcnt lgkmcnt(2)
	v_bfe_u32 v51, v62, 16, 1
	v_lshrrev_b32_e32 v50, 16, v50
	v_add3_u32 v51, v62, v51, s15
	v_and_or_b32 v50, v51, s16, v50
	s_waitcnt lgkmcnt(1)
	v_bfe_u32 v51, v64, 16, 1
	v_add_u32_e32 v70, 16, v68
	v_add3_u32 v51, v64, v51, s15
	s_waitcnt lgkmcnt(0)
	v_bfe_u32 v52, v66, 16, 1
	v_ashrrev_i32_e32 v71, 31, v70
	v_lshrrev_b32_e32 v51, 16, v51
	v_add3_u32 v52, v66, v52, s15
	v_lshlrev_b64 v[70:71], 11, v[70:71]
	v_and_or_b32 v51, v52, s16, v51
	v_lshl_add_u64 v[70:71], v[28:29], 0, v[70:71]
	global_store_dwordx4 v[70:71], v[48:51], off nt
	v_bfe_u32 v52, v67, 16, 1
	v_add3_u32 v52, v67, v52, s15
	v_bfe_u32 v48, v55, 16, 1
	v_add3_u32 v48, v55, v48, s15
	v_bfe_u32 v49, v53, 16, 1
	v_lshrrev_b32_e32 v48, 16, v48
	v_add3_u32 v49, v53, v49, s15
	v_and_or_b32 v48, v49, s16, v48
	v_bfe_u32 v49, v57, 16, 1
	v_add3_u32 v49, v57, v49, s15
	v_bfe_u32 v50, v59, 16, 1
	v_lshrrev_b32_e32 v49, 16, v49
	v_add3_u32 v50, v59, v50, s15
	v_and_or_b32 v49, v50, s16, v49
	v_bfe_u32 v50, v61, 16, 1
	v_add3_u32 v50, v61, v50, s15
	v_bfe_u32 v51, v63, 16, 1
	v_lshrrev_b32_e32 v50, 16, v50
	v_add3_u32 v51, v63, v51, s15
	v_and_or_b32 v50, v51, s16, v50
	v_bfe_u32 v51, v65, 16, 1
	v_add3_u32 v51, v65, v51, s15
	v_lshrrev_b32_e32 v51, 16, v51
	v_and_or_b32 v51, v52, s16, v51
	v_add_u32_e32 v52, 24, v68
	v_ashrrev_i32_e32 v53, 31, v52
	v_lshlrev_b64 v[52:53], 11, v[52:53]
	v_lshl_add_u64 v[28:29], v[28:29], 0, v[52:53]
	global_store_dwordx4 v[28:29], v[48:51], off nt
	s_waitcnt lgkmcnt(0)
	s_branch .LBB0_1329

; __device__ __forceinline__ void tr_item8(const float* W, int ld, int K, int nblk, int item, unsigned char* WT, bool gu, float scale, LAS float* scr, int lane) {
;     const int kb = item / nblk, nb = item % nblk, k0 = 64 * kb, n0 = 32 * nb;
;     int drow0 = n0;
;     if (gu) { const int bj = n0 / FF, j = n0 - bj * FF; drow0 = 256 * (j / 128) + 128 * bj + (j % 128); }
;     { float t_[32];
; #pragma unroll
;       for (int i = 0; i < 32; ++i) t_[i] = W[(size_t)(k0 + 2 * i + (lane >> 5)) * ld + n0 + (lane & 31)];
; #pragma unroll
;       for (int i = 0; i < 32; ++i) scr[(2 * i + (lane >> 5)) * 33 + (lane & 31)] = t_[i] * scale; }
; __device__ __forceinline__ void convert_items(Frame& F, const Args& a, int lo, int hi, int w, int nw) {
;     ...
;     for (int it = lo + w; it < hi; it += nw) {
;         int r = it;
;         if (r < I_FI) { tr_item(a.in[7], 3 * D + 16, D, 96, r, (bf16*)(F.ws + WS_WFOXIN), false, scr, lane); continue; } r -= I_FI;
;         if (r < I_FO) { tr_item(a.in[9], D, D, 32, r, (bf16*)(F.ws + WS_WFOXOUT), false, scr, lane); continue; } r -= I_FO;
;         if (r < I_SI) { tr_item(a.in[10], D + 512, D, 48, r, (bf16*)(F.ws + WS_WSWAIN), false, scr, lane); continue; } r -= I_SI;
;         if (r < I_SO) { tr_item(a.in[12], D, D, 32, r, (bf16*)(F.ws + WS_WSWAOUT), false, scr, lane); continue; } r -= I_SO;
;         if (r < I_GU) { tr_item8(a.in[14], 2 * FF, D, 224, r, F.ws + WS_WGU, true, WSC_GU, scr, lane); continue; } r -= I_GU;
;         if (r < I_DN) { tr_item8(a.in[15], D, FF, 32, r, F.ws + WS_WDN, false, WSC_DN, scr, lane); continue; } r -= I_DN;
;         if (r < NE * I_GU) { const int e = r / I_GU, rr = r % I_GU; tr_item8(a.in[18] + (size_t)e * D * 2 * FF, 2 * FF, D, 224, rr, F.ws + WS_WMGU + (size_t)e * 2 * FF * D, true, WSC_GU, scr, lane); continue; } r -= NE * I_GU;
;         { const int e = r / I_DN, rr = r % I_DN; tr_item8(a.in[19] + (size_t)e * FF * D, D, FF, 32, rr, F.ws + WS_WMDN + (size_t)e * D * FF, false, WSC_DN, scr, lane); }
.LBB0_1406:
	s_cmpk_gt_i32 s3, 0x5ff
	s_mov_b64 s[4:5], -1
	s_cbranch_scc0 .LBB0_1432
	s_cmpk_gt_u32 s3, 0x7ff
	s_cbranch_scc0 .LBB0_1429
	s_cmpk_gt_u32 s3, 0xaff
	s_cbranch_scc0 .LBB0_1426
	s_cmpk_gt_u32 s3, 0xcff
	s_cbranch_scc0 .LBB0_1423
	s_cmpk_gt_u32 s3, 0x1aff
	s_cbranch_scc0 .LBB0_1420
	s_cmpk_gt_u32 s3, 0x21ff
	s_cbranch_scc0 .LBB0_1417
	s_cmpk_gt_u32 s3, 0x91ff
	s_cbranch_scc0 .LBB0_1414
	s_add_i32 s0, s3, 0x6e00
	s_bfe_u32 s4, s0, 0x80008
	s_mulk_i32 s4, 0x2493
	s_lshr_b32 s4, s4, 16
	s_mul_i32 s5, s4, 0x700
	s_sub_i32 s6, s0, s5
	s_mul_i32 s0, s4, 0xe00000
	s_add_u32 s7, s74, s0
	s_addc_u32 s61, s75, 0
	s_mul_i32 s4, s4, 0x380000
	s_add_u32 s4, s66, s4
	s_addc_u32 s5, s88, 0
	s_lshl_b32 s0, s6, 5
	s_and_b32 s0, s0, 0x3e0
	s_lshl_b32 s6, s6, 1
	s_and_b32 s6, s6, 0xfc0
	s_lshl_b32 s62, s0, 2
	v_add_u32_e32 v46, s6, v28
	s_add_u32 s62, s7, s62
	s_addc_u32 s63, s61, 0
	v_ashrrev_i32_e32 v47, 31, v46
	v_lshl_add_u64 v[48:49], s[62:63], 0, v[0:1]
	v_lshlrev_b64 v[46:47], 12, v[46:47]
	v_lshl_add_u64 v[46:47], v[48:49], 0, v[46:47]
	v_add_co_u32_e32 v48, vcc, s10, v46
	s_add_u32 s4, s4, s6
	s_nop 0
	v_addc_co_u32_e32 v49, vcc, 0, v47, vcc
	v_add_co_u32_e32 v50, vcc, s11, v46
	s_addc_u32 s5, s5, 0
	s_nop 0
	v_addc_co_u32_e32 v51, vcc, 0, v47, vcc
	v_add_co_u32_e32 v52, vcc, s12, v46
	s_nop 1
	v_addc_co_u32_e32 v53, vcc, 0, v47, vcc
	v_add_co_u32_e32 v54, vcc, s13, v46
	s_nop 1
	v_addc_co_u32_e32 v55, vcc, 0, v47, vcc
	v_add_co_u32_e32 v56, vcc, s14, v46
	s_nop 1
	v_addc_co_u32_e32 v57, vcc, 0, v47, vcc
	v_add_co_u32_e32 v58, vcc, s15, v46
	s_nop 1
	v_addc_co_u32_e32 v59, vcc, 0, v47, vcc
	v_add_co_u32_e32 v60, vcc, s16, v46
	s_nop 1
	v_addc_co_u32_e32 v61, vcc, 0, v47, vcc
	global_load_dword v64, v[46:47], off nt
	global_load_dword v65, v[48:49], off nt
	global_load_dword v66, v[50:51], off nt
	global_load_dword v67, v[52:53], off nt
	global_load_dword v68, v[54:55], off nt
	global_load_dword v69, v[56:57], off nt
	global_load_dword v70, v[58:59], off nt
	global_load_dword v71, v[60:61], off nt
	v_add_co_u32_e32 v48, vcc, s17, v46
	s_nop 1
	v_addc_co_u32_e32 v49, vcc, 0, v47, vcc
	v_add_co_u32_e32 v50, vcc, s26, v46
	s_nop 1
	v_addc_co_u32_e32 v51, vcc, 0, v47, vcc
	v_add_co_u32_e32 v52, vcc, s27, v46
	s_nop 1
	v_addc_co_u32_e32 v53, vcc, 0, v47, vcc
	v_add_co_u32_e32 v54, vcc, s30, v46
	s_nop 1
	v_addc_co_u32_e32 v55, vcc, 0, v47, vcc
	v_add_co_u32_e32 v56, vcc, s31, v46
	s_nop 1
	v_addc_co_u32_e32 v57, vcc, 0, v47, vcc
	v_add_co_u32_e32 v58, vcc, s36, v46
	s_nop 1
	v_addc_co_u32_e32 v59, vcc, 0, v47, vcc
	v_add_co_u32_e32 v60, vcc, s37, v46
	s_nop 1
	v_addc_co_u32_e32 v61, vcc, 0, v47, vcc
	v_add_co_u32_e32 v62, vcc, s38, v46
	s_nop 1
	v_addc_co_u32_e32 v63, vcc, 0, v47, vcc
	global_load_dword v72, v[48:49], off nt
	global_load_dword v73, v[50:51], off nt
	global_load_dword v74, v[52:53], off nt
	global_load_dword v75, v[54:55], off nt
	global_load_dword v76, v[56:57], off nt
	global_load_dword v77, v[58:59], off nt
	global_load_dword v78, v[60:61], off nt
	global_load_dword v79, v[62:63], off nt
	v_add_co_u32_e32 v48, vcc, s39, v46
	s_nop 1
	v_addc_co_u32_e32 v49, vcc, 0, v47, vcc
	v_add_co_u32_e32 v50, vcc, s40, v46
	s_nop 1
	v_addc_co_u32_e32 v51, vcc, 0, v47, vcc
	v_add_co_u32_e32 v52, vcc, s41, v46
	s_nop 1
	v_addc_co_u32_e32 v53, vcc, 0, v47, vcc
	v_add_co_u32_e32 v54, vcc, s42, v46
	s_nop 1
	v_addc_co_u32_e32 v55, vcc, 0, v47, vcc
	v_add_co_u32_e32 v56, vcc, s43, v46
	s_nop 1
	v_addc_co_u32_e32 v57, vcc, 0, v47, vcc
	v_add_co_u32_e32 v58, vcc, s44, v46
	s_nop 1
	v_addc_co_u32_e32 v59, vcc, 0, v47, vcc
	v_add_co_u32_e32 v60, vcc, s45, v46
	s_nop 1
	v_addc_co_u32_e32 v61, vcc, 0, v47, vcc
	v_add_co_u32_e32 v62, vcc, s46, v46
	s_nop 1
	v_addc_co_u32_e32 v63, vcc, 0, v47, vcc
	global_load_dword v80, v[48:49], off nt
	global_load_dword v81, v[50:51], off nt
	global_load_dword v82, v[52:53], off nt
	global_load_dword v83, v[54:55], off nt
	global_load_dword v84, v[56:57], off nt
	global_load_dword v85, v[58:59], off nt
	s_nop 0
	global_load_dword v60, v[60:61], off nt
	s_nop 0
	global_load_dword v61, v[62:63], off nt
	v_add_co_u32_e32 v48, vcc, s47, v46
	s_nop 1
	v_addc_co_u32_e32 v49, vcc, 0, v47, vcc
	v_add_co_u32_e32 v50, vcc, s48, v46
	s_nop 1
	v_addc_co_u32_e32 v51, vcc, 0, v47, vcc
	v_add_co_u32_e32 v52, vcc, s49, v46
	s_nop 1
	v_addc_co_u32_e32 v53, vcc, 0, v47, vcc
	v_add_co_u32_e32 v54, vcc, s50, v46
	s_nop 1
	v_addc_co_u32_e32 v55, vcc, 0, v47, vcc
	v_add_co_u32_e32 v56, vcc, s51, v46
	s_nop 1
	v_addc_co_u32_e32 v57, vcc, 0, v47, vcc
	v_add_co_u32_e32 v58, vcc, s52, v46
	s_nop 1
	v_addc_co_u32_e32 v59, vcc, 0, v47, vcc
	global_load_dword v62, v[48:49], off nt
	s_nop 0
	global_load_dword v50, v[50:51], off nt
	s_nop 0
	global_load_dword v51, v[52:53], off nt
	s_nop 0
	global_load_dword v52, v[54:55], off nt
	global_load_dword v53, v[56:57], off nt
	s_nop 0
	global_load_dword v54, v[58:59], off nt
	v_add_co_u32_e32 v48, vcc, s53, v46
	s_nop 1
	v_addc_co_u32_e32 v49, vcc, 0, v47, vcc
	v_add_co_u32_e32 v46, vcc, s54, v46
	s_nop 1
	v_addc_co_u32_e32 v47, vcc, 0, v47, vcc
	global_load_dword v48, v[48:49], off nt
	s_nop 0
	global_load_dword v46, v[46:47], off nt
	s_waitcnt vmcnt(31)
	v_mul_f32_e32 v47, 0x43000000, v64
	s_waitcnt vmcnt(30)
	v_mul_f32_e32 v49, 0x43000000, v65
	ds_write2_b32 v29, v47, v49 offset1:66
	s_waitcnt vmcnt(29)
	v_mul_f32_e32 v47, 0x43000000, v66
	s_waitcnt vmcnt(28)
	v_mul_f32_e32 v49, 0x43000000, v67
	ds_write2_b32 v29, v47, v49 offset0:132 offset1:198
	s_waitcnt vmcnt(27)
	v_mul_f32_e32 v47, 0x43000000, v68
	s_waitcnt vmcnt(26)
	v_mul_f32_e32 v49, 0x43000000, v69
	ds_write2_b32 v38, v47, v49 offset0:8 offset1:74
	s_waitcnt vmcnt(25)
; __device__ __forceinline__ unsigned cvt_pk4_fp8(float a, float b, float c, float d) { int w = 0; w = __builtin_amdgcn_cvt_pk_fp8_f32(a, b, w, false); w = __builtin_amdgcn_cvt_pk_fp8_f32(c, d, w, true); return (unsigned)w; }
; #define GAS __attribute__((address_space(1)))
; #define LAS __attribute__((address_space(3)))
; #define LDS_WAIT() asm volatile("s_waitcnt lgkmcnt(0)" ::: "memory")
; __device__ __forceinline__ void tr_item8(const float* W, int ld, int K, int nblk, int item, unsigned char* WT, bool gu, float scale, LAS float* scr, int lane) {
;     ...
;       for (int i = 0; i < 32; ++i) scr[(2 * i + (lane >> 5)) * 33 + (lane & 31)] = t_[i] * scale; }
;     LDS_WAIT(); asm volatile("" ::: "memory");
;     const int c = lane & 3;
; #pragma unroll
;     for (int j = 0; j < 2; ++j) { const int n = (lane >> 2) + 16 * j; const LAS float* sp = scr + (16 * c) * 33 + n;
;         v4u o; o.x = pg8::cvt_pk4_fp8(sp[0 * 33], sp[1 * 33], sp[2 * 33], sp[3 * 33]); o.y = pg8::cvt_pk4_fp8(sp[4 * 33], sp[5 * 33], sp[6 * 33], sp[7 * 33]);
;         o.z = pg8::cvt_pk4_fp8(sp[8 * 33], sp[9 * 33], sp[10 * 33], sp[11 * 33]); o.w = pg8::cvt_pk4_fp8(sp[12 * 33], sp[13 * 33], sp[14 * 33], sp[15 * 33]);
;         *(GAS v4u*)(WT + (size_t)(drow0 + n) * K + k0 + 16 * c) = o; }
;     LDS_WAIT(); asm volatile("" ::: "memory");
	v_mul_f32_e32 v47, 0x43000000, v70
	s_waitcnt vmcnt(24)
	v_mul_f32_e32 v49, 0x43000000, v71
	ds_write2_b32 v38, v47, v49 offset0:140 offset1:206
	s_waitcnt vmcnt(23)
	v_mul_f32_e32 v47, 0x43000000, v72
	s_waitcnt vmcnt(22)
	v_mul_f32_e32 v49, 0x43000000, v73
	ds_write2_b32 v39, v47, v49 offset0:16 offset1:82
	s_waitcnt vmcnt(21)
	v_mul_f32_e32 v47, 0x43000000, v74
	s_waitcnt vmcnt(20)
	v_mul_f32_e32 v49, 0x43000000, v75
	ds_write2_b32 v39, v47, v49 offset0:148 offset1:214
	s_waitcnt vmcnt(19)
	v_mul_f32_e32 v47, 0x43000000, v76
	s_waitcnt vmcnt(18)
	v_mul_f32_e32 v49, 0x43000000, v77
	ds_write2_b32 v40, v47, v49 offset0:24 offset1:90
	s_waitcnt vmcnt(17)
	v_mul_f32_e32 v47, 0x43000000, v78
	s_waitcnt vmcnt(16)
	v_mul_f32_e32 v49, 0x43000000, v79
	ds_write2_b32 v40, v47, v49 offset0:156 offset1:222
	s_waitcnt vmcnt(15)
	v_mul_f32_e32 v47, 0x43000000, v80
	s_waitcnt vmcnt(14)
	v_mul_f32_e32 v49, 0x43000000, v81
	ds_write2_b32 v41, v47, v49 offset0:32 offset1:98
	s_waitcnt vmcnt(13)
	v_mul_f32_e32 v47, 0x43000000, v82
	s_waitcnt vmcnt(12)
	v_mul_f32_e32 v49, 0x43000000, v83
	ds_write2_b32 v41, v47, v49 offset0:164 offset1:230
	s_waitcnt vmcnt(11)
	v_mul_f32_e32 v47, 0x43000000, v84
	s_waitcnt vmcnt(10)
	v_mul_f32_e32 v49, 0x43000000, v85
	ds_write2_b32 v42, v47, v49 offset0:40 offset1:106
	s_waitcnt vmcnt(9)
	v_mul_f32_e32 v47, 0x43000000, v60
	s_waitcnt vmcnt(8)
	v_mul_f32_e32 v49, 0x43000000, v61
	ds_write2_b32 v42, v47, v49 offset0:172 offset1:238
	s_waitcnt vmcnt(7)
	v_mul_f32_e32 v47, 0x43000000, v62
	s_waitcnt vmcnt(6)
	v_mul_f32_e32 v49, 0x43000000, v50
	ds_write2_b32 v43, v47, v49 offset0:48 offset1:114
	s_waitcnt vmcnt(5)
	v_mul_f32_e32 v47, 0x43000000, v51
	s_waitcnt vmcnt(4)
	v_mul_f32_e32 v49, 0x43000000, v52
	ds_write2_b32 v43, v47, v49 offset0:180 offset1:246
	s_waitcnt vmcnt(3)
	v_mul_f32_e32 v47, 0x43000000, v53
	s_waitcnt vmcnt(2)
	v_mul_f32_e32 v49, 0x43000000, v54
	ds_write2_b32 v44, v47, v49 offset0:56 offset1:122
	v_mov_b32_e32 v49, v1
	v_lshl_add_u64 v[50:51], s[4:5], 0, v[2:3]
	s_waitcnt vmcnt(1)
	v_mul_f32_e32 v47, 0x43000000, v48
	s_waitcnt vmcnt(0)
	v_mul_f32_e32 v46, 0x43000000, v46
	ds_write2_b32 v44, v47, v46 offset0:188 offset1:254
	s_waitcnt lgkmcnt(0)
	ds_read2_b32 v[52:53], v31 offset1:16
	ds_read2_b32 v[54:55], v31 offset0:33 offset1:49
	ds_read2_b32 v[56:57], v31 offset0:66 offset1:82
	ds_read2_b32 v[58:59], v31 offset0:99 offset1:115
	ds_read2_b32 v[60:61], v31 offset0:132 offset1:148
	ds_read2_b32 v[62:63], v31 offset0:165 offset1:181
	ds_read2_b32 v[64:65], v31 offset0:198 offset1:214
	ds_read2_b32 v[66:67], v31 offset0:231 offset1:247
	ds_read2_b32 v[68:69], v45 offset0:8 offset1:24
	ds_read2_b32 v[70:71], v45 offset0:41 offset1:57
	ds_read2_b32 v[72:73], v45 offset0:74 offset1:90
	ds_read2_b32 v[74:75], v45 offset0:107 offset1:123
	ds_read2_b32 v[76:77], v45 offset0:140 offset1:156
	ds_read2_b32 v[78:79], v45 offset0:173 offset1:189
	v_mov_b32_e32 v46, v1
	v_mov_b32_e32 v47, v1
	v_mov_b32_e32 v48, v1
	ds_read2_b32 v[80:81], v45 offset0:206 offset1:222
	ds_read2_b32 v[82:83], v45 offset0:239 offset1:255
	s_waitcnt lgkmcnt(14)
	v_cvt_pk_fp8_f32 v46, v52, v54
	s_waitcnt lgkmcnt(10)
	v_cvt_pk_fp8_f32 v47, v60, v62
	s_waitcnt lgkmcnt(6)
	v_cvt_pk_fp8_f32 v48, v68, v70
	s_waitcnt lgkmcnt(2)
	v_cvt_pk_fp8_f32 v49, v76, v78
	v_cvt_pk_fp8_f32 v46, v56, v58 op_sel:[0,0,1]
	v_cvt_pk_fp8_f32 v47, v64, v66 op_sel:[0,0,1]
	v_cvt_pk_fp8_f32 v48, v72, v74 op_sel:[0,0,1]
	s_waitcnt lgkmcnt(0)
	v_cvt_pk_fp8_f32 v49, v80, v82 op_sel:[0,0,1]
	v_add_u32_e32 v52, s0, v30
	v_mad_i64_i32 v[84:85], s[4:5], v52, s55, v[50:51]
	global_store_dwordx4 v[84:85], v[46:49], off nt
	v_add_u32_e32 v52, s0, v32
	v_mad_i64_i32 v[50:51], s[4:5], v52, s55, v[50:51]
	v_mov_b32_e32 v46, v1
	v_mov_b32_e32 v47, v1
	v_mov_b32_e32 v48, v1
	v_mov_b32_e32 v49, v1
	v_cvt_pk_fp8_f32 v46, v53, v55
	v_cvt_pk_fp8_f32 v47, v61, v63
	v_cvt_pk_fp8_f32 v48, v69, v71
	v_cvt_pk_fp8_f32 v49, v77, v79
	v_cvt_pk_fp8_f32 v46, v57, v59 op_sel:[0,0,1]
	v_cvt_pk_fp8_f32 v47, v65, v67 op_sel:[0,0,1]
	v_cvt_pk_fp8_f32 v48, v73, v75 op_sel:[0,0,1]
	v_cvt_pk_fp8_f32 v49, v81, v83 op_sel:[0,0,1]
	s_mov_b64 s[4:5], 0
	global_store_dwordx4 v[50:51], v[46:49], off nt
	s_waitcnt lgkmcnt(0)
; __device__ __forceinline__ void tr_item8(const float* W, int ld, int K, int nblk, int item, unsigned char* WT, bool gu, float scale, LAS float* scr, int lane) {
;     const int kb = item / nblk, nb = item % nblk, k0 = 64 * kb, n0 = 32 * nb;
;     int drow0 = n0;
;     if (gu) { const int bj = n0 / FF, j = n0 - bj * FF; drow0 = 256 * (j / 128) + 128 * bj + (j % 128); }
;     { float t_[32];
; #pragma unroll
;       for (int i = 0; i < 32; ++i) t_[i] = W[(size_t)(k0 + 2 * i + (lane >> 5)) * ld + n0 + (lane & 31)];
; #pragma unroll
;       for (int i = 0; i < 32; ++i) scr[(2 * i + (lane >> 5)) * 33 + (lane & 31)] = t_[i] * scale; }
; __device__ __forceinline__ void convert_items(Frame& F, const Args& a, int lo, int hi, int w, int nw) {
;     ...
;         if (r < NE * I_GU) { const int e = r / I_GU, rr = r % I_GU; tr_item8(a.in[18] + (size_t)e * D * 2 * FF, 2 * FF, D, 224, rr, F.ws + WS_WMGU + (size_t)e * 2 * FF * D, true, WSC_GU, scr, lane); continue; } r -= NE * I_GU;
.LBB0_1414:
	s_andn2_b64 vcc, exec, s[4:5]
	s_cbranch_vccnz .LBB0_1416
	s_add_i32 s0, s3, 0xde00
	s_bfe_u32 s4, s0, 0x70009
	s_mulk_i32 s4, 0x2493
	s_lshr_b32 s4, s4, 16
	s_mul_i32 s5, s4, 0xe00
	s_sub_i32 s0, s0, s5
	s_mul_i32 s5, s4, 0x1c00000
	s_add_u32 s6, s72, s5
	s_addc_u32 s7, s73, 0
	s_mul_i32 s4, s4, 0x700000
	s_add_u32 s4, s89, s4
	s_addc_u32 s5, s90, 0
	s_bfe_u32 s61, s0, 0xb0005
	s_mulk_i32 s61, 0x2493
	s_lshr_b32 s61, s61, 16
	s_mul_i32 s62, s61, 0xe0
	s_sub_i32 s62, s0, s62
	s_lshl_b32 s0, s62, 5
	s_and_b32 s63, s62, 0xffff
	s_cmpk_gt_u32 s63, 0x6f
	s_cselect_b32 s63, 0xfffff200, 0
	s_cselect_b32 s64, 0x80, 0
	s_add_i32 s0, s63, s0
	s_sext_i32_i16 s63, s0
	s_bfe_u32 s63, s63, 0x70018
	s_add_i32 s63, s0, s63
	s_sext_i32_i16 s65, s63
	s_and_b32 s63, s63, 0xff80
	s_sub_i32 s0, s0, s63
	s_lshl_b32 s65, s65, 1
	s_sext_i32_i16 s0, s0
	s_and_b32 s65, s65, 0xffffff00
	s_add_i32 s0, s64, s0
	s_lshl_b32 s62, s62, 7
	s_add_i32 s0, s0, s65
	s_lshl_b32 s61, s61, 6
	s_and_b32 s62, s62, 0x3ff80
	s_add_u32 s6, s6, s62
	s_addc_u32 s7, s7, 0
	v_add_u32_e32 v64, s61, v28
	v_lshl_add_u64 v[46:47], s[6:7], 0, v[0:1]
	v_mad_i64_i32 v[48:49], s[6:7], v64, s56, v[46:47]
	v_add_u32_e32 v50, 2, v64
	v_add_u32_e32 v52, 4, v64
	v_add_u32_e32 v54, 6, v64
	v_add_u32_e32 v56, 8, v64
	v_add_u32_e32 v58, 10, v64
	v_add_u32_e32 v60, 12, v64
	v_add_u32_e32 v62, 14, v64
	v_mad_i64_i32 v[50:51], s[6:7], v50, s56, v[46:47]
	v_mad_i64_i32 v[52:53], s[6:7], v52, s56, v[46:47]
	v_mad_i64_i32 v[54:55], s[6:7], v54, s56, v[46:47]
	v_mad_i64_i32 v[56:57], s[6:7], v56, s56, v[46:47]
	v_mad_i64_i32 v[58:59], s[6:7], v58, s56, v[46:47]
	v_mad_i64_i32 v[60:61], s[6:7], v60, s56, v[46:47]
	v_mad_i64_i32 v[62:63], s[6:7], v62, s56, v[46:47]
	global_load_dword v65, v[48:49], off nt
	global_load_dword v66, v[50:51], off nt
	global_load_dword v67, v[52:53], off nt
	global_load_dword v68, v[54:55], off nt
	global_load_dword v69, v[56:57], off nt
	global_load_dword v70, v[58:59], off nt
	global_load_dword v71, v[60:61], off nt
	global_load_dword v72, v[62:63], off nt
	v_add_u32_e32 v48, 16, v64
	v_mad_i64_i32 v[48:49], s[6:7], v48, s56, v[46:47]
	v_add_u32_e32 v50, 18, v64
	v_add_u32_e32 v52, 20, v64
	v_add_u32_e32 v54, 22, v64
	v_add_u32_e32 v56, 24, v64
	v_add_u32_e32 v58, 26, v64
	v_add_u32_e32 v60, 28, v64
	v_add_u32_e32 v62, 30, v64
	v_mad_i64_i32 v[50:51], s[6:7], v50, s56, v[46:47]
	v_mad_i64_i32 v[52:53], s[6:7], v52, s56, v[46:47]
	v_mad_i64_i32 v[54:55], s[6:7], v54, s56, v[46:47]
	v_mad_i64_i32 v[56:57], s[6:7], v56, s56, v[46:47]
	v_mad_i64_i32 v[58:59], s[6:7], v58, s56, v[46:47]
	v_mad_i64_i32 v[60:61], s[6:7], v60, s56, v[46:47]
	v_mad_i64_i32 v[62:63], s[6:7], v62, s56, v[46:47]
	global_load_dword v73, v[48:49], off nt
	global_load_dword v74, v[50:51], off nt
	global_load_dword v75, v[52:53], off nt
	global_load_dword v76, v[54:55], off nt
	global_load_dword v77, v[56:57], off nt
	global_load_dword v78, v[58:59], off nt
	global_load_dword v79, v[60:61], off nt
	global_load_dword v80, v[62:63], off nt
	v_add_u32_e32 v48, 32, v64
	v_add_u32_e32 v50, 34, v64
	v_add_u32_e32 v52, 36, v64
	v_add_u32_e32 v54, 38, v64
	v_add_u32_e32 v60, 44, v64
	v_mad_i64_i32 v[48:49], s[6:7], v48, s56, v[46:47]
	v_mad_i64_i32 v[50:51], s[6:7], v50, s56, v[46:47]
	v_mad_i64_i32 v[52:53], s[6:7], v52, s56, v[46:47]
	v_mad_i64_i32 v[54:55], s[6:7], v54, s56, v[46:47]
	v_add_u32_e32 v56, 40, v64
	v_add_u32_e32 v58, 42, v64
	v_mad_i64_i32 v[60:61], s[6:7], v60, s56, v[46:47]
	v_add_u32_e32 v62, 46, v64
	v_mad_i64_i32 v[56:57], s[6:7], v56, s56, v[46:47]
	v_mad_i64_i32 v[58:59], s[6:7], v58, s56, v[46:47]
	v_mad_i64_i32 v[62:63], s[6:7], v62, s56, v[46:47]
	global_load_dword v81, v[48:49], off nt
	global_load_dword v82, v[50:51], off nt
	global_load_dword v83, v[52:53], off nt
	global_load_dword v84, v[54:55], off nt
	global_load_dword v85, v[56:57], off nt
	global_load_dword v86, v[58:59], off nt
	s_nop 0
	global_load_dword v60, v[60:61], off nt
	s_nop 0
	global_load_dword v61, v[62:63], off nt
	v_add_u32_e32 v48, 48, v64
	v_add_u32_e32 v50, 50, v64
	v_add_u32_e32 v52, 52, v64
	v_add_u32_e32 v54, 54, v64
	v_mad_i64_i32 v[48:49], s[6:7], v48, s56, v[46:47]
	v_mad_i64_i32 v[50:51], s[6:7], v50, s56, v[46:47]
	v_mad_i64_i32 v[52:53], s[6:7], v52, s56, v[46:47]
	v_mad_i64_i32 v[54:55], s[6:7], v54, s56, v[46:47]
	v_add_u32_e32 v56, 56, v64
	v_add_u32_e32 v58, 58, v64
	v_mad_i64_i32 v[56:57], s[6:7], v56, s56, v[46:47]
	v_mad_i64_i32 v[58:59], s[6:7], v58, s56, v[46:47]
	global_load_dword v62, v[48:49], off nt
	s_nop 0
	global_load_dword v50, v[50:51], off nt
	s_nop 0
	global_load_dword v51, v[52:53], off nt
	s_nop 0
	global_load_dword v52, v[54:55], off nt
	global_load_dword v53, v[56:57], off nt
	s_nop 0
	global_load_dword v54, v[58:59], off nt
	v_add_u32_e32 v48, 60, v64
	v_add_u32_e32 v55, 62, v64
	v_mad_i64_i32 v[48:49], s[6:7], v48, s56, v[46:47]
	v_mad_i64_i32 v[46:47], s[6:7], v55, s56, v[46:47]
	global_load_dword v48, v[48:49], off nt
	s_nop 0
	global_load_dword v46, v[46:47], off nt
	s_waitcnt vmcnt(31)
; __device__ __forceinline__ unsigned cvt_pk4_fp8(float a, float b, float c, float d) { int w = 0; w = __builtin_amdgcn_cvt_pk_fp8_f32(a, b, w, false); w = __builtin_amdgcn_cvt_pk_fp8_f32(c, d, w, true); return (unsigned)w; }
; #define GAS __attribute__((address_space(1)))
; #define LAS __attribute__((address_space(3)))
; #define LDS_WAIT() asm volatile("s_waitcnt lgkmcnt(0)" ::: "memory")
; __device__ __forceinline__ void tr_item8(const float* W, int ld, int K, int nblk, int item, unsigned char* WT, bool gu, float scale, LAS float* scr, int lane) {
;     ...
;       for (int i = 0; i < 32; ++i) scr[(2 * i + (lane >> 5)) * 33 + (lane & 31)] = t_[i] * scale; }
;     LDS_WAIT(); asm volatile("" ::: "memory");
;     const int c = lane & 3;
; #pragma unroll
;     for (int j = 0; j < 2; ++j) { const int n = (lane >> 2) + 16 * j; const LAS float* sp = scr + (16 * c) * 33 + n;
;         v4u o; o.x = pg8::cvt_pk4_fp8(sp[0 * 33], sp[1 * 33], sp[2 * 33], sp[3 * 33]); o.y = pg8::cvt_pk4_fp8(sp[4 * 33], sp[5 * 33], sp[6 * 33], sp[7 * 33]);
;         o.z = pg8::cvt_pk4_fp8(sp[8 * 33], sp[9 * 33], sp[10 * 33], sp[11 * 33]); o.w = pg8::cvt_pk4_fp8(sp[12 * 33], sp[13 * 33], sp[14 * 33], sp[15 * 33]);
;         *(GAS v4u*)(WT + (size_t)(drow0 + n) * K + k0 + 16 * c) = o; }
;     LDS_WAIT(); asm volatile("" ::: "memory");
	v_mul_f32_e32 v47, 0x42800000, v65
	s_waitcnt vmcnt(30)
	v_mul_f32_e32 v49, 0x42800000, v66
	ds_write2_b32 v29, v47, v49 offset1:66
	s_waitcnt vmcnt(29)
	v_mul_f32_e32 v47, 0x42800000, v67
	s_waitcnt vmcnt(28)
	v_mul_f32_e32 v49, 0x42800000, v68
	ds_write2_b32 v29, v47, v49 offset0:132 offset1:198
	s_waitcnt vmcnt(27)
	v_mul_f32_e32 v47, 0x42800000, v69
	s_waitcnt vmcnt(26)
	v_mul_f32_e32 v49, 0x42800000, v70
	ds_write2_b32 v38, v47, v49 offset0:8 offset1:74
	s_waitcnt vmcnt(25)
	v_mul_f32_e32 v47, 0x42800000, v71
	s_waitcnt vmcnt(24)
	v_mul_f32_e32 v49, 0x42800000, v72
	ds_write2_b32 v38, v47, v49 offset0:140 offset1:206
	s_add_u32 s4, s4, s61
	s_addc_u32 s5, s5, 0
	s_waitcnt vmcnt(23)
	v_mul_f32_e32 v47, 0x42800000, v73
	s_waitcnt vmcnt(22)
	v_mul_f32_e32 v49, 0x42800000, v74
	ds_write2_b32 v39, v47, v49 offset0:16 offset1:82
	s_waitcnt vmcnt(21)
	v_mul_f32_e32 v47, 0x42800000, v75
	s_waitcnt vmcnt(20)
	v_mul_f32_e32 v49, 0x42800000, v76
	ds_write2_b32 v39, v47, v49 offset0:148 offset1:214
	s_waitcnt vmcnt(19)
	v_mul_f32_e32 v47, 0x42800000, v77
	s_waitcnt vmcnt(18)
	v_mul_f32_e32 v49, 0x42800000, v78
	ds_write2_b32 v40, v47, v49 offset0:24 offset1:90
	s_waitcnt vmcnt(17)
	v_mul_f32_e32 v47, 0x42800000, v79
	s_waitcnt vmcnt(16)
	v_mul_f32_e32 v49, 0x42800000, v80
	ds_write2_b32 v40, v47, v49 offset0:156 offset1:222
	s_waitcnt vmcnt(15)
	v_mul_f32_e32 v47, 0x42800000, v81
	s_waitcnt vmcnt(14)
	v_mul_f32_e32 v49, 0x42800000, v82
	ds_write2_b32 v41, v47, v49 offset0:32 offset1:98
	s_waitcnt vmcnt(13)
	v_mul_f32_e32 v47, 0x42800000, v83
	s_waitcnt vmcnt(12)
	v_mul_f32_e32 v49, 0x42800000, v84
	ds_write2_b32 v41, v47, v49 offset0:164 offset1:230
	s_waitcnt vmcnt(11)
	v_mul_f32_e32 v47, 0x42800000, v85
	s_waitcnt vmcnt(10)
	v_mul_f32_e32 v49, 0x42800000, v86
	ds_write2_b32 v42, v47, v49 offset0:40 offset1:106
	s_waitcnt vmcnt(9)
	v_mul_f32_e32 v47, 0x42800000, v60
	s_waitcnt vmcnt(8)
	v_mul_f32_e32 v49, 0x42800000, v61
	ds_write2_b32 v42, v47, v49 offset0:172 offset1:238
	v_add_u32_e32 v84, s0, v30
	v_ashrrev_i32_e32 v85, 31, v84
	v_lshlrev_b64 v[84:85], 10, v[84:85]
	s_waitcnt vmcnt(7)
	v_mul_f32_e32 v47, 0x42800000, v62
	s_waitcnt vmcnt(6)
	v_mul_f32_e32 v49, 0x42800000, v50
	ds_write2_b32 v43, v47, v49 offset0:48 offset1:114
	s_waitcnt vmcnt(5)
	v_mul_f32_e32 v47, 0x42800000, v51
	s_waitcnt vmcnt(4)
	v_mul_f32_e32 v49, 0x42800000, v52
	ds_write2_b32 v43, v47, v49 offset0:180 offset1:246
	s_waitcnt vmcnt(3)
	v_mul_f32_e32 v47, 0x42800000, v53
	s_waitcnt vmcnt(2)
	v_mul_f32_e32 v49, 0x42800000, v54
	ds_write2_b32 v44, v47, v49 offset0:56 offset1:122
	v_mov_b32_e32 v49, v1
	v_lshl_add_u64 v[50:51], s[4:5], 0, v[2:3]
	s_waitcnt vmcnt(1)
	v_mul_f32_e32 v47, 0x42800000, v48
	s_waitcnt vmcnt(0)
	v_mul_f32_e32 v46, 0x42800000, v46
	ds_write2_b32 v44, v47, v46 offset0:188 offset1:254
	s_waitcnt lgkmcnt(0)
	ds_read2_b32 v[52:53], v31 offset1:16
	ds_read2_b32 v[54:55], v31 offset0:33 offset1:49
	ds_read2_b32 v[56:57], v31 offset0:66 offset1:82
	ds_read2_b32 v[58:59], v31 offset0:99 offset1:115
	ds_read2_b32 v[60:61], v31 offset0:132 offset1:148
	ds_read2_b32 v[62:63], v31 offset0:165 offset1:181
	ds_read2_b32 v[64:65], v31 offset0:198 offset1:214
	ds_read2_b32 v[66:67], v31 offset0:231 offset1:247
	ds_read2_b32 v[68:69], v45 offset0:8 offset1:24
	ds_read2_b32 v[70:71], v45 offset0:41 offset1:57
	ds_read2_b32 v[72:73], v45 offset0:74 offset1:90
	ds_read2_b32 v[74:75], v45 offset0:107 offset1:123
	ds_read2_b32 v[76:77], v45 offset0:140 offset1:156
	ds_read2_b32 v[78:79], v45 offset0:173 offset1:189
	v_mov_b32_e32 v46, v1
	v_mov_b32_e32 v47, v1
	v_mov_b32_e32 v48, v1
	ds_read2_b32 v[80:81], v45 offset0:206 offset1:222
	ds_read2_b32 v[82:83], v45 offset0:239 offset1:255
	s_waitcnt lgkmcnt(14)
	v_cvt_pk_fp8_f32 v46, v52, v54
	s_waitcnt lgkmcnt(10)
	v_cvt_pk_fp8_f32 v47, v60, v62
	s_waitcnt lgkmcnt(6)
	v_cvt_pk_fp8_f32 v48, v68, v70
	s_waitcnt lgkmcnt(2)
	v_cvt_pk_fp8_f32 v49, v76, v78
	v_cvt_pk_fp8_f32 v46, v56, v58 op_sel:[0,0,1]
	v_cvt_pk_fp8_f32 v47, v64, v66 op_sel:[0,0,1]
	v_cvt_pk_fp8_f32 v48, v72, v74 op_sel:[0,0,1]
	s_waitcnt lgkmcnt(0)
	v_cvt_pk_fp8_f32 v49, v80, v82 op_sel:[0,0,1]
	v_lshl_add_u64 v[84:85], v[50:51], 0, v[84:85]
	v_add_u32_e32 v52, s0, v32
	global_store_dwordx4 v[84:85], v[46:49], off nt
	s_nop 1
	v_mov_b32_e32 v46, v1
	v_mov_b32_e32 v47, v1
	v_mov_b32_e32 v48, v1
	v_mov_b32_e32 v49, v1
	v_cvt_pk_fp8_f32 v46, v53, v55
	v_cvt_pk_fp8_f32 v47, v61, v63
	v_cvt_pk_fp8_f32 v48, v69, v71
	v_cvt_pk_fp8_f32 v49, v77, v79
	v_cvt_pk_fp8_f32 v46, v57, v59 op_sel:[0,0,1]
	v_cvt_pk_fp8_f32 v47, v65, v67 op_sel:[0,0,1]
	v_cvt_pk_fp8_f32 v48, v73, v75 op_sel:[0,0,1]
	v_cvt_pk_fp8_f32 v49, v81, v83 op_sel:[0,0,1]
	v_ashrrev_i32_e32 v53, 31, v52
	v_lshlrev_b64 v[52:53], 10, v[52:53]
	v_lshl_add_u64 v[50:51], v[50:51], 0, v[52:53]
	global_store_dwordx4 v[50:51], v[46:49], off nt
	s_waitcnt lgkmcnt(0)

; __device__ __forceinline__ void tr_item8(const float* W, int ld, int K, int nblk, int item, unsigned char* WT, bool gu, float scale, LAS float* scr, int lane) {
;     const int kb = item / nblk, nb = item % nblk, k0 = 64 * kb, n0 = 32 * nb;
;     int drow0 = n0;
;     if (gu) { const int bj = n0 / FF, j = n0 - bj * FF; drow0 = 256 * (j / 128) + 128 * bj + (j % 128); }
;     { float t_[32];
; #pragma unroll
;       for (int i = 0; i < 32; ++i) t_[i] = W[(size_t)(k0 + 2 * i + (lane >> 5)) * ld + n0 + (lane & 31)];
; #pragma unroll
;       for (int i = 0; i < 32; ++i) scr[(2 * i + (lane >> 5)) * 33 + (lane & 31)] = t_[i] * scale; }
; __device__ __forceinline__ void convert_items(Frame& F, const Args& a, int lo, int hi, int w, int nw) {
;     ...
;         if (r < I_DN) { tr_item8(a.in[15], D, FF, 32, r, F.ws + WS_WDN, false, WSC_DN, scr, lane); continue; } r -= I_DN;
.LBB0_1417:
	s_andn2_b64 vcc, exec, s[4:5]
	s_cbranch_vccnz .LBB0_1419
	s_lshl_b32 s0, s3, 5
	s_and_b32 s4, s9, 0x1ffc0
	s_and_b32 s6, s0, 0x3e0
	v_add_u32_e32 v46, s4, v28
	s_lshl_b32 s0, s6, 2
	v_ashrrev_i32_e32 v47, 31, v46
	v_lshl_add_u64 v[48:49], v[4:5], 0, s[0:1]
	v_lshlrev_b64 v[46:47], 12, v[46:47]
	v_lshl_add_u64 v[46:47], v[48:49], 0, v[46:47]
	v_add_co_u32_e32 v48, vcc, 0x2000, v46
	s_mov_b32 s5, s1
	s_nop 0
	v_addc_co_u32_e32 v49, vcc, 0, v47, vcc
	v_add_co_u32_e32 v50, vcc, 0x4000, v46
	s_nop 1
	v_addc_co_u32_e32 v51, vcc, 0, v47, vcc
	v_add_co_u32_e32 v52, vcc, 0x6000, v46
	s_nop 1
	v_addc_co_u32_e32 v53, vcc, 0, v47, vcc
	v_add_co_u32_e32 v54, vcc, 0x8000, v46
	s_nop 1
	v_addc_co_u32_e32 v55, vcc, 0, v47, vcc
	v_add_co_u32_e32 v56, vcc, 0xa000, v46
	s_nop 1
	v_addc_co_u32_e32 v57, vcc, 0, v47, vcc
	v_add_co_u32_e32 v58, vcc, 0xc000, v46
	s_nop 1
	v_addc_co_u32_e32 v59, vcc, 0, v47, vcc
	v_add_co_u32_e32 v60, vcc, 0xe000, v46
	s_nop 1
	v_addc_co_u32_e32 v61, vcc, 0, v47, vcc
	global_load_dword v64, v[46:47], off nt
	global_load_dword v65, v[48:49], off nt
	global_load_dword v66, v[50:51], off nt
	global_load_dword v67, v[52:53], off nt
	global_load_dword v68, v[54:55], off nt
	global_load_dword v69, v[56:57], off nt
	global_load_dword v70, v[58:59], off nt
	global_load_dword v71, v[60:61], off nt
	v_add_co_u32_e32 v48, vcc, 0x10000, v46
	s_nop 1
	v_addc_co_u32_e32 v49, vcc, 0, v47, vcc
	v_add_co_u32_e32 v50, vcc, 0x12000, v46
	s_nop 1
	v_addc_co_u32_e32 v51, vcc, 0, v47, vcc
	v_add_co_u32_e32 v52, vcc, 0x14000, v46
	s_nop 1
	v_addc_co_u32_e32 v53, vcc, 0, v47, vcc
	v_add_co_u32_e32 v54, vcc, 0x16000, v46
	s_nop 1
	v_addc_co_u32_e32 v55, vcc, 0, v47, vcc
	v_add_co_u32_e32 v56, vcc, 0x18000, v46
	s_nop 1
	v_addc_co_u32_e32 v57, vcc, 0, v47, vcc
	v_add_co_u32_e32 v58, vcc, 0x1a000, v46
	s_nop 1
	v_addc_co_u32_e32 v59, vcc, 0, v47, vcc
	v_add_co_u32_e32 v60, vcc, 0x1c000, v46
	s_nop 1
	v_addc_co_u32_e32 v61, vcc, 0, v47, vcc
	v_add_co_u32_e32 v62, vcc, 0x1e000, v46
	s_nop 1
	v_addc_co_u32_e32 v63, vcc, 0, v47, vcc
	global_load_dword v72, v[48:49], off nt
	global_load_dword v73, v[50:51], off nt
	global_load_dword v74, v[52:53], off nt
	global_load_dword v75, v[54:55], off nt
	global_load_dword v76, v[56:57], off nt
	global_load_dword v77, v[58:59], off nt
	global_load_dword v78, v[60:61], off nt
	global_load_dword v79, v[62:63], off nt
	v_add_co_u32_e32 v48, vcc, 0x20000, v46
	s_nop 1
	v_addc_co_u32_e32 v49, vcc, 0, v47, vcc
	v_add_co_u32_e32 v50, vcc, 0x22000, v46
	s_nop 1
	v_addc_co_u32_e32 v51, vcc, 0, v47, vcc
	v_add_co_u32_e32 v52, vcc, 0x24000, v46
	s_nop 1
	v_addc_co_u32_e32 v53, vcc, 0, v47, vcc
	v_add_co_u32_e32 v54, vcc, 0x26000, v46
	s_nop 1
	v_addc_co_u32_e32 v55, vcc, 0, v47, vcc
	v_add_co_u32_e32 v56, vcc, 0x28000, v46
	s_nop 1
	v_addc_co_u32_e32 v57, vcc, 0, v47, vcc
	v_add_co_u32_e32 v58, vcc, 0x2a000, v46
	s_nop 1
	v_addc_co_u32_e32 v59, vcc, 0, v47, vcc
	v_add_co_u32_e32 v60, vcc, 0x2c000, v46
	s_nop 1
	v_addc_co_u32_e32 v61, vcc, 0, v47, vcc
	v_add_co_u32_e32 v62, vcc, 0x2e000, v46
	s_nop 1
	v_addc_co_u32_e32 v63, vcc, 0, v47, vcc
	global_load_dword v80, v[48:49], off nt
	global_load_dword v81, v[50:51], off nt
	global_load_dword v82, v[52:53], off nt
	global_load_dword v83, v[54:55], off nt
	global_load_dword v84, v[56:57], off nt
	global_load_dword v85, v[58:59], off nt
	s_nop 0
	global_load_dword v60, v[60:61], off nt
	s_nop 0
	global_load_dword v61, v[62:63], off nt
	v_add_co_u32_e32 v48, vcc, 0x30000, v46
	s_nop 1
	v_addc_co_u32_e32 v49, vcc, 0, v47, vcc
	v_add_co_u32_e32 v50, vcc, 0x32000, v46
	s_nop 1
	v_addc_co_u32_e32 v51, vcc, 0, v47, vcc
	v_add_co_u32_e32 v52, vcc, 0x34000, v46
	s_nop 1
	v_addc_co_u32_e32 v53, vcc, 0, v47, vcc
	v_add_co_u32_e32 v54, vcc, 0x36000, v46
	s_nop 1
	v_addc_co_u32_e32 v55, vcc, 0, v47, vcc
	v_add_co_u32_e32 v56, vcc, 0x38000, v46
	s_nop 1
	v_addc_co_u32_e32 v57, vcc, 0, v47, vcc
	v_add_co_u32_e32 v58, vcc, 0x3a000, v46
	s_nop 1
	v_addc_co_u32_e32 v59, vcc, 0, v47, vcc
	global_load_dword v62, v[48:49], off nt
	s_nop 0
	global_load_dword v50, v[50:51], off nt
	s_nop 0
	global_load_dword v51, v[52:53], off nt
	s_nop 0
	global_load_dword v52, v[54:55], off nt
	global_load_dword v53, v[56:57], off nt
	s_nop 0
	global_load_dword v54, v[58:59], off nt
	v_add_co_u32_e32 v48, vcc, 0x3c000, v46
	s_nop 1
	v_addc_co_u32_e32 v49, vcc, 0, v47, vcc
	v_add_co_u32_e32 v46, vcc, 0x3e000, v46
	s_nop 1
	v_addc_co_u32_e32 v47, vcc, 0, v47, vcc
	global_load_dword v48, v[48:49], off nt
	s_nop 0
	global_load_dword v46, v[46:47], off nt
	s_waitcnt vmcnt(31)
	v_mul_f32_e32 v47, 0x43000000, v64
	s_waitcnt vmcnt(30)
; __device__ __forceinline__ unsigned cvt_pk4_fp8(float a, float b, float c, float d) { int w = 0; w = __builtin_amdgcn_cvt_pk_fp8_f32(a, b, w, false); w = __builtin_amdgcn_cvt_pk_fp8_f32(c, d, w, true); return (unsigned)w; }
; #define GAS __attribute__((address_space(1)))
; #define LAS __attribute__((address_space(3)))
; #define LDS_WAIT() asm volatile("s_waitcnt lgkmcnt(0)" ::: "memory")
; __device__ __forceinline__ void tr_item8(const float* W, int ld, int K, int nblk, int item, unsigned char* WT, bool gu, float scale, LAS float* scr, int lane) {
;     ...
;       for (int i = 0; i < 32; ++i) scr[(2 * i + (lane >> 5)) * 33 + (lane & 31)] = t_[i] * scale; }
;     LDS_WAIT(); asm volatile("" ::: "memory");
;     const int c = lane & 3;
; #pragma unroll
;     for (int j = 0; j < 2; ++j) { const int n = (lane >> 2) + 16 * j; const LAS float* sp = scr + (16 * c) * 33 + n;
;         v4u o; o.x = pg8::cvt_pk4_fp8(sp[0 * 33], sp[1 * 33], sp[2 * 33], sp[3 * 33]); o.y = pg8::cvt_pk4_fp8(sp[4 * 33], sp[5 * 33], sp[6 * 33], sp[7 * 33]);
;         o.z = pg8::cvt_pk4_fp8(sp[8 * 33], sp[9 * 33], sp[10 * 33], sp[11 * 33]); o.w = pg8::cvt_pk4_fp8(sp[12 * 33], sp[13 * 33], sp[14 * 33], sp[15 * 33]);
;         *(GAS v4u*)(WT + (size_t)(drow0 + n) * K + k0 + 16 * c) = o; }
;     LDS_WAIT(); asm volatile("" ::: "memory");
	v_mul_f32_e32 v49, 0x43000000, v65
	ds_write2_b32 v29, v47, v49 offset1:66
	s_waitcnt vmcnt(29)
	v_mul_f32_e32 v47, 0x43000000, v66
	s_waitcnt vmcnt(28)
	v_mul_f32_e32 v49, 0x43000000, v67
	ds_write2_b32 v29, v47, v49 offset0:132 offset1:198
	s_waitcnt vmcnt(27)
	v_mul_f32_e32 v47, 0x43000000, v68
	s_waitcnt vmcnt(26)
	v_mul_f32_e32 v49, 0x43000000, v69
	ds_write2_b32 v38, v47, v49 offset0:8 offset1:74
	s_waitcnt vmcnt(25)
	v_mul_f32_e32 v47, 0x43000000, v70
	s_waitcnt vmcnt(24)
	v_mul_f32_e32 v49, 0x43000000, v71
	ds_write2_b32 v38, v47, v49 offset0:140 offset1:206
	s_waitcnt vmcnt(23)
	v_mul_f32_e32 v47, 0x43000000, v72
	s_waitcnt vmcnt(22)
	v_mul_f32_e32 v49, 0x43000000, v73
	ds_write2_b32 v39, v47, v49 offset0:16 offset1:82
	s_waitcnt vmcnt(21)
	v_mul_f32_e32 v47, 0x43000000, v74
	s_waitcnt vmcnt(20)
	v_mul_f32_e32 v49, 0x43000000, v75
	ds_write2_b32 v39, v47, v49 offset0:148 offset1:214
	s_waitcnt vmcnt(19)
	v_mul_f32_e32 v47, 0x43000000, v76
	s_waitcnt vmcnt(18)
	v_mul_f32_e32 v49, 0x43000000, v77
	ds_write2_b32 v40, v47, v49 offset0:24 offset1:90
	s_waitcnt vmcnt(17)
	v_mul_f32_e32 v47, 0x43000000, v78
	s_waitcnt vmcnt(16)
	v_mul_f32_e32 v49, 0x43000000, v79
	ds_write2_b32 v40, v47, v49 offset0:156 offset1:222
	s_waitcnt vmcnt(15)
	v_mul_f32_e32 v47, 0x43000000, v80
	s_waitcnt vmcnt(14)
	v_mul_f32_e32 v49, 0x43000000, v81
	ds_write2_b32 v41, v47, v49 offset0:32 offset1:98
	s_waitcnt vmcnt(13)
	v_mul_f32_e32 v47, 0x43000000, v82
	s_waitcnt vmcnt(12)
	v_mul_f32_e32 v49, 0x43000000, v83
	ds_write2_b32 v41, v47, v49 offset0:164 offset1:230
	s_waitcnt vmcnt(11)
	v_mul_f32_e32 v47, 0x43000000, v84
	s_waitcnt vmcnt(10)
	v_mul_f32_e32 v49, 0x43000000, v85
	ds_write2_b32 v42, v47, v49 offset0:40 offset1:106
	s_waitcnt vmcnt(9)
	v_mul_f32_e32 v47, 0x43000000, v60
	s_waitcnt vmcnt(8)
	v_mul_f32_e32 v49, 0x43000000, v61
	ds_write2_b32 v42, v47, v49 offset0:172 offset1:238
	s_waitcnt vmcnt(7)
	v_mul_f32_e32 v47, 0x43000000, v62
	s_waitcnt vmcnt(6)
	v_mul_f32_e32 v49, 0x43000000, v50
	ds_write2_b32 v43, v47, v49 offset0:48 offset1:114
	s_waitcnt vmcnt(5)
	v_mul_f32_e32 v47, 0x43000000, v51
	s_waitcnt vmcnt(4)
	v_mul_f32_e32 v49, 0x43000000, v52
	ds_write2_b32 v43, v47, v49 offset0:180 offset1:246
	s_waitcnt vmcnt(3)
	v_mul_f32_e32 v47, 0x43000000, v53
	s_waitcnt vmcnt(2)
	v_mul_f32_e32 v49, 0x43000000, v54
	ds_write2_b32 v44, v47, v49 offset0:56 offset1:122
	v_mov_b32_e32 v49, 0
	v_lshl_add_u64 v[50:51], v[16:17], 0, s[4:5]
	s_waitcnt vmcnt(1)
	v_mul_f32_e32 v47, 0x43000000, v48
	s_waitcnt vmcnt(0)
	v_mul_f32_e32 v46, 0x43000000, v46
	ds_write2_b32 v44, v47, v46 offset0:188 offset1:254
	s_waitcnt lgkmcnt(0)
	ds_read2_b32 v[52:53], v31 offset1:16
	ds_read2_b32 v[54:55], v31 offset0:33 offset1:49
	ds_read2_b32 v[56:57], v31 offset0:66 offset1:82
	ds_read2_b32 v[58:59], v31 offset0:99 offset1:115
	ds_read2_b32 v[60:61], v31 offset0:132 offset1:148
	ds_read2_b32 v[62:63], v31 offset0:165 offset1:181
	ds_read2_b32 v[64:65], v31 offset0:198 offset1:214
	ds_read2_b32 v[66:67], v31 offset0:231 offset1:247
	ds_read2_b32 v[68:69], v45 offset0:8 offset1:24
	ds_read2_b32 v[70:71], v45 offset0:41 offset1:57
	ds_read2_b32 v[72:73], v45 offset0:74 offset1:90
	ds_read2_b32 v[74:75], v45 offset0:107 offset1:123
	ds_read2_b32 v[76:77], v45 offset0:140 offset1:156
	ds_read2_b32 v[78:79], v45 offset0:173 offset1:189
	v_mov_b32_e32 v46, 0
	v_mov_b32_e32 v47, 0
	v_mov_b32_e32 v48, 0
	ds_read2_b32 v[80:81], v45 offset0:206 offset1:222
	ds_read2_b32 v[82:83], v45 offset0:239 offset1:255
	s_waitcnt lgkmcnt(14)
	v_cvt_pk_fp8_f32 v46, v52, v54
	s_waitcnt lgkmcnt(10)
	v_cvt_pk_fp8_f32 v47, v60, v62
	s_waitcnt lgkmcnt(6)
	v_cvt_pk_fp8_f32 v48, v68, v70
	s_waitcnt lgkmcnt(2)
	v_cvt_pk_fp8_f32 v49, v76, v78
	v_cvt_pk_fp8_f32 v46, v56, v58 op_sel:[0,0,1]
	v_cvt_pk_fp8_f32 v47, v64, v66 op_sel:[0,0,1]
	v_cvt_pk_fp8_f32 v48, v72, v74 op_sel:[0,0,1]
	s_waitcnt lgkmcnt(0)
	v_cvt_pk_fp8_f32 v49, v80, v82 op_sel:[0,0,1]
	v_add_u32_e32 v52, s6, v30
	v_mad_i64_i32 v[84:85], s[4:5], v52, s55, v[50:51]
	global_store_dwordx4 v[84:85], v[46:49], off nt
	v_add_u32_e32 v52, s6, v32
	v_mad_i64_i32 v[50:51], s[4:5], v52, s55, v[50:51]
	v_mov_b32_e32 v46, 0
	v_mov_b32_e32 v47, 0
	v_mov_b32_e32 v48, 0
	v_mov_b32_e32 v49, 0
	v_cvt_pk_fp8_f32 v46, v53, v55
	v_cvt_pk_fp8_f32 v47, v61, v63
	v_cvt_pk_fp8_f32 v48, v69, v71
	v_cvt_pk_fp8_f32 v49, v77, v79
	v_cvt_pk_fp8_f32 v46, v57, v59 op_sel:[0,0,1]
	v_cvt_pk_fp8_f32 v47, v65, v67 op_sel:[0,0,1]
	v_cvt_pk_fp8_f32 v48, v73, v75 op_sel:[0,0,1]
	v_cvt_pk_fp8_f32 v49, v81, v83 op_sel:[0,0,1]
	global_store_dwordx4 v[50:51], v[46:49], off nt
	s_waitcnt lgkmcnt(0)

; __device__ __forceinline__ void tr_item8(const float* W, int ld, int K, int nblk, int item, unsigned char* WT, bool gu, float scale, LAS float* scr, int lane) {
;     const int kb = item / nblk, nb = item % nblk, k0 = 64 * kb, n0 = 32 * nb;
;     int drow0 = n0;
;     if (gu) { const int bj = n0 / FF, j = n0 - bj * FF; drow0 = 256 * (j / 128) + 128 * bj + (j % 128); }
;     { float t_[32];
; #pragma unroll
;       for (int i = 0; i < 32; ++i) t_[i] = W[(size_t)(k0 + 2 * i + (lane >> 5)) * ld + n0 + (lane & 31)];
; #pragma unroll
;       for (int i = 0; i < 32; ++i) scr[(2 * i + (lane >> 5)) * 33 + (lane & 31)] = t_[i] * scale; }
; __device__ __forceinline__ void convert_items(Frame& F, const Args& a, int lo, int hi, int w, int nw) {
;     ...
;         if (r < I_GU) { tr_item8(a.in[14], 2 * FF, D, 224, r, F.ws + WS_WGU, true, WSC_GU, scr, lane); continue; } r -= I_GU;
.LBB0_1420:
	s_andn2_b64 vcc, exec, s[4:5]
	s_cbranch_vccnz .LBB0_1422
	s_add_i32 s0, s3, 0xf300
	s_bfe_u32 s4, s0, 0xb0005
	s_mulk_i32 s4, 0x2493
	s_lshr_b32 s4, s4, 16
	s_mul_i32 s5, s4, 0xe0
	s_sub_i32 s0, s0, s5
	s_lshl_b32 s5, s0, 5
	s_and_b32 s6, s0, 0xffff
	s_cmpk_gt_u32 s6, 0x6f
	s_cselect_b32 s61, 0xfffff200, 0
	s_cselect_b32 s62, 0x80, 0
	s_lshl_b32 s0, s0, 7
	s_lshl_b32 s4, s4, 6
	s_and_b32 s0, s0, 0x3ff80
	v_add_u32_e32 v64, s4, v28
	v_lshl_add_u64 v[46:47], v[6:7], 0, s[0:1]
	v_mad_i64_i32 v[48:49], s[6:7], v64, s56, v[46:47]
	v_add_u32_e32 v50, 2, v64
	v_add_u32_e32 v52, 4, v64
	v_add_u32_e32 v54, 6, v64
	v_add_u32_e32 v56, 8, v64
	v_add_u32_e32 v58, 10, v64
	v_add_u32_e32 v60, 12, v64
	v_add_u32_e32 v62, 14, v64
	v_mad_i64_i32 v[50:51], s[6:7], v50, s56, v[46:47]
	v_mad_i64_i32 v[52:53], s[6:7], v52, s56, v[46:47]
	v_mad_i64_i32 v[54:55], s[6:7], v54, s56, v[46:47]
	v_mad_i64_i32 v[56:57], s[6:7], v56, s56, v[46:47]
	v_mad_i64_i32 v[58:59], s[6:7], v58, s56, v[46:47]
	v_mad_i64_i32 v[60:61], s[6:7], v60, s56, v[46:47]
	v_mad_i64_i32 v[62:63], s[6:7], v62, s56, v[46:47]
	global_load_dword v65, v[48:49], off nt
	global_load_dword v66, v[50:51], off nt
	global_load_dword v67, v[52:53], off nt
	global_load_dword v68, v[54:55], off nt
	global_load_dword v69, v[56:57], off nt
	global_load_dword v70, v[58:59], off nt
	global_load_dword v71, v[60:61], off nt
	global_load_dword v72, v[62:63], off nt
	v_add_u32_e32 v48, 16, v64
	v_mad_i64_i32 v[48:49], s[6:7], v48, s56, v[46:47]
	v_add_u32_e32 v50, 18, v64
	v_add_u32_e32 v52, 20, v64
	v_add_u32_e32 v54, 22, v64
	v_add_u32_e32 v56, 24, v64
	v_add_u32_e32 v58, 26, v64
	v_add_u32_e32 v60, 28, v64
	v_add_u32_e32 v62, 30, v64
	v_mad_i64_i32 v[50:51], s[6:7], v50, s56, v[46:47]
	v_mad_i64_i32 v[52:53], s[6:7], v52, s56, v[46:47]
	v_mad_i64_i32 v[54:55], s[6:7], v54, s56, v[46:47]
	v_mad_i64_i32 v[56:57], s[6:7], v56, s56, v[46:47]
	v_mad_i64_i32 v[58:59], s[6:7], v58, s56, v[46:47]
	v_mad_i64_i32 v[60:61], s[6:7], v60, s56, v[46:47]
	v_mad_i64_i32 v[62:63], s[6:7], v62, s56, v[46:47]
	global_load_dword v73, v[48:49], off nt
	global_load_dword v74, v[50:51], off nt
	global_load_dword v75, v[52:53], off nt
	global_load_dword v76, v[54:55], off nt
	global_load_dword v77, v[56:57], off nt
	global_load_dword v78, v[58:59], off nt
	global_load_dword v79, v[60:61], off nt
	global_load_dword v80, v[62:63], off nt
	v_add_u32_e32 v48, 32, v64
	v_add_u32_e32 v50, 34, v64
	v_add_u32_e32 v52, 36, v64
	v_add_u32_e32 v54, 38, v64
	v_add_u32_e32 v60, 44, v64
	v_mad_i64_i32 v[48:49], s[6:7], v48, s56, v[46:47]
	v_mad_i64_i32 v[50:51], s[6:7], v50, s56, v[46:47]
	v_mad_i64_i32 v[52:53], s[6:7], v52, s56, v[46:47]
	v_mad_i64_i32 v[54:55], s[6:7], v54, s56, v[46:47]
	v_add_u32_e32 v56, 40, v64
	v_add_u32_e32 v58, 42, v64
	v_mad_i64_i32 v[60:61], s[6:7], v60, s56, v[46:47]
	v_add_u32_e32 v62, 46, v64
	v_mad_i64_i32 v[56:57], s[6:7], v56, s56, v[46:47]
	v_mad_i64_i32 v[58:59], s[6:7], v58, s56, v[46:47]
	v_mad_i64_i32 v[62:63], s[6:7], v62, s56, v[46:47]
	global_load_dword v81, v[48:49], off nt
	global_load_dword v82, v[50:51], off nt
	global_load_dword v83, v[52:53], off nt
	global_load_dword v84, v[54:55], off nt
	global_load_dword v85, v[56:57], off nt
	global_load_dword v86, v[58:59], off nt
	s_nop 0
	global_load_dword v60, v[60:61], off nt
	s_nop 0
	global_load_dword v61, v[62:63], off nt
	v_add_u32_e32 v48, 48, v64
	v_add_u32_e32 v50, 50, v64
	v_add_u32_e32 v52, 52, v64
	v_add_u32_e32 v54, 54, v64
	v_mad_i64_i32 v[48:49], s[6:7], v48, s56, v[46:47]
	v_mad_i64_i32 v[50:51], s[6:7], v50, s56, v[46:47]
	v_mad_i64_i32 v[52:53], s[6:7], v52, s56, v[46:47]
	v_mad_i64_i32 v[54:55], s[6:7], v54, s56, v[46:47]
	v_add_u32_e32 v56, 56, v64
	v_add_u32_e32 v58, 58, v64
	v_mad_i64_i32 v[56:57], s[6:7], v56, s56, v[46:47]
	v_mad_i64_i32 v[58:59], s[6:7], v58, s56, v[46:47]
	global_load_dword v62, v[48:49], off nt
	s_nop 0
	global_load_dword v50, v[50:51], off nt
	s_nop 0
	global_load_dword v51, v[52:53], off nt
	s_nop 0
	global_load_dword v52, v[54:55], off nt
	global_load_dword v53, v[56:57], off nt
	s_nop 0
	global_load_dword v54, v[58:59], off nt
	v_add_u32_e32 v48, 60, v64
	v_add_u32_e32 v55, 62, v64
	v_mad_i64_i32 v[48:49], s[6:7], v48, s56, v[46:47]
	v_mad_i64_i32 v[46:47], s[6:7], v55, s56, v[46:47]
	global_load_dword v48, v[48:49], off nt
	s_nop 0
	global_load_dword v46, v[46:47], off nt
	s_waitcnt vmcnt(31)
	v_mul_f32_e32 v47, 0x42800000, v65
	s_waitcnt vmcnt(30)
	v_mul_f32_e32 v49, 0x42800000, v66
	ds_write2_b32 v29, v47, v49 offset1:66
	s_waitcnt vmcnt(29)
	v_mul_f32_e32 v47, 0x42800000, v67
	s_waitcnt vmcnt(28)
	v_mul_f32_e32 v49, 0x42800000, v68
	ds_write2_b32 v29, v47, v49 offset0:132 offset1:198
	s_waitcnt vmcnt(27)
	v_mul_f32_e32 v47, 0x42800000, v69
	s_waitcnt vmcnt(26)
; __device__ __forceinline__ unsigned cvt_pk4_fp8(float a, float b, float c, float d) { int w = 0; w = __builtin_amdgcn_cvt_pk_fp8_f32(a, b, w, false); w = __builtin_amdgcn_cvt_pk_fp8_f32(c, d, w, true); return (unsigned)w; }
; #define GAS __attribute__((address_space(1)))
; #define LAS __attribute__((address_space(3)))
; #define LDS_WAIT() asm volatile("s_waitcnt lgkmcnt(0)" ::: "memory")
; __device__ __forceinline__ void tr_item8(const float* W, int ld, int K, int nblk, int item, unsigned char* WT, bool gu, float scale, LAS float* scr, int lane) {
;     ...
;       for (int i = 0; i < 32; ++i) scr[(2 * i + (lane >> 5)) * 33 + (lane & 31)] = t_[i] * scale; }
;     LDS_WAIT(); asm volatile("" ::: "memory");
;     const int c = lane & 3;
; #pragma unroll
;     for (int j = 0; j < 2; ++j) { const int n = (lane >> 2) + 16 * j; const LAS float* sp = scr + (16 * c) * 33 + n;
;         v4u o; o.x = pg8::cvt_pk4_fp8(sp[0 * 33], sp[1 * 33], sp[2 * 33], sp[3 * 33]); o.y = pg8::cvt_pk4_fp8(sp[4 * 33], sp[5 * 33], sp[6 * 33], sp[7 * 33]);
;         o.z = pg8::cvt_pk4_fp8(sp[8 * 33], sp[9 * 33], sp[10 * 33], sp[11 * 33]); o.w = pg8::cvt_pk4_fp8(sp[12 * 33], sp[13 * 33], sp[14 * 33], sp[15 * 33]);
;         *(GAS v4u*)(WT + (size_t)(drow0 + n) * K + k0 + 16 * c) = o; }
;     LDS_WAIT(); asm volatile("" ::: "memory");
	v_mul_f32_e32 v49, 0x42800000, v70
	ds_write2_b32 v38, v47, v49 offset0:8 offset1:74
	s_waitcnt vmcnt(25)
	v_mul_f32_e32 v47, 0x42800000, v71
	s_waitcnt vmcnt(24)
	v_mul_f32_e32 v49, 0x42800000, v72
	ds_write2_b32 v38, v47, v49 offset0:140 offset1:206
	s_add_i32 s0, s61, s5
	s_sext_i32_i16 s5, s0
	s_bfe_u32 s5, s5, 0x70018
	s_add_i32 s5, s0, s5
	s_sext_i32_i16 s6, s5
	s_and_b32 s5, s5, 0xff80
	s_sub_i32 s0, s0, s5
	s_lshl_b32 s6, s6, 1
	s_sext_i32_i16 s0, s0
	s_waitcnt vmcnt(23)
	v_mul_f32_e32 v47, 0x42800000, v73
	s_waitcnt vmcnt(22)
	v_mul_f32_e32 v49, 0x42800000, v74
	ds_write2_b32 v39, v47, v49 offset0:16 offset1:82
	s_waitcnt vmcnt(21)
	v_mul_f32_e32 v47, 0x42800000, v75
	s_waitcnt vmcnt(20)
	v_mul_f32_e32 v49, 0x42800000, v76
	ds_write2_b32 v39, v47, v49 offset0:148 offset1:214
	s_waitcnt vmcnt(19)
	v_mul_f32_e32 v47, 0x42800000, v77
	s_waitcnt vmcnt(18)
	v_mul_f32_e32 v49, 0x42800000, v78
	ds_write2_b32 v40, v47, v49 offset0:24 offset1:90
	s_waitcnt vmcnt(17)
	v_mul_f32_e32 v47, 0x42800000, v79
	s_waitcnt vmcnt(16)
	v_mul_f32_e32 v49, 0x42800000, v80
	ds_write2_b32 v40, v47, v49 offset0:156 offset1:222
	s_and_b32 s6, s6, 0xffffff00
	s_add_i32 s0, s62, s0
	s_add_i32 s0, s0, s6
	s_mov_b32 s5, s1
	s_waitcnt vmcnt(15)
	v_mul_f32_e32 v47, 0x42800000, v81
	s_waitcnt vmcnt(14)
	v_mul_f32_e32 v49, 0x42800000, v82
	ds_write2_b32 v41, v47, v49 offset0:32 offset1:98
	s_waitcnt vmcnt(13)
	v_mul_f32_e32 v47, 0x42800000, v83
	s_waitcnt vmcnt(12)
	v_mul_f32_e32 v49, 0x42800000, v84
	ds_write2_b32 v41, v47, v49 offset0:164 offset1:230
	s_waitcnt vmcnt(11)
	v_mul_f32_e32 v47, 0x42800000, v85
	s_waitcnt vmcnt(10)
	v_mul_f32_e32 v49, 0x42800000, v86
	ds_write2_b32 v42, v47, v49 offset0:40 offset1:106
	s_waitcnt vmcnt(9)
	v_mul_f32_e32 v47, 0x42800000, v60
	s_waitcnt vmcnt(8)
	v_mul_f32_e32 v49, 0x42800000, v61
	ds_write2_b32 v42, v47, v49 offset0:172 offset1:238
	v_add_u32_e32 v84, s0, v30
	v_ashrrev_i32_e32 v85, 31, v84
	v_lshlrev_b64 v[84:85], 10, v[84:85]
	s_waitcnt vmcnt(7)
	v_mul_f32_e32 v47, 0x42800000, v62
	s_waitcnt vmcnt(6)
	v_mul_f32_e32 v49, 0x42800000, v50
	ds_write2_b32 v43, v47, v49 offset0:48 offset1:114
	s_waitcnt vmcnt(5)
	v_mul_f32_e32 v47, 0x42800000, v51
	s_waitcnt vmcnt(4)
	v_mul_f32_e32 v49, 0x42800000, v52
	ds_write2_b32 v43, v47, v49 offset0:180 offset1:246
	s_waitcnt vmcnt(3)
	v_mul_f32_e32 v47, 0x42800000, v53
	s_waitcnt vmcnt(2)
	v_mul_f32_e32 v49, 0x42800000, v54
	ds_write2_b32 v44, v47, v49 offset0:56 offset1:122
	v_mov_b32_e32 v49, 0
	v_lshl_add_u64 v[50:51], v[18:19], 0, s[4:5]
	s_waitcnt vmcnt(1)
	v_mul_f32_e32 v47, 0x42800000, v48
	s_waitcnt vmcnt(0)
	v_mul_f32_e32 v46, 0x42800000, v46
	ds_write2_b32 v44, v47, v46 offset0:188 offset1:254
	s_waitcnt lgkmcnt(0)
	ds_read2_b32 v[52:53], v31 offset1:16
	ds_read2_b32 v[54:55], v31 offset0:33 offset1:49
	ds_read2_b32 v[56:57], v31 offset0:66 offset1:82
	ds_read2_b32 v[58:59], v31 offset0:99 offset1:115
	ds_read2_b32 v[60:61], v31 offset0:132 offset1:148
	ds_read2_b32 v[62:63], v31 offset0:165 offset1:181
	ds_read2_b32 v[64:65], v31 offset0:198 offset1:214
	ds_read2_b32 v[66:67], v31 offset0:231 offset1:247
	ds_read2_b32 v[68:69], v45 offset0:8 offset1:24
	ds_read2_b32 v[70:71], v45 offset0:41 offset1:57
	ds_read2_b32 v[72:73], v45 offset0:74 offset1:90
	ds_read2_b32 v[74:75], v45 offset0:107 offset1:123
	ds_read2_b32 v[76:77], v45 offset0:140 offset1:156
	ds_read2_b32 v[78:79], v45 offset0:173 offset1:189
	v_mov_b32_e32 v46, 0
	v_mov_b32_e32 v47, 0
	v_mov_b32_e32 v48, 0
	ds_read2_b32 v[80:81], v45 offset0:206 offset1:222
	ds_read2_b32 v[82:83], v45 offset0:239 offset1:255
	s_waitcnt lgkmcnt(14)
	v_cvt_pk_fp8_f32 v46, v52, v54
	s_waitcnt lgkmcnt(10)
	v_cvt_pk_fp8_f32 v47, v60, v62
	s_waitcnt lgkmcnt(6)
	v_cvt_pk_fp8_f32 v48, v68, v70
	s_waitcnt lgkmcnt(2)
	v_cvt_pk_fp8_f32 v49, v76, v78
	v_cvt_pk_fp8_f32 v46, v56, v58 op_sel:[0,0,1]
	v_cvt_pk_fp8_f32 v47, v64, v66 op_sel:[0,0,1]
	v_cvt_pk_fp8_f32 v48, v72, v74 op_sel:[0,0,1]
	s_waitcnt lgkmcnt(0)
	v_cvt_pk_fp8_f32 v49, v80, v82 op_sel:[0,0,1]
	v_lshl_add_u64 v[84:85], v[50:51], 0, v[84:85]
	v_add_u32_e32 v52, s0, v32
	global_store_dwordx4 v[84:85], v[46:49], off nt
	s_nop 1
	v_mov_b32_e32 v46, 0
	v_mov_b32_e32 v47, 0
	v_mov_b32_e32 v48, 0
	v_mov_b32_e32 v49, 0
	v_cvt_pk_fp8_f32 v46, v53, v55
	v_cvt_pk_fp8_f32 v47, v61, v63
	v_cvt_pk_fp8_f32 v48, v69, v71
	v_cvt_pk_fp8_f32 v49, v77, v79
	v_cvt_pk_fp8_f32 v46, v57, v59 op_sel:[0,0,1]
	v_cvt_pk_fp8_f32 v47, v65, v67 op_sel:[0,0,1]
	v_cvt_pk_fp8_f32 v48, v73, v75 op_sel:[0,0,1]
	v_cvt_pk_fp8_f32 v49, v81, v83 op_sel:[0,0,1]
	v_ashrrev_i32_e32 v53, 31, v52
	v_lshlrev_b64 v[52:53], 10, v[52:53]
	v_lshl_add_u64 v[50:51], v[50:51], 0, v[52:53]
	global_store_dwordx4 v[50:51], v[46:49], off nt
	s_waitcnt lgkmcnt(0)

; #define LDS_WAIT() asm volatile("s_waitcnt lgkmcnt(0)" ::: "memory")
; __device__ __forceinline__ void tr_item(const float* W, int ld, int K, int nblk, int item, bf16* WT, bool gu, LAS float* scr, int lane) {
;     const int kb = item / nblk, nb = item % nblk, k0 = 64 * kb, n0 = 32 * nb;
;     int drow0 = n0;
;     if (gu) { const int bj = n0 / FF, j = n0 - bj * FF; drow0 = 256 * (j / 128) + 128 * bj + (j % 128); }
;     { float t_[32];
; #pragma unroll
;       for (int i = 0; i < 32; ++i) t_[i] = W[(size_t)(k0 + 2 * i + (lane >> 5)) * ld + n0 + (lane & 31)];
; #pragma unroll
;       for (int i = 0; i < 32; ++i) scr[(2 * i + (lane >> 5)) * 33 + (lane & 31)] = t_[i]; }
;     LDS_WAIT(); asm volatile("" ::: "memory");
; __device__ __forceinline__ void convert_items(Frame& F, const Args& a, int lo, int hi, int w, int nw) {
;     ...
;         if (r < I_SO) { tr_item(a.in[12], D, D, 32, r, (bf16*)(F.ws + WS_WSWAOUT), false, scr, lane); continue; } r -= I_SO;
.LBB0_1423:
	s_andn2_b64 vcc, exec, s[4:5]
	s_cbranch_vccnz .LBB0_1425
	s_add_i32 s0, s9, 0x2000
	s_and_b32 s5, s0, 0x1ffc0
	s_and_b32 s4, s8, 0x3e0
	v_add_u32_e32 v46, s5, v28
	s_lshl_b32 s0, s4, 2
	v_ashrrev_i32_e32 v47, 31, v46
	v_lshl_add_u64 v[48:49], v[8:9], 0, s[0:1]
	v_lshlrev_b64 v[46:47], 12, v[46:47]
	v_lshl_add_u64 v[46:47], v[48:49], 0, v[46:47]
	v_add_co_u32_e32 v48, vcc, 0x2000, v46
	s_lshl_b32 s0, s5, 1
	s_nop 0
	v_addc_co_u32_e32 v49, vcc, 0, v47, vcc
	v_add_co_u32_e32 v50, vcc, 0x4000, v46
	s_nop 1
	v_addc_co_u32_e32 v51, vcc, 0, v47, vcc
	v_add_co_u32_e32 v52, vcc, 0x6000, v46
	s_nop 1
	v_addc_co_u32_e32 v53, vcc, 0, v47, vcc
	v_add_co_u32_e32 v54, vcc, 0x8000, v46
	s_nop 1
	v_addc_co_u32_e32 v55, vcc, 0, v47, vcc
	v_add_co_u32_e32 v56, vcc, 0xa000, v46
	s_nop 1
	v_addc_co_u32_e32 v57, vcc, 0, v47, vcc
	v_add_co_u32_e32 v58, vcc, 0xc000, v46
	s_nop 1
	v_addc_co_u32_e32 v59, vcc, 0, v47, vcc
	v_add_co_u32_e32 v60, vcc, 0xe000, v46
	s_nop 1
	v_addc_co_u32_e32 v61, vcc, 0, v47, vcc
	global_load_dword v64, v[46:47], off nt
	global_load_dword v65, v[48:49], off nt
	global_load_dword v66, v[50:51], off nt
	global_load_dword v67, v[52:53], off nt
	global_load_dword v68, v[54:55], off nt
	global_load_dword v69, v[56:57], off nt
	global_load_dword v70, v[58:59], off nt
	global_load_dword v71, v[60:61], off nt
	v_add_co_u32_e32 v48, vcc, 0x10000, v46
	s_nop 1
	v_addc_co_u32_e32 v49, vcc, 0, v47, vcc
	v_add_co_u32_e32 v50, vcc, 0x12000, v46
	s_nop 1
	v_addc_co_u32_e32 v51, vcc, 0, v47, vcc
	v_add_co_u32_e32 v52, vcc, 0x14000, v46
	s_nop 1
	v_addc_co_u32_e32 v53, vcc, 0, v47, vcc
	v_add_co_u32_e32 v54, vcc, 0x16000, v46
	s_nop 1
	v_addc_co_u32_e32 v55, vcc, 0, v47, vcc
	v_add_co_u32_e32 v56, vcc, 0x18000, v46
	s_nop 1
	v_addc_co_u32_e32 v57, vcc, 0, v47, vcc
	v_add_co_u32_e32 v58, vcc, 0x1a000, v46
	s_nop 1
	v_addc_co_u32_e32 v59, vcc, 0, v47, vcc
	v_add_co_u32_e32 v60, vcc, 0x1c000, v46
	s_nop 1
	v_addc_co_u32_e32 v61, vcc, 0, v47, vcc
	v_add_co_u32_e32 v62, vcc, 0x1e000, v46
	s_nop 1
	v_addc_co_u32_e32 v63, vcc, 0, v47, vcc
	global_load_dword v72, v[48:49], off nt
	global_load_dword v73, v[50:51], off nt
	global_load_dword v74, v[52:53], off nt
	global_load_dword v75, v[54:55], off nt
	global_load_dword v76, v[56:57], off nt
	global_load_dword v77, v[58:59], off nt
	global_load_dword v78, v[60:61], off nt
	global_load_dword v79, v[62:63], off nt
	v_add_co_u32_e32 v48, vcc, 0x20000, v46
	s_nop 1
	v_addc_co_u32_e32 v49, vcc, 0, v47, vcc
	v_add_co_u32_e32 v50, vcc, 0x22000, v46
	s_nop 1
	v_addc_co_u32_e32 v51, vcc, 0, v47, vcc
	v_add_co_u32_e32 v52, vcc, 0x24000, v46
	s_nop 1
	v_addc_co_u32_e32 v53, vcc, 0, v47, vcc
	v_add_co_u32_e32 v54, vcc, 0x26000, v46
	s_nop 1
	v_addc_co_u32_e32 v55, vcc, 0, v47, vcc
	v_add_co_u32_e32 v56, vcc, 0x28000, v46
	s_nop 1
	v_addc_co_u32_e32 v57, vcc, 0, v47, vcc
	v_add_co_u32_e32 v58, vcc, 0x2a000, v46
	s_nop 1
	v_addc_co_u32_e32 v59, vcc, 0, v47, vcc
	v_add_co_u32_e32 v60, vcc, 0x2c000, v46
	s_nop 1
	v_addc_co_u32_e32 v61, vcc, 0, v47, vcc
	v_add_co_u32_e32 v62, vcc, 0x2e000, v46
	s_nop 1
	v_addc_co_u32_e32 v63, vcc, 0, v47, vcc
	global_load_dword v80, v[48:49], off nt
	global_load_dword v81, v[50:51], off nt
	global_load_dword v82, v[52:53], off nt
	global_load_dword v83, v[54:55], off nt
	global_load_dword v84, v[56:57], off nt
	global_load_dword v85, v[58:59], off nt
	global_load_dword v86, v[60:61], off nt
	s_nop 0
	global_load_dword v62, v[62:63], off nt
	v_add_co_u32_e32 v48, vcc, 0x30000, v46
	s_nop 1
	v_addc_co_u32_e32 v49, vcc, 0, v47, vcc
	v_add_co_u32_e32 v50, vcc, 0x32000, v46
	s_nop 1
	v_addc_co_u32_e32 v51, vcc, 0, v47, vcc
	v_add_co_u32_e32 v52, vcc, 0x34000, v46
	s_nop 1
	v_addc_co_u32_e32 v53, vcc, 0, v47, vcc
	v_add_co_u32_e32 v54, vcc, 0x36000, v46
	s_nop 1
	v_addc_co_u32_e32 v55, vcc, 0, v47, vcc
	v_add_co_u32_e32 v56, vcc, 0x38000, v46
	s_nop 1
	v_addc_co_u32_e32 v57, vcc, 0, v47, vcc
	v_add_co_u32_e32 v58, vcc, 0x3a000, v46
	s_nop 1
	v_addc_co_u32_e32 v59, vcc, 0, v47, vcc
	v_add_co_u32_e32 v60, vcc, 0x3c000, v46
	s_nop 1
	v_addc_co_u32_e32 v61, vcc, 0, v47, vcc
	v_add_co_u32_e32 v46, vcc, 0x3e000, v46
	s_nop 1
	v_addc_co_u32_e32 v47, vcc, 0, v47, vcc
	global_load_dword v48, v[48:49], off nt
	s_nop 0
	global_load_dword v49, v[50:51], off nt
	s_nop 0
	global_load_dword v50, v[52:53], off nt
	global_load_dword v51, v[54:55], off nt
	s_nop 0
	global_load_dword v52, v[56:57], off nt
	global_load_dword v53, v[58:59], off nt
	global_load_dword v54, v[60:61], off nt
	s_nop 0
	global_load_dword v46, v[46:47], off nt
	s_waitcnt vmcnt(30)
	ds_write2_b32 v29, v64, v65 offset1:66
	s_waitcnt vmcnt(28)
	ds_write2_b32 v29, v66, v67 offset0:132 offset1:198
	s_waitcnt vmcnt(26)
	ds_write2_b32 v38, v68, v69 offset0:8 offset1:74
	s_waitcnt vmcnt(24)
	ds_write2_b32 v38, v70, v71 offset0:140 offset1:206
	s_waitcnt vmcnt(22)
	ds_write2_b32 v39, v72, v73 offset0:16 offset1:82
	s_waitcnt vmcnt(20)
	ds_write2_b32 v39, v74, v75 offset0:148 offset1:214
	s_waitcnt vmcnt(18)
	ds_write2_b32 v40, v76, v77 offset0:24 offset1:90
	s_waitcnt vmcnt(16)
	ds_write2_b32 v40, v78, v79 offset0:156 offset1:222
	s_waitcnt vmcnt(14)
	ds_write2_b32 v41, v80, v81 offset0:32 offset1:98
	s_waitcnt vmcnt(12)
	ds_write2_b32 v41, v82, v83 offset0:164 offset1:230
	s_waitcnt vmcnt(10)
; #define GAS __attribute__((address_space(1)))
; #define LAS __attribute__((address_space(3)))
; #define LDS_WAIT() asm volatile("s_waitcnt lgkmcnt(0)" ::: "memory")
; __device__ __forceinline__ unsigned pk2(float lo, float hi) { return f2bf(lo) | (f2bf(hi) << 16); }
; __device__ __forceinline__ void tr_item(const float* W, int ld, int K, int nblk, int item, bf16* WT, bool gu, LAS float* scr, int lane) {
;     ...
;       for (int i = 0; i < 32; ++i) scr[(2 * i + (lane >> 5)) * 33 + (lane & 31)] = t_[i]; }
;     LDS_WAIT(); asm volatile("" ::: "memory");
;     const int c = lane & 7;
; #pragma unroll
;     for (int j = 0; j < 4; ++j) { const int n = (lane >> 3) + 8 * j; const LAS float* s = scr + (8 * c) * 33 + n;
;         v4u o; o.x = pk2(s[0 * 33], s[1 * 33]); o.y = pk2(s[2 * 33], s[3 * 33]); o.z = pk2(s[4 * 33], s[5 * 33]); o.w = pk2(s[6 * 33], s[7 * 33]);
;         *(GAS v4u*)(WT + (size_t)(drow0 + n) * K + k0 + 8 * c) = o; }
;     LDS_WAIT(); asm volatile("" ::: "memory");
	ds_write2_b32 v42, v84, v85 offset0:40 offset1:106
	s_waitcnt vmcnt(8)
	ds_write2_b32 v42, v86, v62 offset0:172 offset1:238
	s_waitcnt vmcnt(6)
	ds_write2_b32 v43, v48, v49 offset0:48 offset1:114
	s_waitcnt vmcnt(4)
	ds_write2_b32 v43, v50, v51 offset0:180 offset1:246
	s_waitcnt vmcnt(2)
	ds_write2_b32 v44, v52, v53 offset0:56 offset1:122
	s_waitcnt vmcnt(0)
	ds_write2_b32 v44, v54, v46 offset0:188 offset1:254
	s_waitcnt lgkmcnt(0)
	ds_read2_b32 v[50:51], v34 offset1:8
	ds_read2_b32 v[54:55], v34 offset0:33 offset1:41
	ds_read2_b32 v[56:57], v34 offset0:66 offset1:74
	ds_read2_b32 v[58:59], v34 offset0:99 offset1:107
	ds_read2_b32 v[60:61], v34 offset0:132 offset1:140
	s_waitcnt lgkmcnt(4)
	v_bfe_u32 v46, v50, 16, 1
	v_add3_u32 v46, v50, v46, s57
	s_waitcnt lgkmcnt(3)
	v_bfe_u32 v47, v54, 16, 1
	v_lshrrev_b32_e32 v46, 16, v46
	v_add3_u32 v47, v54, v47, s57
	ds_read2_b32 v[62:63], v34 offset0:165 offset1:173
	v_and_or_b32 v46, v47, s58, v46
	s_waitcnt lgkmcnt(3)
	v_bfe_u32 v47, v56, 16, 1
	v_add3_u32 v47, v56, v47, s57
	s_waitcnt lgkmcnt(2)
	v_bfe_u32 v48, v58, 16, 1
	ds_read2_b32 v[64:65], v34 offset0:198 offset1:206
	v_lshrrev_b32_e32 v47, 16, v47
	v_add3_u32 v48, v58, v48, s57
	ds_read2_b32 v[66:67], v34 offset0:231 offset1:239
	v_and_or_b32 v47, v48, s58, v47
	s_waitcnt lgkmcnt(3)
	v_bfe_u32 v48, v60, 16, 1
	v_add3_u32 v48, v60, v48, s57
	s_waitcnt lgkmcnt(2)
	v_bfe_u32 v49, v62, 16, 1
	v_lshrrev_b32_e32 v48, 16, v48
	v_add3_u32 v49, v62, v49, s57
	v_and_or_b32 v48, v49, s58, v48
	s_waitcnt lgkmcnt(1)
	v_bfe_u32 v49, v64, 16, 1
	v_add_u32_e32 v68, s4, v33
	v_add3_u32 v49, v64, v49, s57
	s_waitcnt lgkmcnt(0)
	v_bfe_u32 v50, v66, 16, 1
	v_ashrrev_i32_e32 v69, 31, v68
	v_lshl_add_u64 v[52:53], v[20:21], 0, s[0:1]
	v_lshrrev_b32_e32 v49, 16, v49
	v_add3_u32 v50, v66, v50, s57
	v_lshlrev_b64 v[68:69], 11, v[68:69]
	v_and_or_b32 v49, v50, s58, v49
	v_lshl_add_u64 v[68:69], v[52:53], 0, v[68:69]
	global_store_dwordx4 v[68:69], v[46:49], off nt
	v_bfe_u32 v50, v67, 16, 1
	v_add3_u32 v50, v67, v50, s57
	v_bfe_u32 v46, v51, 16, 1
	v_add3_u32 v46, v51, v46, s57
	v_bfe_u32 v47, v55, 16, 1
	v_lshrrev_b32_e32 v46, 16, v46
	v_add3_u32 v47, v55, v47, s57
	v_and_or_b32 v46, v47, s58, v46
	v_bfe_u32 v47, v57, 16, 1
	v_add3_u32 v47, v57, v47, s57
	v_bfe_u32 v48, v59, 16, 1
	v_lshrrev_b32_e32 v47, 16, v47
	v_add3_u32 v48, v59, v48, s57
	v_and_or_b32 v47, v48, s58, v47
	v_bfe_u32 v48, v61, 16, 1
	v_add3_u32 v48, v61, v48, s57
	v_bfe_u32 v49, v63, 16, 1
	v_lshrrev_b32_e32 v48, 16, v48
	v_add3_u32 v49, v63, v49, s57
	v_and_or_b32 v48, v49, s58, v48
	v_bfe_u32 v49, v65, 16, 1
	v_add3_u32 v49, v65, v49, s57
	v_lshrrev_b32_e32 v49, 16, v49
	v_and_or_b32 v49, v50, s58, v49
	v_add_u32_e32 v50, s4, v35
	v_ashrrev_i32_e32 v51, 31, v50
	v_lshlrev_b64 v[50:51], 11, v[50:51]
	ds_read2_b32 v[54:55], v34 offset0:16 offset1:24
	v_lshl_add_u64 v[50:51], v[52:53], 0, v[50:51]
	global_store_dwordx4 v[50:51], v[46:49], off nt
	ds_read2_b32 v[50:51], v34 offset0:49 offset1:57
	ds_read2_b32 v[56:57], v34 offset0:82 offset1:90
	ds_read2_b32 v[58:59], v34 offset0:115 offset1:123
	s_waitcnt lgkmcnt(3)
	v_bfe_u32 v46, v54, 16, 1
	v_add3_u32 v46, v54, v46, s57
	s_waitcnt lgkmcnt(2)
	v_bfe_u32 v47, v50, 16, 1
	ds_read2_b32 v[60:61], v34 offset0:148 offset1:156
	v_lshrrev_b32_e32 v46, 16, v46
	v_add3_u32 v47, v50, v47, s57
	ds_read2_b32 v[62:63], v34 offset0:181 offset1:189
	v_and_or_b32 v46, v47, s58, v46
	s_waitcnt lgkmcnt(3)
	v_bfe_u32 v47, v56, 16, 1
	v_add3_u32 v47, v56, v47, s57
	s_waitcnt lgkmcnt(2)
	v_bfe_u32 v48, v58, 16, 1
	ds_read2_b32 v[64:65], v34 offset0:214 offset1:222
	v_lshrrev_b32_e32 v47, 16, v47
	v_add3_u32 v48, v58, v48, s57
	ds_read2_b32 v[66:67], v34 offset0:247 offset1:255
	v_and_or_b32 v47, v48, s58, v47
	s_waitcnt lgkmcnt(3)
	v_bfe_u32 v48, v60, 16, 1
	v_add3_u32 v48, v60, v48, s57
	s_waitcnt lgkmcnt(2)
	v_bfe_u32 v49, v62, 16, 1
	v_lshrrev_b32_e32 v48, 16, v48
	v_add3_u32 v49, v62, v49, s57
	v_and_or_b32 v48, v49, s58, v48
	s_waitcnt lgkmcnt(1)
	v_bfe_u32 v49, v64, 16, 1
	v_add_u32_e32 v68, s4, v36
	v_add3_u32 v49, v64, v49, s57
	s_waitcnt lgkmcnt(0)
	v_bfe_u32 v50, v66, 16, 1
	v_ashrrev_i32_e32 v69, 31, v68
	v_lshrrev_b32_e32 v49, 16, v49
	v_add3_u32 v50, v66, v50, s57
	v_lshlrev_b64 v[68:69], 11, v[68:69]
	v_and_or_b32 v49, v50, s58, v49
	v_lshl_add_u64 v[68:69], v[52:53], 0, v[68:69]
	global_store_dwordx4 v[68:69], v[46:49], off nt
	v_bfe_u32 v50, v67, 16, 1
	v_add3_u32 v50, v67, v50, s57
	v_bfe_u32 v46, v55, 16, 1
	v_add3_u32 v46, v55, v46, s57
	v_bfe_u32 v47, v51, 16, 1
	v_lshrrev_b32_e32 v46, 16, v46
	v_add3_u32 v47, v51, v47, s57
	v_and_or_b32 v46, v47, s58, v46
	v_bfe_u32 v47, v57, 16, 1
	v_add3_u32 v47, v57, v47, s57
	v_bfe_u32 v48, v59, 16, 1
	v_lshrrev_b32_e32 v47, 16, v47
	v_add3_u32 v48, v59, v48, s57
	v_and_or_b32 v47, v48, s58, v47
	v_bfe_u32 v48, v61, 16, 1
	v_add3_u32 v48, v61, v48, s57
	v_bfe_u32 v49, v63, 16, 1
	v_lshrrev_b32_e32 v48, 16, v48
	v_add3_u32 v49, v63, v49, s57
	v_and_or_b32 v48, v49, s58, v48
	v_bfe_u32 v49, v65, 16, 1
	v_add3_u32 v49, v65, v49, s57
	v_lshrrev_b32_e32 v49, 16, v49
	v_and_or_b32 v49, v50, s58, v49
	v_add_u32_e32 v50, s4, v37
	v_ashrrev_i32_e32 v51, 31, v50
	v_lshlrev_b64 v[50:51], 11, v[50:51]
	v_lshl_add_u64 v[50:51], v[52:53], 0, v[50:51]
	global_store_dwordx4 v[50:51], v[46:49], off nt
	s_waitcnt lgkmcnt(0)

; #define LAS __attribute__((address_space(3)))
; __device__ __forceinline__ void tr_item(const float* W, int ld, int K, int nblk, int item, bf16* WT, bool gu, LAS float* scr, int lane) {
;     const int kb = item / nblk, nb = item % nblk, k0 = 64 * kb, n0 = 32 * nb;
;     int drow0 = n0;
;     if (gu) { const int bj = n0 / FF, j = n0 - bj * FF; drow0 = 256 * (j / 128) + 128 * bj + (j % 128); }
;     { float t_[32];
; #pragma unroll
;       for (int i = 0; i < 32; ++i) t_[i] = W[(size_t)(k0 + 2 * i + (lane >> 5)) * ld + n0 + (lane & 31)];
; #pragma unroll
;       for (int i = 0; i < 32; ++i) scr[(2 * i + (lane >> 5)) * 33 + (lane & 31)] = t_[i]; }
; __device__ __forceinline__ void convert_items(Frame& F, const Args& a, int lo, int hi, int w, int nw) {
;     ...
;         if (r < I_FI) { tr_item(a.in[7], 3 * D + 16, D, 96, r, (bf16*)(F.ws + WS_WFOXIN), false, scr, lane); continue; } r -= I_FI;
;         if (r < I_FO) { tr_item(a.in[9], D, D, 32, r, (bf16*)(F.ws + WS_WFOXOUT), false, scr, lane); continue; } r -= I_FO;
;         if (r < I_SI) { tr_item(a.in[10], D + 512, D, 48, r, (bf16*)(F.ws + WS_WSWAIN), false, scr, lane); continue; } r -= I_SI;
;         if (r < I_SO) { tr_item(a.in[12], D, D, 32, r, (bf16*)(F.ws + WS_WSWAOUT), false, scr, lane); continue; } r -= I_SO;
.LBB0_1426:
	s_andn2_b64 vcc, exec, s[4:5]
	s_cbranch_vccnz .LBB0_1428
	s_add_i32 s0, s3, 0xf800
	s_and_b32 s4, s0, 0xffff
	s_mul_i32 s4, s4, 0xaaab
	s_lshr_b32 s5, s4, 21
	s_mul_i32 s4, s5, 48
	s_sub_i32 s0, s0, s4
	s_lshl_b32 s0, s0, 5
	s_and_b32 s4, s0, 0xffe0
	v_lshl_add_u32 v64, s5, 6, v28
	s_lshl_b32 s0, s4, 2
	v_lshl_add_u64 v[46:47], v[10:11], 0, s[0:1]
	v_add_u32_e32 v50, 2, v64
	v_add_u32_e32 v52, 4, v64
	v_add_u32_e32 v54, 6, v64
	v_add_u32_e32 v56, 8, v64
	v_add_u32_e32 v58, 10, v64
	v_add_u32_e32 v60, 12, v64
	v_add_u32_e32 v62, 14, v64
	v_mad_i64_i32 v[48:49], s[6:7], v64, s59, v[46:47]
	v_mad_i64_i32 v[50:51], s[6:7], v50, s59, v[46:47]
	v_mad_i64_i32 v[52:53], s[6:7], v52, s59, v[46:47]
	v_mad_i64_i32 v[54:55], s[6:7], v54, s59, v[46:47]
	v_mad_i64_i32 v[56:57], s[6:7], v56, s59, v[46:47]
	v_mad_i64_i32 v[58:59], s[6:7], v58, s59, v[46:47]
	v_mad_i64_i32 v[60:61], s[6:7], v60, s59, v[46:47]
	v_mad_i64_i32 v[62:63], s[6:7], v62, s59, v[46:47]
	global_load_dword v65, v[48:49], off nt
	global_load_dword v66, v[50:51], off nt
	global_load_dword v67, v[52:53], off nt
	global_load_dword v68, v[54:55], off nt
	global_load_dword v69, v[56:57], off nt
	global_load_dword v70, v[58:59], off nt
	global_load_dword v71, v[60:61], off nt
	global_load_dword v72, v[62:63], off nt
	v_add_u32_e32 v48, 16, v64
	v_add_u32_e32 v50, 18, v64
	v_add_u32_e32 v52, 20, v64
	v_add_u32_e32 v54, 22, v64
	v_add_u32_e32 v56, 24, v64
	v_add_u32_e32 v58, 26, v64
	v_add_u32_e32 v60, 28, v64
	v_add_u32_e32 v62, 30, v64
	v_mad_i64_i32 v[48:49], s[6:7], v48, s59, v[46:47]
	v_mad_i64_i32 v[50:51], s[6:7], v50, s59, v[46:47]
	v_mad_i64_i32 v[52:53], s[6:7], v52, s59, v[46:47]
	v_mad_i64_i32 v[54:55], s[6:7], v54, s59, v[46:47]
	v_mad_i64_i32 v[56:57], s[6:7], v56, s59, v[46:47]
	v_mad_i64_i32 v[58:59], s[6:7], v58, s59, v[46:47]
	v_mad_i64_i32 v[60:61], s[6:7], v60, s59, v[46:47]
	v_mad_i64_i32 v[62:63], s[6:7], v62, s59, v[46:47]
	global_load_dword v73, v[48:49], off nt
	global_load_dword v74, v[50:51], off nt
	global_load_dword v75, v[52:53], off nt
	global_load_dword v76, v[54:55], off nt
	global_load_dword v77, v[56:57], off nt
	global_load_dword v78, v[58:59], off nt
	global_load_dword v79, v[60:61], off nt
	global_load_dword v80, v[62:63], off nt
	v_add_u32_e32 v48, 32, v64
	v_add_u32_e32 v50, 34, v64
	v_add_u32_e32 v52, 36, v64
	v_add_u32_e32 v54, 38, v64
	v_add_u32_e32 v56, 40, v64
	v_add_u32_e32 v58, 42, v64
	v_add_u32_e32 v60, 44, v64
	v_add_u32_e32 v62, 46, v64
	v_mad_i64_i32 v[48:49], s[6:7], v48, s59, v[46:47]
	v_mad_i64_i32 v[50:51], s[6:7], v50, s59, v[46:47]
	v_mad_i64_i32 v[52:53], s[6:7], v52, s59, v[46:47]
	v_mad_i64_i32 v[54:55], s[6:7], v54, s59, v[46:47]
	v_mad_i64_i32 v[56:57], s[6:7], v56, s59, v[46:47]
	v_mad_i64_i32 v[58:59], s[6:7], v58, s59, v[46:47]
	v_mad_i64_i32 v[60:61], s[6:7], v60, s59, v[46:47]
	v_mad_i64_i32 v[62:63], s[6:7], v62, s59, v[46:47]
	global_load_dword v81, v[48:49], off nt
	global_load_dword v82, v[50:51], off nt
	global_load_dword v83, v[52:53], off nt
	global_load_dword v84, v[54:55], off nt
	global_load_dword v85, v[56:57], off nt
	global_load_dword v86, v[58:59], off nt
	global_load_dword v87, v[60:61], off nt
	s_nop 0
	global_load_dword v62, v[62:63], off nt
	v_add_u32_e32 v48, 48, v64
	v_add_u32_e32 v50, 50, v64
	v_add_u32_e32 v52, 52, v64
	v_add_u32_e32 v54, 54, v64
	v_add_u32_e32 v56, 56, v64
	v_add_u32_e32 v58, 58, v64
	v_add_u32_e32 v60, 60, v64
	v_add_u32_e32 v63, 62, v64
	v_mad_i64_i32 v[48:49], s[6:7], v48, s59, v[46:47]
	v_mad_i64_i32 v[50:51], s[6:7], v50, s59, v[46:47]
	v_mad_i64_i32 v[52:53], s[6:7], v52, s59, v[46:47]
	v_mad_i64_i32 v[54:55], s[6:7], v54, s59, v[46:47]
	v_mad_i64_i32 v[56:57], s[6:7], v56, s59, v[46:47]
	v_mad_i64_i32 v[58:59], s[6:7], v58, s59, v[46:47]
	v_mad_i64_i32 v[60:61], s[6:7], v60, s59, v[46:47]
	v_mad_i64_i32 v[46:47], s[6:7], v63, s59, v[46:47]
	global_load_dword v48, v[48:49], off nt
	s_nop 0
	global_load_dword v49, v[50:51], off nt
	s_nop 0
	global_load_dword v50, v[52:53], off nt
	global_load_dword v51, v[54:55], off nt
	s_nop 0
	global_load_dword v52, v[56:57], off nt
	global_load_dword v53, v[58:59], off nt
	global_load_dword v54, v[60:61], off nt
	s_nop 0
	global_load_dword v46, v[46:47], off nt
	s_waitcnt vmcnt(30)
	ds_write2_b32 v29, v65, v66 offset1:66
	s_waitcnt vmcnt(28)
	ds_write2_b32 v29, v67, v68 offset0:132 offset1:198
	s_waitcnt vmcnt(26)
	ds_write2_b32 v38, v69, v70 offset0:8 offset1:74
	s_waitcnt vmcnt(24)
	ds_write2_b32 v38, v71, v72 offset0:140 offset1:206
	s_waitcnt vmcnt(22)
	ds_write2_b32 v39, v73, v74 offset0:16 offset1:82
	s_waitcnt vmcnt(20)
	ds_write2_b32 v39, v75, v76 offset0:148 offset1:214
	s_waitcnt vmcnt(18)
	ds_write2_b32 v40, v77, v78 offset0:24 offset1:90
	s_waitcnt vmcnt(16)
	ds_write2_b32 v40, v79, v80 offset0:156 offset1:222
	s_waitcnt vmcnt(14)
	ds_write2_b32 v41, v81, v82 offset0:32 offset1:98
	s_waitcnt vmcnt(12)
	ds_write2_b32 v41, v83, v84 offset0:164 offset1:230
	s_waitcnt vmcnt(10)
	ds_write2_b32 v42, v85, v86 offset0:40 offset1:106
	s_waitcnt vmcnt(8)
	ds_write2_b32 v42, v87, v62 offset0:172 offset1:238
	s_waitcnt vmcnt(6)
	ds_write2_b32 v43, v48, v49 offset0:48 offset1:114
	s_waitcnt vmcnt(4)
; #define GAS __attribute__((address_space(1)))
; #define LAS __attribute__((address_space(3)))
; #define LDS_WAIT() asm volatile("s_waitcnt lgkmcnt(0)" ::: "memory")
; __device__ __forceinline__ unsigned pk2(float lo, float hi) { return f2bf(lo) | (f2bf(hi) << 16); }
; __device__ __forceinline__ void tr_item(const float* W, int ld, int K, int nblk, int item, bf16* WT, bool gu, LAS float* scr, int lane) {
;     ...
;       for (int i = 0; i < 32; ++i) scr[(2 * i + (lane >> 5)) * 33 + (lane & 31)] = t_[i]; }
;     LDS_WAIT(); asm volatile("" ::: "memory");
;     const int c = lane & 7;
; #pragma unroll
;     for (int j = 0; j < 4; ++j) { const int n = (lane >> 3) + 8 * j; const LAS float* s = scr + (8 * c) * 33 + n;
;         v4u o; o.x = pk2(s[0 * 33], s[1 * 33]); o.y = pk2(s[2 * 33], s[3 * 33]); o.z = pk2(s[4 * 33], s[5 * 33]); o.w = pk2(s[6 * 33], s[7 * 33]);
;         *(GAS v4u*)(WT + (size_t)(drow0 + n) * K + k0 + 8 * c) = o; }
;     LDS_WAIT(); asm volatile("" ::: "memory");
	ds_write2_b32 v43, v50, v51 offset0:180 offset1:246
	s_waitcnt vmcnt(2)
	ds_write2_b32 v44, v52, v53 offset0:56 offset1:122
	s_waitcnt vmcnt(0)
	ds_write2_b32 v44, v54, v46 offset0:188 offset1:254
	s_waitcnt lgkmcnt(0)
	ds_read2_b32 v[50:51], v34 offset1:8
	ds_read2_b32 v[54:55], v34 offset0:33 offset1:41
	ds_read2_b32 v[56:57], v34 offset0:66 offset1:74
	ds_read2_b32 v[58:59], v34 offset0:99 offset1:107
	ds_read2_b32 v[60:61], v34 offset0:132 offset1:140
	s_waitcnt lgkmcnt(4)
	v_bfe_u32 v46, v50, 16, 1
	v_add3_u32 v46, v50, v46, s57
	s_waitcnt lgkmcnt(3)
	v_bfe_u32 v47, v54, 16, 1
	v_lshrrev_b32_e32 v46, 16, v46
	v_add3_u32 v47, v54, v47, s57
	ds_read2_b32 v[62:63], v34 offset0:165 offset1:173
	v_and_or_b32 v46, v47, s58, v46
	s_waitcnt lgkmcnt(3)
	v_bfe_u32 v47, v56, 16, 1
	v_add3_u32 v47, v56, v47, s57
	s_waitcnt lgkmcnt(2)
	v_bfe_u32 v48, v58, 16, 1
	ds_read2_b32 v[64:65], v34 offset0:198 offset1:206
	v_lshrrev_b32_e32 v47, 16, v47
	v_add3_u32 v48, v58, v48, s57
	ds_read2_b32 v[66:67], v34 offset0:231 offset1:239
	v_and_or_b32 v47, v48, s58, v47
	s_waitcnt lgkmcnt(3)
	v_bfe_u32 v48, v60, 16, 1
	v_add3_u32 v48, v60, v48, s57
	s_waitcnt lgkmcnt(2)
	v_bfe_u32 v49, v62, 16, 1
	v_lshrrev_b32_e32 v48, 16, v48
	v_add3_u32 v49, v62, v49, s57
	v_and_or_b32 v48, v49, s58, v48
	s_waitcnt lgkmcnt(1)
	v_bfe_u32 v49, v64, 16, 1
	v_add_u32_e32 v68, s4, v33
	s_lshl_b32 s0, s5, 7
	v_add3_u32 v49, v64, v49, s57
	s_waitcnt lgkmcnt(0)
	v_bfe_u32 v50, v66, 16, 1
	v_ashrrev_i32_e32 v69, 31, v68
	v_lshl_add_u64 v[52:53], v[22:23], 0, s[0:1]
	v_lshrrev_b32_e32 v49, 16, v49
	v_add3_u32 v50, v66, v50, s57
	v_lshlrev_b64 v[68:69], 11, v[68:69]
	v_and_or_b32 v49, v50, s58, v49
	v_lshl_add_u64 v[68:69], v[52:53], 0, v[68:69]
	global_store_dwordx4 v[68:69], v[46:49], off nt
	v_bfe_u32 v50, v67, 16, 1
	v_add3_u32 v50, v67, v50, s57
	v_bfe_u32 v46, v51, 16, 1
	v_add3_u32 v46, v51, v46, s57
	v_bfe_u32 v47, v55, 16, 1
	v_lshrrev_b32_e32 v46, 16, v46
	v_add3_u32 v47, v55, v47, s57
	v_and_or_b32 v46, v47, s58, v46
	v_bfe_u32 v47, v57, 16, 1
	v_add3_u32 v47, v57, v47, s57
	v_bfe_u32 v48, v59, 16, 1
	v_lshrrev_b32_e32 v47, 16, v47
	v_add3_u32 v48, v59, v48, s57
	v_and_or_b32 v47, v48, s58, v47
	v_bfe_u32 v48, v61, 16, 1
	v_add3_u32 v48, v61, v48, s57
	v_bfe_u32 v49, v63, 16, 1
	v_lshrrev_b32_e32 v48, 16, v48
	v_add3_u32 v49, v63, v49, s57
	v_and_or_b32 v48, v49, s58, v48
	v_bfe_u32 v49, v65, 16, 1
	v_add3_u32 v49, v65, v49, s57
	v_lshrrev_b32_e32 v49, 16, v49
	v_and_or_b32 v49, v50, s58, v49
	v_add_u32_e32 v50, s4, v35
	v_ashrrev_i32_e32 v51, 31, v50
	v_lshlrev_b64 v[50:51], 11, v[50:51]
	ds_read2_b32 v[54:55], v34 offset0:16 offset1:24
	v_lshl_add_u64 v[50:51], v[52:53], 0, v[50:51]
	global_store_dwordx4 v[50:51], v[46:49], off nt
	ds_read2_b32 v[50:51], v34 offset0:49 offset1:57
	ds_read2_b32 v[56:57], v34 offset0:82 offset1:90
	ds_read2_b32 v[58:59], v34 offset0:115 offset1:123
	s_waitcnt lgkmcnt(3)
	v_bfe_u32 v46, v54, 16, 1
	v_add3_u32 v46, v54, v46, s57
	s_waitcnt lgkmcnt(2)
	v_bfe_u32 v47, v50, 16, 1
	ds_read2_b32 v[60:61], v34 offset0:148 offset1:156
	v_lshrrev_b32_e32 v46, 16, v46
	v_add3_u32 v47, v50, v47, s57
	ds_read2_b32 v[62:63], v34 offset0:181 offset1:189
	v_and_or_b32 v46, v47, s58, v46
	s_waitcnt lgkmcnt(3)
	v_bfe_u32 v47, v56, 16, 1
	v_add3_u32 v47, v56, v47, s57
	s_waitcnt lgkmcnt(2)
	v_bfe_u32 v48, v58, 16, 1
	ds_read2_b32 v[64:65], v34 offset0:214 offset1:222
	v_lshrrev_b32_e32 v47, 16, v47
	v_add3_u32 v48, v58, v48, s57
	ds_read2_b32 v[66:67], v34 offset0:247 offset1:255
	v_and_or_b32 v47, v48, s58, v47
	s_waitcnt lgkmcnt(3)
	v_bfe_u32 v48, v60, 16, 1
	v_add3_u32 v48, v60, v48, s57
	s_waitcnt lgkmcnt(2)
	v_bfe_u32 v49, v62, 16, 1
	v_lshrrev_b32_e32 v48, 16, v48
	v_add3_u32 v49, v62, v49, s57
	v_and_or_b32 v48, v49, s58, v48
	s_waitcnt lgkmcnt(1)
	v_bfe_u32 v49, v64, 16, 1
	v_add_u32_e32 v68, s4, v36
	v_add3_u32 v49, v64, v49, s57
	s_waitcnt lgkmcnt(0)
	v_bfe_u32 v50, v66, 16, 1
	v_ashrrev_i32_e32 v69, 31, v68
	v_lshrrev_b32_e32 v49, 16, v49
	v_add3_u32 v50, v66, v50, s57
	v_lshlrev_b64 v[68:69], 11, v[68:69]
	v_and_or_b32 v49, v50, s58, v49
	v_lshl_add_u64 v[68:69], v[52:53], 0, v[68:69]
	global_store_dwordx4 v[68:69], v[46:49], off nt
	v_bfe_u32 v50, v67, 16, 1
	v_add3_u32 v50, v67, v50, s57
	v_bfe_u32 v46, v55, 16, 1
	v_add3_u32 v46, v55, v46, s57
	v_bfe_u32 v47, v51, 16, 1
	v_lshrrev_b32_e32 v46, 16, v46
	v_add3_u32 v47, v51, v47, s57
	v_and_or_b32 v46, v47, s58, v46
	v_bfe_u32 v47, v57, 16, 1
	v_add3_u32 v47, v57, v47, s57
	v_bfe_u32 v48, v59, 16, 1
	v_lshrrev_b32_e32 v47, 16, v47
	v_add3_u32 v48, v59, v48, s57
	v_and_or_b32 v47, v48, s58, v47
	v_bfe_u32 v48, v61, 16, 1
	v_add3_u32 v48, v61, v48, s57
	v_bfe_u32 v49, v63, 16, 1
	v_lshrrev_b32_e32 v48, 16, v48
	v_add3_u32 v49, v63, v49, s57
	v_and_or_b32 v48, v49, s58, v48
	v_bfe_u32 v49, v65, 16, 1
	v_add3_u32 v49, v65, v49, s57
	v_lshrrev_b32_e32 v49, 16, v49
	v_and_or_b32 v49, v50, s58, v49
	v_add_u32_e32 v50, s4, v37
	v_ashrrev_i32_e32 v51, 31, v50
	v_lshlrev_b64 v[50:51], 11, v[50:51]
	v_lshl_add_u64 v[50:51], v[52:53], 0, v[50:51]
	global_store_dwordx4 v[50:51], v[46:49], off nt
	s_waitcnt lgkmcnt(0)

; #define LAS __attribute__((address_space(3)))
; __device__ __forceinline__ void tr_item(const float* W, int ld, int K, int nblk, int item, bf16* WT, bool gu, LAS float* scr, int lane) {
;     const int kb = item / nblk, nb = item % nblk, k0 = 64 * kb, n0 = 32 * nb;
;     int drow0 = n0;
;     if (gu) { const int bj = n0 / FF, j = n0 - bj * FF; drow0 = 256 * (j / 128) + 128 * bj + (j % 128); }
;     { float t_[32];
; #pragma unroll
;       for (int i = 0; i < 32; ++i) t_[i] = W[(size_t)(k0 + 2 * i + (lane >> 5)) * ld + n0 + (lane & 31)];
; #pragma unroll
;       for (int i = 0; i < 32; ++i) scr[(2 * i + (lane >> 5)) * 33 + (lane & 31)] = t_[i]; }
; __device__ __forceinline__ void convert_items(Frame& F, const Args& a, int lo, int hi, int w, int nw) {
;     ...
;         if (r < I_FO) { tr_item(a.in[9], D, D, 32, r, (bf16*)(F.ws + WS_WFOXOUT), false, scr, lane); continue; } r -= I_FO;
.LBB0_1429:
	s_andn2_b64 vcc, exec, s[4:5]
	s_cbranch_vccnz .LBB0_1431
	s_add_i32 s0, s9, 0x2a00
	s_and_b32 s5, s0, 0x1ffc0
	s_and_b32 s4, s8, 0x3e0
	v_add_u32_e32 v46, s5, v28
	s_lshl_b32 s0, s4, 2
	v_ashrrev_i32_e32 v47, 31, v46
	v_lshl_add_u64 v[48:49], v[12:13], 0, s[0:1]
	v_lshlrev_b64 v[46:47], 12, v[46:47]
	v_lshl_add_u64 v[46:47], v[48:49], 0, v[46:47]
	v_add_co_u32_e32 v48, vcc, 0x2000, v46
	s_lshl_b32 s0, s5, 1
	s_nop 0
	v_addc_co_u32_e32 v49, vcc, 0, v47, vcc
	v_add_co_u32_e32 v50, vcc, 0x4000, v46
	s_nop 1
	v_addc_co_u32_e32 v51, vcc, 0, v47, vcc
	v_add_co_u32_e32 v52, vcc, 0x6000, v46
	s_nop 1
	v_addc_co_u32_e32 v53, vcc, 0, v47, vcc
	v_add_co_u32_e32 v54, vcc, 0x8000, v46
	s_nop 1
	v_addc_co_u32_e32 v55, vcc, 0, v47, vcc
	v_add_co_u32_e32 v56, vcc, 0xa000, v46
	s_nop 1
	v_addc_co_u32_e32 v57, vcc, 0, v47, vcc
	v_add_co_u32_e32 v58, vcc, 0xc000, v46
	s_nop 1
	v_addc_co_u32_e32 v59, vcc, 0, v47, vcc
	v_add_co_u32_e32 v60, vcc, 0xe000, v46
	s_nop 1
	v_addc_co_u32_e32 v61, vcc, 0, v47, vcc
	global_load_dword v64, v[46:47], off nt
	global_load_dword v65, v[48:49], off nt
	global_load_dword v66, v[50:51], off nt
	global_load_dword v67, v[52:53], off nt
	global_load_dword v68, v[54:55], off nt
	global_load_dword v69, v[56:57], off nt
	global_load_dword v70, v[58:59], off nt
	global_load_dword v71, v[60:61], off nt
	v_add_co_u32_e32 v48, vcc, 0x10000, v46
	s_nop 1
	v_addc_co_u32_e32 v49, vcc, 0, v47, vcc
	v_add_co_u32_e32 v50, vcc, 0x12000, v46
	s_nop 1
	v_addc_co_u32_e32 v51, vcc, 0, v47, vcc
	v_add_co_u32_e32 v52, vcc, 0x14000, v46
	s_nop 1
	v_addc_co_u32_e32 v53, vcc, 0, v47, vcc
	v_add_co_u32_e32 v54, vcc, 0x16000, v46
	s_nop 1
	v_addc_co_u32_e32 v55, vcc, 0, v47, vcc
	v_add_co_u32_e32 v56, vcc, 0x18000, v46
	s_nop 1
	v_addc_co_u32_e32 v57, vcc, 0, v47, vcc
	v_add_co_u32_e32 v58, vcc, 0x1a000, v46
	s_nop 1
	v_addc_co_u32_e32 v59, vcc, 0, v47, vcc
	v_add_co_u32_e32 v60, vcc, 0x1c000, v46
	s_nop 1
	v_addc_co_u32_e32 v61, vcc, 0, v47, vcc
	v_add_co_u32_e32 v62, vcc, 0x1e000, v46
	s_nop 1
	v_addc_co_u32_e32 v63, vcc, 0, v47, vcc
	global_load_dword v72, v[48:49], off nt
	global_load_dword v73, v[50:51], off nt
	global_load_dword v74, v[52:53], off nt
	global_load_dword v75, v[54:55], off nt
	global_load_dword v76, v[56:57], off nt
	global_load_dword v77, v[58:59], off nt
	global_load_dword v78, v[60:61], off nt
	global_load_dword v79, v[62:63], off nt
	v_add_co_u32_e32 v48, vcc, 0x20000, v46
	s_nop 1
	v_addc_co_u32_e32 v49, vcc, 0, v47, vcc
	v_add_co_u32_e32 v50, vcc, 0x22000, v46
	s_nop 1
	v_addc_co_u32_e32 v51, vcc, 0, v47, vcc
	v_add_co_u32_e32 v52, vcc, 0x24000, v46
	s_nop 1
	v_addc_co_u32_e32 v53, vcc, 0, v47, vcc
	v_add_co_u32_e32 v54, vcc, 0x26000, v46
	s_nop 1
	v_addc_co_u32_e32 v55, vcc, 0, v47, vcc
	v_add_co_u32_e32 v56, vcc, 0x28000, v46
	s_nop 1
	v_addc_co_u32_e32 v57, vcc, 0, v47, vcc
	v_add_co_u32_e32 v58, vcc, 0x2a000, v46
	s_nop 1
	v_addc_co_u32_e32 v59, vcc, 0, v47, vcc
	v_add_co_u32_e32 v60, vcc, 0x2c000, v46
	s_nop 1
	v_addc_co_u32_e32 v61, vcc, 0, v47, vcc
	v_add_co_u32_e32 v62, vcc, 0x2e000, v46
	s_nop 1
	v_addc_co_u32_e32 v63, vcc, 0, v47, vcc
	global_load_dword v80, v[48:49], off nt
	global_load_dword v81, v[50:51], off nt
	global_load_dword v82, v[52:53], off nt
	global_load_dword v83, v[54:55], off nt
	global_load_dword v84, v[56:57], off nt
	global_load_dword v85, v[58:59], off nt
	global_load_dword v86, v[60:61], off nt
	s_nop 0
	global_load_dword v62, v[62:63], off nt
	v_add_co_u32_e32 v48, vcc, 0x30000, v46
	s_nop 1
	v_addc_co_u32_e32 v49, vcc, 0, v47, vcc
	v_add_co_u32_e32 v50, vcc, 0x32000, v46
	s_nop 1
	v_addc_co_u32_e32 v51, vcc, 0, v47, vcc
	v_add_co_u32_e32 v52, vcc, 0x34000, v46
	s_nop 1
	v_addc_co_u32_e32 v53, vcc, 0, v47, vcc
	v_add_co_u32_e32 v54, vcc, 0x36000, v46
	s_nop 1
	v_addc_co_u32_e32 v55, vcc, 0, v47, vcc
	v_add_co_u32_e32 v56, vcc, 0x38000, v46
	s_nop 1
	v_addc_co_u32_e32 v57, vcc, 0, v47, vcc
	v_add_co_u32_e32 v58, vcc, 0x3a000, v46
	s_nop 1
	v_addc_co_u32_e32 v59, vcc, 0, v47, vcc
	v_add_co_u32_e32 v60, vcc, 0x3c000, v46
	s_nop 1
	v_addc_co_u32_e32 v61, vcc, 0, v47, vcc
	v_add_co_u32_e32 v46, vcc, 0x3e000, v46
	s_nop 1
	v_addc_co_u32_e32 v47, vcc, 0, v47, vcc
	global_load_dword v48, v[48:49], off nt
	s_nop 0
	global_load_dword v49, v[50:51], off nt
	s_nop 0
	global_load_dword v50, v[52:53], off nt
	global_load_dword v51, v[54:55], off nt
	s_nop 0
	global_load_dword v52, v[56:57], off nt
	global_load_dword v53, v[58:59], off nt
	global_load_dword v54, v[60:61], off nt
	s_nop 0
	global_load_dword v46, v[46:47], off nt
	s_waitcnt vmcnt(30)
	ds_write2_b32 v29, v64, v65 offset1:66
	s_waitcnt vmcnt(28)
	ds_write2_b32 v29, v66, v67 offset0:132 offset1:198
	s_waitcnt vmcnt(26)
	ds_write2_b32 v38, v68, v69 offset0:8 offset1:74
	s_waitcnt vmcnt(24)
	ds_write2_b32 v38, v70, v71 offset0:140 offset1:206
	s_waitcnt vmcnt(22)
	ds_write2_b32 v39, v72, v73 offset0:16 offset1:82
	s_waitcnt vmcnt(20)
	ds_write2_b32 v39, v74, v75 offset0:148 offset1:214
	s_waitcnt vmcnt(18)
	ds_write2_b32 v40, v76, v77 offset0:24 offset1:90
	s_waitcnt vmcnt(16)
	ds_write2_b32 v40, v78, v79 offset0:156 offset1:222
	s_waitcnt vmcnt(14)
	ds_write2_b32 v41, v80, v81 offset0:32 offset1:98
	s_waitcnt vmcnt(12)
	ds_write2_b32 v41, v82, v83 offset0:164 offset1:230
	s_waitcnt vmcnt(10)
; #define GAS __attribute__((address_space(1)))
; #define LAS __attribute__((address_space(3)))
; #define LDS_WAIT() asm volatile("s_waitcnt lgkmcnt(0)" ::: "memory")
; __device__ __forceinline__ unsigned pk2(float lo, float hi) { return f2bf(lo) | (f2bf(hi) << 16); }
; __device__ __forceinline__ void tr_item(const float* W, int ld, int K, int nblk, int item, bf16* WT, bool gu, LAS float* scr, int lane) {
;     ...
;       for (int i = 0; i < 32; ++i) scr[(2 * i + (lane >> 5)) * 33 + (lane & 31)] = t_[i]; }
;     LDS_WAIT(); asm volatile("" ::: "memory");
;     const int c = lane & 7;
; #pragma unroll
;     for (int j = 0; j < 4; ++j) { const int n = (lane >> 3) + 8 * j; const LAS float* s = scr + (8 * c) * 33 + n;
;         v4u o; o.x = pk2(s[0 * 33], s[1 * 33]); o.y = pk2(s[2 * 33], s[3 * 33]); o.z = pk2(s[4 * 33], s[5 * 33]); o.w = pk2(s[6 * 33], s[7 * 33]);
;         *(GAS v4u*)(WT + (size_t)(drow0 + n) * K + k0 + 8 * c) = o; }
;     LDS_WAIT(); asm volatile("" ::: "memory");
	ds_write2_b32 v42, v84, v85 offset0:40 offset1:106
	s_waitcnt vmcnt(8)
	ds_write2_b32 v42, v86, v62 offset0:172 offset1:238
	s_waitcnt vmcnt(6)
	ds_write2_b32 v43, v48, v49 offset0:48 offset1:114
	s_waitcnt vmcnt(4)
	ds_write2_b32 v43, v50, v51 offset0:180 offset1:246
	s_waitcnt vmcnt(2)
	ds_write2_b32 v44, v52, v53 offset0:56 offset1:122
	s_waitcnt vmcnt(0)
	ds_write2_b32 v44, v54, v46 offset0:188 offset1:254
	s_waitcnt lgkmcnt(0)
	ds_read2_b32 v[50:51], v34 offset1:8
	ds_read2_b32 v[54:55], v34 offset0:33 offset1:41
	ds_read2_b32 v[56:57], v34 offset0:66 offset1:74
	ds_read2_b32 v[58:59], v34 offset0:99 offset1:107
	ds_read2_b32 v[60:61], v34 offset0:132 offset1:140
	s_waitcnt lgkmcnt(4)
	v_bfe_u32 v46, v50, 16, 1
	v_add3_u32 v46, v50, v46, s57
	s_waitcnt lgkmcnt(3)
	v_bfe_u32 v47, v54, 16, 1
	v_lshrrev_b32_e32 v46, 16, v46
	v_add3_u32 v47, v54, v47, s57
	ds_read2_b32 v[62:63], v34 offset0:165 offset1:173
	v_and_or_b32 v46, v47, s58, v46
	s_waitcnt lgkmcnt(3)
	v_bfe_u32 v47, v56, 16, 1
	v_add3_u32 v47, v56, v47, s57
	s_waitcnt lgkmcnt(2)
	v_bfe_u32 v48, v58, 16, 1
	ds_read2_b32 v[64:65], v34 offset0:198 offset1:206
	v_lshrrev_b32_e32 v47, 16, v47
	v_add3_u32 v48, v58, v48, s57
	ds_read2_b32 v[66:67], v34 offset0:231 offset1:239
	v_and_or_b32 v47, v48, s58, v47
	s_waitcnt lgkmcnt(3)
	v_bfe_u32 v48, v60, 16, 1
	v_add3_u32 v48, v60, v48, s57
	s_waitcnt lgkmcnt(2)
	v_bfe_u32 v49, v62, 16, 1
	v_lshrrev_b32_e32 v48, 16, v48
	v_add3_u32 v49, v62, v49, s57
	v_and_or_b32 v48, v49, s58, v48
	s_waitcnt lgkmcnt(1)
	v_bfe_u32 v49, v64, 16, 1
	v_add_u32_e32 v68, s4, v33
	v_add3_u32 v49, v64, v49, s57
	s_waitcnt lgkmcnt(0)
	v_bfe_u32 v50, v66, 16, 1
	v_ashrrev_i32_e32 v69, 31, v68
	v_lshl_add_u64 v[52:53], v[24:25], 0, s[0:1]
	v_lshrrev_b32_e32 v49, 16, v49
	v_add3_u32 v50, v66, v50, s57
	v_lshlrev_b64 v[68:69], 11, v[68:69]
	v_and_or_b32 v49, v50, s58, v49
	v_lshl_add_u64 v[68:69], v[52:53], 0, v[68:69]
	global_store_dwordx4 v[68:69], v[46:49], off nt
	v_bfe_u32 v50, v67, 16, 1
	v_add3_u32 v50, v67, v50, s57
	v_bfe_u32 v46, v51, 16, 1
	v_add3_u32 v46, v51, v46, s57
	v_bfe_u32 v47, v55, 16, 1
	v_lshrrev_b32_e32 v46, 16, v46
	v_add3_u32 v47, v55, v47, s57
	v_and_or_b32 v46, v47, s58, v46
	v_bfe_u32 v47, v57, 16, 1
	v_add3_u32 v47, v57, v47, s57
	v_bfe_u32 v48, v59, 16, 1
	v_lshrrev_b32_e32 v47, 16, v47
	v_add3_u32 v48, v59, v48, s57
	v_and_or_b32 v47, v48, s58, v47
	v_bfe_u32 v48, v61, 16, 1
	v_add3_u32 v48, v61, v48, s57
	v_bfe_u32 v49, v63, 16, 1
	v_lshrrev_b32_e32 v48, 16, v48
	v_add3_u32 v49, v63, v49, s57
	v_and_or_b32 v48, v49, s58, v48
	v_bfe_u32 v49, v65, 16, 1
	v_add3_u32 v49, v65, v49, s57
	v_lshrrev_b32_e32 v49, 16, v49
	v_and_or_b32 v49, v50, s58, v49
	v_add_u32_e32 v50, s4, v35
	v_ashrrev_i32_e32 v51, 31, v50
	v_lshlrev_b64 v[50:51], 11, v[50:51]
	ds_read2_b32 v[54:55], v34 offset0:16 offset1:24
	v_lshl_add_u64 v[50:51], v[52:53], 0, v[50:51]
	global_store_dwordx4 v[50:51], v[46:49], off nt
	ds_read2_b32 v[50:51], v34 offset0:49 offset1:57
	ds_read2_b32 v[56:57], v34 offset0:82 offset1:90
	ds_read2_b32 v[58:59], v34 offset0:115 offset1:123
	s_waitcnt lgkmcnt(3)
	v_bfe_u32 v46, v54, 16, 1
	v_add3_u32 v46, v54, v46, s57
	s_waitcnt lgkmcnt(2)
	v_bfe_u32 v47, v50, 16, 1
	ds_read2_b32 v[60:61], v34 offset0:148 offset1:156
	v_lshrrev_b32_e32 v46, 16, v46
	v_add3_u32 v47, v50, v47, s57
	ds_read2_b32 v[62:63], v34 offset0:181 offset1:189
	v_and_or_b32 v46, v47, s58, v46
	s_waitcnt lgkmcnt(3)
	v_bfe_u32 v47, v56, 16, 1
	v_add3_u32 v47, v56, v47, s57
	s_waitcnt lgkmcnt(2)
	v_bfe_u32 v48, v58, 16, 1
	ds_read2_b32 v[64:65], v34 offset0:214 offset1:222
	v_lshrrev_b32_e32 v47, 16, v47
	v_add3_u32 v48, v58, v48, s57
	ds_read2_b32 v[66:67], v34 offset0:247 offset1:255
	v_and_or_b32 v47, v48, s58, v47
	s_waitcnt lgkmcnt(3)
	v_bfe_u32 v48, v60, 16, 1
	v_add3_u32 v48, v60, v48, s57
	s_waitcnt lgkmcnt(2)
	v_bfe_u32 v49, v62, 16, 1
	v_lshrrev_b32_e32 v48, 16, v48
	v_add3_u32 v49, v62, v49, s57
	v_and_or_b32 v48, v49, s58, v48
	s_waitcnt lgkmcnt(1)
	v_bfe_u32 v49, v64, 16, 1
	v_add_u32_e32 v68, s4, v36
	v_add3_u32 v49, v64, v49, s57
	s_waitcnt lgkmcnt(0)
	v_bfe_u32 v50, v66, 16, 1
	v_ashrrev_i32_e32 v69, 31, v68
	v_lshrrev_b32_e32 v49, 16, v49
	v_add3_u32 v50, v66, v50, s57
	v_lshlrev_b64 v[68:69], 11, v[68:69]
	v_and_or_b32 v49, v50, s58, v49
	v_lshl_add_u64 v[68:69], v[52:53], 0, v[68:69]
	global_store_dwordx4 v[68:69], v[46:49], off nt
	v_bfe_u32 v50, v67, 16, 1
	v_add3_u32 v50, v67, v50, s57
	v_bfe_u32 v46, v55, 16, 1
	v_add3_u32 v46, v55, v46, s57
	v_bfe_u32 v47, v51, 16, 1
	v_lshrrev_b32_e32 v46, 16, v46
	v_add3_u32 v47, v51, v47, s57
	v_and_or_b32 v46, v47, s58, v46
	v_bfe_u32 v47, v57, 16, 1
	v_add3_u32 v47, v57, v47, s57
	v_bfe_u32 v48, v59, 16, 1
	v_lshrrev_b32_e32 v47, 16, v47
	v_add3_u32 v48, v59, v48, s57
	v_and_or_b32 v47, v48, s58, v47
	v_bfe_u32 v48, v61, 16, 1
	v_add3_u32 v48, v61, v48, s57
	v_bfe_u32 v49, v63, 16, 1
	v_lshrrev_b32_e32 v48, 16, v48
	v_add3_u32 v49, v63, v49, s57
	v_and_or_b32 v48, v49, s58, v48
	v_bfe_u32 v49, v65, 16, 1
	v_add3_u32 v49, v65, v49, s57
	v_lshrrev_b32_e32 v49, 16, v49
	v_and_or_b32 v49, v50, s58, v49
	v_add_u32_e32 v50, s4, v37
	v_ashrrev_i32_e32 v51, 31, v50
	v_lshlrev_b64 v[50:51], 11, v[50:51]
	v_lshl_add_u64 v[50:51], v[52:53], 0, v[50:51]
	global_store_dwordx4 v[50:51], v[46:49], off nt
	s_waitcnt lgkmcnt(0)

; #define LAS __attribute__((address_space(3)))
; __device__ __forceinline__ void tr_item(const float* W, int ld, int K, int nblk, int item, bf16* WT, bool gu, LAS float* scr, int lane) {
;     const int kb = item / nblk, nb = item % nblk, k0 = 64 * kb, n0 = 32 * nb;
;     int drow0 = n0;
;     if (gu) { const int bj = n0 / FF, j = n0 - bj * FF; drow0 = 256 * (j / 128) + 128 * bj + (j % 128); }
;     { float t_[32];
; #pragma unroll
;       for (int i = 0; i < 32; ++i) t_[i] = W[(size_t)(k0 + 2 * i + (lane >> 5)) * ld + n0 + (lane & 31)];
; #pragma unroll
;       for (int i = 0; i < 32; ++i) scr[(2 * i + (lane >> 5)) * 33 + (lane & 31)] = t_[i]; }
; __device__ __forceinline__ void convert_items(Frame& F, const Args& a, int lo, int hi, int w, int nw) {
;     ...
;         if (r < I_FI) { tr_item(a.in[7], 3 * D + 16, D, 96, r, (bf16*)(F.ws + WS_WFOXIN), false, scr, lane); continue; } r -= I_FI;
.LBB0_1432:
	s_andn2_b64 vcc, exec, s[4:5]
	s_cbranch_vccnz .LBB0_1405
	s_mul_hi_i32 s0, s3, 0x2aaaaaab
	s_lshr_b32 s4, s0, 31
	s_ashr_i32 s0, s0, 4
	s_add_i32 s0, s0, s4
	s_lshl_b32 s6, s0, 6
	s_mulk_i32 s0, 0xf400
	s_add_i32 s4, s8, s0
	v_add_u32_e32 v64, s6, v28
	s_ashr_i32 s5, s4, 31
	v_lshl_add_u64 v[46:47], s[4:5], 2, v[14:15]
	v_add_u32_e32 v50, 2, v64
	v_add_u32_e32 v52, 4, v64
	v_add_u32_e32 v54, 6, v64
	v_add_u32_e32 v56, 8, v64
	v_add_u32_e32 v58, 10, v64
	v_add_u32_e32 v60, 12, v64
	v_add_u32_e32 v62, 14, v64
	v_mad_i64_i32 v[48:49], s[62:63], v64, s60, v[46:47]
	v_mad_i64_i32 v[50:51], s[62:63], v50, s60, v[46:47]
	v_mad_i64_i32 v[52:53], s[62:63], v52, s60, v[46:47]
	v_mad_i64_i32 v[54:55], s[62:63], v54, s60, v[46:47]
	v_mad_i64_i32 v[56:57], s[62:63], v56, s60, v[46:47]
	v_mad_i64_i32 v[58:59], s[62:63], v58, s60, v[46:47]
	v_mad_i64_i32 v[60:61], s[62:63], v60, s60, v[46:47]
	v_mad_i64_i32 v[62:63], s[62:63], v62, s60, v[46:47]
	global_load_dword v65, v[48:49], off nt
	global_load_dword v66, v[50:51], off nt
	global_load_dword v67, v[52:53], off nt
	global_load_dword v68, v[54:55], off nt
	global_load_dword v69, v[56:57], off nt
	global_load_dword v70, v[58:59], off nt
	global_load_dword v71, v[60:61], off nt
	global_load_dword v72, v[62:63], off nt
	v_add_u32_e32 v48, 16, v64
	v_add_u32_e32 v50, 18, v64
	v_add_u32_e32 v52, 20, v64
	v_add_u32_e32 v54, 22, v64
	v_add_u32_e32 v56, 24, v64
	v_add_u32_e32 v58, 26, v64
	v_add_u32_e32 v60, 28, v64
	v_add_u32_e32 v62, 30, v64
	v_mad_i64_i32 v[48:49], s[62:63], v48, s60, v[46:47]
	v_mad_i64_i32 v[50:51], s[62:63], v50, s60, v[46:47]
	v_mad_i64_i32 v[52:53], s[62:63], v52, s60, v[46:47]
	v_mad_i64_i32 v[54:55], s[62:63], v54, s60, v[46:47]
	v_mad_i64_i32 v[56:57], s[62:63], v56, s60, v[46:47]
	v_mad_i64_i32 v[58:59], s[62:63], v58, s60, v[46:47]
	v_mad_i64_i32 v[60:61], s[62:63], v60, s60, v[46:47]
	v_mad_i64_i32 v[62:63], s[62:63], v62, s60, v[46:47]
	global_load_dword v73, v[48:49], off nt
	global_load_dword v74, v[50:51], off nt
	global_load_dword v75, v[52:53], off nt
	global_load_dword v76, v[54:55], off nt
	global_load_dword v77, v[56:57], off nt
	global_load_dword v78, v[58:59], off nt
	global_load_dword v79, v[60:61], off nt
	global_load_dword v80, v[62:63], off nt
	v_add_u32_e32 v48, 32, v64
	v_add_u32_e32 v50, 34, v64
	v_add_u32_e32 v52, 36, v64
	v_add_u32_e32 v54, 38, v64
	v_add_u32_e32 v56, 40, v64
	v_add_u32_e32 v58, 42, v64
	v_add_u32_e32 v60, 44, v64
	v_add_u32_e32 v62, 46, v64
	v_mad_i64_i32 v[48:49], s[62:63], v48, s60, v[46:47]
	v_mad_i64_i32 v[50:51], s[62:63], v50, s60, v[46:47]
	v_mad_i64_i32 v[52:53], s[62:63], v52, s60, v[46:47]
	v_mad_i64_i32 v[54:55], s[62:63], v54, s60, v[46:47]
	v_mad_i64_i32 v[56:57], s[62:63], v56, s60, v[46:47]
	v_mad_i64_i32 v[58:59], s[62:63], v58, s60, v[46:47]
	v_mad_i64_i32 v[60:61], s[62:63], v60, s60, v[46:47]
	v_mad_i64_i32 v[62:63], s[62:63], v62, s60, v[46:47]
	global_load_dword v81, v[48:49], off nt
	global_load_dword v82, v[50:51], off nt
	global_load_dword v83, v[52:53], off nt
	global_load_dword v84, v[54:55], off nt
	global_load_dword v85, v[56:57], off nt
	global_load_dword v86, v[58:59], off nt
	global_load_dword v87, v[60:61], off nt
	s_nop 0
	global_load_dword v62, v[62:63], off nt
	v_add_u32_e32 v48, 48, v64
	v_add_u32_e32 v50, 50, v64
	v_add_u32_e32 v52, 52, v64
	v_add_u32_e32 v54, 54, v64
	v_add_u32_e32 v56, 56, v64
	v_add_u32_e32 v58, 58, v64
	v_add_u32_e32 v60, 60, v64
	v_add_u32_e32 v63, 62, v64
	v_mad_i64_i32 v[48:49], s[62:63], v48, s60, v[46:47]
	v_mad_i64_i32 v[50:51], s[62:63], v50, s60, v[46:47]
	v_mad_i64_i32 v[52:53], s[62:63], v52, s60, v[46:47]
	v_mad_i64_i32 v[54:55], s[62:63], v54, s60, v[46:47]
	v_mad_i64_i32 v[56:57], s[62:63], v56, s60, v[46:47]
	v_mad_i64_i32 v[58:59], s[62:63], v58, s60, v[46:47]
	v_mad_i64_i32 v[60:61], s[62:63], v60, s60, v[46:47]
	v_mad_i64_i32 v[46:47], s[62:63], v63, s60, v[46:47]
	global_load_dword v48, v[48:49], off nt
	s_nop 0
	global_load_dword v49, v[50:51], off nt
	s_nop 0
	global_load_dword v50, v[52:53], off nt
	global_load_dword v51, v[54:55], off nt
	s_nop 0
	global_load_dword v52, v[56:57], off nt
	global_load_dword v53, v[58:59], off nt
	global_load_dword v54, v[60:61], off nt
	s_nop 0
	global_load_dword v46, v[46:47], off nt
	s_waitcnt vmcnt(30)
	ds_write2_b32 v29, v65, v66 offset1:66
	s_waitcnt vmcnt(28)
	ds_write2_b32 v29, v67, v68 offset0:132 offset1:198
	s_waitcnt vmcnt(26)
	ds_write2_b32 v38, v69, v70 offset0:8 offset1:74
	s_waitcnt vmcnt(24)
	ds_write2_b32 v38, v71, v72 offset0:140 offset1:206
	s_waitcnt vmcnt(22)
	ds_write2_b32 v39, v73, v74 offset0:16 offset1:82
	s_waitcnt vmcnt(20)
	ds_write2_b32 v39, v75, v76 offset0:148 offset1:214
	s_waitcnt vmcnt(18)
	ds_write2_b32 v40, v77, v78 offset0:24 offset1:90
	s_waitcnt vmcnt(16)
	ds_write2_b32 v40, v79, v80 offset0:156 offset1:222
	s_waitcnt vmcnt(14)
	ds_write2_b32 v41, v81, v82 offset0:32 offset1:98
	s_waitcnt vmcnt(12)
	ds_write2_b32 v41, v83, v84 offset0:164 offset1:230
	s_waitcnt vmcnt(10)
	ds_write2_b32 v42, v85, v86 offset0:40 offset1:106
	s_waitcnt vmcnt(8)
	ds_write2_b32 v42, v87, v62 offset0:172 offset1:238
	s_waitcnt vmcnt(6)
; #define GAS __attribute__((address_space(1)))
; #define LAS __attribute__((address_space(3)))
; #define LDS_WAIT() asm volatile("s_waitcnt lgkmcnt(0)" ::: "memory")
; __device__ __forceinline__ unsigned pk2(float lo, float hi) { return f2bf(lo) | (f2bf(hi) << 16); }
; __device__ __forceinline__ void tr_item(const float* W, int ld, int K, int nblk, int item, bf16* WT, bool gu, LAS float* scr, int lane) {
;     ...
;       for (int i = 0; i < 32; ++i) scr[(2 * i + (lane >> 5)) * 33 + (lane & 31)] = t_[i]; }
;     LDS_WAIT(); asm volatile("" ::: "memory");
;     const int c = lane & 7;
; #pragma unroll
;     for (int j = 0; j < 4; ++j) { const int n = (lane >> 3) + 8 * j; const LAS float* s = scr + (8 * c) * 33 + n;
;         v4u o; o.x = pk2(s[0 * 33], s[1 * 33]); o.y = pk2(s[2 * 33], s[3 * 33]); o.z = pk2(s[4 * 33], s[5 * 33]); o.w = pk2(s[6 * 33], s[7 * 33]);
;         *(GAS v4u*)(WT + (size_t)(drow0 + n) * K + k0 + 8 * c) = o; }
;     LDS_WAIT(); asm volatile("" ::: "memory");
; __device__ __forceinline__ void convert_items(Frame& F, const Args& a, int lo, int hi, int w, int nw) {
;     ...
;     for (int it = lo + w; it < hi; it += nw) {
	ds_write2_b32 v43, v48, v49 offset0:48 offset1:114
	s_waitcnt vmcnt(4)
	ds_write2_b32 v43, v50, v51 offset0:180 offset1:246
	s_waitcnt vmcnt(2)
	ds_write2_b32 v44, v52, v53 offset0:56 offset1:122
	s_waitcnt vmcnt(0)
	ds_write2_b32 v44, v54, v46 offset0:188 offset1:254
	s_waitcnt lgkmcnt(0)
	ds_read2_b32 v[50:51], v34 offset1:8
	ds_read2_b32 v[54:55], v34 offset0:33 offset1:41
	ds_read2_b32 v[56:57], v34 offset0:66 offset1:74
	ds_read2_b32 v[58:59], v34 offset0:99 offset1:107
	ds_read2_b32 v[60:61], v34 offset0:132 offset1:140
	s_waitcnt lgkmcnt(4)
	v_bfe_u32 v46, v50, 16, 1
	v_add3_u32 v46, v50, v46, s57
	s_waitcnt lgkmcnt(3)
	v_bfe_u32 v47, v54, 16, 1
	v_lshrrev_b32_e32 v46, 16, v46
	v_add3_u32 v47, v54, v47, s57
	ds_read2_b32 v[62:63], v34 offset0:165 offset1:173
	v_and_or_b32 v46, v47, s58, v46
	s_waitcnt lgkmcnt(3)
	v_bfe_u32 v47, v56, 16, 1
	v_add3_u32 v47, v56, v47, s57
	s_waitcnt lgkmcnt(2)
	v_bfe_u32 v48, v58, 16, 1
	ds_read2_b32 v[64:65], v34 offset0:198 offset1:206
	v_lshrrev_b32_e32 v47, 16, v47
	v_add3_u32 v48, v58, v48, s57
	ds_read2_b32 v[66:67], v34 offset0:231 offset1:239
	v_and_or_b32 v47, v48, s58, v47
	s_waitcnt lgkmcnt(3)
	v_bfe_u32 v48, v60, 16, 1
	v_add3_u32 v48, v60, v48, s57
	s_waitcnt lgkmcnt(2)
	v_bfe_u32 v49, v62, 16, 1
	v_lshrrev_b32_e32 v48, 16, v48
	v_add3_u32 v49, v62, v49, s57
	v_and_or_b32 v48, v49, s58, v48
	s_waitcnt lgkmcnt(1)
	v_bfe_u32 v49, v64, 16, 1
	v_add_u32_e32 v68, s4, v33
	s_ashr_i32 s7, s6, 31
	v_add3_u32 v49, v64, v49, s57
	s_waitcnt lgkmcnt(0)
	v_bfe_u32 v50, v66, 16, 1
	v_ashrrev_i32_e32 v69, 31, v68
	v_lshl_add_u64 v[52:53], s[6:7], 1, v[26:27]
	v_lshrrev_b32_e32 v49, 16, v49
	v_add3_u32 v50, v66, v50, s57
	v_lshlrev_b64 v[70:71], 11, v[68:69]
	v_and_or_b32 v49, v50, s58, v49
	v_lshl_add_u64 v[70:71], v[52:53], 0, v[70:71]
	global_store_dwordx4 v[70:71], v[46:49], off nt
	v_bfe_u32 v50, v67, 16, 1
	v_add3_u32 v50, v67, v50, s57
	v_bfe_u32 v46, v51, 16, 1
	v_add3_u32 v46, v51, v46, s57
	v_bfe_u32 v47, v55, 16, 1
	v_lshrrev_b32_e32 v46, 16, v46
	v_add3_u32 v47, v55, v47, s57
	v_and_or_b32 v46, v47, s58, v46
	v_bfe_u32 v47, v57, 16, 1
	v_add3_u32 v47, v57, v47, s57
	v_bfe_u32 v48, v59, 16, 1
	v_lshrrev_b32_e32 v47, 16, v47
	v_add3_u32 v48, v59, v48, s57
	v_and_or_b32 v47, v48, s58, v47
	v_bfe_u32 v48, v61, 16, 1
	v_add3_u32 v48, v61, v48, s57
	v_bfe_u32 v49, v63, 16, 1
	v_lshrrev_b32_e32 v48, 16, v48
	v_add3_u32 v49, v63, v49, s57
	v_and_or_b32 v48, v49, s58, v48
	v_bfe_u32 v49, v65, 16, 1
	v_add3_u32 v49, v65, v49, s57
	v_lshrrev_b32_e32 v49, 16, v49
	v_and_or_b32 v49, v50, s58, v49
	v_add_u32_e32 v50, 8, v68
	v_ashrrev_i32_e32 v51, 31, v50
	v_lshlrev_b64 v[50:51], 11, v[50:51]
	ds_read2_b32 v[54:55], v34 offset0:16 offset1:24
	v_lshl_add_u64 v[50:51], v[52:53], 0, v[50:51]
	global_store_dwordx4 v[50:51], v[46:49], off nt
	ds_read2_b32 v[50:51], v34 offset0:49 offset1:57
	ds_read2_b32 v[56:57], v34 offset0:82 offset1:90
	ds_read2_b32 v[58:59], v34 offset0:115 offset1:123
	s_waitcnt lgkmcnt(3)
	v_bfe_u32 v46, v54, 16, 1
	v_add3_u32 v46, v54, v46, s57
	s_waitcnt lgkmcnt(2)
	v_bfe_u32 v47, v50, 16, 1
	ds_read2_b32 v[60:61], v34 offset0:148 offset1:156
	v_lshrrev_b32_e32 v46, 16, v46
	v_add3_u32 v47, v50, v47, s57
	ds_read2_b32 v[62:63], v34 offset0:181 offset1:189
	v_and_or_b32 v46, v47, s58, v46
	s_waitcnt lgkmcnt(3)
	v_bfe_u32 v47, v56, 16, 1
	v_add3_u32 v47, v56, v47, s57
	s_waitcnt lgkmcnt(2)
	v_bfe_u32 v48, v58, 16, 1
	ds_read2_b32 v[64:65], v34 offset0:214 offset1:222
	v_lshrrev_b32_e32 v47, 16, v47
	v_add3_u32 v48, v58, v48, s57
	ds_read2_b32 v[66:67], v34 offset0:247 offset1:255
	v_and_or_b32 v47, v48, s58, v47
	s_waitcnt lgkmcnt(3)
	v_bfe_u32 v48, v60, 16, 1
	v_add3_u32 v48, v60, v48, s57
	s_waitcnt lgkmcnt(2)
	v_bfe_u32 v49, v62, 16, 1
	v_lshrrev_b32_e32 v48, 16, v48
	v_add3_u32 v49, v62, v49, s57
	v_and_or_b32 v48, v49, s58, v48
	s_waitcnt lgkmcnt(1)
	v_bfe_u32 v49, v64, 16, 1
	v_add_u32_e32 v70, 16, v68
	v_add3_u32 v49, v64, v49, s57
	s_waitcnt lgkmcnt(0)
	v_bfe_u32 v50, v66, 16, 1
	v_ashrrev_i32_e32 v71, 31, v70
	v_lshrrev_b32_e32 v49, 16, v49
	v_add3_u32 v50, v66, v50, s57
	v_lshlrev_b64 v[70:71], 11, v[70:71]
	v_and_or_b32 v49, v50, s58, v49
	v_lshl_add_u64 v[70:71], v[52:53], 0, v[70:71]
	global_store_dwordx4 v[70:71], v[46:49], off nt
	v_bfe_u32 v50, v67, 16, 1
	v_add3_u32 v50, v67, v50, s57
	v_bfe_u32 v46, v55, 16, 1
	v_add3_u32 v46, v55, v46, s57
	v_bfe_u32 v47, v51, 16, 1
	v_lshrrev_b32_e32 v46, 16, v46
	v_add3_u32 v47, v51, v47, s57
	v_and_or_b32 v46, v47, s58, v46
	v_bfe_u32 v47, v57, 16, 1
	v_add3_u32 v47, v57, v47, s57
	v_bfe_u32 v48, v59, 16, 1
	v_lshrrev_b32_e32 v47, 16, v47
	v_add3_u32 v48, v59, v48, s57
	v_and_or_b32 v47, v48, s58, v47
	v_bfe_u32 v48, v61, 16, 1
	v_add3_u32 v48, v61, v48, s57
	v_bfe_u32 v49, v63, 16, 1
	v_lshrrev_b32_e32 v48, 16, v48
	v_add3_u32 v49, v63, v49, s57
	v_and_or_b32 v48, v49, s58, v48
	v_bfe_u32 v49, v65, 16, 1
	v_add3_u32 v49, v65, v49, s57
	v_lshrrev_b32_e32 v49, 16, v49
	v_and_or_b32 v49, v50, s58, v49
	v_add_u32_e32 v50, 24, v68
	v_ashrrev_i32_e32 v51, 31, v50
	v_lshlrev_b64 v[50:51], 11, v[50:51]
	v_lshl_add_u64 v[50:51], v[52:53], 0, v[50:51]
	global_store_dwordx4 v[50:51], v[46:49], off nt
	s_waitcnt lgkmcnt(0)
	s_branch .LBB0_1405
